# v102: v100 + s_setprio moved across the block-edge barriers (raise before the pre-MFMA barrier, drop after the post-MFMA barrier)
# speedup vs baseline: 1.0020x; 1.0020x over previous
; #define PG8_GIDX(G_, PM_) do { if constexpr (Sched::GATHER) { _Pragma("unroll") for (int h_ = 0; h_ < 2; ++h_) _Pragma("unroll") for (int i_ = 0; i_ < 2; ++i_) { int R_, C_; stage_rc(tid * 16 + i_ * 8192, R_, C_); \
;         const int src_ = S.rowsrc[(PM_) * BM + h_ * HALF + R_]; G_[h_][i_] = (unsigned)(src_ * K + C_) * 2u; } } } while (0)
; #define PG8_STAGE_A(b, h, ptr, NX) do { if constexpr (Sched::GATHER) { unsigned gs_[2]; gs_[0] = ((NX) && last_) ? gN[h][0] : gA[h][0]; gs_[1] = ((NX) && last_) ? gN[h][1] : gA[h][1]; PG8_STAGE(PG8_SA(b, h), ptr, gs_); } \
;         else PG8_STAGE(PG8_SA(b, h), (ptr) + ((h) ? hstep : (size_t)0), voffA); } while (0)
; #define PG8_LDA(dst, b, h) do { _Pragma("unroll") for (int m = 0; m < 4; ++m) _Pragma("unroll") for (int k = 0; k < 2; ++k) dst[m][k] = *(const PG8_LAS bf16x8*)(lds + PG8_SA(b, h) + aoff + m * 2048 + k * 1024); } while (0)
; template <class Epi, class Sched, bool ALIGN_EPI = false, bool SP2 = false>
; __device__ __forceinline__ void gemm_phase(PG8_LAS unsigned char* lds, const Gemm g, const Sched& S, const Epi& E, const bool skip_epi = false) {
;     ...
;         const bool has_next = S.next(ui + 1, nxt);
;         if (has_next) PG8_GIDX(gN, nxt.pm);
;         const char* nA = has_next ? (const char*)g.A + (size_t)nxt.pm * pmstepA + nxt.ko : cA; const char* nB = has_next ? (const char*)g.Bt + (size_t)nxt.pn * tstep + nxt.ko : cB;
;         for (int t = 0; t < nt; t += 2) {
;             const bool last = (t == nt - 2); last_ = last && has_next;
;             const char* a1 = cA + (size_t)(t + 1) * kstep;
;             const char* a2 = last ? nA : cA + (size_t)(t + 2) * kstep; const char* b2 = last ? nB : cB + (size_t)(t + 2) * kstep;
;             const char* a3 = a2 + kstep; const char* b3 = b2 + kstep;
;             if (last && has_next) S.a_ready(nxt);
;             if constexpr (SP2) {
;             PG8_LDB(B0, 0, 0); PG8_LDB(B1, 0, 1); PG8_SCHED; PG8_LDA(At, 0, 0); PG8_STAGE_A(1, 1, a1, false);
;             PG8_WAIT_V(8); PG8_WAIT_L(0); PG8_BAR; PG8_MMA(0, 0, At, B0); PG8_MMA(0, 1, At, B1); PG8_BAR; PG8_SCHED;
;             PG8_LDA(At, 0, 1); PG8_STAGE(PG8_SB(0, 0), b2, voffB); PG8_STAGE(PG8_SB(0, 1), b2 + hstep, voffB); PG8_STAGE_A(0, 0, a2, true);
;             PG8_WAIT_V(8); PG8_WAIT_L(0); PG8_BAR; PG8_MMA(1, 0, At, B0); PG8_MMA(1, 1, At, B1); PG8_BAR; PG8_SCHED;
.LBB0_252:
	s_ashr_i32 s17, s16, 31
	s_lshl_b64 s[18:19], s[16:17], 19
	s_add_u32 s18, s86, s18
	s_addc_u32 s19, s87, s19
	s_and_b64 s[20:21], s[4:5], exec
	s_cselect_b32 s17, s19, s25
	s_cselect_b32 s56, s18, s24
	s_ashr_i32 s15, s14, 31
	s_lshl_b64 s[20:21], s[14:15], 19
	v_readlane_b32 s28, v254, 36
	v_readlane_b32 s29, v254, 37
	s_add_u32 s20, s28, s20
	s_addc_u32 s21, s29, s21
	s_and_b64 s[28:29], s[4:5], exec
	s_cselect_b32 s15, s21, s27
	s_cselect_b32 s57, s20, s26
	s_add_u32 s24, s24, 0x40080
	s_addc_u32 s25, s25, 0
	s_add_u32 s58, s26, 0x100
	s_addc_u32 s59, s27, 0
	s_mov_b32 s60, -2
	s_waitcnt vmcnt(0)
	ds_read_b128 v[148:151], v170
	ds_read_b128 v[152:155], v170 offset:1024
	ds_read_b128 v[156:159], v170 offset:2048
	ds_read_b128 v[160:163], v170 offset:3072
	ds_read_b128 v[176:179], v171
	ds_read_b128 v[180:183], v171 offset:1024
	ds_read_b128 v[184:187], v171 offset:2048
	ds_read_b128 v[188:191], v171 offset:3072
	s_add_u32 s26, s24, 0xfffc0080
	s_addc_u32 s27, s25, -1
	s_cmp_eq_u32 s60, 12
	s_cselect_b32 s29, s17, s27
	s_cselect_b32 s28, s56, s26
	s_cselect_b32 s27, s15, s59
	s_cselect_b32 s26, s57, s58
	s_add_i32 m0, s23, 0xc000
	ds_read_b128 v[192:195], v172
	ds_read_b128 v[196:199], v172 offset:1024
	ds_read_b128 v[200:203], v172 offset:2048
	ds_read_b128 v[204:207], v172 offset:3072
	ds_read_b128 v[208:211], v172 offset:4096
	ds_read_b128 v[212:215], v172 offset:5120
	ds_read_b128 v[216:219], v172 offset:6144
	ds_read_b128 v[220:223], v172 offset:7168
	global_load_lds_dwordx4 v140, s[24:25]
	s_add_i32 m0, s23, 0xe000
	s_nop 0
	global_load_lds_dwordx4 v142, s[24:25]
	s_waitcnt vmcnt(8)
	s_waitcnt lgkmcnt(0)
	s_setprio 3
	s_barrier
	s_waitcnt lgkmcnt(0)
	v_mfma_f32_16x16x32_bf16 v[126:129], v[148:151], v[192:195], 0
	v_mfma_f32_16x16x32_bf16 v[122:125], v[156:159], v[192:195], 0
	v_mfma_f32_16x16x32_bf16 v[114:117], v[148:151], v[200:203], 0
	v_mfma_f32_16x16x32_bf16 v[106:109], v[156:159], v[200:203], 0
	v_mfma_f32_16x16x32_bf16 v[98:101], v[148:151], v[208:211], 0
	v_mfma_f32_16x16x32_bf16 v[90:93], v[156:159], v[208:211], 0
	v_mfma_f32_16x16x32_bf16 v[82:85], v[148:151], v[216:219], 0
	v_mfma_f32_16x16x32_bf16 v[74:77], v[156:159], v[216:219], 0
	v_mfma_f32_16x16x32_bf16 v[126:129], v[152:155], v[196:199], v[126:129]
	v_mfma_f32_16x16x32_bf16 v[122:125], v[160:163], v[196:199], v[122:125]
	v_mfma_f32_16x16x32_bf16 v[114:117], v[152:155], v[204:207], v[114:117]
	v_mfma_f32_16x16x32_bf16 v[106:109], v[160:163], v[204:207], v[106:109]
	v_mfma_f32_16x16x32_bf16 v[98:101], v[152:155], v[212:215], v[98:101]
	v_mfma_f32_16x16x32_bf16 v[90:93], v[160:163], v[212:215], v[90:93]
	v_mfma_f32_16x16x32_bf16 v[82:85], v[152:155], v[220:223], v[82:85]
	v_mfma_f32_16x16x32_bf16 v[74:77], v[160:163], v[220:223], v[74:77]
	v_mfma_f32_16x16x32_bf16 v[118:121], v[176:179], v[192:195], 0
	v_mfma_f32_16x16x32_bf16 v[110:113], v[184:187], v[192:195], 0
	v_mfma_f32_16x16x32_bf16 v[102:105], v[176:179], v[200:203], 0
	v_mfma_f32_16x16x32_bf16 v[94:97], v[184:187], v[200:203], 0
	v_mfma_f32_16x16x32_bf16 v[86:89], v[176:179], v[208:211], 0
	v_mfma_f32_16x16x32_bf16 v[78:81], v[184:187], v[208:211], 0
	v_mfma_f32_16x16x32_bf16 v[70:73], v[176:179], v[216:219], 0
	v_mfma_f32_16x16x32_bf16 v[66:69], v[184:187], v[216:219], 0
	v_mfma_f32_16x16x32_bf16 v[118:121], v[180:183], v[196:199], v[118:121]
	v_mfma_f32_16x16x32_bf16 v[110:113], v[188:191], v[196:199], v[110:113]
	v_mfma_f32_16x16x32_bf16 v[102:105], v[180:183], v[204:207], v[102:105]
	v_mfma_f32_16x16x32_bf16 v[94:97], v[188:191], v[204:207], v[94:97]
	v_mfma_f32_16x16x32_bf16 v[86:89], v[180:183], v[212:215], v[86:89]
	v_mfma_f32_16x16x32_bf16 v[78:81], v[188:191], v[212:215], v[78:81]
	v_mfma_f32_16x16x32_bf16 v[70:73], v[180:183], v[220:223], v[70:73]
	v_mfma_f32_16x16x32_bf16 v[66:69], v[188:191], v[220:223], v[66:69]
	s_barrier
	s_setprio 0
	s_add_i32 s61, s46, s2
	v_lshl_add_u64 v[164:165], s[26:27], 0, v[134:135]
	s_mov_b32 m0, s61
	ds_read_b128 v[192:195], v172 offset:16384
	ds_read_b128 v[196:199], v172 offset:17408
	ds_read_b128 v[200:203], v172 offset:18432
	ds_read_b128 v[204:207], v172 offset:19456
	ds_read_b128 v[208:211], v172 offset:20480
	ds_read_b128 v[212:215], v172 offset:21504
	ds_read_b128 v[216:219], v172 offset:22528
	ds_read_b128 v[220:223], v172 offset:23552
	global_load_lds_dwordx4 v[164:165], off
	s_add_i32 m0, s61, 0x2000
	s_add_u32 s62, s26, 0x40000
	v_lshl_add_u64 v[224:225], s[26:27], 0, v[130:131]
	s_addc_u32 s63, s27, 0
	s_add_i32 s61, s47, s2
	global_load_lds_dwordx4 v[224:225], off
	s_mov_b32 m0, s61
	v_lshl_add_u64 v[230:231], s[28:29], 0, v[132:133]
	global_load_lds_dwordx4 v134, s[62:63]
	s_add_i32 m0, s61, 0x2000
	s_nop 0
	global_load_lds_dwordx4 v130, s[62:63]
	v_lshl_add_u64 v[226:227], s[28:29], 0, v[136:137]
	s_mov_b32 m0, s23
	s_nop 0
	global_load_lds_dwordx4 v[226:227], off
	s_mov_b32 m0, s31
	s_nop 0
	global_load_lds_dwordx4 v[230:231], off
	s_waitcnt vmcnt(8)
	s_waitcnt lgkmcnt(0)
	s_setprio 3
	s_barrier
; #define PG8_STAGE_A(b, h, ptr, NX) do { if constexpr (Sched::GATHER) { unsigned gs_[2]; gs_[0] = ((NX) && last_) ? gN[h][0] : gA[h][0]; gs_[1] = ((NX) && last_) ? gN[h][1] : gA[h][1]; PG8_STAGE(PG8_SA(b, h), ptr, gs_); } \
;         else PG8_STAGE(PG8_SA(b, h), (ptr) + ((h) ? hstep : (size_t)0), voffA); } while (0)
; #define PG8_STAGE(bufoff, gbase, voff) do { _Pragma("unroll") for (int _i = 0; _i < 2; ++_i) \
;         __builtin_amdgcn_global_load_lds((const unsigned*)((const char*)(gbase) + (voff)[_i]), (PG8_LAS unsigned*)(lds + (bufoff) + ldsw + _i * 8192), 16, 0, 0); } while (0)
; #define PG8_LDA(dst, b, h) do { _Pragma("unroll") for (int m = 0; m < 4; ++m) _Pragma("unroll") for (int k = 0; k < 2; ++k) dst[m][k] = *(const PG8_LAS bf16x8*)(lds + PG8_SA(b, h) + aoff + m * 2048 + k * 1024); } while (0)
; #define PG8_LDB(dst, b, h) do { _Pragma("unroll") for (int n = 0; n < 2; ++n) _Pragma("unroll") for (int k = 0; k < 2; ++k) dst[n][k] = *(const PG8_LAS bf16x8*)(lds + PG8_SB(b, h) + boff + n * 2048 + k * 1024); } while (0)
; #define PG8_MMA(ai, bj, At, Bt) do { __builtin_amdgcn_s_setprio(1); _Pragma("unroll") for (int m = 0; m < 4; ++m) _Pragma("unroll") for (int n = 0; n < 2; ++n) _Pragma("unroll") for (int k = 0; k < 2; ++k) \
;         acc[ai][bj][m][n] = __builtin_amdgcn_mfma_f32_16x16x32_bf16(Bt[n][k], At[m][k], acc[ai][bj][m][n], 0, 0, 0); __builtin_amdgcn_s_setprio(0); } while (0)
; #define PG8_WAIT_V(n) asm volatile("s_waitcnt vmcnt(" #n ")" ::: "memory")
; #define PG8_WAIT_L(n) asm volatile("s_waitcnt lgkmcnt(" #n ")" ::: "memory")
; #define PG8_BAR __builtin_amdgcn_s_barrier()
; #define PG8_SCHED __builtin_amdgcn_sched_barrier(0)
; template <class Epi, class Sched, bool ALIGN_EPI = false, bool SP2 = false>
; __device__ __forceinline__ void gemm_phase(PG8_LAS unsigned char* lds, const Gemm g, const Sched& S, const Epi& E, const bool skip_epi = false) {
;     ...
;             PG8_WAIT_V(8); PG8_WAIT_L(0); PG8_BAR; PG8_MMA(1, 0, At, B0); PG8_MMA(1, 1, At, B1); PG8_BAR; PG8_SCHED;
;             PG8_LDB(B0, 1, 0); PG8_LDB(B1, 1, 1); PG8_SCHED; PG8_LDA(At, 1, 0); PG8_STAGE_A(0, 1, a2, true);
;             PG8_WAIT_V(8); PG8_WAIT_L(0); PG8_BAR; PG8_MMA(0, 0, At, B0); PG8_MMA(0, 1, At, B1); PG8_BAR; PG8_SCHED;
;             PG8_LDA(At, 1, 1); PG8_STAGE(PG8_SB(1, 0), b3, voffB); PG8_STAGE(PG8_SB(1, 1), b3 + hstep, voffB); PG8_STAGE_A(1, 0, a3, true);
	s_waitcnt lgkmcnt(0)
	v_mfma_f32_16x16x32_bf16 v[62:65], v[148:151], v[192:195], 0
	v_mfma_f32_16x16x32_bf16 v[58:61], v[156:159], v[192:195], 0
	v_mfma_f32_16x16x32_bf16 v[50:53], v[148:151], v[200:203], 0
	v_mfma_f32_16x16x32_bf16 v[42:45], v[156:159], v[200:203], 0
	v_mfma_f32_16x16x32_bf16 v[34:37], v[148:151], v[208:211], 0
	v_mfma_f32_16x16x32_bf16 v[26:29], v[156:159], v[208:211], 0
	v_mfma_f32_16x16x32_bf16 v[18:21], v[148:151], v[216:219], 0
	v_mfma_f32_16x16x32_bf16 v[10:13], v[156:159], v[216:219], 0
	v_mfma_f32_16x16x32_bf16 v[62:65], v[152:155], v[196:199], v[62:65]
	v_mfma_f32_16x16x32_bf16 v[58:61], v[160:163], v[196:199], v[58:61]
	v_mfma_f32_16x16x32_bf16 v[50:53], v[152:155], v[204:207], v[50:53]
	v_mfma_f32_16x16x32_bf16 v[42:45], v[160:163], v[204:207], v[42:45]
	v_mfma_f32_16x16x32_bf16 v[34:37], v[152:155], v[212:215], v[34:37]
	v_mfma_f32_16x16x32_bf16 v[26:29], v[160:163], v[212:215], v[26:29]
	v_mfma_f32_16x16x32_bf16 v[18:21], v[152:155], v[220:223], v[18:21]
	v_mfma_f32_16x16x32_bf16 v[10:13], v[160:163], v[220:223], v[10:13]
	v_mfma_f32_16x16x32_bf16 v[54:57], v[176:179], v[192:195], 0
	v_mfma_f32_16x16x32_bf16 v[46:49], v[184:187], v[192:195], 0
	v_mfma_f32_16x16x32_bf16 v[38:41], v[176:179], v[200:203], 0
	v_mfma_f32_16x16x32_bf16 v[30:33], v[184:187], v[200:203], 0
	v_mfma_f32_16x16x32_bf16 v[22:25], v[176:179], v[208:211], 0
	v_mfma_f32_16x16x32_bf16 v[14:17], v[184:187], v[208:211], 0
	v_mfma_f32_16x16x32_bf16 v[6:9], v[176:179], v[216:219], 0
	v_mfma_f32_16x16x32_bf16 v[2:5], v[184:187], v[216:219], 0
	v_mfma_f32_16x16x32_bf16 v[54:57], v[180:183], v[196:199], v[54:57]
	v_mfma_f32_16x16x32_bf16 v[46:49], v[188:191], v[196:199], v[46:49]
	v_mfma_f32_16x16x32_bf16 v[38:41], v[180:183], v[204:207], v[38:41]
	v_mfma_f32_16x16x32_bf16 v[30:33], v[188:191], v[204:207], v[30:33]
	v_mfma_f32_16x16x32_bf16 v[22:25], v[180:183], v[212:215], v[22:25]
	v_mfma_f32_16x16x32_bf16 v[14:17], v[188:191], v[212:215], v[14:17]
	v_mfma_f32_16x16x32_bf16 v[6:9], v[180:183], v[220:223], v[6:9]
	v_mfma_f32_16x16x32_bf16 v[2:5], v[188:191], v[220:223], v[2:5]
	s_barrier
	s_setprio 0
	s_add_i32 s61, 0, 0x18000
	s_add_i32 s62, 0, 0x1c000
	v_add_u32_e32 v160, s61, v1
	v_add_u32_e32 v188, s62, v1
	ds_read_b128 v[148:151], v160
	ds_read_b128 v[152:155], v160 offset:1024
	ds_read_b128 v[156:159], v160 offset:2048
	ds_read_b128 v[160:163], v160 offset:3072
	ds_read_b128 v[176:179], v188
	ds_read_b128 v[180:183], v188 offset:1024
	ds_read_b128 v[184:187], v188 offset:2048
	ds_read_b128 v[188:191], v188 offset:3072
	s_add_u32 s28, s28, 0x40000
	s_addc_u32 s29, s29, 0
	s_mov_b32 m0, s34
	ds_read_b128 v[192:195], v172 offset:32768
	ds_read_b128 v[196:199], v172 offset:33792
	ds_read_b128 v[200:203], v172 offset:34816
	ds_read_b128 v[204:207], v172 offset:35840
	ds_read_b128 v[208:211], v172 offset:36864
	ds_read_b128 v[212:215], v172 offset:37888
	ds_read_b128 v[216:219], v172 offset:38912
	ds_read_b128 v[220:223], v172 offset:39936
	global_load_lds_dwordx4 v136, s[28:29]
	s_mov_b32 m0, s35
	s_nop 0
	global_load_lds_dwordx4 v132, s[28:29]
	s_waitcnt vmcnt(8)
	s_waitcnt lgkmcnt(0)
	s_setprio 3
	s_barrier
	s_waitcnt lgkmcnt(0)
	v_mfma_f32_16x16x32_bf16 v[126:129], v[148:151], v[192:195], v[126:129]
	v_mfma_f32_16x16x32_bf16 v[122:125], v[156:159], v[192:195], v[122:125]
	v_mfma_f32_16x16x32_bf16 v[114:117], v[148:151], v[200:203], v[114:117]
	v_mfma_f32_16x16x32_bf16 v[106:109], v[156:159], v[200:203], v[106:109]
	v_mfma_f32_16x16x32_bf16 v[98:101], v[148:151], v[208:211], v[98:101]
	v_mfma_f32_16x16x32_bf16 v[90:93], v[156:159], v[208:211], v[90:93]
	v_mfma_f32_16x16x32_bf16 v[82:85], v[148:151], v[216:219], v[82:85]
	v_mfma_f32_16x16x32_bf16 v[74:77], v[156:159], v[216:219], v[74:77]
	v_mfma_f32_16x16x32_bf16 v[126:129], v[152:155], v[196:199], v[126:129]
	v_mfma_f32_16x16x32_bf16 v[122:125], v[160:163], v[196:199], v[122:125]
	v_mfma_f32_16x16x32_bf16 v[114:117], v[152:155], v[204:207], v[114:117]
	v_mfma_f32_16x16x32_bf16 v[106:109], v[160:163], v[204:207], v[106:109]
	v_mfma_f32_16x16x32_bf16 v[98:101], v[152:155], v[212:215], v[98:101]
	v_mfma_f32_16x16x32_bf16 v[90:93], v[160:163], v[212:215], v[90:93]
	v_mfma_f32_16x16x32_bf16 v[82:85], v[152:155], v[220:223], v[82:85]
	v_mfma_f32_16x16x32_bf16 v[74:77], v[160:163], v[220:223], v[74:77]
	v_mfma_f32_16x16x32_bf16 v[118:121], v[176:179], v[192:195], v[118:121]
	v_mfma_f32_16x16x32_bf16 v[110:113], v[184:187], v[192:195], v[110:113]
	v_mfma_f32_16x16x32_bf16 v[102:105], v[176:179], v[200:203], v[102:105]
	v_mfma_f32_16x16x32_bf16 v[94:97], v[184:187], v[200:203], v[94:97]
	v_mfma_f32_16x16x32_bf16 v[86:89], v[176:179], v[208:211], v[86:89]
	v_mfma_f32_16x16x32_bf16 v[78:81], v[184:187], v[208:211], v[78:81]
	v_mfma_f32_16x16x32_bf16 v[70:73], v[176:179], v[216:219], v[70:73]
	v_mfma_f32_16x16x32_bf16 v[66:69], v[184:187], v[216:219], v[66:69]
	v_mfma_f32_16x16x32_bf16 v[118:121], v[180:183], v[196:199], v[118:121]
	v_mfma_f32_16x16x32_bf16 v[110:113], v[188:191], v[196:199], v[110:113]
	v_mfma_f32_16x16x32_bf16 v[102:105], v[180:183], v[204:207], v[102:105]
	v_mfma_f32_16x16x32_bf16 v[94:97], v[188:191], v[204:207], v[94:97]
	v_mfma_f32_16x16x32_bf16 v[86:89], v[180:183], v[212:215], v[86:89]
	v_mfma_f32_16x16x32_bf16 v[78:81], v[188:191], v[212:215], v[78:81]
	v_mfma_f32_16x16x32_bf16 v[70:73], v[180:183], v[220:223], v[70:73]
	v_mfma_f32_16x16x32_bf16 v[66:69], v[188:191], v[220:223], v[66:69]
	s_barrier
; #define PG8_STAGE_A(b, h, ptr, NX) do { if constexpr (Sched::GATHER) { unsigned gs_[2]; gs_[0] = ((NX) && last_) ? gN[h][0] : gA[h][0]; gs_[1] = ((NX) && last_) ? gN[h][1] : gA[h][1]; PG8_STAGE(PG8_SA(b, h), ptr, gs_); } \
;         else PG8_STAGE(PG8_SA(b, h), (ptr) + ((h) ? hstep : (size_t)0), voffA); } while (0)
; #define PG8_STAGE(bufoff, gbase, voff) do { _Pragma("unroll") for (int _i = 0; _i < 2; ++_i) \
;         __builtin_amdgcn_global_load_lds((const unsigned*)((const char*)(gbase) + (voff)[_i]), (PG8_LAS unsigned*)(lds + (bufoff) + ldsw + _i * 8192), 16, 0, 0); } while (0)
; #define PG8_LDA(dst, b, h) do { _Pragma("unroll") for (int m = 0; m < 4; ++m) _Pragma("unroll") for (int k = 0; k < 2; ++k) dst[m][k] = *(const PG8_LAS bf16x8*)(lds + PG8_SA(b, h) + aoff + m * 2048 + k * 1024); } while (0)
; #define PG8_LDB(dst, b, h) do { _Pragma("unroll") for (int n = 0; n < 2; ++n) _Pragma("unroll") for (int k = 0; k < 2; ++k) dst[n][k] = *(const PG8_LAS bf16x8*)(lds + PG8_SB(b, h) + boff + n * 2048 + k * 1024); } while (0)
; #define PG8_WAIT_V(n) asm volatile("s_waitcnt vmcnt(" #n ")" ::: "memory")
; #define PG8_BAR __builtin_amdgcn_s_barrier()
; template <class Epi, class Sched, bool ALIGN_EPI = false, bool SP2 = false>
; __device__ __forceinline__ void gemm_phase(PG8_LAS unsigned char* lds, const Gemm g, const Sched& S, const Epi& E, const bool skip_epi = false) {
;     ...
;             PG8_LDB(B0, 0, 0); PG8_LDB(B1, 0, 1); PG8_SCHED; PG8_LDA(At, 0, 0); PG8_STAGE_A(1, 1, a1, false);
;             PG8_WAIT_V(8); PG8_WAIT_L(0); PG8_BAR; PG8_MMA(0, 0, At, B0); PG8_MMA(0, 1, At, B1); PG8_BAR; PG8_SCHED;
;             PG8_LDA(At, 0, 1); PG8_STAGE(PG8_SB(0, 0), b2, voffB); PG8_STAGE(PG8_SB(0, 1), b2 + hstep, voffB); PG8_STAGE_A(0, 0, a2, true);
;             PG8_WAIT_V(8); PG8_WAIT_L(0); PG8_BAR; PG8_MMA(1, 0, At, B0); PG8_MMA(1, 1, At, B1); PG8_BAR; PG8_SCHED;
;             PG8_LDB(B0, 1, 0); PG8_LDB(B1, 1, 1); PG8_SCHED; PG8_LDA(At, 1, 0); PG8_STAGE_A(0, 1, a2, true);
;             PG8_WAIT_V(8); PG8_WAIT_L(0); PG8_BAR; PG8_MMA(0, 0, At, B0); PG8_MMA(0, 1, At, B1); PG8_BAR; PG8_SCHED;
;             PG8_LDA(At, 1, 1); PG8_STAGE(PG8_SB(1, 0), b3, voffB); PG8_STAGE(PG8_SB(1, 1), b3 + hstep, voffB); PG8_STAGE_A(1, 0, a3, true);
;             PG8_WAIT_V(8); PG8_WAIT_L(0); PG8_BAR; PG8_MMA(1, 0, At, B0); PG8_MMA(1, 1, At, B1); PG8_BAR; PG8_SCHED;
	s_setprio 0
	s_add_i32 s28, s61, s2
	s_add_i32 m0, s28, 0xffffff80
	ds_read_b128 v[192:195], v172 offset:49152
	ds_read_b128 v[196:199], v172 offset:50176
	ds_read_b128 v[200:203], v172 offset:51200
	ds_read_b128 v[204:207], v172 offset:52224
	ds_read_b128 v[208:211], v172 offset:53248
	ds_read_b128 v[212:215], v172 offset:54272
	ds_read_b128 v[216:219], v172 offset:55296
	ds_read_b128 v[220:223], v172 offset:56320
	global_load_lds_dwordx4 v[164:165], off offset:128
	s_add_i32 m0, s28, 0x1f80
	s_add_u32 s26, s26, 0x40080
	s_addc_u32 s27, s27, 0
	s_add_i32 s28, s62, s2
	global_load_lds_dwordx4 v[224:225], off offset:128
	s_mov_b32 m0, s28
	s_nop 0
	global_load_lds_dwordx4 v134, s[26:27]
	s_add_i32 m0, s28, 0x2000
	s_nop 0
	global_load_lds_dwordx4 v130, s[26:27]
	s_add_i32 m0, s37, 0xffffff80
	s_nop 0
	global_load_lds_dwordx4 v[226:227], off offset:128
	s_add_i32 m0, s38, 0xffffff80
	s_nop 0
	global_load_lds_dwordx4 v[230:231], off offset:128
	s_waitcnt vmcnt(8)
	s_waitcnt lgkmcnt(0)
	s_setprio 3
	s_barrier
	s_waitcnt lgkmcnt(0)
	v_mfma_f32_16x16x32_bf16 v[62:65], v[148:151], v[192:195], v[62:65]
	v_mfma_f32_16x16x32_bf16 v[58:61], v[156:159], v[192:195], v[58:61]
	v_mfma_f32_16x16x32_bf16 v[50:53], v[148:151], v[200:203], v[50:53]
	v_mfma_f32_16x16x32_bf16 v[42:45], v[156:159], v[200:203], v[42:45]
	v_mfma_f32_16x16x32_bf16 v[34:37], v[148:151], v[208:211], v[34:37]
	v_mfma_f32_16x16x32_bf16 v[26:29], v[156:159], v[208:211], v[26:29]
	v_mfma_f32_16x16x32_bf16 v[18:21], v[148:151], v[216:219], v[18:21]
	v_mfma_f32_16x16x32_bf16 v[10:13], v[156:159], v[216:219], v[10:13]
	v_mfma_f32_16x16x32_bf16 v[62:65], v[152:155], v[196:199], v[62:65]
	v_mfma_f32_16x16x32_bf16 v[58:61], v[160:163], v[196:199], v[58:61]
	v_mfma_f32_16x16x32_bf16 v[50:53], v[152:155], v[204:207], v[50:53]
	v_mfma_f32_16x16x32_bf16 v[42:45], v[160:163], v[204:207], v[42:45]
	v_mfma_f32_16x16x32_bf16 v[34:37], v[152:155], v[212:215], v[34:37]
	v_mfma_f32_16x16x32_bf16 v[26:29], v[160:163], v[212:215], v[26:29]
	v_mfma_f32_16x16x32_bf16 v[18:21], v[152:155], v[220:223], v[18:21]
	v_mfma_f32_16x16x32_bf16 v[10:13], v[160:163], v[220:223], v[10:13]
	v_mfma_f32_16x16x32_bf16 v[54:57], v[176:179], v[192:195], v[54:57]
	v_mfma_f32_16x16x32_bf16 v[46:49], v[184:187], v[192:195], v[46:49]
	v_mfma_f32_16x16x32_bf16 v[38:41], v[176:179], v[200:203], v[38:41]
	v_mfma_f32_16x16x32_bf16 v[30:33], v[184:187], v[200:203], v[30:33]
	v_mfma_f32_16x16x32_bf16 v[22:25], v[176:179], v[208:211], v[22:25]
	v_mfma_f32_16x16x32_bf16 v[14:17], v[184:187], v[208:211], v[14:17]
	v_mfma_f32_16x16x32_bf16 v[6:9], v[176:179], v[216:219], v[6:9]
	v_mfma_f32_16x16x32_bf16 v[2:5], v[184:187], v[216:219], v[2:5]
	v_mfma_f32_16x16x32_bf16 v[54:57], v[180:183], v[196:199], v[54:57]
	v_mfma_f32_16x16x32_bf16 v[46:49], v[188:191], v[196:199], v[46:49]
	v_mfma_f32_16x16x32_bf16 v[38:41], v[180:183], v[204:207], v[38:41]
	v_mfma_f32_16x16x32_bf16 v[30:33], v[188:191], v[204:207], v[30:33]
	v_mfma_f32_16x16x32_bf16 v[22:25], v[180:183], v[212:215], v[22:25]
	v_mfma_f32_16x16x32_bf16 v[14:17], v[188:191], v[212:215], v[14:17]
	v_mfma_f32_16x16x32_bf16 v[6:9], v[180:183], v[220:223], v[6:9]
	v_mfma_f32_16x16x32_bf16 v[2:5], v[188:191], v[220:223], v[2:5]
	s_barrier
	s_setprio 0
	s_add_i32 s60, s60, 2
	s_add_u32 s24, s24, 0x100
	s_addc_u32 s25, s25, 0
	s_add_u32 s58, s58, 0x100
	s_addc_u32 s59, s59, 0
	s_cmp_gt_u32 s60, 13
.LBB0_253:
	ds_read_b128 v[148:151], v170
	ds_read_b128 v[152:155], v170 offset:1024
	ds_read_b128 v[156:159], v170 offset:2048
	ds_read_b128 v[160:163], v170 offset:3072
	ds_read_b128 v[176:179], v171
	ds_read_b128 v[180:183], v171 offset:1024
	ds_read_b128 v[184:187], v171 offset:2048
	ds_read_b128 v[188:191], v171 offset:3072
	s_add_u32 s26, s24, 0xfffc0080
	s_addc_u32 s27, s25, -1
	s_cmp_eq_u32 s60, 12
	s_cselect_b32 s29, s17, s27
	s_cselect_b32 s28, s56, s26
	s_cselect_b32 s27, s15, s59
	s_cselect_b32 s26, s57, s58
	s_add_i32 m0, s23, 0xc000
	ds_read_b128 v[192:195], v172
	ds_read_b128 v[196:199], v172 offset:1024
	ds_read_b128 v[200:203], v172 offset:2048
	ds_read_b128 v[204:207], v172 offset:3072
	ds_read_b128 v[208:211], v172 offset:4096
	ds_read_b128 v[212:215], v172 offset:5120
	ds_read_b128 v[216:219], v172 offset:6144
	ds_read_b128 v[220:223], v172 offset:7168
	global_load_lds_dwordx4 v140, s[24:25]
	s_add_i32 m0, s23, 0xe000
	s_nop 0
	global_load_lds_dwordx4 v142, s[24:25]
	s_waitcnt vmcnt(8)
	s_waitcnt lgkmcnt(0)
	s_setprio 3
	s_barrier
	s_waitcnt lgkmcnt(0)
	v_mfma_f32_16x16x32_bf16 v[126:129], v[148:151], v[192:195], v[126:129]
	v_mfma_f32_16x16x32_bf16 v[122:125], v[156:159], v[192:195], v[122:125]
	v_mfma_f32_16x16x32_bf16 v[114:117], v[148:151], v[200:203], v[114:117]
	v_mfma_f32_16x16x32_bf16 v[106:109], v[156:159], v[200:203], v[106:109]
	v_mfma_f32_16x16x32_bf16 v[98:101], v[148:151], v[208:211], v[98:101]
	v_mfma_f32_16x16x32_bf16 v[90:93], v[156:159], v[208:211], v[90:93]
	v_mfma_f32_16x16x32_bf16 v[82:85], v[148:151], v[216:219], v[82:85]
	v_mfma_f32_16x16x32_bf16 v[74:77], v[156:159], v[216:219], v[74:77]
	v_mfma_f32_16x16x32_bf16 v[126:129], v[152:155], v[196:199], v[126:129]
	v_mfma_f32_16x16x32_bf16 v[122:125], v[160:163], v[196:199], v[122:125]
	v_mfma_f32_16x16x32_bf16 v[114:117], v[152:155], v[204:207], v[114:117]
	v_mfma_f32_16x16x32_bf16 v[106:109], v[160:163], v[204:207], v[106:109]
	v_mfma_f32_16x16x32_bf16 v[98:101], v[152:155], v[212:215], v[98:101]
	v_mfma_f32_16x16x32_bf16 v[90:93], v[160:163], v[212:215], v[90:93]
	v_mfma_f32_16x16x32_bf16 v[82:85], v[152:155], v[220:223], v[82:85]
	v_mfma_f32_16x16x32_bf16 v[74:77], v[160:163], v[220:223], v[74:77]
	v_mfma_f32_16x16x32_bf16 v[118:121], v[176:179], v[192:195], v[118:121]
	v_mfma_f32_16x16x32_bf16 v[110:113], v[184:187], v[192:195], v[110:113]
	v_mfma_f32_16x16x32_bf16 v[102:105], v[176:179], v[200:203], v[102:105]
	v_mfma_f32_16x16x32_bf16 v[94:97], v[184:187], v[200:203], v[94:97]
	v_mfma_f32_16x16x32_bf16 v[86:89], v[176:179], v[208:211], v[86:89]
	v_mfma_f32_16x16x32_bf16 v[78:81], v[184:187], v[208:211], v[78:81]
	v_mfma_f32_16x16x32_bf16 v[70:73], v[176:179], v[216:219], v[70:73]
	v_mfma_f32_16x16x32_bf16 v[66:69], v[184:187], v[216:219], v[66:69]
	v_mfma_f32_16x16x32_bf16 v[118:121], v[180:183], v[196:199], v[118:121]
	v_mfma_f32_16x16x32_bf16 v[110:113], v[188:191], v[196:199], v[110:113]
	v_mfma_f32_16x16x32_bf16 v[102:105], v[180:183], v[204:207], v[102:105]
	v_mfma_f32_16x16x32_bf16 v[94:97], v[188:191], v[204:207], v[94:97]
	v_mfma_f32_16x16x32_bf16 v[86:89], v[180:183], v[212:215], v[86:89]
	v_mfma_f32_16x16x32_bf16 v[78:81], v[188:191], v[212:215], v[78:81]
	v_mfma_f32_16x16x32_bf16 v[70:73], v[180:183], v[220:223], v[70:73]
	v_mfma_f32_16x16x32_bf16 v[66:69], v[188:191], v[220:223], v[66:69]
	s_barrier
; #define PG8_STAGE_A(b, h, ptr, NX) do { if constexpr (Sched::GATHER) { unsigned gs_[2]; gs_[0] = ((NX) && last_) ? gN[h][0] : gA[h][0]; gs_[1] = ((NX) && last_) ? gN[h][1] : gA[h][1]; PG8_STAGE(PG8_SA(b, h), ptr, gs_); } \
;         else PG8_STAGE(PG8_SA(b, h), (ptr) + ((h) ? hstep : (size_t)0), voffA); } while (0)
; #define PG8_STAGE(bufoff, gbase, voff) do { _Pragma("unroll") for (int _i = 0; _i < 2; ++_i) \
;         __builtin_amdgcn_global_load_lds((const unsigned*)((const char*)(gbase) + (voff)[_i]), (PG8_LAS unsigned*)(lds + (bufoff) + ldsw + _i * 8192), 16, 0, 0); } while (0)
; #define PG8_LDA(dst, b, h) do { _Pragma("unroll") for (int m = 0; m < 4; ++m) _Pragma("unroll") for (int k = 0; k < 2; ++k) dst[m][k] = *(const PG8_LAS bf16x8*)(lds + PG8_SA(b, h) + aoff + m * 2048 + k * 1024); } while (0)
; #define PG8_LDB(dst, b, h) do { _Pragma("unroll") for (int n = 0; n < 2; ++n) _Pragma("unroll") for (int k = 0; k < 2; ++k) dst[n][k] = *(const PG8_LAS bf16x8*)(lds + PG8_SB(b, h) + boff + n * 2048 + k * 1024); } while (0)
; #define PG8_MMA(ai, bj, At, Bt) do { __builtin_amdgcn_s_setprio(1); _Pragma("unroll") for (int m = 0; m < 4; ++m) _Pragma("unroll") for (int n = 0; n < 2; ++n) _Pragma("unroll") for (int k = 0; k < 2; ++k) \
;         acc[ai][bj][m][n] = __builtin_amdgcn_mfma_f32_16x16x32_bf16(Bt[n][k], At[m][k], acc[ai][bj][m][n], 0, 0, 0); __builtin_amdgcn_s_setprio(0); } while (0)
; #define PG8_WAIT_V(n) asm volatile("s_waitcnt vmcnt(" #n ")" ::: "memory")
; #define PG8_WAIT_L(n) asm volatile("s_waitcnt lgkmcnt(" #n ")" ::: "memory")
; #define PG8_BAR __builtin_amdgcn_s_barrier()
; #define PG8_SCHED __builtin_amdgcn_sched_barrier(0)
; template <class Epi, class Sched, bool ALIGN_EPI = false, bool SP2 = false>
; __device__ __forceinline__ void gemm_phase(PG8_LAS unsigned char* lds, const Gemm g, const Sched& S, const Epi& E, const bool skip_epi = false) {
;     ...
;             PG8_LDA(At, 0, 1); PG8_STAGE(PG8_SB(0, 0), b2, voffB); PG8_STAGE(PG8_SB(0, 1), b2 + hstep, voffB); PG8_STAGE_A(0, 0, a2, true);
;             PG8_WAIT_V(8); PG8_WAIT_L(0); PG8_BAR; PG8_MMA(1, 0, At, B0); PG8_MMA(1, 1, At, B1); PG8_BAR; PG8_SCHED;
;             PG8_LDB(B0, 1, 0); PG8_LDB(B1, 1, 1); PG8_SCHED; PG8_LDA(At, 1, 0); PG8_STAGE_A(0, 1, a2, true);
;             PG8_WAIT_V(8); PG8_WAIT_L(0); PG8_BAR; PG8_MMA(0, 0, At, B0); PG8_MMA(0, 1, At, B1); PG8_BAR; PG8_SCHED;
	s_setprio 0
	s_add_i32 s61, s46, s2
	v_lshl_add_u64 v[164:165], s[26:27], 0, v[134:135]
	s_mov_b32 m0, s61
	ds_read_b128 v[192:195], v172 offset:16384
	ds_read_b128 v[196:199], v172 offset:17408
	ds_read_b128 v[200:203], v172 offset:18432
	ds_read_b128 v[204:207], v172 offset:19456
	ds_read_b128 v[208:211], v172 offset:20480
	ds_read_b128 v[212:215], v172 offset:21504
	ds_read_b128 v[216:219], v172 offset:22528
	ds_read_b128 v[220:223], v172 offset:23552
	global_load_lds_dwordx4 v[164:165], off
	s_add_i32 m0, s61, 0x2000
	s_add_u32 s62, s26, 0x40000
	v_lshl_add_u64 v[224:225], s[26:27], 0, v[130:131]
	s_addc_u32 s63, s27, 0
	s_add_i32 s61, s47, s2
	global_load_lds_dwordx4 v[224:225], off
	s_mov_b32 m0, s61
	v_lshl_add_u64 v[230:231], s[28:29], 0, v[132:133]
	global_load_lds_dwordx4 v134, s[62:63]
	s_add_i32 m0, s61, 0x2000
	s_nop 0
	global_load_lds_dwordx4 v130, s[62:63]
	v_lshl_add_u64 v[226:227], s[28:29], 0, v[136:137]
	s_mov_b32 m0, s23
	s_nop 0
	global_load_lds_dwordx4 v[226:227], off
	s_mov_b32 m0, s31
	s_nop 0
	global_load_lds_dwordx4 v[230:231], off
	s_waitcnt vmcnt(8)
	s_waitcnt lgkmcnt(0)
	s_setprio 3
	s_barrier
	s_waitcnt lgkmcnt(0)
	v_mfma_f32_16x16x32_bf16 v[62:65], v[148:151], v[192:195], v[62:65]
	v_mfma_f32_16x16x32_bf16 v[58:61], v[156:159], v[192:195], v[58:61]
	v_mfma_f32_16x16x32_bf16 v[50:53], v[148:151], v[200:203], v[50:53]
	v_mfma_f32_16x16x32_bf16 v[42:45], v[156:159], v[200:203], v[42:45]
	v_mfma_f32_16x16x32_bf16 v[34:37], v[148:151], v[208:211], v[34:37]
	v_mfma_f32_16x16x32_bf16 v[26:29], v[156:159], v[208:211], v[26:29]
	v_mfma_f32_16x16x32_bf16 v[18:21], v[148:151], v[216:219], v[18:21]
	v_mfma_f32_16x16x32_bf16 v[10:13], v[156:159], v[216:219], v[10:13]
	v_mfma_f32_16x16x32_bf16 v[62:65], v[152:155], v[196:199], v[62:65]
	v_mfma_f32_16x16x32_bf16 v[58:61], v[160:163], v[196:199], v[58:61]
	v_mfma_f32_16x16x32_bf16 v[50:53], v[152:155], v[204:207], v[50:53]
	v_mfma_f32_16x16x32_bf16 v[42:45], v[160:163], v[204:207], v[42:45]
	v_mfma_f32_16x16x32_bf16 v[34:37], v[152:155], v[212:215], v[34:37]
	v_mfma_f32_16x16x32_bf16 v[26:29], v[160:163], v[212:215], v[26:29]
	v_mfma_f32_16x16x32_bf16 v[18:21], v[152:155], v[220:223], v[18:21]
	v_mfma_f32_16x16x32_bf16 v[10:13], v[160:163], v[220:223], v[10:13]
	v_mfma_f32_16x16x32_bf16 v[54:57], v[176:179], v[192:195], v[54:57]
	v_mfma_f32_16x16x32_bf16 v[46:49], v[184:187], v[192:195], v[46:49]
	v_mfma_f32_16x16x32_bf16 v[38:41], v[176:179], v[200:203], v[38:41]
	v_mfma_f32_16x16x32_bf16 v[30:33], v[184:187], v[200:203], v[30:33]
	v_mfma_f32_16x16x32_bf16 v[22:25], v[176:179], v[208:211], v[22:25]
	v_mfma_f32_16x16x32_bf16 v[14:17], v[184:187], v[208:211], v[14:17]
	v_mfma_f32_16x16x32_bf16 v[6:9], v[176:179], v[216:219], v[6:9]
	v_mfma_f32_16x16x32_bf16 v[2:5], v[184:187], v[216:219], v[2:5]
	v_mfma_f32_16x16x32_bf16 v[54:57], v[180:183], v[196:199], v[54:57]
	v_mfma_f32_16x16x32_bf16 v[46:49], v[188:191], v[196:199], v[46:49]
	v_mfma_f32_16x16x32_bf16 v[38:41], v[180:183], v[204:207], v[38:41]
	v_mfma_f32_16x16x32_bf16 v[30:33], v[188:191], v[204:207], v[30:33]
	v_mfma_f32_16x16x32_bf16 v[22:25], v[180:183], v[212:215], v[22:25]
	v_mfma_f32_16x16x32_bf16 v[14:17], v[188:191], v[212:215], v[14:17]
	v_mfma_f32_16x16x32_bf16 v[6:9], v[180:183], v[220:223], v[6:9]
	v_mfma_f32_16x16x32_bf16 v[2:5], v[188:191], v[220:223], v[2:5]
	s_barrier
	s_setprio 0
	s_add_i32 s61, 0, 0x18000
	s_add_i32 s62, 0, 0x1c000
	v_add_u32_e32 v160, s61, v1
	v_add_u32_e32 v188, s62, v1
	ds_read_b128 v[148:151], v160
	ds_read_b128 v[152:155], v160 offset:1024
	ds_read_b128 v[156:159], v160 offset:2048
	ds_read_b128 v[160:163], v160 offset:3072
	ds_read_b128 v[176:179], v188
	ds_read_b128 v[180:183], v188 offset:1024
	ds_read_b128 v[184:187], v188 offset:2048
	ds_read_b128 v[188:191], v188 offset:3072
	s_add_u32 s28, s28, 0x40000
	s_addc_u32 s29, s29, 0
	s_mov_b32 m0, s34
	ds_read_b128 v[192:195], v172 offset:32768
	ds_read_b128 v[196:199], v172 offset:33792
	ds_read_b128 v[200:203], v172 offset:34816
	ds_read_b128 v[204:207], v172 offset:35840
	ds_read_b128 v[208:211], v172 offset:36864
	ds_read_b128 v[212:215], v172 offset:37888
	ds_read_b128 v[216:219], v172 offset:38912
	ds_read_b128 v[220:223], v172 offset:39936
	global_load_lds_dwordx4 v136, s[28:29]
	s_mov_b32 m0, s35
	s_nop 0
	global_load_lds_dwordx4 v132, s[28:29]
	s_waitcnt vmcnt(8)
	s_waitcnt lgkmcnt(0)
	s_setprio 3
	s_barrier
; #define PG8_STAGE_A(b, h, ptr, NX) do { if constexpr (Sched::GATHER) { unsigned gs_[2]; gs_[0] = ((NX) && last_) ? gN[h][0] : gA[h][0]; gs_[1] = ((NX) && last_) ? gN[h][1] : gA[h][1]; PG8_STAGE(PG8_SA(b, h), ptr, gs_); } \
;         else PG8_STAGE(PG8_SA(b, h), (ptr) + ((h) ? hstep : (size_t)0), voffA); } while (0)
; #define PG8_STAGE(bufoff, gbase, voff) do { _Pragma("unroll") for (int _i = 0; _i < 2; ++_i) \
;         __builtin_amdgcn_global_load_lds((const unsigned*)((const char*)(gbase) + (voff)[_i]), (PG8_LAS unsigned*)(lds + (bufoff) + ldsw + _i * 8192), 16, 0, 0); } while (0)
; #define PG8_LDA(dst, b, h) do { _Pragma("unroll") for (int m = 0; m < 4; ++m) _Pragma("unroll") for (int k = 0; k < 2; ++k) dst[m][k] = *(const PG8_LAS bf16x8*)(lds + PG8_SA(b, h) + aoff + m * 2048 + k * 1024); } while (0)
; #define PG8_MMA(ai, bj, At, Bt) do { __builtin_amdgcn_s_setprio(1); _Pragma("unroll") for (int m = 0; m < 4; ++m) _Pragma("unroll") for (int n = 0; n < 2; ++n) _Pragma("unroll") for (int k = 0; k < 2; ++k) \
;         acc[ai][bj][m][n] = __builtin_amdgcn_mfma_f32_16x16x32_bf16(Bt[n][k], At[m][k], acc[ai][bj][m][n], 0, 0, 0); __builtin_amdgcn_s_setprio(0); } while (0)
; #define PG8_WAIT_V(n) asm volatile("s_waitcnt vmcnt(" #n ")" ::: "memory")
; #define PG8_BAR __builtin_amdgcn_s_barrier()
; __device__ __forceinline__ void rstd8(const float* SS, int rowb, int lane, float (&rs)[2][4]) {
;     f32x4 p[2][4];
; #pragma unroll
;     for (int ai = 0; ai < 2; ++ai)
; #pragma unroll
;         for (int m = 0; m < 4; ++m) p[ai][m] = *(const f32x4*)(SS + (size_t)(rowb + HALF * ai + 16 * m + (lane >> 2)) * 16 + 4 * (lane & 3));
;     asm volatile("" : "+v"(p[0][0]), "+v"(p[0][1]), "+v"(p[0][2]), "+v"(p[0][3]), "+v"(p[1][0]), "+v"(p[1][1]), "+v"(p[1][2]), "+v"(p[1][3]));
; template <class Epi, class Sched, bool ALIGN_EPI = false, bool SP2 = false>
; __device__ __forceinline__ void gemm_phase(PG8_LAS unsigned char* lds, const Gemm g, const Sched& S, const Epi& E, const bool skip_epi = false) {
;     ...
;             PG8_WAIT_V(8); PG8_WAIT_L(0); PG8_BAR; PG8_MMA(0, 0, At, B0); PG8_MMA(0, 1, At, B1); PG8_BAR; PG8_SCHED;
;             PG8_LDA(At, 1, 1); PG8_STAGE(PG8_SB(1, 0), b3, voffB); PG8_STAGE(PG8_SB(1, 1), b3 + hstep, voffB); PG8_STAGE_A(1, 0, a3, true);
;             PG8_WAIT_V(8); PG8_WAIT_L(0); PG8_BAR; PG8_MMA(1, 0, At, B0); PG8_MMA(1, 1, At, B1); PG8_BAR; PG8_SCHED;
	s_waitcnt lgkmcnt(0)
	v_mfma_f32_16x16x32_bf16 v[126:129], v[148:151], v[192:195], v[126:129]
	v_mfma_f32_16x16x32_bf16 v[122:125], v[156:159], v[192:195], v[122:125]
	v_mfma_f32_16x16x32_bf16 v[114:117], v[148:151], v[200:203], v[114:117]
	v_mfma_f32_16x16x32_bf16 v[106:109], v[156:159], v[200:203], v[106:109]
	v_mfma_f32_16x16x32_bf16 v[98:101], v[148:151], v[208:211], v[98:101]
	v_mfma_f32_16x16x32_bf16 v[90:93], v[156:159], v[208:211], v[90:93]
	v_mfma_f32_16x16x32_bf16 v[82:85], v[148:151], v[216:219], v[82:85]
	v_mfma_f32_16x16x32_bf16 v[74:77], v[156:159], v[216:219], v[74:77]
	v_mfma_f32_16x16x32_bf16 v[126:129], v[152:155], v[196:199], v[126:129]
	v_mfma_f32_16x16x32_bf16 v[122:125], v[160:163], v[196:199], v[122:125]
	v_mfma_f32_16x16x32_bf16 v[114:117], v[152:155], v[204:207], v[114:117]
	v_mfma_f32_16x16x32_bf16 v[106:109], v[160:163], v[204:207], v[106:109]
	v_mfma_f32_16x16x32_bf16 v[98:101], v[152:155], v[212:215], v[98:101]
	v_mfma_f32_16x16x32_bf16 v[90:93], v[160:163], v[212:215], v[90:93]
	v_mfma_f32_16x16x32_bf16 v[82:85], v[152:155], v[220:223], v[82:85]
	v_mfma_f32_16x16x32_bf16 v[74:77], v[160:163], v[220:223], v[74:77]
	v_mfma_f32_16x16x32_bf16 v[118:121], v[176:179], v[192:195], v[118:121]
	v_mfma_f32_16x16x32_bf16 v[110:113], v[184:187], v[192:195], v[110:113]
	v_mfma_f32_16x16x32_bf16 v[102:105], v[176:179], v[200:203], v[102:105]
	v_mfma_f32_16x16x32_bf16 v[94:97], v[184:187], v[200:203], v[94:97]
	v_mfma_f32_16x16x32_bf16 v[86:89], v[176:179], v[208:211], v[86:89]
	v_mfma_f32_16x16x32_bf16 v[78:81], v[184:187], v[208:211], v[78:81]
	v_mfma_f32_16x16x32_bf16 v[70:73], v[176:179], v[216:219], v[70:73]
	v_mfma_f32_16x16x32_bf16 v[66:69], v[184:187], v[216:219], v[66:69]
	v_mfma_f32_16x16x32_bf16 v[118:121], v[180:183], v[196:199], v[118:121]
	v_mfma_f32_16x16x32_bf16 v[110:113], v[188:191], v[196:199], v[110:113]
	v_mfma_f32_16x16x32_bf16 v[102:105], v[180:183], v[204:207], v[102:105]
	v_mfma_f32_16x16x32_bf16 v[94:97], v[188:191], v[204:207], v[94:97]
	v_mfma_f32_16x16x32_bf16 v[86:89], v[180:183], v[212:215], v[86:89]
	v_mfma_f32_16x16x32_bf16 v[78:81], v[188:191], v[212:215], v[78:81]
	v_mfma_f32_16x16x32_bf16 v[70:73], v[180:183], v[220:223], v[70:73]
	v_mfma_f32_16x16x32_bf16 v[66:69], v[188:191], v[220:223], v[66:69]
	s_barrier
	s_setprio 0
	s_add_i32 s28, s61, s2
	s_add_i32 m0, s28, 0xffffff80
	ds_read_b128 v[192:195], v172 offset:49152
	ds_read_b128 v[196:199], v172 offset:50176
	ds_read_b128 v[200:203], v172 offset:51200
	ds_read_b128 v[204:207], v172 offset:52224
	ds_read_b128 v[208:211], v172 offset:53248
	ds_read_b128 v[212:215], v172 offset:54272
	ds_read_b128 v[216:219], v172 offset:55296
	ds_read_b128 v[220:223], v172 offset:56320
	global_load_lds_dwordx4 v[164:165], off offset:128
	s_add_i32 m0, s28, 0x1f80
	s_add_u32 s26, s26, 0x40080
	s_addc_u32 s27, s27, 0
	s_add_i32 s28, s62, s2
	global_load_lds_dwordx4 v[224:225], off offset:128
	s_mov_b32 m0, s28
	s_nop 0
	global_load_lds_dwordx4 v134, s[26:27]
	s_add_i32 m0, s28, 0x2000
	s_nop 0
	global_load_lds_dwordx4 v130, s[26:27]
	s_add_i32 m0, s37, 0xffffff80
	s_nop 0
	global_load_lds_dwordx4 v[226:227], off offset:128
	s_add_i32 m0, s38, 0xffffff80
	s_nop 0
	global_load_lds_dwordx4 v[230:231], off offset:128
	s_waitcnt vmcnt(8)
	s_waitcnt lgkmcnt(0)
	s_setprio 3
	s_barrier
	s_waitcnt lgkmcnt(0)
	v_mfma_f32_16x16x32_bf16 v[62:65], v[148:151], v[192:195], v[62:65]
	v_mfma_f32_16x16x32_bf16 v[58:61], v[156:159], v[192:195], v[58:61]
	v_mfma_f32_16x16x32_bf16 v[50:53], v[148:151], v[200:203], v[50:53]
	v_mfma_f32_16x16x32_bf16 v[42:45], v[156:159], v[200:203], v[42:45]
	v_mfma_f32_16x16x32_bf16 v[34:37], v[148:151], v[208:211], v[34:37]
	v_mfma_f32_16x16x32_bf16 v[26:29], v[156:159], v[208:211], v[26:29]
	v_mfma_f32_16x16x32_bf16 v[18:21], v[148:151], v[216:219], v[18:21]
	v_mfma_f32_16x16x32_bf16 v[10:13], v[156:159], v[216:219], v[10:13]
	v_mfma_f32_16x16x32_bf16 v[62:65], v[152:155], v[196:199], v[62:65]
	v_mfma_f32_16x16x32_bf16 v[58:61], v[160:163], v[196:199], v[58:61]
	v_mfma_f32_16x16x32_bf16 v[50:53], v[152:155], v[204:207], v[50:53]
	v_mfma_f32_16x16x32_bf16 v[42:45], v[160:163], v[204:207], v[42:45]
	v_mfma_f32_16x16x32_bf16 v[34:37], v[152:155], v[212:215], v[34:37]
	v_mfma_f32_16x16x32_bf16 v[26:29], v[160:163], v[212:215], v[26:29]
	v_mfma_f32_16x16x32_bf16 v[18:21], v[152:155], v[220:223], v[18:21]
	v_mfma_f32_16x16x32_bf16 v[10:13], v[160:163], v[220:223], v[10:13]
	v_mfma_f32_16x16x32_bf16 v[54:57], v[176:179], v[192:195], v[54:57]
	v_mfma_f32_16x16x32_bf16 v[46:49], v[184:187], v[192:195], v[46:49]
	v_mfma_f32_16x16x32_bf16 v[38:41], v[176:179], v[200:203], v[38:41]
	v_mfma_f32_16x16x32_bf16 v[30:33], v[184:187], v[200:203], v[30:33]
	v_mfma_f32_16x16x32_bf16 v[22:25], v[176:179], v[208:211], v[22:25]
	v_mfma_f32_16x16x32_bf16 v[14:17], v[184:187], v[208:211], v[14:17]
	v_mfma_f32_16x16x32_bf16 v[6:9], v[176:179], v[216:219], v[6:9]
	v_mfma_f32_16x16x32_bf16 v[2:5], v[184:187], v[216:219], v[2:5]
	v_mfma_f32_16x16x32_bf16 v[54:57], v[180:183], v[196:199], v[54:57]
	v_mfma_f32_16x16x32_bf16 v[46:49], v[188:191], v[196:199], v[46:49]
	v_mfma_f32_16x16x32_bf16 v[38:41], v[180:183], v[204:207], v[38:41]
	v_mfma_f32_16x16x32_bf16 v[30:33], v[188:191], v[204:207], v[30:33]
	v_mfma_f32_16x16x32_bf16 v[22:25], v[180:183], v[212:215], v[22:25]
	v_mfma_f32_16x16x32_bf16 v[14:17], v[188:191], v[212:215], v[14:17]
	v_mfma_f32_16x16x32_bf16 v[6:9], v[180:183], v[220:223], v[6:9]
	v_mfma_f32_16x16x32_bf16 v[2:5], v[188:191], v[220:223], v[2:5]
	s_barrier
	s_setprio 0
	s_add_i32 s60, s60, 2
	s_add_u32 s24, s24, 0x100
	s_addc_u32 s25, s25, 0
	s_add_u32 s58, s58, 0x100
	s_addc_u32 s59, s59, 0
	s_cmp_gt_u32 s60, 13
	s_cbranch_scc0 .LBB0_253
	v_lshl_add_u32 v164, s22, 8, v167
	v_ashrrev_i32_e32 v165, 31, v164
	v_lshlrev_b64 v[148:149], 6, v[164:165]
	v_lshl_add_u64 v[148:149], v[138:139], 0, v[148:149]
	v_add_co_u32_e32 v150, vcc, 0x2000, v148
	v_addc_co_u32_e32 v151, vcc, 0, v149, vcc
	global_load_dwordx4 v[176:179], v[148:149], off
	global_load_dwordx4 v[180:183], v[148:149], off offset:1024
	global_load_dwordx4 v[184:187], v[148:149], off offset:2048
	global_load_dwordx4 v[188:191], v[148:149], off offset:3072
	global_load_dwordx4 v[192:195], v[150:151], off
	global_load_dwordx4 v[196:199], v[150:151], off offset:1024
	global_load_dwordx4 v[200:203], v[150:151], off offset:2048
	global_load_dwordx4 v[204:207], v[150:151], off offset:3072
	s_and_b64 vcc, exec, s[12:13]
	s_cbranch_vccz .LBB0_256
	s_barrier

; #define PG8_GIDX(G_, PM_) do { if constexpr (Sched::GATHER) { _Pragma("unroll") for (int h_ = 0; h_ < 2; ++h_) _Pragma("unroll") for (int i_ = 0; i_ < 2; ++i_) { int R_, C_; stage_rc(tid * 16 + i_ * 8192, R_, C_); \
;         const int src_ = S.rowsrc[(PM_) * BM + h_ * HALF + R_]; G_[h_][i_] = (unsigned)(src_ * K + C_) * 2u; } } } while (0)
; #define PG8_STAGE_A(b, h, ptr, NX) do { if constexpr (Sched::GATHER) { unsigned gs_[2]; gs_[0] = ((NX) && last_) ? gN[h][0] : gA[h][0]; gs_[1] = ((NX) && last_) ? gN[h][1] : gA[h][1]; PG8_STAGE(PG8_SA(b, h), ptr, gs_); } \
;         else PG8_STAGE(PG8_SA(b, h), (ptr) + ((h) ? hstep : (size_t)0), voffA); } while (0)
; #define PG8_LDA(dst, b, h) do { _Pragma("unroll") for (int m = 0; m < 4; ++m) _Pragma("unroll") for (int k = 0; k < 2; ++k) dst[m][k] = *(const PG8_LAS bf16x8*)(lds + PG8_SA(b, h) + aoff + m * 2048 + k * 1024); } while (0)
; template <class Epi, class Sched, bool ALIGN_EPI = false, bool SP2 = false>
; __device__ __forceinline__ void gemm_phase(PG8_LAS unsigned char* lds, const Gemm g, const Sched& S, const Epi& E, const bool skip_epi = false) {
;     ...
;         const bool has_next = S.next(ui + 1, nxt);
;         if (has_next) PG8_GIDX(gN, nxt.pm);
;         const char* nA = has_next ? (const char*)g.A + (size_t)nxt.pm * pmstepA + nxt.ko : cA; const char* nB = has_next ? (const char*)g.Bt + (size_t)nxt.pn * tstep + nxt.ko : cB;
;         for (int t = 0; t < nt; t += 2) {
;             const bool last = (t == nt - 2); last_ = last && has_next;
;             const char* a1 = cA + (size_t)(t + 1) * kstep;
;             const char* a2 = last ? nA : cA + (size_t)(t + 2) * kstep; const char* b2 = last ? nB : cB + (size_t)(t + 2) * kstep;
;             const char* a3 = a2 + kstep; const char* b3 = b2 + kstep;
;             if (last && has_next) S.a_ready(nxt);
;             if constexpr (SP2) {
;             PG8_LDB(B0, 0, 0); PG8_LDB(B1, 0, 1); PG8_SCHED; PG8_LDA(At, 0, 0); PG8_STAGE_A(1, 1, a1, false);
;             PG8_WAIT_V(8); PG8_WAIT_L(0); PG8_BAR; PG8_MMA(0, 0, At, B0); PG8_MMA(0, 1, At, B1); PG8_BAR; PG8_SCHED;
;             PG8_LDA(At, 0, 1); PG8_STAGE(PG8_SB(0, 0), b2, voffB); PG8_STAGE(PG8_SB(0, 1), b2 + hstep, voffB); PG8_STAGE_A(0, 0, a2, true);
;             PG8_WAIT_V(8); PG8_WAIT_L(0); PG8_BAR; PG8_MMA(1, 0, At, B0); PG8_MMA(1, 1, At, B1); PG8_BAR; PG8_SCHED;
.LBB0_633:
	s_ashr_i32 s19, s18, 31
	s_lshl_b64 s[20:21], s[18:19], 19
	s_add_u32 s20, s46, s20
	s_addc_u32 s21, s47, s21
	s_and_b64 s[22:23], s[6:7], exec
	s_cselect_b32 s19, s21, s27
	s_cselect_b32 s25, s20, s26
	s_ashr_i32 s17, s16, 31
	s_lshl_b64 s[22:23], s[16:17], 19
	v_readlane_b32 s17, v254, 40
	s_add_u32 s22, s17, s22
	v_readlane_b32 s17, v254, 41
	s_addc_u32 s23, s17, s23
	s_and_b64 s[30:31], s[6:7], exec
	s_cselect_b32 s17, s23, s29
	s_cselect_b32 s60, s22, s28
	s_add_u32 s26, s26, 0x40080
	s_addc_u32 s27, s27, 0
	s_add_u32 s61, s28, 0x100
	s_addc_u32 s62, s29, 0
	s_mov_b32 s63, -2
	s_waitcnt lgkmcnt(0)
	ds_read_b128 v[98:101], v234
	ds_read_b128 v[110:113], v234 offset:1024
	ds_read_b128 v[122:125], v234 offset:2048
	ds_read_b128 v[126:129], v234 offset:3072
	ds_read_b128 v[138:141], v235
	ds_read_b128 v[142:145], v235 offset:1024
	ds_read_b128 v[146:149], v235 offset:2048
	ds_read_b128 v[150:153], v235 offset:3072
	s_add_u32 s28, s26, 0xfffc0080
	s_addc_u32 s29, s27, -1
	s_cmp_eq_u32 s63, 12
	s_cselect_b32 s31, s19, s29
	s_cselect_b32 s30, s25, s28
	s_cselect_b32 s29, s17, s62
	s_cselect_b32 s28, s60, s61
	s_add_i32 m0, s3, 0xc000
	ds_read_b128 v[154:157], v236
	ds_read_b128 v[166:169], v236 offset:1024
	ds_read_b128 v[170:173], v236 offset:2048
	ds_read_b128 v[174:177], v236 offset:3072
	ds_read_b128 v[178:181], v236 offset:4096
	ds_read_b128 v[182:185], v236 offset:5120
	ds_read_b128 v[186:189], v236 offset:6144
	ds_read_b128 v[206:209], v236 offset:7168
	global_load_lds_dwordx4 v198, s[26:27]
	s_add_i32 m0, s3, 0xe000
	s_nop 0
	global_load_lds_dwordx4 v200, s[26:27]
	s_waitcnt vmcnt(8)
	s_waitcnt lgkmcnt(0)
	s_setprio 3
	s_barrier
	s_waitcnt lgkmcnt(0)
	v_mfma_f32_16x16x32_bf16 v[162:165], v[98:101], v[154:157], 0
	v_mfma_f32_16x16x32_bf16 v[158:161], v[122:125], v[154:157], 0
	v_mfma_f32_16x16x32_bf16 v[118:121], v[98:101], v[170:173], 0
	v_mfma_f32_16x16x32_bf16 v[114:117], v[122:125], v[170:173], 0
	v_mfma_f32_16x16x32_bf16 v[94:97], v[98:101], v[178:181], 0
	v_mfma_f32_16x16x32_bf16 v[90:93], v[122:125], v[178:181], 0
	v_mfma_f32_16x16x32_bf16 v[78:81], v[98:101], v[186:189], 0
	v_mfma_f32_16x16x32_bf16 v[74:77], v[122:125], v[186:189], 0
	v_mfma_f32_16x16x32_bf16 v[162:165], v[110:113], v[166:169], v[162:165]
	v_mfma_f32_16x16x32_bf16 v[158:161], v[126:129], v[166:169], v[158:161]
	v_mfma_f32_16x16x32_bf16 v[118:121], v[110:113], v[174:177], v[118:121]
	v_mfma_f32_16x16x32_bf16 v[114:117], v[126:129], v[174:177], v[114:117]
	v_mfma_f32_16x16x32_bf16 v[94:97], v[110:113], v[182:185], v[94:97]
	v_mfma_f32_16x16x32_bf16 v[90:93], v[126:129], v[182:185], v[90:93]
	v_mfma_f32_16x16x32_bf16 v[78:81], v[110:113], v[206:209], v[78:81]
	v_mfma_f32_16x16x32_bf16 v[74:77], v[126:129], v[206:209], v[74:77]
	v_mfma_f32_16x16x32_bf16 v[134:137], v[138:141], v[154:157], 0
	v_mfma_f32_16x16x32_bf16 v[130:133], v[146:149], v[154:157], 0
	v_mfma_f32_16x16x32_bf16 v[106:109], v[138:141], v[170:173], 0
	v_mfma_f32_16x16x32_bf16 v[102:105], v[146:149], v[170:173], 0
	v_mfma_f32_16x16x32_bf16 v[86:89], v[138:141], v[178:181], 0
	v_mfma_f32_16x16x32_bf16 v[82:85], v[146:149], v[178:181], 0
	v_mfma_f32_16x16x32_bf16 v[70:73], v[138:141], v[186:189], 0
	v_mfma_f32_16x16x32_bf16 v[66:69], v[146:149], v[186:189], 0
	v_mfma_f32_16x16x32_bf16 v[134:137], v[142:145], v[166:169], v[134:137]
	v_mfma_f32_16x16x32_bf16 v[130:133], v[150:153], v[166:169], v[130:133]
	v_mfma_f32_16x16x32_bf16 v[106:109], v[142:145], v[174:177], v[106:109]
	v_mfma_f32_16x16x32_bf16 v[102:105], v[150:153], v[174:177], v[102:105]
	v_mfma_f32_16x16x32_bf16 v[86:89], v[142:145], v[182:185], v[86:89]
	v_mfma_f32_16x16x32_bf16 v[82:85], v[150:153], v[182:185], v[82:85]
	v_mfma_f32_16x16x32_bf16 v[70:73], v[142:145], v[206:209], v[70:73]
	v_mfma_f32_16x16x32_bf16 v[66:69], v[150:153], v[206:209], v[66:69]
	s_barrier
	s_setprio 0
	s_add_i32 s64, s57, s2
	v_lshl_add_u64 v[210:211], s[28:29], 0, v[192:193]
	s_mov_b32 m0, s64
	ds_read_b128 v[154:157], v236 offset:16384
	ds_read_b128 v[166:169], v236 offset:17408
	ds_read_b128 v[170:173], v236 offset:18432
	ds_read_b128 v[174:177], v236 offset:19456
	ds_read_b128 v[178:181], v236 offset:20480
	ds_read_b128 v[182:185], v236 offset:21504
	ds_read_b128 v[186:189], v236 offset:22528
	ds_read_b128 v[206:209], v236 offset:23552
	global_load_lds_dwordx4 v[210:211], off
	s_add_i32 m0, s64, 0x2000
	s_add_u32 s64, s28, 0x40000
	v_lshl_add_u64 v[212:213], s[28:29], 0, v[196:197]
	s_addc_u32 s65, s29, 0
	s_add_i32 s66, s58, s2
	global_load_lds_dwordx4 v[212:213], off
	s_mov_b32 m0, s66
	v_lshl_add_u64 v[216:217], s[30:31], 0, v[194:195]
	global_load_lds_dwordx4 v192, s[64:65]
	s_add_i32 m0, s66, 0x2000
	s_nop 0
	global_load_lds_dwordx4 v196, s[64:65]
	v_lshl_add_u64 v[214:215], s[30:31], 0, v[190:191]
	s_mov_b32 m0, s3
	s_nop 0
	global_load_lds_dwordx4 v[214:215], off
	s_mov_b32 m0, s34
	s_nop 0
	global_load_lds_dwordx4 v[216:217], off
	s_waitcnt vmcnt(8)
	s_waitcnt lgkmcnt(0)
	s_setprio 3
	s_barrier
; #define PG8_STAGE_A(b, h, ptr, NX) do { if constexpr (Sched::GATHER) { unsigned gs_[2]; gs_[0] = ((NX) && last_) ? gN[h][0] : gA[h][0]; gs_[1] = ((NX) && last_) ? gN[h][1] : gA[h][1]; PG8_STAGE(PG8_SA(b, h), ptr, gs_); } \
;         else PG8_STAGE(PG8_SA(b, h), (ptr) + ((h) ? hstep : (size_t)0), voffA); } while (0)
; #define PG8_STAGE(bufoff, gbase, voff) do { _Pragma("unroll") for (int _i = 0; _i < 2; ++_i) \
;         __builtin_amdgcn_global_load_lds((const unsigned*)((const char*)(gbase) + (voff)[_i]), (PG8_LAS unsigned*)(lds + (bufoff) + ldsw + _i * 8192), 16, 0, 0); } while (0)
; #define PG8_LDA(dst, b, h) do { _Pragma("unroll") for (int m = 0; m < 4; ++m) _Pragma("unroll") for (int k = 0; k < 2; ++k) dst[m][k] = *(const PG8_LAS bf16x8*)(lds + PG8_SA(b, h) + aoff + m * 2048 + k * 1024); } while (0)
; #define PG8_LDB(dst, b, h) do { _Pragma("unroll") for (int n = 0; n < 2; ++n) _Pragma("unroll") for (int k = 0; k < 2; ++k) dst[n][k] = *(const PG8_LAS bf16x8*)(lds + PG8_SB(b, h) + boff + n * 2048 + k * 1024); } while (0)
; #define PG8_MMA(ai, bj, At, Bt) do { __builtin_amdgcn_s_setprio(1); _Pragma("unroll") for (int m = 0; m < 4; ++m) _Pragma("unroll") for (int n = 0; n < 2; ++n) _Pragma("unroll") for (int k = 0; k < 2; ++k) \
;         acc[ai][bj][m][n] = __builtin_amdgcn_mfma_f32_16x16x32_bf16(Bt[n][k], At[m][k], acc[ai][bj][m][n], 0, 0, 0); __builtin_amdgcn_s_setprio(0); } while (0)
; #define PG8_WAIT_V(n) asm volatile("s_waitcnt vmcnt(" #n ")" ::: "memory")
; #define PG8_WAIT_L(n) asm volatile("s_waitcnt lgkmcnt(" #n ")" ::: "memory")
; #define PG8_BAR __builtin_amdgcn_s_barrier()
; #define PG8_SCHED __builtin_amdgcn_sched_barrier(0)
; template <class Epi, class Sched, bool ALIGN_EPI = false, bool SP2 = false>
; __device__ __forceinline__ void gemm_phase(PG8_LAS unsigned char* lds, const Gemm g, const Sched& S, const Epi& E, const bool skip_epi = false) {
;     ...
;             PG8_WAIT_V(8); PG8_WAIT_L(0); PG8_BAR; PG8_MMA(1, 0, At, B0); PG8_MMA(1, 1, At, B1); PG8_BAR; PG8_SCHED;
;             PG8_LDB(B0, 1, 0); PG8_LDB(B1, 1, 1); PG8_SCHED; PG8_LDA(At, 1, 0); PG8_STAGE_A(0, 1, a2, true);
;             PG8_WAIT_V(8); PG8_WAIT_L(0); PG8_BAR; PG8_MMA(0, 0, At, B0); PG8_MMA(0, 1, At, B1); PG8_BAR; PG8_SCHED;
;             PG8_LDA(At, 1, 1); PG8_STAGE(PG8_SB(1, 0), b3, voffB); PG8_STAGE(PG8_SB(1, 1), b3 + hstep, voffB); PG8_STAGE_A(1, 0, a3, true);
	s_waitcnt lgkmcnt(0)
	v_mfma_f32_16x16x32_bf16 v[62:65], v[98:101], v[154:157], 0
	v_mfma_f32_16x16x32_bf16 v[58:61], v[122:125], v[154:157], 0
	v_mfma_f32_16x16x32_bf16 v[46:49], v[98:101], v[170:173], 0
	v_mfma_f32_16x16x32_bf16 v[42:45], v[122:125], v[170:173], 0
	v_mfma_f32_16x16x32_bf16 v[30:33], v[98:101], v[178:181], 0
	v_mfma_f32_16x16x32_bf16 v[26:29], v[122:125], v[178:181], 0
	v_mfma_f32_16x16x32_bf16 v[14:17], v[98:101], v[186:189], 0
	v_mfma_f32_16x16x32_bf16 v[10:13], v[122:125], v[186:189], 0
	v_mfma_f32_16x16x32_bf16 v[62:65], v[110:113], v[166:169], v[62:65]
	v_mfma_f32_16x16x32_bf16 v[58:61], v[126:129], v[166:169], v[58:61]
	v_mfma_f32_16x16x32_bf16 v[46:49], v[110:113], v[174:177], v[46:49]
	v_mfma_f32_16x16x32_bf16 v[42:45], v[126:129], v[174:177], v[42:45]
	v_mfma_f32_16x16x32_bf16 v[30:33], v[110:113], v[182:185], v[30:33]
	v_mfma_f32_16x16x32_bf16 v[26:29], v[126:129], v[182:185], v[26:29]
	v_mfma_f32_16x16x32_bf16 v[14:17], v[110:113], v[206:209], v[14:17]
	v_mfma_f32_16x16x32_bf16 v[10:13], v[126:129], v[206:209], v[10:13]
	v_mfma_f32_16x16x32_bf16 v[54:57], v[138:141], v[154:157], 0
	v_mfma_f32_16x16x32_bf16 v[50:53], v[146:149], v[154:157], 0
	v_mfma_f32_16x16x32_bf16 v[38:41], v[138:141], v[170:173], 0
	v_mfma_f32_16x16x32_bf16 v[34:37], v[146:149], v[170:173], 0
	v_mfma_f32_16x16x32_bf16 v[22:25], v[138:141], v[178:181], 0
	v_mfma_f32_16x16x32_bf16 v[18:21], v[146:149], v[178:181], 0
	v_mfma_f32_16x16x32_bf16 v[6:9], v[138:141], v[186:189], 0
	v_mfma_f32_16x16x32_bf16 v[2:5], v[146:149], v[186:189], 0
	v_mfma_f32_16x16x32_bf16 v[54:57], v[142:145], v[166:169], v[54:57]
	v_mfma_f32_16x16x32_bf16 v[50:53], v[150:153], v[166:169], v[50:53]
	v_mfma_f32_16x16x32_bf16 v[38:41], v[142:145], v[174:177], v[38:41]
	v_mfma_f32_16x16x32_bf16 v[34:37], v[150:153], v[174:177], v[34:37]
	v_mfma_f32_16x16x32_bf16 v[22:25], v[142:145], v[182:185], v[22:25]
	v_mfma_f32_16x16x32_bf16 v[18:21], v[150:153], v[182:185], v[18:21]
	v_mfma_f32_16x16x32_bf16 v[6:9], v[142:145], v[206:209], v[6:9]
	v_mfma_f32_16x16x32_bf16 v[2:5], v[150:153], v[206:209], v[2:5]
	s_barrier
	s_setprio 0
	s_add_i32 s64, 0, 0x18000
	s_add_i32 s65, 0, 0x1c000
	v_add_u32_e32 v126, s64, v229
	v_add_u32_e32 v150, s65, v229
	ds_read_b128 v[98:101], v126
	ds_read_b128 v[110:113], v126 offset:1024
	ds_read_b128 v[122:125], v126 offset:2048
	ds_read_b128 v[126:129], v126 offset:3072
	ds_read_b128 v[138:141], v150
	ds_read_b128 v[142:145], v150 offset:1024
	ds_read_b128 v[146:149], v150 offset:2048
	ds_read_b128 v[150:153], v150 offset:3072
	s_add_u32 s30, s30, 0x40000
	s_addc_u32 s31, s31, 0
	s_mov_b32 m0, s35
	ds_read_b128 v[154:157], v236 offset:32768
	ds_read_b128 v[166:169], v236 offset:33792
	ds_read_b128 v[170:173], v236 offset:34816
	ds_read_b128 v[174:177], v236 offset:35840
	ds_read_b128 v[178:181], v236 offset:36864
	ds_read_b128 v[182:185], v236 offset:37888
	ds_read_b128 v[186:189], v236 offset:38912
	ds_read_b128 v[206:209], v236 offset:39936
	global_load_lds_dwordx4 v190, s[30:31]
	s_mov_b32 m0, s36
	s_nop 0
	global_load_lds_dwordx4 v194, s[30:31]
	s_waitcnt vmcnt(8)
	s_waitcnt lgkmcnt(0)
	s_setprio 3
	s_barrier
	s_waitcnt lgkmcnt(0)
	v_mfma_f32_16x16x32_bf16 v[162:165], v[98:101], v[154:157], v[162:165]
	v_mfma_f32_16x16x32_bf16 v[158:161], v[122:125], v[154:157], v[158:161]
	v_mfma_f32_16x16x32_bf16 v[118:121], v[98:101], v[170:173], v[118:121]
	v_mfma_f32_16x16x32_bf16 v[114:117], v[122:125], v[170:173], v[114:117]
	v_mfma_f32_16x16x32_bf16 v[94:97], v[98:101], v[178:181], v[94:97]
	v_mfma_f32_16x16x32_bf16 v[90:93], v[122:125], v[178:181], v[90:93]
	v_mfma_f32_16x16x32_bf16 v[78:81], v[98:101], v[186:189], v[78:81]
	v_mfma_f32_16x16x32_bf16 v[74:77], v[122:125], v[186:189], v[74:77]
	v_mfma_f32_16x16x32_bf16 v[162:165], v[110:113], v[166:169], v[162:165]
	v_mfma_f32_16x16x32_bf16 v[158:161], v[126:129], v[166:169], v[158:161]
	v_mfma_f32_16x16x32_bf16 v[118:121], v[110:113], v[174:177], v[118:121]
	v_mfma_f32_16x16x32_bf16 v[114:117], v[126:129], v[174:177], v[114:117]
	v_mfma_f32_16x16x32_bf16 v[94:97], v[110:113], v[182:185], v[94:97]
	v_mfma_f32_16x16x32_bf16 v[90:93], v[126:129], v[182:185], v[90:93]
	v_mfma_f32_16x16x32_bf16 v[78:81], v[110:113], v[206:209], v[78:81]
	v_mfma_f32_16x16x32_bf16 v[74:77], v[126:129], v[206:209], v[74:77]
	v_mfma_f32_16x16x32_bf16 v[134:137], v[138:141], v[154:157], v[134:137]
	v_mfma_f32_16x16x32_bf16 v[130:133], v[146:149], v[154:157], v[130:133]
	v_mfma_f32_16x16x32_bf16 v[106:109], v[138:141], v[170:173], v[106:109]
	v_mfma_f32_16x16x32_bf16 v[102:105], v[146:149], v[170:173], v[102:105]
	v_mfma_f32_16x16x32_bf16 v[86:89], v[138:141], v[178:181], v[86:89]
	v_mfma_f32_16x16x32_bf16 v[82:85], v[146:149], v[178:181], v[82:85]
	v_mfma_f32_16x16x32_bf16 v[70:73], v[138:141], v[186:189], v[70:73]
	v_mfma_f32_16x16x32_bf16 v[66:69], v[146:149], v[186:189], v[66:69]
	v_mfma_f32_16x16x32_bf16 v[134:137], v[142:145], v[166:169], v[134:137]
	v_mfma_f32_16x16x32_bf16 v[130:133], v[150:153], v[166:169], v[130:133]
	v_mfma_f32_16x16x32_bf16 v[106:109], v[142:145], v[174:177], v[106:109]
	v_mfma_f32_16x16x32_bf16 v[102:105], v[150:153], v[174:177], v[102:105]
	v_mfma_f32_16x16x32_bf16 v[86:89], v[142:145], v[182:185], v[86:89]
	v_mfma_f32_16x16x32_bf16 v[82:85], v[150:153], v[182:185], v[82:85]
	v_mfma_f32_16x16x32_bf16 v[70:73], v[142:145], v[206:209], v[70:73]
	v_mfma_f32_16x16x32_bf16 v[66:69], v[150:153], v[206:209], v[66:69]
	s_barrier
; #define PG8_STAGE_A(b, h, ptr, NX) do { if constexpr (Sched::GATHER) { unsigned gs_[2]; gs_[0] = ((NX) && last_) ? gN[h][0] : gA[h][0]; gs_[1] = ((NX) && last_) ? gN[h][1] : gA[h][1]; PG8_STAGE(PG8_SA(b, h), ptr, gs_); } \
;         else PG8_STAGE(PG8_SA(b, h), (ptr) + ((h) ? hstep : (size_t)0), voffA); } while (0)
; #define PG8_STAGE(bufoff, gbase, voff) do { _Pragma("unroll") for (int _i = 0; _i < 2; ++_i) \
;         __builtin_amdgcn_global_load_lds((const unsigned*)((const char*)(gbase) + (voff)[_i]), (PG8_LAS unsigned*)(lds + (bufoff) + ldsw + _i * 8192), 16, 0, 0); } while (0)
; #define PG8_LDA(dst, b, h) do { _Pragma("unroll") for (int m = 0; m < 4; ++m) _Pragma("unroll") for (int k = 0; k < 2; ++k) dst[m][k] = *(const PG8_LAS bf16x8*)(lds + PG8_SA(b, h) + aoff + m * 2048 + k * 1024); } while (0)
; #define PG8_LDB(dst, b, h) do { _Pragma("unroll") for (int n = 0; n < 2; ++n) _Pragma("unroll") for (int k = 0; k < 2; ++k) dst[n][k] = *(const PG8_LAS bf16x8*)(lds + PG8_SB(b, h) + boff + n * 2048 + k * 1024); } while (0)
; #define PG8_WAIT_V(n) asm volatile("s_waitcnt vmcnt(" #n ")" ::: "memory")
; #define PG8_BAR __builtin_amdgcn_s_barrier()
; template <class Epi, class Sched, bool ALIGN_EPI = false, bool SP2 = false>
; __device__ __forceinline__ void gemm_phase(PG8_LAS unsigned char* lds, const Gemm g, const Sched& S, const Epi& E, const bool skip_epi = false) {
;     ...
;             PG8_LDB(B0, 0, 0); PG8_LDB(B1, 0, 1); PG8_SCHED; PG8_LDA(At, 0, 0); PG8_STAGE_A(1, 1, a1, false);
;             PG8_WAIT_V(8); PG8_WAIT_L(0); PG8_BAR; PG8_MMA(0, 0, At, B0); PG8_MMA(0, 1, At, B1); PG8_BAR; PG8_SCHED;
;             PG8_LDA(At, 0, 1); PG8_STAGE(PG8_SB(0, 0), b2, voffB); PG8_STAGE(PG8_SB(0, 1), b2 + hstep, voffB); PG8_STAGE_A(0, 0, a2, true);
;             PG8_WAIT_V(8); PG8_WAIT_L(0); PG8_BAR; PG8_MMA(1, 0, At, B0); PG8_MMA(1, 1, At, B1); PG8_BAR; PG8_SCHED;
;             PG8_LDB(B0, 1, 0); PG8_LDB(B1, 1, 1); PG8_SCHED; PG8_LDA(At, 1, 0); PG8_STAGE_A(0, 1, a2, true);
;             PG8_WAIT_V(8); PG8_WAIT_L(0); PG8_BAR; PG8_MMA(0, 0, At, B0); PG8_MMA(0, 1, At, B1); PG8_BAR; PG8_SCHED;
;             PG8_LDA(At, 1, 1); PG8_STAGE(PG8_SB(1, 0), b3, voffB); PG8_STAGE(PG8_SB(1, 1), b3 + hstep, voffB); PG8_STAGE_A(1, 0, a3, true);
;             PG8_WAIT_V(8); PG8_WAIT_L(0); PG8_BAR; PG8_MMA(1, 0, At, B0); PG8_MMA(1, 1, At, B1); PG8_BAR; PG8_SCHED;
	s_setprio 0
	s_add_i32 s30, s64, s2
	s_add_i32 m0, s30, 0xffffff80
	ds_read_b128 v[154:157], v236 offset:49152
	ds_read_b128 v[166:169], v236 offset:50176
	ds_read_b128 v[170:173], v236 offset:51200
	ds_read_b128 v[174:177], v236 offset:52224
	ds_read_b128 v[178:181], v236 offset:53248
	ds_read_b128 v[182:185], v236 offset:54272
	ds_read_b128 v[186:189], v236 offset:55296
	ds_read_b128 v[206:209], v236 offset:56320
	global_load_lds_dwordx4 v[210:211], off offset:128
	s_add_i32 m0, s30, 0x1f80
	s_add_u32 s28, s28, 0x40080
	s_addc_u32 s29, s29, 0
	s_add_i32 s30, s65, s2
	global_load_lds_dwordx4 v[212:213], off offset:128
	s_mov_b32 m0, s30
	s_nop 0
	global_load_lds_dwordx4 v192, s[28:29]
	s_add_i32 m0, s30, 0x2000
	s_nop 0
	global_load_lds_dwordx4 v196, s[28:29]
	s_add_i32 m0, s39, 0xffffff80
	s_nop 0
	global_load_lds_dwordx4 v[214:215], off offset:128
	s_add_i32 m0, s48, 0xffffff80
	s_nop 0
	global_load_lds_dwordx4 v[216:217], off offset:128
	s_waitcnt vmcnt(8)
	s_waitcnt lgkmcnt(0)
	s_setprio 3
	s_barrier
	s_waitcnt lgkmcnt(0)
	v_mfma_f32_16x16x32_bf16 v[62:65], v[98:101], v[154:157], v[62:65]
	v_mfma_f32_16x16x32_bf16 v[58:61], v[122:125], v[154:157], v[58:61]
	v_mfma_f32_16x16x32_bf16 v[46:49], v[98:101], v[170:173], v[46:49]
	v_mfma_f32_16x16x32_bf16 v[42:45], v[122:125], v[170:173], v[42:45]
	v_mfma_f32_16x16x32_bf16 v[30:33], v[98:101], v[178:181], v[30:33]
	v_mfma_f32_16x16x32_bf16 v[26:29], v[122:125], v[178:181], v[26:29]
	v_mfma_f32_16x16x32_bf16 v[14:17], v[98:101], v[186:189], v[14:17]
	v_mfma_f32_16x16x32_bf16 v[10:13], v[122:125], v[186:189], v[10:13]
	v_mfma_f32_16x16x32_bf16 v[62:65], v[110:113], v[166:169], v[62:65]
	v_mfma_f32_16x16x32_bf16 v[58:61], v[126:129], v[166:169], v[58:61]
	v_mfma_f32_16x16x32_bf16 v[46:49], v[110:113], v[174:177], v[46:49]
	v_mfma_f32_16x16x32_bf16 v[42:45], v[126:129], v[174:177], v[42:45]
	v_mfma_f32_16x16x32_bf16 v[30:33], v[110:113], v[182:185], v[30:33]
	v_mfma_f32_16x16x32_bf16 v[26:29], v[126:129], v[182:185], v[26:29]
	v_mfma_f32_16x16x32_bf16 v[14:17], v[110:113], v[206:209], v[14:17]
	v_mfma_f32_16x16x32_bf16 v[10:13], v[126:129], v[206:209], v[10:13]
	v_mfma_f32_16x16x32_bf16 v[54:57], v[138:141], v[154:157], v[54:57]
	v_mfma_f32_16x16x32_bf16 v[50:53], v[146:149], v[154:157], v[50:53]
	v_mfma_f32_16x16x32_bf16 v[38:41], v[138:141], v[170:173], v[38:41]
	v_mfma_f32_16x16x32_bf16 v[34:37], v[146:149], v[170:173], v[34:37]
	v_mfma_f32_16x16x32_bf16 v[22:25], v[138:141], v[178:181], v[22:25]
	v_mfma_f32_16x16x32_bf16 v[18:21], v[146:149], v[178:181], v[18:21]
	v_mfma_f32_16x16x32_bf16 v[6:9], v[138:141], v[186:189], v[6:9]
	v_mfma_f32_16x16x32_bf16 v[2:5], v[146:149], v[186:189], v[2:5]
	v_mfma_f32_16x16x32_bf16 v[54:57], v[142:145], v[166:169], v[54:57]
	v_mfma_f32_16x16x32_bf16 v[50:53], v[150:153], v[166:169], v[50:53]
	v_mfma_f32_16x16x32_bf16 v[38:41], v[142:145], v[174:177], v[38:41]
	v_mfma_f32_16x16x32_bf16 v[34:37], v[150:153], v[174:177], v[34:37]
	v_mfma_f32_16x16x32_bf16 v[22:25], v[142:145], v[182:185], v[22:25]
	v_mfma_f32_16x16x32_bf16 v[18:21], v[150:153], v[182:185], v[18:21]
	v_mfma_f32_16x16x32_bf16 v[6:9], v[142:145], v[206:209], v[6:9]
	v_mfma_f32_16x16x32_bf16 v[2:5], v[150:153], v[206:209], v[2:5]
	s_barrier
	s_setprio 0
	s_add_i32 s63, s63, 2
	s_add_u32 s26, s26, 0x100
	s_addc_u32 s27, s27, 0
	s_add_u32 s61, s61, 0x100
	s_addc_u32 s62, s62, 0
	s_cmp_gt_u32 s63, 13
.LBB0_634:
	ds_read_b128 v[98:101], v234
	ds_read_b128 v[110:113], v234 offset:1024
	ds_read_b128 v[122:125], v234 offset:2048
	ds_read_b128 v[126:129], v234 offset:3072
	ds_read_b128 v[138:141], v235
	ds_read_b128 v[142:145], v235 offset:1024
	ds_read_b128 v[146:149], v235 offset:2048
	ds_read_b128 v[150:153], v235 offset:3072
	s_add_u32 s28, s26, 0xfffc0080
	s_addc_u32 s29, s27, -1
	s_cmp_eq_u32 s63, 12
	s_cselect_b32 s31, s19, s29
	s_cselect_b32 s30, s25, s28
	s_cselect_b32 s29, s17, s62
	s_cselect_b32 s28, s60, s61
	s_add_i32 m0, s3, 0xc000
	ds_read_b128 v[154:157], v236
	ds_read_b128 v[166:169], v236 offset:1024
	ds_read_b128 v[170:173], v236 offset:2048
	ds_read_b128 v[174:177], v236 offset:3072
	ds_read_b128 v[178:181], v236 offset:4096
	ds_read_b128 v[182:185], v236 offset:5120
	ds_read_b128 v[186:189], v236 offset:6144
	ds_read_b128 v[206:209], v236 offset:7168
	global_load_lds_dwordx4 v198, s[26:27]
	s_add_i32 m0, s3, 0xe000
	s_nop 0
	global_load_lds_dwordx4 v200, s[26:27]
	s_waitcnt vmcnt(8)
	s_waitcnt lgkmcnt(0)
	s_setprio 3
	s_barrier
	s_waitcnt lgkmcnt(0)
	v_mfma_f32_16x16x32_bf16 v[162:165], v[98:101], v[154:157], v[162:165]
	v_mfma_f32_16x16x32_bf16 v[158:161], v[122:125], v[154:157], v[158:161]
	v_mfma_f32_16x16x32_bf16 v[118:121], v[98:101], v[170:173], v[118:121]
	v_mfma_f32_16x16x32_bf16 v[114:117], v[122:125], v[170:173], v[114:117]
	v_mfma_f32_16x16x32_bf16 v[94:97], v[98:101], v[178:181], v[94:97]
	v_mfma_f32_16x16x32_bf16 v[90:93], v[122:125], v[178:181], v[90:93]
	v_mfma_f32_16x16x32_bf16 v[78:81], v[98:101], v[186:189], v[78:81]
	v_mfma_f32_16x16x32_bf16 v[74:77], v[122:125], v[186:189], v[74:77]
	v_mfma_f32_16x16x32_bf16 v[162:165], v[110:113], v[166:169], v[162:165]
	v_mfma_f32_16x16x32_bf16 v[158:161], v[126:129], v[166:169], v[158:161]
	v_mfma_f32_16x16x32_bf16 v[118:121], v[110:113], v[174:177], v[118:121]
	v_mfma_f32_16x16x32_bf16 v[114:117], v[126:129], v[174:177], v[114:117]
	v_mfma_f32_16x16x32_bf16 v[94:97], v[110:113], v[182:185], v[94:97]
	v_mfma_f32_16x16x32_bf16 v[90:93], v[126:129], v[182:185], v[90:93]
	v_mfma_f32_16x16x32_bf16 v[78:81], v[110:113], v[206:209], v[78:81]
	v_mfma_f32_16x16x32_bf16 v[74:77], v[126:129], v[206:209], v[74:77]
	v_mfma_f32_16x16x32_bf16 v[134:137], v[138:141], v[154:157], v[134:137]
	v_mfma_f32_16x16x32_bf16 v[130:133], v[146:149], v[154:157], v[130:133]
	v_mfma_f32_16x16x32_bf16 v[106:109], v[138:141], v[170:173], v[106:109]
	v_mfma_f32_16x16x32_bf16 v[102:105], v[146:149], v[170:173], v[102:105]
	v_mfma_f32_16x16x32_bf16 v[86:89], v[138:141], v[178:181], v[86:89]
	v_mfma_f32_16x16x32_bf16 v[82:85], v[146:149], v[178:181], v[82:85]
	v_mfma_f32_16x16x32_bf16 v[70:73], v[138:141], v[186:189], v[70:73]
	v_mfma_f32_16x16x32_bf16 v[66:69], v[146:149], v[186:189], v[66:69]
	v_mfma_f32_16x16x32_bf16 v[134:137], v[142:145], v[166:169], v[134:137]
	v_mfma_f32_16x16x32_bf16 v[130:133], v[150:153], v[166:169], v[130:133]
	v_mfma_f32_16x16x32_bf16 v[106:109], v[142:145], v[174:177], v[106:109]
	v_mfma_f32_16x16x32_bf16 v[102:105], v[150:153], v[174:177], v[102:105]
	v_mfma_f32_16x16x32_bf16 v[86:89], v[142:145], v[182:185], v[86:89]
	v_mfma_f32_16x16x32_bf16 v[82:85], v[150:153], v[182:185], v[82:85]
	v_mfma_f32_16x16x32_bf16 v[70:73], v[142:145], v[206:209], v[70:73]
	v_mfma_f32_16x16x32_bf16 v[66:69], v[150:153], v[206:209], v[66:69]
	s_barrier
; #define PG8_STAGE_A(b, h, ptr, NX) do { if constexpr (Sched::GATHER) { unsigned gs_[2]; gs_[0] = ((NX) && last_) ? gN[h][0] : gA[h][0]; gs_[1] = ((NX) && last_) ? gN[h][1] : gA[h][1]; PG8_STAGE(PG8_SA(b, h), ptr, gs_); } \
;         else PG8_STAGE(PG8_SA(b, h), (ptr) + ((h) ? hstep : (size_t)0), voffA); } while (0)
; #define PG8_STAGE(bufoff, gbase, voff) do { _Pragma("unroll") for (int _i = 0; _i < 2; ++_i) \
;         __builtin_amdgcn_global_load_lds((const unsigned*)((const char*)(gbase) + (voff)[_i]), (PG8_LAS unsigned*)(lds + (bufoff) + ldsw + _i * 8192), 16, 0, 0); } while (0)
; #define PG8_LDA(dst, b, h) do { _Pragma("unroll") for (int m = 0; m < 4; ++m) _Pragma("unroll") for (int k = 0; k < 2; ++k) dst[m][k] = *(const PG8_LAS bf16x8*)(lds + PG8_SA(b, h) + aoff + m * 2048 + k * 1024); } while (0)
; #define PG8_LDB(dst, b, h) do { _Pragma("unroll") for (int n = 0; n < 2; ++n) _Pragma("unroll") for (int k = 0; k < 2; ++k) dst[n][k] = *(const PG8_LAS bf16x8*)(lds + PG8_SB(b, h) + boff + n * 2048 + k * 1024); } while (0)
; #define PG8_MMA(ai, bj, At, Bt) do { __builtin_amdgcn_s_setprio(1); _Pragma("unroll") for (int m = 0; m < 4; ++m) _Pragma("unroll") for (int n = 0; n < 2; ++n) _Pragma("unroll") for (int k = 0; k < 2; ++k) \
;         acc[ai][bj][m][n] = __builtin_amdgcn_mfma_f32_16x16x32_bf16(Bt[n][k], At[m][k], acc[ai][bj][m][n], 0, 0, 0); __builtin_amdgcn_s_setprio(0); } while (0)
; #define PG8_WAIT_V(n) asm volatile("s_waitcnt vmcnt(" #n ")" ::: "memory")
; #define PG8_WAIT_L(n) asm volatile("s_waitcnt lgkmcnt(" #n ")" ::: "memory")
; #define PG8_BAR __builtin_amdgcn_s_barrier()
; #define PG8_SCHED __builtin_amdgcn_sched_barrier(0)
; template <class Epi, class Sched, bool ALIGN_EPI = false, bool SP2 = false>
; __device__ __forceinline__ void gemm_phase(PG8_LAS unsigned char* lds, const Gemm g, const Sched& S, const Epi& E, const bool skip_epi = false) {
;     ...
;             PG8_LDA(At, 0, 1); PG8_STAGE(PG8_SB(0, 0), b2, voffB); PG8_STAGE(PG8_SB(0, 1), b2 + hstep, voffB); PG8_STAGE_A(0, 0, a2, true);
;             PG8_WAIT_V(8); PG8_WAIT_L(0); PG8_BAR; PG8_MMA(1, 0, At, B0); PG8_MMA(1, 1, At, B1); PG8_BAR; PG8_SCHED;
;             PG8_LDB(B0, 1, 0); PG8_LDB(B1, 1, 1); PG8_SCHED; PG8_LDA(At, 1, 0); PG8_STAGE_A(0, 1, a2, true);
;             PG8_WAIT_V(8); PG8_WAIT_L(0); PG8_BAR; PG8_MMA(0, 0, At, B0); PG8_MMA(0, 1, At, B1); PG8_BAR; PG8_SCHED;
	s_setprio 0
	s_add_i32 s64, s57, s2
	v_lshl_add_u64 v[210:211], s[28:29], 0, v[192:193]
	s_mov_b32 m0, s64
	ds_read_b128 v[154:157], v236 offset:16384
	ds_read_b128 v[166:169], v236 offset:17408
	ds_read_b128 v[170:173], v236 offset:18432
	ds_read_b128 v[174:177], v236 offset:19456
	ds_read_b128 v[178:181], v236 offset:20480
	ds_read_b128 v[182:185], v236 offset:21504
	ds_read_b128 v[186:189], v236 offset:22528
	ds_read_b128 v[206:209], v236 offset:23552
	global_load_lds_dwordx4 v[210:211], off
	s_add_i32 m0, s64, 0x2000
	s_add_u32 s64, s28, 0x40000
	v_lshl_add_u64 v[212:213], s[28:29], 0, v[196:197]
	s_addc_u32 s65, s29, 0
	s_add_i32 s66, s58, s2
	global_load_lds_dwordx4 v[212:213], off
	s_mov_b32 m0, s66
	v_lshl_add_u64 v[216:217], s[30:31], 0, v[194:195]
	global_load_lds_dwordx4 v192, s[64:65]
	s_add_i32 m0, s66, 0x2000
	s_nop 0
	global_load_lds_dwordx4 v196, s[64:65]
	v_lshl_add_u64 v[214:215], s[30:31], 0, v[190:191]
	s_mov_b32 m0, s3
	s_nop 0
	global_load_lds_dwordx4 v[214:215], off
	s_mov_b32 m0, s34
	s_nop 0
	global_load_lds_dwordx4 v[216:217], off
	s_waitcnt vmcnt(8)
	s_waitcnt lgkmcnt(0)
	s_setprio 3
	s_barrier
	s_waitcnt lgkmcnt(0)
	v_mfma_f32_16x16x32_bf16 v[62:65], v[98:101], v[154:157], v[62:65]
	v_mfma_f32_16x16x32_bf16 v[58:61], v[122:125], v[154:157], v[58:61]
	v_mfma_f32_16x16x32_bf16 v[46:49], v[98:101], v[170:173], v[46:49]
	v_mfma_f32_16x16x32_bf16 v[42:45], v[122:125], v[170:173], v[42:45]
	v_mfma_f32_16x16x32_bf16 v[30:33], v[98:101], v[178:181], v[30:33]
	v_mfma_f32_16x16x32_bf16 v[26:29], v[122:125], v[178:181], v[26:29]
	v_mfma_f32_16x16x32_bf16 v[14:17], v[98:101], v[186:189], v[14:17]
	v_mfma_f32_16x16x32_bf16 v[10:13], v[122:125], v[186:189], v[10:13]
	v_mfma_f32_16x16x32_bf16 v[62:65], v[110:113], v[166:169], v[62:65]
	v_mfma_f32_16x16x32_bf16 v[58:61], v[126:129], v[166:169], v[58:61]
	v_mfma_f32_16x16x32_bf16 v[46:49], v[110:113], v[174:177], v[46:49]
	v_mfma_f32_16x16x32_bf16 v[42:45], v[126:129], v[174:177], v[42:45]
	v_mfma_f32_16x16x32_bf16 v[30:33], v[110:113], v[182:185], v[30:33]
	v_mfma_f32_16x16x32_bf16 v[26:29], v[126:129], v[182:185], v[26:29]
	v_mfma_f32_16x16x32_bf16 v[14:17], v[110:113], v[206:209], v[14:17]
	v_mfma_f32_16x16x32_bf16 v[10:13], v[126:129], v[206:209], v[10:13]
	v_mfma_f32_16x16x32_bf16 v[54:57], v[138:141], v[154:157], v[54:57]
	v_mfma_f32_16x16x32_bf16 v[50:53], v[146:149], v[154:157], v[50:53]
	v_mfma_f32_16x16x32_bf16 v[38:41], v[138:141], v[170:173], v[38:41]
	v_mfma_f32_16x16x32_bf16 v[34:37], v[146:149], v[170:173], v[34:37]
	v_mfma_f32_16x16x32_bf16 v[22:25], v[138:141], v[178:181], v[22:25]
	v_mfma_f32_16x16x32_bf16 v[18:21], v[146:149], v[178:181], v[18:21]
	v_mfma_f32_16x16x32_bf16 v[6:9], v[138:141], v[186:189], v[6:9]
	v_mfma_f32_16x16x32_bf16 v[2:5], v[146:149], v[186:189], v[2:5]
	v_mfma_f32_16x16x32_bf16 v[54:57], v[142:145], v[166:169], v[54:57]
	v_mfma_f32_16x16x32_bf16 v[50:53], v[150:153], v[166:169], v[50:53]
	v_mfma_f32_16x16x32_bf16 v[38:41], v[142:145], v[174:177], v[38:41]
	v_mfma_f32_16x16x32_bf16 v[34:37], v[150:153], v[174:177], v[34:37]
	v_mfma_f32_16x16x32_bf16 v[22:25], v[142:145], v[182:185], v[22:25]
	v_mfma_f32_16x16x32_bf16 v[18:21], v[150:153], v[182:185], v[18:21]
	v_mfma_f32_16x16x32_bf16 v[6:9], v[142:145], v[206:209], v[6:9]
	v_mfma_f32_16x16x32_bf16 v[2:5], v[150:153], v[206:209], v[2:5]
	s_barrier
	s_setprio 0
	s_add_i32 s64, 0, 0x18000
	s_add_i32 s65, 0, 0x1c000
	v_add_u32_e32 v126, s64, v229
	v_add_u32_e32 v150, s65, v229
	ds_read_b128 v[98:101], v126
	ds_read_b128 v[110:113], v126 offset:1024
	ds_read_b128 v[122:125], v126 offset:2048
	ds_read_b128 v[126:129], v126 offset:3072
	ds_read_b128 v[138:141], v150
	ds_read_b128 v[142:145], v150 offset:1024
	ds_read_b128 v[146:149], v150 offset:2048
	ds_read_b128 v[150:153], v150 offset:3072
	s_add_u32 s30, s30, 0x40000
	s_addc_u32 s31, s31, 0
	s_mov_b32 m0, s35
	ds_read_b128 v[154:157], v236 offset:32768
	ds_read_b128 v[166:169], v236 offset:33792
	ds_read_b128 v[170:173], v236 offset:34816
	ds_read_b128 v[174:177], v236 offset:35840
	ds_read_b128 v[178:181], v236 offset:36864
	ds_read_b128 v[182:185], v236 offset:37888
	ds_read_b128 v[186:189], v236 offset:38912
	ds_read_b128 v[206:209], v236 offset:39936
	global_load_lds_dwordx4 v190, s[30:31]
	s_mov_b32 m0, s36
	s_nop 0
	global_load_lds_dwordx4 v194, s[30:31]
	s_waitcnt vmcnt(8)
	s_waitcnt lgkmcnt(0)
	s_setprio 3
	s_barrier
; #define PG8_STAGE_A(b, h, ptr, NX) do { if constexpr (Sched::GATHER) { unsigned gs_[2]; gs_[0] = ((NX) && last_) ? gN[h][0] : gA[h][0]; gs_[1] = ((NX) && last_) ? gN[h][1] : gA[h][1]; PG8_STAGE(PG8_SA(b, h), ptr, gs_); } \
;         else PG8_STAGE(PG8_SA(b, h), (ptr) + ((h) ? hstep : (size_t)0), voffA); } while (0)
; #define PG8_STAGE(bufoff, gbase, voff) do { _Pragma("unroll") for (int _i = 0; _i < 2; ++_i) \
;         __builtin_amdgcn_global_load_lds((const unsigned*)((const char*)(gbase) + (voff)[_i]), (PG8_LAS unsigned*)(lds + (bufoff) + ldsw + _i * 8192), 16, 0, 0); } while (0)
; #define PG8_LDA(dst, b, h) do { _Pragma("unroll") for (int m = 0; m < 4; ++m) _Pragma("unroll") for (int k = 0; k < 2; ++k) dst[m][k] = *(const PG8_LAS bf16x8*)(lds + PG8_SA(b, h) + aoff + m * 2048 + k * 1024); } while (0)
; #define PG8_MMA(ai, bj, At, Bt) do { __builtin_amdgcn_s_setprio(1); _Pragma("unroll") for (int m = 0; m < 4; ++m) _Pragma("unroll") for (int n = 0; n < 2; ++n) _Pragma("unroll") for (int k = 0; k < 2; ++k) \
;         acc[ai][bj][m][n] = __builtin_amdgcn_mfma_f32_16x16x32_bf16(Bt[n][k], At[m][k], acc[ai][bj][m][n], 0, 0, 0); __builtin_amdgcn_s_setprio(0); } while (0)
; #define PG8_WAIT_V(n) asm volatile("s_waitcnt vmcnt(" #n ")" ::: "memory")
; #define PG8_WAIT_L(n) asm volatile("s_waitcnt lgkmcnt(" #n ")" ::: "memory")
; #define PG8_BAR __builtin_amdgcn_s_barrier()
; #define PG8_SCHED __builtin_amdgcn_sched_barrier(0)
; template <class Epi, class Sched, bool ALIGN_EPI = false, bool SP2 = false>
; __device__ __forceinline__ void gemm_phase(PG8_LAS unsigned char* lds, const Gemm g, const Sched& S, const Epi& E, const bool skip_epi = false) {
;     ...
;             PG8_WAIT_V(8); PG8_WAIT_L(0); PG8_BAR; PG8_MMA(0, 0, At, B0); PG8_MMA(0, 1, At, B1); PG8_BAR; PG8_SCHED;
;             PG8_LDA(At, 1, 1); PG8_STAGE(PG8_SB(1, 0), b3, voffB); PG8_STAGE(PG8_SB(1, 1), b3 + hstep, voffB); PG8_STAGE_A(1, 0, a3, true);
;             PG8_WAIT_V(8); PG8_WAIT_L(0); PG8_BAR; PG8_MMA(1, 0, At, B0); PG8_MMA(1, 1, At, B1); PG8_BAR; PG8_SCHED;
;     ...
;         if constexpr (ALIGN_EPI) { if (wr == 0) PG8_BAR; }
	s_waitcnt lgkmcnt(0)
	v_mfma_f32_16x16x32_bf16 v[162:165], v[98:101], v[154:157], v[162:165]
	v_mfma_f32_16x16x32_bf16 v[158:161], v[122:125], v[154:157], v[158:161]
	v_mfma_f32_16x16x32_bf16 v[118:121], v[98:101], v[170:173], v[118:121]
	v_mfma_f32_16x16x32_bf16 v[114:117], v[122:125], v[170:173], v[114:117]
	v_mfma_f32_16x16x32_bf16 v[94:97], v[98:101], v[178:181], v[94:97]
	v_mfma_f32_16x16x32_bf16 v[90:93], v[122:125], v[178:181], v[90:93]
	v_mfma_f32_16x16x32_bf16 v[78:81], v[98:101], v[186:189], v[78:81]
	v_mfma_f32_16x16x32_bf16 v[74:77], v[122:125], v[186:189], v[74:77]
	v_mfma_f32_16x16x32_bf16 v[162:165], v[110:113], v[166:169], v[162:165]
	v_mfma_f32_16x16x32_bf16 v[158:161], v[126:129], v[166:169], v[158:161]
	v_mfma_f32_16x16x32_bf16 v[118:121], v[110:113], v[174:177], v[118:121]
	v_mfma_f32_16x16x32_bf16 v[114:117], v[126:129], v[174:177], v[114:117]
	v_mfma_f32_16x16x32_bf16 v[94:97], v[110:113], v[182:185], v[94:97]
	v_mfma_f32_16x16x32_bf16 v[90:93], v[126:129], v[182:185], v[90:93]
	v_mfma_f32_16x16x32_bf16 v[78:81], v[110:113], v[206:209], v[78:81]
	v_mfma_f32_16x16x32_bf16 v[74:77], v[126:129], v[206:209], v[74:77]
	v_mfma_f32_16x16x32_bf16 v[134:137], v[138:141], v[154:157], v[134:137]
	v_mfma_f32_16x16x32_bf16 v[130:133], v[146:149], v[154:157], v[130:133]
	v_mfma_f32_16x16x32_bf16 v[106:109], v[138:141], v[170:173], v[106:109]
	v_mfma_f32_16x16x32_bf16 v[102:105], v[146:149], v[170:173], v[102:105]
	v_mfma_f32_16x16x32_bf16 v[86:89], v[138:141], v[178:181], v[86:89]
	v_mfma_f32_16x16x32_bf16 v[82:85], v[146:149], v[178:181], v[82:85]
	v_mfma_f32_16x16x32_bf16 v[70:73], v[138:141], v[186:189], v[70:73]
	v_mfma_f32_16x16x32_bf16 v[66:69], v[146:149], v[186:189], v[66:69]
	v_mfma_f32_16x16x32_bf16 v[134:137], v[142:145], v[166:169], v[134:137]
	v_mfma_f32_16x16x32_bf16 v[130:133], v[150:153], v[166:169], v[130:133]
	v_mfma_f32_16x16x32_bf16 v[106:109], v[142:145], v[174:177], v[106:109]
	v_mfma_f32_16x16x32_bf16 v[102:105], v[150:153], v[174:177], v[102:105]
	v_mfma_f32_16x16x32_bf16 v[86:89], v[142:145], v[182:185], v[86:89]
	v_mfma_f32_16x16x32_bf16 v[82:85], v[150:153], v[182:185], v[82:85]
	v_mfma_f32_16x16x32_bf16 v[70:73], v[142:145], v[206:209], v[70:73]
	v_mfma_f32_16x16x32_bf16 v[66:69], v[150:153], v[206:209], v[66:69]
	s_barrier
	s_setprio 0
	s_add_i32 s30, s64, s2
	s_add_i32 m0, s30, 0xffffff80
	ds_read_b128 v[154:157], v236 offset:49152
	ds_read_b128 v[166:169], v236 offset:50176
	ds_read_b128 v[170:173], v236 offset:51200
	ds_read_b128 v[174:177], v236 offset:52224
	ds_read_b128 v[178:181], v236 offset:53248
	ds_read_b128 v[182:185], v236 offset:54272
	ds_read_b128 v[186:189], v236 offset:55296
	ds_read_b128 v[206:209], v236 offset:56320
	global_load_lds_dwordx4 v[210:211], off offset:128
	s_add_i32 m0, s30, 0x1f80
	s_add_u32 s28, s28, 0x40080
	s_addc_u32 s29, s29, 0
	s_add_i32 s30, s65, s2
	global_load_lds_dwordx4 v[212:213], off offset:128
	s_mov_b32 m0, s30
	s_nop 0
	global_load_lds_dwordx4 v192, s[28:29]
	s_add_i32 m0, s30, 0x2000
	s_nop 0
	global_load_lds_dwordx4 v196, s[28:29]
	s_add_i32 m0, s39, 0xffffff80
	s_nop 0
	global_load_lds_dwordx4 v[214:215], off offset:128
	s_add_i32 m0, s48, 0xffffff80
	s_nop 0
	global_load_lds_dwordx4 v[216:217], off offset:128
	s_waitcnt vmcnt(8)
	s_waitcnt lgkmcnt(0)
	s_setprio 3
	s_barrier
	s_waitcnt lgkmcnt(0)
	v_mfma_f32_16x16x32_bf16 v[62:65], v[98:101], v[154:157], v[62:65]
	v_mfma_f32_16x16x32_bf16 v[58:61], v[122:125], v[154:157], v[58:61]
	v_mfma_f32_16x16x32_bf16 v[46:49], v[98:101], v[170:173], v[46:49]
	v_mfma_f32_16x16x32_bf16 v[42:45], v[122:125], v[170:173], v[42:45]
	v_mfma_f32_16x16x32_bf16 v[30:33], v[98:101], v[178:181], v[30:33]
	v_mfma_f32_16x16x32_bf16 v[26:29], v[122:125], v[178:181], v[26:29]
	v_mfma_f32_16x16x32_bf16 v[14:17], v[98:101], v[186:189], v[14:17]
	v_mfma_f32_16x16x32_bf16 v[10:13], v[122:125], v[186:189], v[10:13]
	v_mfma_f32_16x16x32_bf16 v[62:65], v[110:113], v[166:169], v[62:65]
	v_mfma_f32_16x16x32_bf16 v[58:61], v[126:129], v[166:169], v[58:61]
	v_mfma_f32_16x16x32_bf16 v[46:49], v[110:113], v[174:177], v[46:49]
	v_mfma_f32_16x16x32_bf16 v[42:45], v[126:129], v[174:177], v[42:45]
	v_mfma_f32_16x16x32_bf16 v[30:33], v[110:113], v[182:185], v[30:33]
	v_mfma_f32_16x16x32_bf16 v[26:29], v[126:129], v[182:185], v[26:29]
	v_mfma_f32_16x16x32_bf16 v[14:17], v[110:113], v[206:209], v[14:17]
	v_mfma_f32_16x16x32_bf16 v[10:13], v[126:129], v[206:209], v[10:13]
	v_mfma_f32_16x16x32_bf16 v[54:57], v[138:141], v[154:157], v[54:57]
	v_mfma_f32_16x16x32_bf16 v[50:53], v[146:149], v[154:157], v[50:53]
	v_mfma_f32_16x16x32_bf16 v[38:41], v[138:141], v[170:173], v[38:41]
	v_mfma_f32_16x16x32_bf16 v[34:37], v[146:149], v[170:173], v[34:37]
	v_mfma_f32_16x16x32_bf16 v[22:25], v[138:141], v[178:181], v[22:25]
	v_mfma_f32_16x16x32_bf16 v[18:21], v[146:149], v[178:181], v[18:21]
	v_mfma_f32_16x16x32_bf16 v[6:9], v[138:141], v[186:189], v[6:9]
	v_mfma_f32_16x16x32_bf16 v[2:5], v[146:149], v[186:189], v[2:5]
	v_mfma_f32_16x16x32_bf16 v[54:57], v[142:145], v[166:169], v[54:57]
	v_mfma_f32_16x16x32_bf16 v[50:53], v[150:153], v[166:169], v[50:53]
	v_mfma_f32_16x16x32_bf16 v[38:41], v[142:145], v[174:177], v[38:41]
	v_mfma_f32_16x16x32_bf16 v[34:37], v[150:153], v[174:177], v[34:37]
	v_mfma_f32_16x16x32_bf16 v[22:25], v[142:145], v[182:185], v[22:25]
	v_mfma_f32_16x16x32_bf16 v[18:21], v[150:153], v[182:185], v[18:21]
	v_mfma_f32_16x16x32_bf16 v[6:9], v[142:145], v[206:209], v[6:9]
	v_mfma_f32_16x16x32_bf16 v[2:5], v[150:153], v[206:209], v[2:5]
	s_barrier
	s_setprio 0
	s_add_i32 s63, s63, 2
	s_add_u32 s26, s26, 0x100
	s_addc_u32 s27, s27, 0
	s_add_u32 s61, s61, 0x100
	s_addc_u32 s62, s62, 0
	s_cmp_gt_u32 s63, 13
	s_cbranch_scc0 .LBB0_634
	s_and_b64 vcc, exec, s[14:15]
	s_cbranch_vccz .LBB0_637
	s_barrier

; #define PG8_GIDX(G_, PM_) do { if constexpr (Sched::GATHER) { _Pragma("unroll") for (int h_ = 0; h_ < 2; ++h_) _Pragma("unroll") for (int i_ = 0; i_ < 2; ++i_) { int R_, C_; stage_rc(tid * 16 + i_ * 8192, R_, C_); \
;         const int src_ = S.rowsrc[(PM_) * BM + h_ * HALF + R_]; G_[h_][i_] = (unsigned)(src_ * K + C_) * 2u; } } } while (0)
; #define PG8_WAIT_V(n) asm volatile("s_waitcnt vmcnt(" #n ")" ::: "memory")
; __device__ __forceinline__ void rstd8(const float* SS, int rowb, int lane, float (&rs)[2][4]) {
;     f32x4 p[2][4];
; #pragma unroll
;     for (int ai = 0; ai < 2; ++ai)
; #pragma unroll
;         for (int m = 0; m < 4; ++m) p[ai][m] = *(const f32x4*)(SS + (size_t)(rowb + HALF * ai + 16 * m + (lane >> 2)) * 16 + 4 * (lane & 3));
;     asm volatile("" : "+v"(p[0][0]), "+v"(p[0][1]), "+v"(p[0][2]), "+v"(p[0][3]), "+v"(p[1][0]), "+v"(p[1][1]), "+v"(p[1][2]), "+v"(p[1][3]));
; template <class Epi, class Sched, bool ALIGN_EPI = false, bool SP2 = false>
; __device__ __forceinline__ void gemm_phase(PG8_LAS unsigned char* lds, const Gemm g, const Sched& S, const Epi& E, const bool skip_epi = false) {
;     ...
;         const bool has_next = S.next(ui + 1, nxt);
;         if (has_next) PG8_GIDX(gN, nxt.pm);
;         const char* nA = has_next ? (const char*)g.A + (size_t)nxt.pm * pmstepA + nxt.ko : cA; const char* nB = has_next ? (const char*)g.Bt + (size_t)nxt.pn * tstep + nxt.ko : cB;
;         for (int t = 0; t < nt; t += 2) {
;             const bool last = (t == nt - 2); last_ = last && has_next;
;             const char* a1 = cA + (size_t)(t + 1) * kstep;
;             const char* a2 = last ? nA : cA + (size_t)(t + 2) * kstep; const char* b2 = last ? nB : cB + (size_t)(t + 2) * kstep;
;             const char* a3 = a2 + kstep; const char* b3 = b2 + kstep;
;             if (last && has_next) S.a_ready(nxt);
;             if constexpr (SP2) {
;             PG8_LDB(B0, 0, 0); PG8_LDB(B1, 0, 1); PG8_SCHED; PG8_LDA(At, 0, 0); PG8_STAGE_A(1, 1, a1, false);
;             PG8_WAIT_V(8); PG8_WAIT_L(0); PG8_BAR; PG8_MMA(0, 0, At, B0); PG8_MMA(0, 1, At, B1); PG8_BAR; PG8_SCHED;
;             PG8_LDA(At, 0, 1); PG8_STAGE(PG8_SB(0, 0), b2, voffB); PG8_STAGE(PG8_SB(0, 1), b2 + hstep, voffB); PG8_STAGE_A(0, 0, a2, true);
;             PG8_WAIT_V(8); PG8_WAIT_L(0); PG8_BAR; PG8_MMA(1, 0, At, B0); PG8_MMA(1, 1, At, B1); PG8_BAR; PG8_SCHED;
.LBB0_720:
	s_ashr_i32 s15, s14, 31
	s_lshl_b64 s[16:17], s[14:15], 19
	s_add_u32 s16, s86, s16
	s_addc_u32 s17, s87, s17
	s_and_b64 s[18:19], s[4:5], exec
	s_cselect_b32 s15, s17, s23
	s_cselect_b32 s56, s16, s22
	s_ashr_i32 s13, s12, 31
	s_lshl_b64 s[18:19], s[12:13], 19
	v_readlane_b32 s26, v254, 15
	v_readlane_b32 s27, v254, 16
	s_add_u32 s18, s26, s18
	s_addc_u32 s19, s27, s19
	s_and_b64 s[26:27], s[4:5], exec
	s_cselect_b32 s13, s19, s25
	s_cselect_b32 s57, s18, s24
	s_add_u32 s22, s22, 0x40080
	s_addc_u32 s23, s23, 0
	s_add_u32 s58, s24, 0x100
	s_addc_u32 s59, s25, 0
	s_mov_b32 s60, -2
	s_waitcnt vmcnt(0)
	v_lshl_add_u32 v130, s20, 8, v175
	v_ashrrev_i32_e32 v131, 31, v130
	v_lshlrev_b64 v[130:131], 6, v[130:131]
	v_lshl_add_u64 v[130:131], v[150:151], 0, v[130:131]
	global_load_dwordx4 v[238:241], v[130:131], off
	global_load_dwordx4 v[242:245], v[130:131], off offset:1024
	global_load_dwordx4 v[246:249], v[130:131], off offset:2048
	global_load_dwordx4 v[250:253], v[130:131], off offset:3072
	ds_read_b128 v[130:133], v187
	ds_read_b128 v[134:137], v187 offset:1024
	ds_read_b128 v[138:141], v187 offset:2048
	ds_read_b128 v[160:163], v187 offset:3072
	ds_read_b128 v[164:167], v188
	ds_read_b128 v[182:185], v188 offset:1024
	ds_read_b128 v[192:195], v188 offset:2048
	ds_read_b128 v[196:199], v188 offset:3072
	s_add_u32 s24, s22, 0xfffc0080
	s_addc_u32 s25, s23, -1
	s_cmp_eq_u32 s60, 12
	s_cselect_b32 s27, s15, s25
	s_cselect_b32 s26, s56, s24
	s_cselect_b32 s25, s13, s59
	s_cselect_b32 s24, s57, s58
	s_add_i32 m0, s29, 0xc000
	ds_read_b128 v[200:203], v189
	ds_read_b128 v[204:207], v189 offset:1024
	ds_read_b128 v[208:211], v189 offset:2048
	ds_read_b128 v[212:215], v189 offset:3072
	ds_read_b128 v[216:219], v189 offset:4096
	ds_read_b128 v[220:223], v189 offset:5120
	ds_read_b128 v[224:227], v189 offset:6144
	ds_read_b128 v[230:233], v189 offset:7168
	global_load_lds_dwordx4 v152, s[22:23]
	s_add_i32 m0, s29, 0xe000
	s_nop 0
	global_load_lds_dwordx4 v154, s[22:23]
	s_waitcnt vmcnt(8)
	s_waitcnt lgkmcnt(0)
	s_setprio 3
	s_barrier
	s_waitcnt lgkmcnt(0)
	v_mfma_f32_16x16x32_bf16 v[126:129], v[130:133], v[200:203], 0
	v_mfma_f32_16x16x32_bf16 v[122:125], v[138:141], v[200:203], 0
	v_mfma_f32_16x16x32_bf16 v[110:113], v[130:133], v[208:211], 0
	v_mfma_f32_16x16x32_bf16 v[106:109], v[138:141], v[208:211], 0
	v_mfma_f32_16x16x32_bf16 v[94:97], v[130:133], v[216:219], 0
	v_mfma_f32_16x16x32_bf16 v[90:93], v[138:141], v[216:219], 0
	v_mfma_f32_16x16x32_bf16 v[78:81], v[130:133], v[224:227], 0
	v_mfma_f32_16x16x32_bf16 v[74:77], v[138:141], v[224:227], 0
	v_mfma_f32_16x16x32_bf16 v[126:129], v[134:137], v[204:207], v[126:129]
	v_mfma_f32_16x16x32_bf16 v[122:125], v[160:163], v[204:207], v[122:125]
	v_mfma_f32_16x16x32_bf16 v[110:113], v[134:137], v[212:215], v[110:113]
	v_mfma_f32_16x16x32_bf16 v[106:109], v[160:163], v[212:215], v[106:109]
	v_mfma_f32_16x16x32_bf16 v[94:97], v[134:137], v[220:223], v[94:97]
	v_mfma_f32_16x16x32_bf16 v[90:93], v[160:163], v[220:223], v[90:93]
	v_mfma_f32_16x16x32_bf16 v[78:81], v[134:137], v[230:233], v[78:81]
	v_mfma_f32_16x16x32_bf16 v[74:77], v[160:163], v[230:233], v[74:77]
	v_mfma_f32_16x16x32_bf16 v[118:121], v[164:167], v[200:203], 0
	v_mfma_f32_16x16x32_bf16 v[114:117], v[192:195], v[200:203], 0
	v_mfma_f32_16x16x32_bf16 v[102:105], v[164:167], v[208:211], 0
	v_mfma_f32_16x16x32_bf16 v[98:101], v[192:195], v[208:211], 0
	v_mfma_f32_16x16x32_bf16 v[86:89], v[164:167], v[216:219], 0
	v_mfma_f32_16x16x32_bf16 v[82:85], v[192:195], v[216:219], 0
	v_mfma_f32_16x16x32_bf16 v[70:73], v[164:167], v[224:227], 0
	v_mfma_f32_16x16x32_bf16 v[66:69], v[192:195], v[224:227], 0
	v_mfma_f32_16x16x32_bf16 v[118:121], v[182:185], v[204:207], v[118:121]
	v_mfma_f32_16x16x32_bf16 v[114:117], v[196:199], v[204:207], v[114:117]
	v_mfma_f32_16x16x32_bf16 v[102:105], v[182:185], v[212:215], v[102:105]
	v_mfma_f32_16x16x32_bf16 v[98:101], v[196:199], v[212:215], v[98:101]
	v_mfma_f32_16x16x32_bf16 v[86:89], v[182:185], v[220:223], v[86:89]
	v_mfma_f32_16x16x32_bf16 v[82:85], v[196:199], v[220:223], v[82:85]
	v_mfma_f32_16x16x32_bf16 v[70:73], v[182:185], v[230:233], v[70:73]
	v_mfma_f32_16x16x32_bf16 v[66:69], v[196:199], v[230:233], v[66:69]
	s_barrier
	s_setprio 0
	s_add_i32 s61, s39, s2
	v_lshl_add_u64 v[168:169], s[24:25], 0, v[146:147]
	s_mov_b32 m0, s61
	ds_read_b128 v[200:203], v189 offset:16384
	ds_read_b128 v[204:207], v189 offset:17408
	ds_read_b128 v[208:211], v189 offset:18432
	ds_read_b128 v[212:215], v189 offset:19456
	ds_read_b128 v[216:219], v189 offset:20480
	ds_read_b128 v[220:223], v189 offset:21504
	ds_read_b128 v[224:227], v189 offset:22528
	ds_read_b128 v[230:233], v189 offset:23552
	global_load_lds_dwordx4 v[168:169], off
	s_add_i32 m0, s61, 0x2000
	s_add_u32 s62, s24, 0x40000
	v_lshl_add_u64 v[172:173], s[24:25], 0, v[142:143]
	s_addc_u32 s63, s25, 0
	s_add_i32 s61, s48, s2
	global_load_lds_dwordx4 v[172:173], off
	s_mov_b32 m0, s61
	v_lshl_add_u64 v[234:235], s[26:27], 0, v[144:145]
	global_load_lds_dwordx4 v146, s[62:63]
	s_add_i32 m0, s61, 0x2000
	s_nop 0
	global_load_lds_dwordx4 v142, s[62:63]
	v_lshl_add_u64 v[176:177], s[26:27], 0, v[148:149]
	s_mov_b32 m0, s29
	s_nop 0
	global_load_lds_dwordx4 v[176:177], off
	s_mov_b32 m0, s30
	s_nop 0
	global_load_lds_dwordx4 v[234:235], off
	s_waitcnt vmcnt(8)
	s_waitcnt lgkmcnt(0)
	s_setprio 3
	s_barrier
; #define PG8_STAGE_A(b, h, ptr, NX) do { if constexpr (Sched::GATHER) { unsigned gs_[2]; gs_[0] = ((NX) && last_) ? gN[h][0] : gA[h][0]; gs_[1] = ((NX) && last_) ? gN[h][1] : gA[h][1]; PG8_STAGE(PG8_SA(b, h), ptr, gs_); } \
;         else PG8_STAGE(PG8_SA(b, h), (ptr) + ((h) ? hstep : (size_t)0), voffA); } while (0)
; #define PG8_STAGE(bufoff, gbase, voff) do { _Pragma("unroll") for (int _i = 0; _i < 2; ++_i) \
;         __builtin_amdgcn_global_load_lds((const unsigned*)((const char*)(gbase) + (voff)[_i]), (PG8_LAS unsigned*)(lds + (bufoff) + ldsw + _i * 8192), 16, 0, 0); } while (0)
; #define PG8_LDA(dst, b, h) do { _Pragma("unroll") for (int m = 0; m < 4; ++m) _Pragma("unroll") for (int k = 0; k < 2; ++k) dst[m][k] = *(const PG8_LAS bf16x8*)(lds + PG8_SA(b, h) + aoff + m * 2048 + k * 1024); } while (0)
; #define PG8_LDB(dst, b, h) do { _Pragma("unroll") for (int n = 0; n < 2; ++n) _Pragma("unroll") for (int k = 0; k < 2; ++k) dst[n][k] = *(const PG8_LAS bf16x8*)(lds + PG8_SB(b, h) + boff + n * 2048 + k * 1024); } while (0)
; #define PG8_MMA(ai, bj, At, Bt) do { __builtin_amdgcn_s_setprio(1); _Pragma("unroll") for (int m = 0; m < 4; ++m) _Pragma("unroll") for (int n = 0; n < 2; ++n) _Pragma("unroll") for (int k = 0; k < 2; ++k) \
;         acc[ai][bj][m][n] = __builtin_amdgcn_mfma_f32_16x16x32_bf16(Bt[n][k], At[m][k], acc[ai][bj][m][n], 0, 0, 0); __builtin_amdgcn_s_setprio(0); } while (0)
; #define PG8_WAIT_V(n) asm volatile("s_waitcnt vmcnt(" #n ")" ::: "memory")
; #define PG8_WAIT_L(n) asm volatile("s_waitcnt lgkmcnt(" #n ")" ::: "memory")
; #define PG8_BAR __builtin_amdgcn_s_barrier()
; #define PG8_SCHED __builtin_amdgcn_sched_barrier(0)
; template <class Epi, class Sched, bool ALIGN_EPI = false, bool SP2 = false>
; __device__ __forceinline__ void gemm_phase(PG8_LAS unsigned char* lds, const Gemm g, const Sched& S, const Epi& E, const bool skip_epi = false) {
;     ...
;             PG8_WAIT_V(8); PG8_WAIT_L(0); PG8_BAR; PG8_MMA(1, 0, At, B0); PG8_MMA(1, 1, At, B1); PG8_BAR; PG8_SCHED;
;             PG8_LDB(B0, 1, 0); PG8_LDB(B1, 1, 1); PG8_SCHED; PG8_LDA(At, 1, 0); PG8_STAGE_A(0, 1, a2, true);
;             PG8_WAIT_V(8); PG8_WAIT_L(0); PG8_BAR; PG8_MMA(0, 0, At, B0); PG8_MMA(0, 1, At, B1); PG8_BAR; PG8_SCHED;
;             PG8_LDA(At, 1, 1); PG8_STAGE(PG8_SB(1, 0), b3, voffB); PG8_STAGE(PG8_SB(1, 1), b3 + hstep, voffB); PG8_STAGE_A(1, 0, a3, true);
	s_waitcnt lgkmcnt(0)
	v_mfma_f32_16x16x32_bf16 v[62:65], v[130:133], v[200:203], 0
	v_mfma_f32_16x16x32_bf16 v[58:61], v[138:141], v[200:203], 0
	v_mfma_f32_16x16x32_bf16 v[46:49], v[130:133], v[208:211], 0
	v_mfma_f32_16x16x32_bf16 v[42:45], v[138:141], v[208:211], 0
	v_mfma_f32_16x16x32_bf16 v[30:33], v[130:133], v[216:219], 0
	v_mfma_f32_16x16x32_bf16 v[26:29], v[138:141], v[216:219], 0
	v_mfma_f32_16x16x32_bf16 v[14:17], v[130:133], v[224:227], 0
	v_mfma_f32_16x16x32_bf16 v[10:13], v[138:141], v[224:227], 0
	v_mfma_f32_16x16x32_bf16 v[62:65], v[134:137], v[204:207], v[62:65]
	v_mfma_f32_16x16x32_bf16 v[58:61], v[160:163], v[204:207], v[58:61]
	v_mfma_f32_16x16x32_bf16 v[46:49], v[134:137], v[212:215], v[46:49]
	v_mfma_f32_16x16x32_bf16 v[42:45], v[160:163], v[212:215], v[42:45]
	v_mfma_f32_16x16x32_bf16 v[30:33], v[134:137], v[220:223], v[30:33]
	v_mfma_f32_16x16x32_bf16 v[26:29], v[160:163], v[220:223], v[26:29]
	v_mfma_f32_16x16x32_bf16 v[14:17], v[134:137], v[230:233], v[14:17]
	v_mfma_f32_16x16x32_bf16 v[10:13], v[160:163], v[230:233], v[10:13]
	v_mfma_f32_16x16x32_bf16 v[54:57], v[164:167], v[200:203], 0
	v_mfma_f32_16x16x32_bf16 v[50:53], v[192:195], v[200:203], 0
	v_mfma_f32_16x16x32_bf16 v[38:41], v[164:167], v[208:211], 0
	v_mfma_f32_16x16x32_bf16 v[34:37], v[192:195], v[208:211], 0
	v_mfma_f32_16x16x32_bf16 v[22:25], v[164:167], v[216:219], 0
	v_mfma_f32_16x16x32_bf16 v[18:21], v[192:195], v[216:219], 0
	v_mfma_f32_16x16x32_bf16 v[6:9], v[164:167], v[224:227], 0
	v_mfma_f32_16x16x32_bf16 v[2:5], v[192:195], v[224:227], 0
	v_mfma_f32_16x16x32_bf16 v[54:57], v[182:185], v[204:207], v[54:57]
	v_mfma_f32_16x16x32_bf16 v[50:53], v[196:199], v[204:207], v[50:53]
	v_mfma_f32_16x16x32_bf16 v[38:41], v[182:185], v[212:215], v[38:41]
	v_mfma_f32_16x16x32_bf16 v[34:37], v[196:199], v[212:215], v[34:37]
	v_mfma_f32_16x16x32_bf16 v[22:25], v[182:185], v[220:223], v[22:25]
	v_mfma_f32_16x16x32_bf16 v[18:21], v[196:199], v[220:223], v[18:21]
	v_mfma_f32_16x16x32_bf16 v[6:9], v[182:185], v[230:233], v[6:9]
	v_mfma_f32_16x16x32_bf16 v[2:5], v[196:199], v[230:233], v[2:5]
	s_barrier
	s_setprio 0
	s_add_i32 s61, 0, 0x18000
	s_add_i32 s62, 0, 0x1c000
	v_add_u32_e32 v160, s61, v1
	v_add_u32_e32 v170, s62, v1
	ds_read_b128 v[130:133], v160
	ds_read_b128 v[134:137], v160 offset:1024
	ds_read_b128 v[138:141], v160 offset:2048
	ds_read_b128 v[160:163], v160 offset:3072
	ds_read_b128 v[164:167], v170
	ds_read_b128 v[182:185], v170 offset:1024
	ds_read_b128 v[192:195], v170 offset:2048
	ds_read_b128 v[196:199], v170 offset:3072
	s_add_u32 s26, s26, 0x40000
	s_addc_u32 s27, s27, 0
	s_mov_b32 m0, s31
	ds_read_b128 v[200:203], v189 offset:32768
	ds_read_b128 v[204:207], v189 offset:33792
	ds_read_b128 v[208:211], v189 offset:34816
	ds_read_b128 v[212:215], v189 offset:35840
	ds_read_b128 v[216:219], v189 offset:36864
	ds_read_b128 v[220:223], v189 offset:37888
	ds_read_b128 v[224:227], v189 offset:38912
	ds_read_b128 v[230:233], v189 offset:39936
	global_load_lds_dwordx4 v148, s[26:27]
	s_mov_b32 m0, s34
	s_nop 0
	global_load_lds_dwordx4 v144, s[26:27]
	s_waitcnt vmcnt(8)
	s_waitcnt lgkmcnt(0)
	s_setprio 3
	s_barrier
	s_waitcnt lgkmcnt(0)
	v_mfma_f32_16x16x32_bf16 v[126:129], v[130:133], v[200:203], v[126:129]
	v_mfma_f32_16x16x32_bf16 v[122:125], v[138:141], v[200:203], v[122:125]
	v_mfma_f32_16x16x32_bf16 v[110:113], v[130:133], v[208:211], v[110:113]
	v_mfma_f32_16x16x32_bf16 v[106:109], v[138:141], v[208:211], v[106:109]
	v_mfma_f32_16x16x32_bf16 v[94:97], v[130:133], v[216:219], v[94:97]
	v_mfma_f32_16x16x32_bf16 v[90:93], v[138:141], v[216:219], v[90:93]
	v_mfma_f32_16x16x32_bf16 v[78:81], v[130:133], v[224:227], v[78:81]
	v_mfma_f32_16x16x32_bf16 v[74:77], v[138:141], v[224:227], v[74:77]
	v_mfma_f32_16x16x32_bf16 v[126:129], v[134:137], v[204:207], v[126:129]
	v_mfma_f32_16x16x32_bf16 v[122:125], v[160:163], v[204:207], v[122:125]
	v_mfma_f32_16x16x32_bf16 v[110:113], v[134:137], v[212:215], v[110:113]
	v_mfma_f32_16x16x32_bf16 v[106:109], v[160:163], v[212:215], v[106:109]
	v_mfma_f32_16x16x32_bf16 v[94:97], v[134:137], v[220:223], v[94:97]
	v_mfma_f32_16x16x32_bf16 v[90:93], v[160:163], v[220:223], v[90:93]
	v_mfma_f32_16x16x32_bf16 v[78:81], v[134:137], v[230:233], v[78:81]
	v_mfma_f32_16x16x32_bf16 v[74:77], v[160:163], v[230:233], v[74:77]
	v_mfma_f32_16x16x32_bf16 v[118:121], v[164:167], v[200:203], v[118:121]
	v_mfma_f32_16x16x32_bf16 v[114:117], v[192:195], v[200:203], v[114:117]
	v_mfma_f32_16x16x32_bf16 v[102:105], v[164:167], v[208:211], v[102:105]
	v_mfma_f32_16x16x32_bf16 v[98:101], v[192:195], v[208:211], v[98:101]
	v_mfma_f32_16x16x32_bf16 v[86:89], v[164:167], v[216:219], v[86:89]
	v_mfma_f32_16x16x32_bf16 v[82:85], v[192:195], v[216:219], v[82:85]
	v_mfma_f32_16x16x32_bf16 v[70:73], v[164:167], v[224:227], v[70:73]
	v_mfma_f32_16x16x32_bf16 v[66:69], v[192:195], v[224:227], v[66:69]
	v_mfma_f32_16x16x32_bf16 v[118:121], v[182:185], v[204:207], v[118:121]
	v_mfma_f32_16x16x32_bf16 v[114:117], v[196:199], v[204:207], v[114:117]
	v_mfma_f32_16x16x32_bf16 v[102:105], v[182:185], v[212:215], v[102:105]
	v_mfma_f32_16x16x32_bf16 v[98:101], v[196:199], v[212:215], v[98:101]
	v_mfma_f32_16x16x32_bf16 v[86:89], v[182:185], v[220:223], v[86:89]
	v_mfma_f32_16x16x32_bf16 v[82:85], v[196:199], v[220:223], v[82:85]
	v_mfma_f32_16x16x32_bf16 v[70:73], v[182:185], v[230:233], v[70:73]
	v_mfma_f32_16x16x32_bf16 v[66:69], v[196:199], v[230:233], v[66:69]
	s_barrier
; #define PG8_STAGE_A(b, h, ptr, NX) do { if constexpr (Sched::GATHER) { unsigned gs_[2]; gs_[0] = ((NX) && last_) ? gN[h][0] : gA[h][0]; gs_[1] = ((NX) && last_) ? gN[h][1] : gA[h][1]; PG8_STAGE(PG8_SA(b, h), ptr, gs_); } \
;         else PG8_STAGE(PG8_SA(b, h), (ptr) + ((h) ? hstep : (size_t)0), voffA); } while (0)
; #define PG8_STAGE(bufoff, gbase, voff) do { _Pragma("unroll") for (int _i = 0; _i < 2; ++_i) \
;         __builtin_amdgcn_global_load_lds((const unsigned*)((const char*)(gbase) + (voff)[_i]), (PG8_LAS unsigned*)(lds + (bufoff) + ldsw + _i * 8192), 16, 0, 0); } while (0)
; #define PG8_LDA(dst, b, h) do { _Pragma("unroll") for (int m = 0; m < 4; ++m) _Pragma("unroll") for (int k = 0; k < 2; ++k) dst[m][k] = *(const PG8_LAS bf16x8*)(lds + PG8_SA(b, h) + aoff + m * 2048 + k * 1024); } while (0)
; #define PG8_LDB(dst, b, h) do { _Pragma("unroll") for (int n = 0; n < 2; ++n) _Pragma("unroll") for (int k = 0; k < 2; ++k) dst[n][k] = *(const PG8_LAS bf16x8*)(lds + PG8_SB(b, h) + boff + n * 2048 + k * 1024); } while (0)
; #define PG8_WAIT_V(n) asm volatile("s_waitcnt vmcnt(" #n ")" ::: "memory")
; #define PG8_BAR __builtin_amdgcn_s_barrier()
; template <class Epi, class Sched, bool ALIGN_EPI = false, bool SP2 = false>
; __device__ __forceinline__ void gemm_phase(PG8_LAS unsigned char* lds, const Gemm g, const Sched& S, const Epi& E, const bool skip_epi = false) {
;     ...
;             PG8_LDB(B0, 0, 0); PG8_LDB(B1, 0, 1); PG8_SCHED; PG8_LDA(At, 0, 0); PG8_STAGE_A(1, 1, a1, false);
;             PG8_WAIT_V(8); PG8_WAIT_L(0); PG8_BAR; PG8_MMA(0, 0, At, B0); PG8_MMA(0, 1, At, B1); PG8_BAR; PG8_SCHED;
;             PG8_LDA(At, 0, 1); PG8_STAGE(PG8_SB(0, 0), b2, voffB); PG8_STAGE(PG8_SB(0, 1), b2 + hstep, voffB); PG8_STAGE_A(0, 0, a2, true);
;             PG8_WAIT_V(8); PG8_WAIT_L(0); PG8_BAR; PG8_MMA(1, 0, At, B0); PG8_MMA(1, 1, At, B1); PG8_BAR; PG8_SCHED;
;             PG8_LDB(B0, 1, 0); PG8_LDB(B1, 1, 1); PG8_SCHED; PG8_LDA(At, 1, 0); PG8_STAGE_A(0, 1, a2, true);
;             PG8_WAIT_V(8); PG8_WAIT_L(0); PG8_BAR; PG8_MMA(0, 0, At, B0); PG8_MMA(0, 1, At, B1); PG8_BAR; PG8_SCHED;
;             PG8_LDA(At, 1, 1); PG8_STAGE(PG8_SB(1, 0), b3, voffB); PG8_STAGE(PG8_SB(1, 1), b3 + hstep, voffB); PG8_STAGE_A(1, 0, a3, true);
;             PG8_WAIT_V(8); PG8_WAIT_L(0); PG8_BAR; PG8_MMA(1, 0, At, B0); PG8_MMA(1, 1, At, B1); PG8_BAR; PG8_SCHED;
	s_setprio 0
	s_add_i32 s26, s61, s2
	s_add_i32 m0, s26, 0xffffff80
	ds_read_b128 v[200:203], v189 offset:49152
	ds_read_b128 v[204:207], v189 offset:50176
	ds_read_b128 v[208:211], v189 offset:51200
	ds_read_b128 v[212:215], v189 offset:52224
	ds_read_b128 v[216:219], v189 offset:53248
	ds_read_b128 v[220:223], v189 offset:54272
	ds_read_b128 v[224:227], v189 offset:55296
	ds_read_b128 v[230:233], v189 offset:56320
	global_load_lds_dwordx4 v[168:169], off offset:128
	s_add_i32 m0, s26, 0x1f80
	s_add_u32 s24, s24, 0x40080
	s_addc_u32 s25, s25, 0
	s_add_i32 s26, s62, s2
	global_load_lds_dwordx4 v[172:173], off offset:128
	s_mov_b32 m0, s26
	s_nop 0
	global_load_lds_dwordx4 v146, s[24:25]
	s_add_i32 m0, s26, 0x2000
	s_nop 0
	global_load_lds_dwordx4 v142, s[24:25]
	s_add_i32 m0, s36, 0xffffff80
	s_nop 0
	global_load_lds_dwordx4 v[176:177], off offset:128
	s_add_i32 m0, s37, 0xffffff80
	s_nop 0
	global_load_lds_dwordx4 v[234:235], off offset:128
	s_waitcnt vmcnt(8)
	s_waitcnt lgkmcnt(0)
	s_setprio 3
	s_barrier
	s_waitcnt lgkmcnt(0)
	v_mfma_f32_16x16x32_bf16 v[62:65], v[130:133], v[200:203], v[62:65]
	v_mfma_f32_16x16x32_bf16 v[58:61], v[138:141], v[200:203], v[58:61]
	v_mfma_f32_16x16x32_bf16 v[46:49], v[130:133], v[208:211], v[46:49]
	v_mfma_f32_16x16x32_bf16 v[42:45], v[138:141], v[208:211], v[42:45]
	v_mfma_f32_16x16x32_bf16 v[30:33], v[130:133], v[216:219], v[30:33]
	v_mfma_f32_16x16x32_bf16 v[26:29], v[138:141], v[216:219], v[26:29]
	v_mfma_f32_16x16x32_bf16 v[14:17], v[130:133], v[224:227], v[14:17]
	v_mfma_f32_16x16x32_bf16 v[10:13], v[138:141], v[224:227], v[10:13]
	v_mfma_f32_16x16x32_bf16 v[62:65], v[134:137], v[204:207], v[62:65]
	v_mfma_f32_16x16x32_bf16 v[58:61], v[160:163], v[204:207], v[58:61]
	v_mfma_f32_16x16x32_bf16 v[46:49], v[134:137], v[212:215], v[46:49]
	v_mfma_f32_16x16x32_bf16 v[42:45], v[160:163], v[212:215], v[42:45]
	v_mfma_f32_16x16x32_bf16 v[30:33], v[134:137], v[220:223], v[30:33]
	v_mfma_f32_16x16x32_bf16 v[26:29], v[160:163], v[220:223], v[26:29]
	v_mfma_f32_16x16x32_bf16 v[14:17], v[134:137], v[230:233], v[14:17]
	v_mfma_f32_16x16x32_bf16 v[10:13], v[160:163], v[230:233], v[10:13]
	v_mfma_f32_16x16x32_bf16 v[54:57], v[164:167], v[200:203], v[54:57]
	v_mfma_f32_16x16x32_bf16 v[50:53], v[192:195], v[200:203], v[50:53]
	v_mfma_f32_16x16x32_bf16 v[38:41], v[164:167], v[208:211], v[38:41]
	v_mfma_f32_16x16x32_bf16 v[34:37], v[192:195], v[208:211], v[34:37]
	v_mfma_f32_16x16x32_bf16 v[22:25], v[164:167], v[216:219], v[22:25]
	v_mfma_f32_16x16x32_bf16 v[18:21], v[192:195], v[216:219], v[18:21]
	v_mfma_f32_16x16x32_bf16 v[6:9], v[164:167], v[224:227], v[6:9]
	v_mfma_f32_16x16x32_bf16 v[2:5], v[192:195], v[224:227], v[2:5]
	v_mfma_f32_16x16x32_bf16 v[54:57], v[182:185], v[204:207], v[54:57]
	v_mfma_f32_16x16x32_bf16 v[50:53], v[196:199], v[204:207], v[50:53]
	v_mfma_f32_16x16x32_bf16 v[38:41], v[182:185], v[212:215], v[38:41]
	v_mfma_f32_16x16x32_bf16 v[34:37], v[196:199], v[212:215], v[34:37]
	v_mfma_f32_16x16x32_bf16 v[22:25], v[182:185], v[220:223], v[22:25]
	v_mfma_f32_16x16x32_bf16 v[18:21], v[196:199], v[220:223], v[18:21]
	v_mfma_f32_16x16x32_bf16 v[6:9], v[182:185], v[230:233], v[6:9]
	v_mfma_f32_16x16x32_bf16 v[2:5], v[196:199], v[230:233], v[2:5]
	s_barrier
	s_setprio 0
	s_add_i32 s60, s60, 2
	s_add_u32 s22, s22, 0x100
	s_addc_u32 s23, s23, 0
	s_add_u32 s58, s58, 0x100
	s_addc_u32 s59, s59, 0
	s_cmp_gt_u32 s60, 13
.LBB0_721:
	ds_read_b128 v[130:133], v187
	ds_read_b128 v[134:137], v187 offset:1024
	ds_read_b128 v[138:141], v187 offset:2048
	ds_read_b128 v[160:163], v187 offset:3072
	ds_read_b128 v[164:167], v188
	ds_read_b128 v[182:185], v188 offset:1024
	ds_read_b128 v[192:195], v188 offset:2048
	ds_read_b128 v[196:199], v188 offset:3072
	s_add_u32 s24, s22, 0xfffc0080
	s_addc_u32 s25, s23, -1
	s_cmp_eq_u32 s60, 12
	s_cselect_b32 s27, s15, s25
	s_cselect_b32 s26, s56, s24
	s_cselect_b32 s25, s13, s59
	s_cselect_b32 s24, s57, s58
	s_add_i32 m0, s29, 0xc000
	ds_read_b128 v[200:203], v189
	ds_read_b128 v[204:207], v189 offset:1024
	ds_read_b128 v[208:211], v189 offset:2048
	ds_read_b128 v[212:215], v189 offset:3072
	ds_read_b128 v[216:219], v189 offset:4096
	ds_read_b128 v[220:223], v189 offset:5120
	ds_read_b128 v[224:227], v189 offset:6144
	ds_read_b128 v[230:233], v189 offset:7168
	global_load_lds_dwordx4 v152, s[22:23]
	s_add_i32 m0, s29, 0xe000
	s_nop 0
	global_load_lds_dwordx4 v154, s[22:23]
	s_waitcnt vmcnt(8)
	s_waitcnt lgkmcnt(0)
	s_setprio 3
	s_barrier
	s_waitcnt lgkmcnt(0)
	v_mfma_f32_16x16x32_bf16 v[126:129], v[130:133], v[200:203], v[126:129]
	v_mfma_f32_16x16x32_bf16 v[122:125], v[138:141], v[200:203], v[122:125]
	v_mfma_f32_16x16x32_bf16 v[110:113], v[130:133], v[208:211], v[110:113]
	v_mfma_f32_16x16x32_bf16 v[106:109], v[138:141], v[208:211], v[106:109]
	v_mfma_f32_16x16x32_bf16 v[94:97], v[130:133], v[216:219], v[94:97]
	v_mfma_f32_16x16x32_bf16 v[90:93], v[138:141], v[216:219], v[90:93]
	v_mfma_f32_16x16x32_bf16 v[78:81], v[130:133], v[224:227], v[78:81]
	v_mfma_f32_16x16x32_bf16 v[74:77], v[138:141], v[224:227], v[74:77]
	v_mfma_f32_16x16x32_bf16 v[126:129], v[134:137], v[204:207], v[126:129]
	v_mfma_f32_16x16x32_bf16 v[122:125], v[160:163], v[204:207], v[122:125]
	v_mfma_f32_16x16x32_bf16 v[110:113], v[134:137], v[212:215], v[110:113]
	v_mfma_f32_16x16x32_bf16 v[106:109], v[160:163], v[212:215], v[106:109]
	v_mfma_f32_16x16x32_bf16 v[94:97], v[134:137], v[220:223], v[94:97]
	v_mfma_f32_16x16x32_bf16 v[90:93], v[160:163], v[220:223], v[90:93]
	v_mfma_f32_16x16x32_bf16 v[78:81], v[134:137], v[230:233], v[78:81]
	v_mfma_f32_16x16x32_bf16 v[74:77], v[160:163], v[230:233], v[74:77]
	v_mfma_f32_16x16x32_bf16 v[118:121], v[164:167], v[200:203], v[118:121]
	v_mfma_f32_16x16x32_bf16 v[114:117], v[192:195], v[200:203], v[114:117]
	v_mfma_f32_16x16x32_bf16 v[102:105], v[164:167], v[208:211], v[102:105]
	v_mfma_f32_16x16x32_bf16 v[98:101], v[192:195], v[208:211], v[98:101]
	v_mfma_f32_16x16x32_bf16 v[86:89], v[164:167], v[216:219], v[86:89]
	v_mfma_f32_16x16x32_bf16 v[82:85], v[192:195], v[216:219], v[82:85]
	v_mfma_f32_16x16x32_bf16 v[70:73], v[164:167], v[224:227], v[70:73]
	v_mfma_f32_16x16x32_bf16 v[66:69], v[192:195], v[224:227], v[66:69]
	v_mfma_f32_16x16x32_bf16 v[118:121], v[182:185], v[204:207], v[118:121]
	v_mfma_f32_16x16x32_bf16 v[114:117], v[196:199], v[204:207], v[114:117]
	v_mfma_f32_16x16x32_bf16 v[102:105], v[182:185], v[212:215], v[102:105]
	v_mfma_f32_16x16x32_bf16 v[98:101], v[196:199], v[212:215], v[98:101]
	v_mfma_f32_16x16x32_bf16 v[86:89], v[182:185], v[220:223], v[86:89]
	v_mfma_f32_16x16x32_bf16 v[82:85], v[196:199], v[220:223], v[82:85]
	v_mfma_f32_16x16x32_bf16 v[70:73], v[182:185], v[230:233], v[70:73]
	v_mfma_f32_16x16x32_bf16 v[66:69], v[196:199], v[230:233], v[66:69]
	s_barrier
; #define PG8_STAGE_A(b, h, ptr, NX) do { if constexpr (Sched::GATHER) { unsigned gs_[2]; gs_[0] = ((NX) && last_) ? gN[h][0] : gA[h][0]; gs_[1] = ((NX) && last_) ? gN[h][1] : gA[h][1]; PG8_STAGE(PG8_SA(b, h), ptr, gs_); } \
;         else PG8_STAGE(PG8_SA(b, h), (ptr) + ((h) ? hstep : (size_t)0), voffA); } while (0)
; #define PG8_STAGE(bufoff, gbase, voff) do { _Pragma("unroll") for (int _i = 0; _i < 2; ++_i) \
;         __builtin_amdgcn_global_load_lds((const unsigned*)((const char*)(gbase) + (voff)[_i]), (PG8_LAS unsigned*)(lds + (bufoff) + ldsw + _i * 8192), 16, 0, 0); } while (0)
; #define PG8_LDA(dst, b, h) do { _Pragma("unroll") for (int m = 0; m < 4; ++m) _Pragma("unroll") for (int k = 0; k < 2; ++k) dst[m][k] = *(const PG8_LAS bf16x8*)(lds + PG8_SA(b, h) + aoff + m * 2048 + k * 1024); } while (0)
; #define PG8_LDB(dst, b, h) do { _Pragma("unroll") for (int n = 0; n < 2; ++n) _Pragma("unroll") for (int k = 0; k < 2; ++k) dst[n][k] = *(const PG8_LAS bf16x8*)(lds + PG8_SB(b, h) + boff + n * 2048 + k * 1024); } while (0)
; #define PG8_MMA(ai, bj, At, Bt) do { __builtin_amdgcn_s_setprio(1); _Pragma("unroll") for (int m = 0; m < 4; ++m) _Pragma("unroll") for (int n = 0; n < 2; ++n) _Pragma("unroll") for (int k = 0; k < 2; ++k) \
;         acc[ai][bj][m][n] = __builtin_amdgcn_mfma_f32_16x16x32_bf16(Bt[n][k], At[m][k], acc[ai][bj][m][n], 0, 0, 0); __builtin_amdgcn_s_setprio(0); } while (0)
; #define PG8_WAIT_V(n) asm volatile("s_waitcnt vmcnt(" #n ")" ::: "memory")
; #define PG8_WAIT_L(n) asm volatile("s_waitcnt lgkmcnt(" #n ")" ::: "memory")
; #define PG8_BAR __builtin_amdgcn_s_barrier()
; #define PG8_SCHED __builtin_amdgcn_sched_barrier(0)
; template <class Epi, class Sched, bool ALIGN_EPI = false, bool SP2 = false>
; __device__ __forceinline__ void gemm_phase(PG8_LAS unsigned char* lds, const Gemm g, const Sched& S, const Epi& E, const bool skip_epi = false) {
;     ...
;             PG8_LDA(At, 0, 1); PG8_STAGE(PG8_SB(0, 0), b2, voffB); PG8_STAGE(PG8_SB(0, 1), b2 + hstep, voffB); PG8_STAGE_A(0, 0, a2, true);
;             PG8_WAIT_V(8); PG8_WAIT_L(0); PG8_BAR; PG8_MMA(1, 0, At, B0); PG8_MMA(1, 1, At, B1); PG8_BAR; PG8_SCHED;
;             PG8_LDB(B0, 1, 0); PG8_LDB(B1, 1, 1); PG8_SCHED; PG8_LDA(At, 1, 0); PG8_STAGE_A(0, 1, a2, true);
;             PG8_WAIT_V(8); PG8_WAIT_L(0); PG8_BAR; PG8_MMA(0, 0, At, B0); PG8_MMA(0, 1, At, B1); PG8_BAR; PG8_SCHED;
	s_setprio 0
	s_add_i32 s61, s39, s2
	v_lshl_add_u64 v[168:169], s[24:25], 0, v[146:147]
	s_mov_b32 m0, s61
	ds_read_b128 v[200:203], v189 offset:16384
	ds_read_b128 v[204:207], v189 offset:17408
	ds_read_b128 v[208:211], v189 offset:18432
	ds_read_b128 v[212:215], v189 offset:19456
	ds_read_b128 v[216:219], v189 offset:20480
	ds_read_b128 v[220:223], v189 offset:21504
	ds_read_b128 v[224:227], v189 offset:22528
	ds_read_b128 v[230:233], v189 offset:23552
	global_load_lds_dwordx4 v[168:169], off
	s_add_i32 m0, s61, 0x2000
	s_add_u32 s62, s24, 0x40000
	v_lshl_add_u64 v[172:173], s[24:25], 0, v[142:143]
	s_addc_u32 s63, s25, 0
	s_add_i32 s61, s48, s2
	global_load_lds_dwordx4 v[172:173], off
	s_mov_b32 m0, s61
	v_lshl_add_u64 v[234:235], s[26:27], 0, v[144:145]
	global_load_lds_dwordx4 v146, s[62:63]
	s_add_i32 m0, s61, 0x2000
	s_nop 0
	global_load_lds_dwordx4 v142, s[62:63]
	v_lshl_add_u64 v[176:177], s[26:27], 0, v[148:149]
	s_mov_b32 m0, s29
	s_nop 0
	global_load_lds_dwordx4 v[176:177], off
	s_mov_b32 m0, s30
	s_nop 0
	global_load_lds_dwordx4 v[234:235], off
	s_waitcnt vmcnt(8)
	s_waitcnt lgkmcnt(0)
	s_setprio 3
	s_barrier
	s_waitcnt lgkmcnt(0)
	v_mfma_f32_16x16x32_bf16 v[62:65], v[130:133], v[200:203], v[62:65]
	v_mfma_f32_16x16x32_bf16 v[58:61], v[138:141], v[200:203], v[58:61]
	v_mfma_f32_16x16x32_bf16 v[46:49], v[130:133], v[208:211], v[46:49]
	v_mfma_f32_16x16x32_bf16 v[42:45], v[138:141], v[208:211], v[42:45]
	v_mfma_f32_16x16x32_bf16 v[30:33], v[130:133], v[216:219], v[30:33]
	v_mfma_f32_16x16x32_bf16 v[26:29], v[138:141], v[216:219], v[26:29]
	v_mfma_f32_16x16x32_bf16 v[14:17], v[130:133], v[224:227], v[14:17]
	v_mfma_f32_16x16x32_bf16 v[10:13], v[138:141], v[224:227], v[10:13]
	v_mfma_f32_16x16x32_bf16 v[62:65], v[134:137], v[204:207], v[62:65]
	v_mfma_f32_16x16x32_bf16 v[58:61], v[160:163], v[204:207], v[58:61]
	v_mfma_f32_16x16x32_bf16 v[46:49], v[134:137], v[212:215], v[46:49]
	v_mfma_f32_16x16x32_bf16 v[42:45], v[160:163], v[212:215], v[42:45]
	v_mfma_f32_16x16x32_bf16 v[30:33], v[134:137], v[220:223], v[30:33]
	v_mfma_f32_16x16x32_bf16 v[26:29], v[160:163], v[220:223], v[26:29]
	v_mfma_f32_16x16x32_bf16 v[14:17], v[134:137], v[230:233], v[14:17]
	v_mfma_f32_16x16x32_bf16 v[10:13], v[160:163], v[230:233], v[10:13]
	v_mfma_f32_16x16x32_bf16 v[54:57], v[164:167], v[200:203], v[54:57]
	v_mfma_f32_16x16x32_bf16 v[50:53], v[192:195], v[200:203], v[50:53]
	v_mfma_f32_16x16x32_bf16 v[38:41], v[164:167], v[208:211], v[38:41]
	v_mfma_f32_16x16x32_bf16 v[34:37], v[192:195], v[208:211], v[34:37]
	v_mfma_f32_16x16x32_bf16 v[22:25], v[164:167], v[216:219], v[22:25]
	v_mfma_f32_16x16x32_bf16 v[18:21], v[192:195], v[216:219], v[18:21]
	v_mfma_f32_16x16x32_bf16 v[6:9], v[164:167], v[224:227], v[6:9]
	v_mfma_f32_16x16x32_bf16 v[2:5], v[192:195], v[224:227], v[2:5]
	v_mfma_f32_16x16x32_bf16 v[54:57], v[182:185], v[204:207], v[54:57]
	v_mfma_f32_16x16x32_bf16 v[50:53], v[196:199], v[204:207], v[50:53]
	v_mfma_f32_16x16x32_bf16 v[38:41], v[182:185], v[212:215], v[38:41]
	v_mfma_f32_16x16x32_bf16 v[34:37], v[196:199], v[212:215], v[34:37]
	v_mfma_f32_16x16x32_bf16 v[22:25], v[182:185], v[220:223], v[22:25]
	v_mfma_f32_16x16x32_bf16 v[18:21], v[196:199], v[220:223], v[18:21]
	v_mfma_f32_16x16x32_bf16 v[6:9], v[182:185], v[230:233], v[6:9]
	v_mfma_f32_16x16x32_bf16 v[2:5], v[196:199], v[230:233], v[2:5]
	s_barrier
	s_setprio 0
	s_add_i32 s61, 0, 0x18000
	s_add_i32 s62, 0, 0x1c000
	v_add_u32_e32 v160, s61, v1
	v_add_u32_e32 v170, s62, v1
	ds_read_b128 v[130:133], v160
	ds_read_b128 v[134:137], v160 offset:1024
	ds_read_b128 v[138:141], v160 offset:2048
	ds_read_b128 v[160:163], v160 offset:3072
	ds_read_b128 v[164:167], v170
	ds_read_b128 v[182:185], v170 offset:1024
	ds_read_b128 v[192:195], v170 offset:2048
	ds_read_b128 v[196:199], v170 offset:3072
	s_add_u32 s26, s26, 0x40000
	s_addc_u32 s27, s27, 0
	s_mov_b32 m0, s31
	ds_read_b128 v[200:203], v189 offset:32768
	ds_read_b128 v[204:207], v189 offset:33792
	ds_read_b128 v[208:211], v189 offset:34816
	ds_read_b128 v[212:215], v189 offset:35840
	ds_read_b128 v[216:219], v189 offset:36864
	ds_read_b128 v[220:223], v189 offset:37888
	ds_read_b128 v[224:227], v189 offset:38912
	ds_read_b128 v[230:233], v189 offset:39936
	global_load_lds_dwordx4 v148, s[26:27]
	s_mov_b32 m0, s34
	s_nop 0
	global_load_lds_dwordx4 v144, s[26:27]
	s_waitcnt vmcnt(8)
	s_waitcnt lgkmcnt(0)
	s_setprio 3
	s_barrier
; #define PG8_STAGE_A(b, h, ptr, NX) do { if constexpr (Sched::GATHER) { unsigned gs_[2]; gs_[0] = ((NX) && last_) ? gN[h][0] : gA[h][0]; gs_[1] = ((NX) && last_) ? gN[h][1] : gA[h][1]; PG8_STAGE(PG8_SA(b, h), ptr, gs_); } \
;         else PG8_STAGE(PG8_SA(b, h), (ptr) + ((h) ? hstep : (size_t)0), voffA); } while (0)
; #define PG8_STAGE(bufoff, gbase, voff) do { _Pragma("unroll") for (int _i = 0; _i < 2; ++_i) \
;         __builtin_amdgcn_global_load_lds((const unsigned*)((const char*)(gbase) + (voff)[_i]), (PG8_LAS unsigned*)(lds + (bufoff) + ldsw + _i * 8192), 16, 0, 0); } while (0)
; #define PG8_LDA(dst, b, h) do { _Pragma("unroll") for (int m = 0; m < 4; ++m) _Pragma("unroll") for (int k = 0; k < 2; ++k) dst[m][k] = *(const PG8_LAS bf16x8*)(lds + PG8_SA(b, h) + aoff + m * 2048 + k * 1024); } while (0)
; #define PG8_MMA(ai, bj, At, Bt) do { __builtin_amdgcn_s_setprio(1); _Pragma("unroll") for (int m = 0; m < 4; ++m) _Pragma("unroll") for (int n = 0; n < 2; ++n) _Pragma("unroll") for (int k = 0; k < 2; ++k) \
;         acc[ai][bj][m][n] = __builtin_amdgcn_mfma_f32_16x16x32_bf16(Bt[n][k], At[m][k], acc[ai][bj][m][n], 0, 0, 0); __builtin_amdgcn_s_setprio(0); } while (0)
; #define PG8_WAIT_V(n) asm volatile("s_waitcnt vmcnt(" #n ")" ::: "memory")
; #define PG8_WAIT_L(n) asm volatile("s_waitcnt lgkmcnt(" #n ")" ::: "memory")
; #define PG8_BAR __builtin_amdgcn_s_barrier()
; #define PG8_SCHED __builtin_amdgcn_sched_barrier(0)
; template <class Epi, class Sched, bool ALIGN_EPI = false, bool SP2 = false>
; __device__ __forceinline__ void gemm_phase(PG8_LAS unsigned char* lds, const Gemm g, const Sched& S, const Epi& E, const bool skip_epi = false) {
;     ...
;             PG8_WAIT_V(8); PG8_WAIT_L(0); PG8_BAR; PG8_MMA(0, 0, At, B0); PG8_MMA(0, 1, At, B1); PG8_BAR; PG8_SCHED;
;             PG8_LDA(At, 1, 1); PG8_STAGE(PG8_SB(1, 0), b3, voffB); PG8_STAGE(PG8_SB(1, 1), b3 + hstep, voffB); PG8_STAGE_A(1, 0, a3, true);
;             PG8_WAIT_V(8); PG8_WAIT_L(0); PG8_BAR; PG8_MMA(1, 0, At, B0); PG8_MMA(1, 1, At, B1); PG8_BAR; PG8_SCHED;
;     ...
;         if constexpr (ALIGN_EPI) { if (wr == 0) PG8_BAR; }
	s_waitcnt lgkmcnt(0)
	v_mfma_f32_16x16x32_bf16 v[126:129], v[130:133], v[200:203], v[126:129]
	v_mfma_f32_16x16x32_bf16 v[122:125], v[138:141], v[200:203], v[122:125]
	v_mfma_f32_16x16x32_bf16 v[110:113], v[130:133], v[208:211], v[110:113]
	v_mfma_f32_16x16x32_bf16 v[106:109], v[138:141], v[208:211], v[106:109]
	v_mfma_f32_16x16x32_bf16 v[94:97], v[130:133], v[216:219], v[94:97]
	v_mfma_f32_16x16x32_bf16 v[90:93], v[138:141], v[216:219], v[90:93]
	v_mfma_f32_16x16x32_bf16 v[78:81], v[130:133], v[224:227], v[78:81]
	v_mfma_f32_16x16x32_bf16 v[74:77], v[138:141], v[224:227], v[74:77]
	v_mfma_f32_16x16x32_bf16 v[126:129], v[134:137], v[204:207], v[126:129]
	v_mfma_f32_16x16x32_bf16 v[122:125], v[160:163], v[204:207], v[122:125]
	v_mfma_f32_16x16x32_bf16 v[110:113], v[134:137], v[212:215], v[110:113]
	v_mfma_f32_16x16x32_bf16 v[106:109], v[160:163], v[212:215], v[106:109]
	v_mfma_f32_16x16x32_bf16 v[94:97], v[134:137], v[220:223], v[94:97]
	v_mfma_f32_16x16x32_bf16 v[90:93], v[160:163], v[220:223], v[90:93]
	v_mfma_f32_16x16x32_bf16 v[78:81], v[134:137], v[230:233], v[78:81]
	v_mfma_f32_16x16x32_bf16 v[74:77], v[160:163], v[230:233], v[74:77]
	v_mfma_f32_16x16x32_bf16 v[118:121], v[164:167], v[200:203], v[118:121]
	v_mfma_f32_16x16x32_bf16 v[114:117], v[192:195], v[200:203], v[114:117]
	v_mfma_f32_16x16x32_bf16 v[102:105], v[164:167], v[208:211], v[102:105]
	v_mfma_f32_16x16x32_bf16 v[98:101], v[192:195], v[208:211], v[98:101]
	v_mfma_f32_16x16x32_bf16 v[86:89], v[164:167], v[216:219], v[86:89]
	v_mfma_f32_16x16x32_bf16 v[82:85], v[192:195], v[216:219], v[82:85]
	v_mfma_f32_16x16x32_bf16 v[70:73], v[164:167], v[224:227], v[70:73]
	v_mfma_f32_16x16x32_bf16 v[66:69], v[192:195], v[224:227], v[66:69]
	v_mfma_f32_16x16x32_bf16 v[118:121], v[182:185], v[204:207], v[118:121]
	v_mfma_f32_16x16x32_bf16 v[114:117], v[196:199], v[204:207], v[114:117]
	v_mfma_f32_16x16x32_bf16 v[102:105], v[182:185], v[212:215], v[102:105]
	v_mfma_f32_16x16x32_bf16 v[98:101], v[196:199], v[212:215], v[98:101]
	v_mfma_f32_16x16x32_bf16 v[86:89], v[182:185], v[220:223], v[86:89]
	v_mfma_f32_16x16x32_bf16 v[82:85], v[196:199], v[220:223], v[82:85]
	v_mfma_f32_16x16x32_bf16 v[70:73], v[182:185], v[230:233], v[70:73]
	v_mfma_f32_16x16x32_bf16 v[66:69], v[196:199], v[230:233], v[66:69]
	s_barrier
	s_setprio 0
	s_add_i32 s26, s61, s2
	s_add_i32 m0, s26, 0xffffff80
	ds_read_b128 v[200:203], v189 offset:49152
	ds_read_b128 v[204:207], v189 offset:50176
	ds_read_b128 v[208:211], v189 offset:51200
	ds_read_b128 v[212:215], v189 offset:52224
	ds_read_b128 v[216:219], v189 offset:53248
	ds_read_b128 v[220:223], v189 offset:54272
	ds_read_b128 v[224:227], v189 offset:55296
	ds_read_b128 v[230:233], v189 offset:56320
	global_load_lds_dwordx4 v[168:169], off offset:128
	s_add_i32 m0, s26, 0x1f80
	s_add_u32 s24, s24, 0x40080
	s_addc_u32 s25, s25, 0
	s_add_i32 s26, s62, s2
	global_load_lds_dwordx4 v[172:173], off offset:128
	s_mov_b32 m0, s26
	s_nop 0
	global_load_lds_dwordx4 v146, s[24:25]
	s_add_i32 m0, s26, 0x2000
	s_nop 0
	global_load_lds_dwordx4 v142, s[24:25]
	s_add_i32 m0, s36, 0xffffff80
	s_nop 0
	global_load_lds_dwordx4 v[176:177], off offset:128
	s_add_i32 m0, s37, 0xffffff80
	s_nop 0
	global_load_lds_dwordx4 v[234:235], off offset:128
	s_waitcnt vmcnt(8)
	s_waitcnt lgkmcnt(0)
	s_setprio 3
	s_barrier
	s_waitcnt lgkmcnt(0)
	v_mfma_f32_16x16x32_bf16 v[62:65], v[130:133], v[200:203], v[62:65]
	v_mfma_f32_16x16x32_bf16 v[58:61], v[138:141], v[200:203], v[58:61]
	v_mfma_f32_16x16x32_bf16 v[46:49], v[130:133], v[208:211], v[46:49]
	v_mfma_f32_16x16x32_bf16 v[42:45], v[138:141], v[208:211], v[42:45]
	v_mfma_f32_16x16x32_bf16 v[30:33], v[130:133], v[216:219], v[30:33]
	v_mfma_f32_16x16x32_bf16 v[26:29], v[138:141], v[216:219], v[26:29]
	v_mfma_f32_16x16x32_bf16 v[14:17], v[130:133], v[224:227], v[14:17]
	v_mfma_f32_16x16x32_bf16 v[10:13], v[138:141], v[224:227], v[10:13]
	v_mfma_f32_16x16x32_bf16 v[62:65], v[134:137], v[204:207], v[62:65]
	v_mfma_f32_16x16x32_bf16 v[58:61], v[160:163], v[204:207], v[58:61]
	v_mfma_f32_16x16x32_bf16 v[46:49], v[134:137], v[212:215], v[46:49]
	v_mfma_f32_16x16x32_bf16 v[42:45], v[160:163], v[212:215], v[42:45]
	v_mfma_f32_16x16x32_bf16 v[30:33], v[134:137], v[220:223], v[30:33]
	v_mfma_f32_16x16x32_bf16 v[26:29], v[160:163], v[220:223], v[26:29]
	v_mfma_f32_16x16x32_bf16 v[14:17], v[134:137], v[230:233], v[14:17]
	v_mfma_f32_16x16x32_bf16 v[10:13], v[160:163], v[230:233], v[10:13]
	v_mfma_f32_16x16x32_bf16 v[54:57], v[164:167], v[200:203], v[54:57]
	v_mfma_f32_16x16x32_bf16 v[50:53], v[192:195], v[200:203], v[50:53]
	v_mfma_f32_16x16x32_bf16 v[38:41], v[164:167], v[208:211], v[38:41]
	v_mfma_f32_16x16x32_bf16 v[34:37], v[192:195], v[208:211], v[34:37]
	v_mfma_f32_16x16x32_bf16 v[22:25], v[164:167], v[216:219], v[22:25]
	v_mfma_f32_16x16x32_bf16 v[18:21], v[192:195], v[216:219], v[18:21]
	v_mfma_f32_16x16x32_bf16 v[6:9], v[164:167], v[224:227], v[6:9]
	v_mfma_f32_16x16x32_bf16 v[2:5], v[192:195], v[224:227], v[2:5]
	v_mfma_f32_16x16x32_bf16 v[54:57], v[182:185], v[204:207], v[54:57]
	v_mfma_f32_16x16x32_bf16 v[50:53], v[196:199], v[204:207], v[50:53]
	v_mfma_f32_16x16x32_bf16 v[38:41], v[182:185], v[212:215], v[38:41]
	v_mfma_f32_16x16x32_bf16 v[34:37], v[196:199], v[212:215], v[34:37]
	v_mfma_f32_16x16x32_bf16 v[22:25], v[182:185], v[220:223], v[22:25]
	v_mfma_f32_16x16x32_bf16 v[18:21], v[196:199], v[220:223], v[18:21]
	v_mfma_f32_16x16x32_bf16 v[6:9], v[182:185], v[230:233], v[6:9]
	v_mfma_f32_16x16x32_bf16 v[2:5], v[196:199], v[230:233], v[2:5]
	s_barrier
	s_setprio 0
	s_add_i32 s60, s60, 2
	s_add_u32 s22, s22, 0x100
	s_addc_u32 s23, s23, 0
	s_add_u32 s58, s58, 0x100
	s_addc_u32 s59, s59, 0
	s_cmp_gt_u32 s60, 13
	s_cbranch_scc0 .LBB0_721
	s_and_b64 vcc, exec, s[10:11]
	s_cbranch_vccz .LBB0_724
	s_barrier

; #define PG8_GIDX(G_, PM_) do { if constexpr (Sched::GATHER) { _Pragma("unroll") for (int h_ = 0; h_ < 2; ++h_) _Pragma("unroll") for (int i_ = 0; i_ < 2; ++i_) { int R_, C_; stage_rc(tid * 16 + i_ * 8192, R_, C_); \
;         const int src_ = S.rowsrc[(PM_) * BM + h_ * HALF + R_]; G_[h_][i_] = (unsigned)(src_ * K + C_) * 2u; } } } while (0)
; #define PG8_STAGE_A(b, h, ptr, NX) do { if constexpr (Sched::GATHER) { unsigned gs_[2]; gs_[0] = ((NX) && last_) ? gN[h][0] : gA[h][0]; gs_[1] = ((NX) && last_) ? gN[h][1] : gA[h][1]; PG8_STAGE(PG8_SA(b, h), ptr, gs_); } \
;         else PG8_STAGE(PG8_SA(b, h), (ptr) + ((h) ? hstep : (size_t)0), voffA); } while (0)
; #define PG8_LDA(dst, b, h) do { _Pragma("unroll") for (int m = 0; m < 4; ++m) _Pragma("unroll") for (int k = 0; k < 2; ++k) dst[m][k] = *(const PG8_LAS bf16x8*)(lds + PG8_SA(b, h) + aoff + m * 2048 + k * 1024); } while (0)
; template <class Epi, class Sched, bool ALIGN_EPI = false, bool SP2 = false>
; __device__ __forceinline__ void gemm_phase(PG8_LAS unsigned char* lds, const Gemm g, const Sched& S, const Epi& E, const bool skip_epi = false) {
;     ...
;         const bool has_next = S.next(ui + 1, nxt);
;         if (has_next) PG8_GIDX(gN, nxt.pm);
;         const char* nA = has_next ? (const char*)g.A + (size_t)nxt.pm * pmstepA + nxt.ko : cA; const char* nB = has_next ? (const char*)g.Bt + (size_t)nxt.pn * tstep + nxt.ko : cB;
;         for (int t = 0; t < nt; t += 2) {
;             const bool last = (t == nt - 2); last_ = last && has_next;
;             const char* a1 = cA + (size_t)(t + 1) * kstep;
;             const char* a2 = last ? nA : cA + (size_t)(t + 2) * kstep; const char* b2 = last ? nB : cB + (size_t)(t + 2) * kstep;
;             const char* a3 = a2 + kstep; const char* b3 = b2 + kstep;
;             if (last && has_next) S.a_ready(nxt);
;             if constexpr (SP2) {
;             PG8_LDB(B0, 0, 0); PG8_LDB(B1, 0, 1); PG8_SCHED; PG8_LDA(At, 0, 0); PG8_STAGE_A(1, 1, a1, false);
;             PG8_WAIT_V(8); PG8_WAIT_L(0); PG8_BAR; PG8_MMA(0, 0, At, B0); PG8_MMA(0, 1, At, B1); PG8_BAR; PG8_SCHED;
;             PG8_LDA(At, 0, 1); PG8_STAGE(PG8_SB(0, 0), b2, voffB); PG8_STAGE(PG8_SB(0, 1), b2 + hstep, voffB); PG8_STAGE_A(0, 0, a2, true);
;             PG8_WAIT_V(8); PG8_WAIT_L(0); PG8_BAR; PG8_MMA(1, 0, At, B0); PG8_MMA(1, 1, At, B1); PG8_BAR; PG8_SCHED;
.LBB0_856:
	s_add_u32 s55, s22, 0x100
	s_addc_u32 s56, s23, 0
	s_mov_b32 s57, -2
	s_waitcnt vmcnt(0)
	s_waitcnt lgkmcnt(0)
	ds_read_b128 v[98:101], v234
	ds_read_b128 v[110:113], v234 offset:1024
	ds_read_b128 v[122:125], v234 offset:2048
	ds_read_b128 v[126:129], v234 offset:3072
	ds_read_b128 v[138:141], v235
	ds_read_b128 v[142:145], v235 offset:1024
	ds_read_b128 v[146:149], v235 offset:2048
	ds_read_b128 v[150:153], v235 offset:3072
	s_add_u32 s22, s20, 0x100
	s_addc_u32 s23, s21, 0
	s_cmp_eq_u32 s57, 40
	s_cselect_b32 s27, s9, s23
	s_cselect_b32 s26, s8, s22
	s_cselect_b32 s25, s19, s56
	s_cselect_b32 s24, s18, s55
	v_lshl_add_u64 v[210:211], s[20:21], 0, v[198:199]
	s_add_i32 m0, s3, 0xc000
	ds_read_b128 v[154:157], v236
	ds_read_b128 v[166:169], v236 offset:1024
	ds_read_b128 v[170:173], v236 offset:2048
	ds_read_b128 v[174:177], v236 offset:3072
	ds_read_b128 v[178:181], v236 offset:4096
	ds_read_b128 v[182:185], v236 offset:5120
	ds_read_b128 v[186:189], v236 offset:6144
	ds_read_b128 v[206:209], v236 offset:7168
	global_load_lds_dwordx4 v[210:211], off
	v_lshl_add_u64 v[210:211], s[20:21], 0, v[200:201]
	s_add_i32 m0, s3, 0xe000
	s_nop 0
	global_load_lds_dwordx4 v[210:211], off
	s_waitcnt vmcnt(8)
	s_waitcnt lgkmcnt(0)
	s_setprio 3
	s_barrier
	s_waitcnt lgkmcnt(0)
	v_mfma_f32_16x16x32_bf16 v[162:165], v[98:101], v[154:157], 0
	v_mfma_f32_16x16x32_bf16 v[158:161], v[122:125], v[154:157], 0
	v_mfma_f32_16x16x32_bf16 v[118:121], v[98:101], v[170:173], 0
	v_mfma_f32_16x16x32_bf16 v[114:117], v[122:125], v[170:173], 0
	v_mfma_f32_16x16x32_bf16 v[94:97], v[98:101], v[178:181], 0
	v_mfma_f32_16x16x32_bf16 v[90:93], v[122:125], v[178:181], 0
	v_mfma_f32_16x16x32_bf16 v[78:81], v[98:101], v[186:189], 0
	v_mfma_f32_16x16x32_bf16 v[74:77], v[122:125], v[186:189], 0
	v_mfma_f32_16x16x32_bf16 v[162:165], v[110:113], v[166:169], v[162:165]
	v_mfma_f32_16x16x32_bf16 v[158:161], v[126:129], v[166:169], v[158:161]
	v_mfma_f32_16x16x32_bf16 v[118:121], v[110:113], v[174:177], v[118:121]
	v_mfma_f32_16x16x32_bf16 v[114:117], v[126:129], v[174:177], v[114:117]
	v_mfma_f32_16x16x32_bf16 v[94:97], v[110:113], v[182:185], v[94:97]
	v_mfma_f32_16x16x32_bf16 v[90:93], v[126:129], v[182:185], v[90:93]
	v_mfma_f32_16x16x32_bf16 v[78:81], v[110:113], v[206:209], v[78:81]
	v_mfma_f32_16x16x32_bf16 v[74:77], v[126:129], v[206:209], v[74:77]
	v_mfma_f32_16x16x32_bf16 v[134:137], v[138:141], v[154:157], 0
	v_mfma_f32_16x16x32_bf16 v[130:133], v[146:149], v[154:157], 0
	v_mfma_f32_16x16x32_bf16 v[106:109], v[138:141], v[170:173], 0
	v_mfma_f32_16x16x32_bf16 v[102:105], v[146:149], v[170:173], 0
	v_mfma_f32_16x16x32_bf16 v[86:89], v[138:141], v[178:181], 0
	v_mfma_f32_16x16x32_bf16 v[82:85], v[146:149], v[178:181], 0
	v_mfma_f32_16x16x32_bf16 v[70:73], v[138:141], v[186:189], 0
	v_mfma_f32_16x16x32_bf16 v[66:69], v[146:149], v[186:189], 0
	v_mfma_f32_16x16x32_bf16 v[134:137], v[142:145], v[166:169], v[134:137]
	v_mfma_f32_16x16x32_bf16 v[130:133], v[150:153], v[166:169], v[130:133]
	v_mfma_f32_16x16x32_bf16 v[106:109], v[142:145], v[174:177], v[106:109]
	v_mfma_f32_16x16x32_bf16 v[102:105], v[150:153], v[174:177], v[102:105]
	v_mfma_f32_16x16x32_bf16 v[86:89], v[142:145], v[182:185], v[86:89]
	v_mfma_f32_16x16x32_bf16 v[82:85], v[150:153], v[182:185], v[82:85]
	v_mfma_f32_16x16x32_bf16 v[70:73], v[142:145], v[206:209], v[70:73]
	v_mfma_f32_16x16x32_bf16 v[66:69], v[150:153], v[206:209], v[66:69]
	s_barrier
	s_setprio 0
	s_add_i32 s20, s39, s2
	v_lshl_add_u64 v[210:211], s[24:25], 0, v[192:193]
	s_mov_b32 m0, s20
	ds_read_b128 v[154:157], v236 offset:16384
	ds_read_b128 v[166:169], v236 offset:17408
	ds_read_b128 v[170:173], v236 offset:18432
	ds_read_b128 v[174:177], v236 offset:19456
	ds_read_b128 v[178:181], v236 offset:20480
	ds_read_b128 v[182:185], v236 offset:21504
	ds_read_b128 v[186:189], v236 offset:22528
	ds_read_b128 v[206:209], v236 offset:23552
	global_load_lds_dwordx4 v[210:211], off
	s_add_i32 m0, s20, 0x2000
	s_add_u32 s20, s24, 0xb0000
	v_lshl_add_u64 v[212:213], s[24:25], 0, v[196:197]
	s_addc_u32 s21, s25, 0
	s_add_i32 s58, s48, s2
	global_load_lds_dwordx4 v[212:213], off
	s_mov_b32 m0, s58
	v_lshl_add_u64 v[216:217], s[26:27], 0, v[194:195]
	global_load_lds_dwordx4 v192, s[20:21]
	s_add_i32 m0, s58, 0x2000
	s_nop 0
	global_load_lds_dwordx4 v196, s[20:21]
	v_lshl_add_u64 v[214:215], s[26:27], 0, v[190:191]
	s_mov_b32 m0, s3
	s_nop 0
	global_load_lds_dwordx4 v[214:215], off
	s_mov_b32 m0, s28
	s_nop 0
	global_load_lds_dwordx4 v[216:217], off
	s_waitcnt vmcnt(8)
	s_waitcnt lgkmcnt(0)
	s_setprio 3
	s_barrier
; #define PG8_STAGE_A(b, h, ptr, NX) do { if constexpr (Sched::GATHER) { unsigned gs_[2]; gs_[0] = ((NX) && last_) ? gN[h][0] : gA[h][0]; gs_[1] = ((NX) && last_) ? gN[h][1] : gA[h][1]; PG8_STAGE(PG8_SA(b, h), ptr, gs_); } \
;         else PG8_STAGE(PG8_SA(b, h), (ptr) + ((h) ? hstep : (size_t)0), voffA); } while (0)
; #define PG8_STAGE(bufoff, gbase, voff) do { _Pragma("unroll") for (int _i = 0; _i < 2; ++_i) \
;         __builtin_amdgcn_global_load_lds((const unsigned*)((const char*)(gbase) + (voff)[_i]), (PG8_LAS unsigned*)(lds + (bufoff) + ldsw + _i * 8192), 16, 0, 0); } while (0)
; #define PG8_LDA(dst, b, h) do { _Pragma("unroll") for (int m = 0; m < 4; ++m) _Pragma("unroll") for (int k = 0; k < 2; ++k) dst[m][k] = *(const PG8_LAS bf16x8*)(lds + PG8_SA(b, h) + aoff + m * 2048 + k * 1024); } while (0)
; #define PG8_LDB(dst, b, h) do { _Pragma("unroll") for (int n = 0; n < 2; ++n) _Pragma("unroll") for (int k = 0; k < 2; ++k) dst[n][k] = *(const PG8_LAS bf16x8*)(lds + PG8_SB(b, h) + boff + n * 2048 + k * 1024); } while (0)
; #define PG8_MMA(ai, bj, At, Bt) do { __builtin_amdgcn_s_setprio(1); _Pragma("unroll") for (int m = 0; m < 4; ++m) _Pragma("unroll") for (int n = 0; n < 2; ++n) _Pragma("unroll") for (int k = 0; k < 2; ++k) \
;         acc[ai][bj][m][n] = __builtin_amdgcn_mfma_f32_16x16x32_bf16(Bt[n][k], At[m][k], acc[ai][bj][m][n], 0, 0, 0); __builtin_amdgcn_s_setprio(0); } while (0)
; #define PG8_WAIT_V(n) asm volatile("s_waitcnt vmcnt(" #n ")" ::: "memory")
; #define PG8_WAIT_L(n) asm volatile("s_waitcnt lgkmcnt(" #n ")" ::: "memory")
; #define PG8_BAR __builtin_amdgcn_s_barrier()
; #define PG8_SCHED __builtin_amdgcn_sched_barrier(0)
; template <class Epi, class Sched, bool ALIGN_EPI = false, bool SP2 = false>
; __device__ __forceinline__ void gemm_phase(PG8_LAS unsigned char* lds, const Gemm g, const Sched& S, const Epi& E, const bool skip_epi = false) {
;     ...
;             PG8_WAIT_V(8); PG8_WAIT_L(0); PG8_BAR; PG8_MMA(1, 0, At, B0); PG8_MMA(1, 1, At, B1); PG8_BAR; PG8_SCHED;
;             PG8_LDB(B0, 1, 0); PG8_LDB(B1, 1, 1); PG8_SCHED; PG8_LDA(At, 1, 0); PG8_STAGE_A(0, 1, a2, true);
;             PG8_WAIT_V(8); PG8_WAIT_L(0); PG8_BAR; PG8_MMA(0, 0, At, B0); PG8_MMA(0, 1, At, B1); PG8_BAR; PG8_SCHED;
;             PG8_LDA(At, 1, 1); PG8_STAGE(PG8_SB(1, 0), b3, voffB); PG8_STAGE(PG8_SB(1, 1), b3 + hstep, voffB); PG8_STAGE_A(1, 0, a3, true);
	s_waitcnt lgkmcnt(0)
	v_mfma_f32_16x16x32_bf16 v[62:65], v[98:101], v[154:157], 0
	v_mfma_f32_16x16x32_bf16 v[58:61], v[122:125], v[154:157], 0
	v_mfma_f32_16x16x32_bf16 v[46:49], v[98:101], v[170:173], 0
	v_mfma_f32_16x16x32_bf16 v[42:45], v[122:125], v[170:173], 0
	v_mfma_f32_16x16x32_bf16 v[30:33], v[98:101], v[178:181], 0
	v_mfma_f32_16x16x32_bf16 v[26:29], v[122:125], v[178:181], 0
	v_mfma_f32_16x16x32_bf16 v[14:17], v[98:101], v[186:189], 0
	v_mfma_f32_16x16x32_bf16 v[10:13], v[122:125], v[186:189], 0
	v_mfma_f32_16x16x32_bf16 v[62:65], v[110:113], v[166:169], v[62:65]
	v_mfma_f32_16x16x32_bf16 v[58:61], v[126:129], v[166:169], v[58:61]
	v_mfma_f32_16x16x32_bf16 v[46:49], v[110:113], v[174:177], v[46:49]
	v_mfma_f32_16x16x32_bf16 v[42:45], v[126:129], v[174:177], v[42:45]
	v_mfma_f32_16x16x32_bf16 v[30:33], v[110:113], v[182:185], v[30:33]
	v_mfma_f32_16x16x32_bf16 v[26:29], v[126:129], v[182:185], v[26:29]
	v_mfma_f32_16x16x32_bf16 v[14:17], v[110:113], v[206:209], v[14:17]
	v_mfma_f32_16x16x32_bf16 v[10:13], v[126:129], v[206:209], v[10:13]
	v_mfma_f32_16x16x32_bf16 v[54:57], v[138:141], v[154:157], 0
	v_mfma_f32_16x16x32_bf16 v[50:53], v[146:149], v[154:157], 0
	v_mfma_f32_16x16x32_bf16 v[38:41], v[138:141], v[170:173], 0
	v_mfma_f32_16x16x32_bf16 v[34:37], v[146:149], v[170:173], 0
	v_mfma_f32_16x16x32_bf16 v[22:25], v[138:141], v[178:181], 0
	v_mfma_f32_16x16x32_bf16 v[18:21], v[146:149], v[178:181], 0
	v_mfma_f32_16x16x32_bf16 v[6:9], v[138:141], v[186:189], 0
	v_mfma_f32_16x16x32_bf16 v[2:5], v[146:149], v[186:189], 0
	v_mfma_f32_16x16x32_bf16 v[54:57], v[142:145], v[166:169], v[54:57]
	v_mfma_f32_16x16x32_bf16 v[50:53], v[150:153], v[166:169], v[50:53]
	v_mfma_f32_16x16x32_bf16 v[38:41], v[142:145], v[174:177], v[38:41]
	v_mfma_f32_16x16x32_bf16 v[34:37], v[150:153], v[174:177], v[34:37]
	v_mfma_f32_16x16x32_bf16 v[22:25], v[142:145], v[182:185], v[22:25]
	v_mfma_f32_16x16x32_bf16 v[18:21], v[150:153], v[182:185], v[18:21]
	v_mfma_f32_16x16x32_bf16 v[6:9], v[142:145], v[206:209], v[6:9]
	v_mfma_f32_16x16x32_bf16 v[2:5], v[150:153], v[206:209], v[2:5]
	s_barrier
	s_setprio 0
	s_add_i32 s58, 0, 0x18000
	s_add_i32 s59, 0, 0x1c000
	v_add_u32_e32 v126, s58, v229
	v_add_u32_e32 v150, s59, v229
	ds_read_b128 v[98:101], v126
	ds_read_b128 v[110:113], v126 offset:1024
	ds_read_b128 v[122:125], v126 offset:2048
	ds_read_b128 v[126:129], v126 offset:3072
	ds_read_b128 v[138:141], v150
	ds_read_b128 v[142:145], v150 offset:1024
	ds_read_b128 v[146:149], v150 offset:2048
	ds_read_b128 v[150:153], v150 offset:3072
	s_add_u32 s20, s26, 0xb0000
	s_addc_u32 s21, s27, 0
	s_mov_b32 m0, s29
	ds_read_b128 v[154:157], v236 offset:32768
	ds_read_b128 v[166:169], v236 offset:33792
	ds_read_b128 v[170:173], v236 offset:34816
	ds_read_b128 v[174:177], v236 offset:35840
	ds_read_b128 v[178:181], v236 offset:36864
	ds_read_b128 v[182:185], v236 offset:37888
	ds_read_b128 v[186:189], v236 offset:38912
	ds_read_b128 v[206:209], v236 offset:39936
	global_load_lds_dwordx4 v190, s[20:21]
	s_mov_b32 m0, s30
	s_nop 0
	global_load_lds_dwordx4 v194, s[20:21]
	s_waitcnt vmcnt(8)
	s_waitcnt lgkmcnt(0)
	s_setprio 3
	s_barrier
	s_waitcnt lgkmcnt(0)
	v_mfma_f32_16x16x32_bf16 v[162:165], v[98:101], v[154:157], v[162:165]
	v_mfma_f32_16x16x32_bf16 v[158:161], v[122:125], v[154:157], v[158:161]
	v_mfma_f32_16x16x32_bf16 v[118:121], v[98:101], v[170:173], v[118:121]
	v_mfma_f32_16x16x32_bf16 v[114:117], v[122:125], v[170:173], v[114:117]
	v_mfma_f32_16x16x32_bf16 v[94:97], v[98:101], v[178:181], v[94:97]
	v_mfma_f32_16x16x32_bf16 v[90:93], v[122:125], v[178:181], v[90:93]
	v_mfma_f32_16x16x32_bf16 v[78:81], v[98:101], v[186:189], v[78:81]
	v_mfma_f32_16x16x32_bf16 v[74:77], v[122:125], v[186:189], v[74:77]
	v_mfma_f32_16x16x32_bf16 v[162:165], v[110:113], v[166:169], v[162:165]
	v_mfma_f32_16x16x32_bf16 v[158:161], v[126:129], v[166:169], v[158:161]
	v_mfma_f32_16x16x32_bf16 v[118:121], v[110:113], v[174:177], v[118:121]
	v_mfma_f32_16x16x32_bf16 v[114:117], v[126:129], v[174:177], v[114:117]
	v_mfma_f32_16x16x32_bf16 v[94:97], v[110:113], v[182:185], v[94:97]
	v_mfma_f32_16x16x32_bf16 v[90:93], v[126:129], v[182:185], v[90:93]
	v_mfma_f32_16x16x32_bf16 v[78:81], v[110:113], v[206:209], v[78:81]
	v_mfma_f32_16x16x32_bf16 v[74:77], v[126:129], v[206:209], v[74:77]
	v_mfma_f32_16x16x32_bf16 v[134:137], v[138:141], v[154:157], v[134:137]
	v_mfma_f32_16x16x32_bf16 v[130:133], v[146:149], v[154:157], v[130:133]
	v_mfma_f32_16x16x32_bf16 v[106:109], v[138:141], v[170:173], v[106:109]
	v_mfma_f32_16x16x32_bf16 v[102:105], v[146:149], v[170:173], v[102:105]
	v_mfma_f32_16x16x32_bf16 v[86:89], v[138:141], v[178:181], v[86:89]
	v_mfma_f32_16x16x32_bf16 v[82:85], v[146:149], v[178:181], v[82:85]
	v_mfma_f32_16x16x32_bf16 v[70:73], v[138:141], v[186:189], v[70:73]
	v_mfma_f32_16x16x32_bf16 v[66:69], v[146:149], v[186:189], v[66:69]
	v_mfma_f32_16x16x32_bf16 v[134:137], v[142:145], v[166:169], v[134:137]
	v_mfma_f32_16x16x32_bf16 v[130:133], v[150:153], v[166:169], v[130:133]
	v_mfma_f32_16x16x32_bf16 v[106:109], v[142:145], v[174:177], v[106:109]
	v_mfma_f32_16x16x32_bf16 v[102:105], v[150:153], v[174:177], v[102:105]
	v_mfma_f32_16x16x32_bf16 v[86:89], v[142:145], v[182:185], v[86:89]
	v_mfma_f32_16x16x32_bf16 v[82:85], v[150:153], v[182:185], v[82:85]
	v_mfma_f32_16x16x32_bf16 v[70:73], v[142:145], v[206:209], v[70:73]
	v_mfma_f32_16x16x32_bf16 v[66:69], v[150:153], v[206:209], v[66:69]
	s_barrier
; #define PG8_STAGE_A(b, h, ptr, NX) do { if constexpr (Sched::GATHER) { unsigned gs_[2]; gs_[0] = ((NX) && last_) ? gN[h][0] : gA[h][0]; gs_[1] = ((NX) && last_) ? gN[h][1] : gA[h][1]; PG8_STAGE(PG8_SA(b, h), ptr, gs_); } \
;         else PG8_STAGE(PG8_SA(b, h), (ptr) + ((h) ? hstep : (size_t)0), voffA); } while (0)
; #define PG8_STAGE(bufoff, gbase, voff) do { _Pragma("unroll") for (int _i = 0; _i < 2; ++_i) \
;         __builtin_amdgcn_global_load_lds((const unsigned*)((const char*)(gbase) + (voff)[_i]), (PG8_LAS unsigned*)(lds + (bufoff) + ldsw + _i * 8192), 16, 0, 0); } while (0)
; #define PG8_LDA(dst, b, h) do { _Pragma("unroll") for (int m = 0; m < 4; ++m) _Pragma("unroll") for (int k = 0; k < 2; ++k) dst[m][k] = *(const PG8_LAS bf16x8*)(lds + PG8_SA(b, h) + aoff + m * 2048 + k * 1024); } while (0)
; #define PG8_LDB(dst, b, h) do { _Pragma("unroll") for (int n = 0; n < 2; ++n) _Pragma("unroll") for (int k = 0; k < 2; ++k) dst[n][k] = *(const PG8_LAS bf16x8*)(lds + PG8_SB(b, h) + boff + n * 2048 + k * 1024); } while (0)
; #define PG8_WAIT_V(n) asm volatile("s_waitcnt vmcnt(" #n ")" ::: "memory")
; #define PG8_BAR __builtin_amdgcn_s_barrier()
; template <class Epi, class Sched, bool ALIGN_EPI = false, bool SP2 = false>
; __device__ __forceinline__ void gemm_phase(PG8_LAS unsigned char* lds, const Gemm g, const Sched& S, const Epi& E, const bool skip_epi = false) {
;     ...
;             PG8_LDB(B0, 0, 0); PG8_LDB(B1, 0, 1); PG8_SCHED; PG8_LDA(At, 0, 0); PG8_STAGE_A(1, 1, a1, false);
;             PG8_WAIT_V(8); PG8_WAIT_L(0); PG8_BAR; PG8_MMA(0, 0, At, B0); PG8_MMA(0, 1, At, B1); PG8_BAR; PG8_SCHED;
;             PG8_LDA(At, 0, 1); PG8_STAGE(PG8_SB(0, 0), b2, voffB); PG8_STAGE(PG8_SB(0, 1), b2 + hstep, voffB); PG8_STAGE_A(0, 0, a2, true);
;             PG8_WAIT_V(8); PG8_WAIT_L(0); PG8_BAR; PG8_MMA(1, 0, At, B0); PG8_MMA(1, 1, At, B1); PG8_BAR; PG8_SCHED;
;             PG8_LDB(B0, 1, 0); PG8_LDB(B1, 1, 1); PG8_SCHED; PG8_LDA(At, 1, 0); PG8_STAGE_A(0, 1, a2, true);
;             PG8_WAIT_V(8); PG8_WAIT_L(0); PG8_BAR; PG8_MMA(0, 0, At, B0); PG8_MMA(0, 1, At, B1); PG8_BAR; PG8_SCHED;
;             PG8_LDA(At, 1, 1); PG8_STAGE(PG8_SB(1, 0), b3, voffB); PG8_STAGE(PG8_SB(1, 1), b3 + hstep, voffB); PG8_STAGE_A(1, 0, a3, true);
;             PG8_WAIT_V(8); PG8_WAIT_L(0); PG8_BAR; PG8_MMA(1, 0, At, B0); PG8_MMA(1, 1, At, B1); PG8_BAR; PG8_SCHED;
	s_setprio 0
	s_add_i32 s20, s58, s2
	s_add_i32 m0, s20, 0xffffff80
	ds_read_b128 v[154:157], v236 offset:49152
	ds_read_b128 v[166:169], v236 offset:50176
	ds_read_b128 v[170:173], v236 offset:51200
	ds_read_b128 v[174:177], v236 offset:52224
	ds_read_b128 v[178:181], v236 offset:53248
	ds_read_b128 v[182:185], v236 offset:54272
	ds_read_b128 v[186:189], v236 offset:55296
	ds_read_b128 v[206:209], v236 offset:56320
	global_load_lds_dwordx4 v[210:211], off offset:128
	s_add_i32 m0, s20, 0x1f80
	s_add_u32 s20, s24, 0xb0080
	s_addc_u32 s21, s25, 0
	s_add_i32 s24, s59, s2
	global_load_lds_dwordx4 v[212:213], off offset:128
	s_mov_b32 m0, s24
	s_nop 0
	global_load_lds_dwordx4 v192, s[20:21]
	s_add_i32 m0, s24, 0x2000
	s_nop 0
	global_load_lds_dwordx4 v196, s[20:21]
	s_add_i32 m0, s35, 0xffffff80
	s_nop 0
	global_load_lds_dwordx4 v[214:215], off offset:128
	s_add_i32 m0, s36, 0xffffff80
	s_nop 0
	global_load_lds_dwordx4 v[216:217], off offset:128
	s_waitcnt vmcnt(8)
	s_waitcnt lgkmcnt(0)
	s_setprio 3
	s_barrier
	s_waitcnt lgkmcnt(0)
	v_mfma_f32_16x16x32_bf16 v[62:65], v[98:101], v[154:157], v[62:65]
	v_mfma_f32_16x16x32_bf16 v[58:61], v[122:125], v[154:157], v[58:61]
	v_mfma_f32_16x16x32_bf16 v[46:49], v[98:101], v[170:173], v[46:49]
	v_mfma_f32_16x16x32_bf16 v[42:45], v[122:125], v[170:173], v[42:45]
	v_mfma_f32_16x16x32_bf16 v[30:33], v[98:101], v[178:181], v[30:33]
	v_mfma_f32_16x16x32_bf16 v[26:29], v[122:125], v[178:181], v[26:29]
	v_mfma_f32_16x16x32_bf16 v[14:17], v[98:101], v[186:189], v[14:17]
	v_mfma_f32_16x16x32_bf16 v[10:13], v[122:125], v[186:189], v[10:13]
	v_mfma_f32_16x16x32_bf16 v[62:65], v[110:113], v[166:169], v[62:65]
	v_mfma_f32_16x16x32_bf16 v[58:61], v[126:129], v[166:169], v[58:61]
	v_mfma_f32_16x16x32_bf16 v[46:49], v[110:113], v[174:177], v[46:49]
	v_mfma_f32_16x16x32_bf16 v[42:45], v[126:129], v[174:177], v[42:45]
	v_mfma_f32_16x16x32_bf16 v[30:33], v[110:113], v[182:185], v[30:33]
	v_mfma_f32_16x16x32_bf16 v[26:29], v[126:129], v[182:185], v[26:29]
	v_mfma_f32_16x16x32_bf16 v[14:17], v[110:113], v[206:209], v[14:17]
	v_mfma_f32_16x16x32_bf16 v[10:13], v[126:129], v[206:209], v[10:13]
	v_mfma_f32_16x16x32_bf16 v[54:57], v[138:141], v[154:157], v[54:57]
	v_mfma_f32_16x16x32_bf16 v[50:53], v[146:149], v[154:157], v[50:53]
	v_mfma_f32_16x16x32_bf16 v[38:41], v[138:141], v[170:173], v[38:41]
	v_mfma_f32_16x16x32_bf16 v[34:37], v[146:149], v[170:173], v[34:37]
	v_mfma_f32_16x16x32_bf16 v[22:25], v[138:141], v[178:181], v[22:25]
	v_mfma_f32_16x16x32_bf16 v[18:21], v[146:149], v[178:181], v[18:21]
	v_mfma_f32_16x16x32_bf16 v[6:9], v[138:141], v[186:189], v[6:9]
	v_mfma_f32_16x16x32_bf16 v[2:5], v[146:149], v[186:189], v[2:5]
	v_mfma_f32_16x16x32_bf16 v[54:57], v[142:145], v[166:169], v[54:57]
	v_mfma_f32_16x16x32_bf16 v[50:53], v[150:153], v[166:169], v[50:53]
	v_mfma_f32_16x16x32_bf16 v[38:41], v[142:145], v[174:177], v[38:41]
	v_mfma_f32_16x16x32_bf16 v[34:37], v[150:153], v[174:177], v[34:37]
	v_mfma_f32_16x16x32_bf16 v[22:25], v[142:145], v[182:185], v[22:25]
	v_mfma_f32_16x16x32_bf16 v[18:21], v[150:153], v[182:185], v[18:21]
	v_mfma_f32_16x16x32_bf16 v[6:9], v[142:145], v[206:209], v[6:9]
	v_mfma_f32_16x16x32_bf16 v[2:5], v[150:153], v[206:209], v[2:5]
	s_barrier
	s_setprio 0
	s_add_i32 s57, s57, 2
	s_add_u32 s55, s55, 0x100
	s_addc_u32 s56, s56, 0
	s_cmp_gt_u32 s57, 41
	s_mov_b64 s[20:21], s[22:23]
.LBB0_857:
	ds_read_b128 v[98:101], v234
	ds_read_b128 v[110:113], v234 offset:1024
	ds_read_b128 v[122:125], v234 offset:2048
	ds_read_b128 v[126:129], v234 offset:3072
	ds_read_b128 v[138:141], v235
	ds_read_b128 v[142:145], v235 offset:1024
	ds_read_b128 v[146:149], v235 offset:2048
	ds_read_b128 v[150:153], v235 offset:3072
	s_add_u32 s22, s20, 0x100
	s_addc_u32 s23, s21, 0
	s_cmp_eq_u32 s57, 40
	s_cselect_b32 s27, s9, s23
	s_cselect_b32 s26, s8, s22
	s_cselect_b32 s25, s19, s56
	s_cselect_b32 s24, s18, s55
	v_lshl_add_u64 v[210:211], s[20:21], 0, v[198:199]
	s_add_i32 m0, s3, 0xc000
	ds_read_b128 v[154:157], v236
	ds_read_b128 v[166:169], v236 offset:1024
	ds_read_b128 v[170:173], v236 offset:2048
	ds_read_b128 v[174:177], v236 offset:3072
	ds_read_b128 v[178:181], v236 offset:4096
	ds_read_b128 v[182:185], v236 offset:5120
	ds_read_b128 v[186:189], v236 offset:6144
	ds_read_b128 v[206:209], v236 offset:7168
	global_load_lds_dwordx4 v[210:211], off
	v_lshl_add_u64 v[210:211], s[20:21], 0, v[200:201]
	s_add_i32 m0, s3, 0xe000
	s_nop 0
	global_load_lds_dwordx4 v[210:211], off
	s_waitcnt vmcnt(8)
	s_waitcnt lgkmcnt(0)
	s_setprio 3
	s_barrier
; #define PG8_STAGE_A(b, h, ptr, NX) do { if constexpr (Sched::GATHER) { unsigned gs_[2]; gs_[0] = ((NX) && last_) ? gN[h][0] : gA[h][0]; gs_[1] = ((NX) && last_) ? gN[h][1] : gA[h][1]; PG8_STAGE(PG8_SA(b, h), ptr, gs_); } \
;         else PG8_STAGE(PG8_SA(b, h), (ptr) + ((h) ? hstep : (size_t)0), voffA); } while (0)
; #define PG8_STAGE(bufoff, gbase, voff) do { _Pragma("unroll") for (int _i = 0; _i < 2; ++_i) \
;         __builtin_amdgcn_global_load_lds((const unsigned*)((const char*)(gbase) + (voff)[_i]), (PG8_LAS unsigned*)(lds + (bufoff) + ldsw + _i * 8192), 16, 0, 0); } while (0)
; #define PG8_LDA(dst, b, h) do { _Pragma("unroll") for (int m = 0; m < 4; ++m) _Pragma("unroll") for (int k = 0; k < 2; ++k) dst[m][k] = *(const PG8_LAS bf16x8*)(lds + PG8_SA(b, h) + aoff + m * 2048 + k * 1024); } while (0)
; #define PG8_LDB(dst, b, h) do { _Pragma("unroll") for (int n = 0; n < 2; ++n) _Pragma("unroll") for (int k = 0; k < 2; ++k) dst[n][k] = *(const PG8_LAS bf16x8*)(lds + PG8_SB(b, h) + boff + n * 2048 + k * 1024); } while (0)
; #define PG8_MMA(ai, bj, At, Bt) do { __builtin_amdgcn_s_setprio(1); _Pragma("unroll") for (int m = 0; m < 4; ++m) _Pragma("unroll") for (int n = 0; n < 2; ++n) _Pragma("unroll") for (int k = 0; k < 2; ++k) \
;         acc[ai][bj][m][n] = __builtin_amdgcn_mfma_f32_16x16x32_bf16(Bt[n][k], At[m][k], acc[ai][bj][m][n], 0, 0, 0); __builtin_amdgcn_s_setprio(0); } while (0)
; #define PG8_WAIT_V(n) asm volatile("s_waitcnt vmcnt(" #n ")" ::: "memory")
; #define PG8_WAIT_L(n) asm volatile("s_waitcnt lgkmcnt(" #n ")" ::: "memory")
; #define PG8_BAR __builtin_amdgcn_s_barrier()
; #define PG8_SCHED __builtin_amdgcn_sched_barrier(0)
; template <class Epi, class Sched, bool ALIGN_EPI = false, bool SP2 = false>
; __device__ __forceinline__ void gemm_phase(PG8_LAS unsigned char* lds, const Gemm g, const Sched& S, const Epi& E, const bool skip_epi = false) {
;     ...
;             PG8_LDA(At, 0, 1); PG8_STAGE(PG8_SB(0, 0), b2, voffB); PG8_STAGE(PG8_SB(0, 1), b2 + hstep, voffB); PG8_STAGE_A(0, 0, a2, true);
;             PG8_WAIT_V(8); PG8_WAIT_L(0); PG8_BAR; PG8_MMA(1, 0, At, B0); PG8_MMA(1, 1, At, B1); PG8_BAR; PG8_SCHED;
;             PG8_LDB(B0, 1, 0); PG8_LDB(B1, 1, 1); PG8_SCHED; PG8_LDA(At, 1, 0); PG8_STAGE_A(0, 1, a2, true);
;             PG8_WAIT_V(8); PG8_WAIT_L(0); PG8_BAR; PG8_MMA(0, 0, At, B0); PG8_MMA(0, 1, At, B1); PG8_BAR; PG8_SCHED;
	s_waitcnt lgkmcnt(0)
	v_mfma_f32_16x16x32_bf16 v[162:165], v[98:101], v[154:157], v[162:165]
	v_mfma_f32_16x16x32_bf16 v[158:161], v[122:125], v[154:157], v[158:161]
	v_mfma_f32_16x16x32_bf16 v[118:121], v[98:101], v[170:173], v[118:121]
	v_mfma_f32_16x16x32_bf16 v[114:117], v[122:125], v[170:173], v[114:117]
	v_mfma_f32_16x16x32_bf16 v[94:97], v[98:101], v[178:181], v[94:97]
	v_mfma_f32_16x16x32_bf16 v[90:93], v[122:125], v[178:181], v[90:93]
	v_mfma_f32_16x16x32_bf16 v[78:81], v[98:101], v[186:189], v[78:81]
	v_mfma_f32_16x16x32_bf16 v[74:77], v[122:125], v[186:189], v[74:77]
	v_mfma_f32_16x16x32_bf16 v[162:165], v[110:113], v[166:169], v[162:165]
	v_mfma_f32_16x16x32_bf16 v[158:161], v[126:129], v[166:169], v[158:161]
	v_mfma_f32_16x16x32_bf16 v[118:121], v[110:113], v[174:177], v[118:121]
	v_mfma_f32_16x16x32_bf16 v[114:117], v[126:129], v[174:177], v[114:117]
	v_mfma_f32_16x16x32_bf16 v[94:97], v[110:113], v[182:185], v[94:97]
	v_mfma_f32_16x16x32_bf16 v[90:93], v[126:129], v[182:185], v[90:93]
	v_mfma_f32_16x16x32_bf16 v[78:81], v[110:113], v[206:209], v[78:81]
	v_mfma_f32_16x16x32_bf16 v[74:77], v[126:129], v[206:209], v[74:77]
	v_mfma_f32_16x16x32_bf16 v[134:137], v[138:141], v[154:157], v[134:137]
	v_mfma_f32_16x16x32_bf16 v[130:133], v[146:149], v[154:157], v[130:133]
	v_mfma_f32_16x16x32_bf16 v[106:109], v[138:141], v[170:173], v[106:109]
	v_mfma_f32_16x16x32_bf16 v[102:105], v[146:149], v[170:173], v[102:105]
	v_mfma_f32_16x16x32_bf16 v[86:89], v[138:141], v[178:181], v[86:89]
	v_mfma_f32_16x16x32_bf16 v[82:85], v[146:149], v[178:181], v[82:85]
	v_mfma_f32_16x16x32_bf16 v[70:73], v[138:141], v[186:189], v[70:73]
	v_mfma_f32_16x16x32_bf16 v[66:69], v[146:149], v[186:189], v[66:69]
	v_mfma_f32_16x16x32_bf16 v[134:137], v[142:145], v[166:169], v[134:137]
	v_mfma_f32_16x16x32_bf16 v[130:133], v[150:153], v[166:169], v[130:133]
	v_mfma_f32_16x16x32_bf16 v[106:109], v[142:145], v[174:177], v[106:109]
	v_mfma_f32_16x16x32_bf16 v[102:105], v[150:153], v[174:177], v[102:105]
	v_mfma_f32_16x16x32_bf16 v[86:89], v[142:145], v[182:185], v[86:89]
	v_mfma_f32_16x16x32_bf16 v[82:85], v[150:153], v[182:185], v[82:85]
	v_mfma_f32_16x16x32_bf16 v[70:73], v[142:145], v[206:209], v[70:73]
	v_mfma_f32_16x16x32_bf16 v[66:69], v[150:153], v[206:209], v[66:69]
	s_barrier
	s_setprio 0
	s_add_i32 s20, s39, s2
	v_lshl_add_u64 v[210:211], s[24:25], 0, v[192:193]
	s_mov_b32 m0, s20
	ds_read_b128 v[154:157], v236 offset:16384
	ds_read_b128 v[166:169], v236 offset:17408
	ds_read_b128 v[170:173], v236 offset:18432
	ds_read_b128 v[174:177], v236 offset:19456
	ds_read_b128 v[178:181], v236 offset:20480
	ds_read_b128 v[182:185], v236 offset:21504
	ds_read_b128 v[186:189], v236 offset:22528
	ds_read_b128 v[206:209], v236 offset:23552
	global_load_lds_dwordx4 v[210:211], off
	s_add_i32 m0, s20, 0x2000
	s_add_u32 s20, s24, 0xb0000
	v_lshl_add_u64 v[212:213], s[24:25], 0, v[196:197]
	s_addc_u32 s21, s25, 0
	s_add_i32 s58, s48, s2
	global_load_lds_dwordx4 v[212:213], off
	s_mov_b32 m0, s58
	v_lshl_add_u64 v[216:217], s[26:27], 0, v[194:195]
	global_load_lds_dwordx4 v192, s[20:21]
	s_add_i32 m0, s58, 0x2000
	s_nop 0
	global_load_lds_dwordx4 v196, s[20:21]
	v_lshl_add_u64 v[214:215], s[26:27], 0, v[190:191]
	s_mov_b32 m0, s3
	s_nop 0
	global_load_lds_dwordx4 v[214:215], off
	s_mov_b32 m0, s28
	s_nop 0
	global_load_lds_dwordx4 v[216:217], off
	s_waitcnt vmcnt(8)
	s_waitcnt lgkmcnt(0)
	s_setprio 3
	s_barrier
	s_waitcnt lgkmcnt(0)
	v_mfma_f32_16x16x32_bf16 v[62:65], v[98:101], v[154:157], v[62:65]
	v_mfma_f32_16x16x32_bf16 v[58:61], v[122:125], v[154:157], v[58:61]
	v_mfma_f32_16x16x32_bf16 v[46:49], v[98:101], v[170:173], v[46:49]
	v_mfma_f32_16x16x32_bf16 v[42:45], v[122:125], v[170:173], v[42:45]
	v_mfma_f32_16x16x32_bf16 v[30:33], v[98:101], v[178:181], v[30:33]
	v_mfma_f32_16x16x32_bf16 v[26:29], v[122:125], v[178:181], v[26:29]
	v_mfma_f32_16x16x32_bf16 v[14:17], v[98:101], v[186:189], v[14:17]
	v_mfma_f32_16x16x32_bf16 v[10:13], v[122:125], v[186:189], v[10:13]
	v_mfma_f32_16x16x32_bf16 v[62:65], v[110:113], v[166:169], v[62:65]
	v_mfma_f32_16x16x32_bf16 v[58:61], v[126:129], v[166:169], v[58:61]
	v_mfma_f32_16x16x32_bf16 v[46:49], v[110:113], v[174:177], v[46:49]
	v_mfma_f32_16x16x32_bf16 v[42:45], v[126:129], v[174:177], v[42:45]
	v_mfma_f32_16x16x32_bf16 v[30:33], v[110:113], v[182:185], v[30:33]
	v_mfma_f32_16x16x32_bf16 v[26:29], v[126:129], v[182:185], v[26:29]
	v_mfma_f32_16x16x32_bf16 v[14:17], v[110:113], v[206:209], v[14:17]
	v_mfma_f32_16x16x32_bf16 v[10:13], v[126:129], v[206:209], v[10:13]
	v_mfma_f32_16x16x32_bf16 v[54:57], v[138:141], v[154:157], v[54:57]
	v_mfma_f32_16x16x32_bf16 v[50:53], v[146:149], v[154:157], v[50:53]
	v_mfma_f32_16x16x32_bf16 v[38:41], v[138:141], v[170:173], v[38:41]
	v_mfma_f32_16x16x32_bf16 v[34:37], v[146:149], v[170:173], v[34:37]
	v_mfma_f32_16x16x32_bf16 v[22:25], v[138:141], v[178:181], v[22:25]
	v_mfma_f32_16x16x32_bf16 v[18:21], v[146:149], v[178:181], v[18:21]
	v_mfma_f32_16x16x32_bf16 v[6:9], v[138:141], v[186:189], v[6:9]
	v_mfma_f32_16x16x32_bf16 v[2:5], v[146:149], v[186:189], v[2:5]
	v_mfma_f32_16x16x32_bf16 v[54:57], v[142:145], v[166:169], v[54:57]
	v_mfma_f32_16x16x32_bf16 v[50:53], v[150:153], v[166:169], v[50:53]
	v_mfma_f32_16x16x32_bf16 v[38:41], v[142:145], v[174:177], v[38:41]
	v_mfma_f32_16x16x32_bf16 v[34:37], v[150:153], v[174:177], v[34:37]
	v_mfma_f32_16x16x32_bf16 v[22:25], v[142:145], v[182:185], v[22:25]
	v_mfma_f32_16x16x32_bf16 v[18:21], v[150:153], v[182:185], v[18:21]
	v_mfma_f32_16x16x32_bf16 v[6:9], v[142:145], v[206:209], v[6:9]
	v_mfma_f32_16x16x32_bf16 v[2:5], v[150:153], v[206:209], v[2:5]
	s_barrier
; #define PG8_STAGE_A(b, h, ptr, NX) do { if constexpr (Sched::GATHER) { unsigned gs_[2]; gs_[0] = ((NX) && last_) ? gN[h][0] : gA[h][0]; gs_[1] = ((NX) && last_) ? gN[h][1] : gA[h][1]; PG8_STAGE(PG8_SA(b, h), ptr, gs_); } \
;         else PG8_STAGE(PG8_SA(b, h), (ptr) + ((h) ? hstep : (size_t)0), voffA); } while (0)
; #define PG8_STAGE(bufoff, gbase, voff) do { _Pragma("unroll") for (int _i = 0; _i < 2; ++_i) \
;         __builtin_amdgcn_global_load_lds((const unsigned*)((const char*)(gbase) + (voff)[_i]), (PG8_LAS unsigned*)(lds + (bufoff) + ldsw + _i * 8192), 16, 0, 0); } while (0)
; #define PG8_LDA(dst, b, h) do { _Pragma("unroll") for (int m = 0; m < 4; ++m) _Pragma("unroll") for (int k = 0; k < 2; ++k) dst[m][k] = *(const PG8_LAS bf16x8*)(lds + PG8_SA(b, h) + aoff + m * 2048 + k * 1024); } while (0)
; #define PG8_LDB(dst, b, h) do { _Pragma("unroll") for (int n = 0; n < 2; ++n) _Pragma("unroll") for (int k = 0; k < 2; ++k) dst[n][k] = *(const PG8_LAS bf16x8*)(lds + PG8_SB(b, h) + boff + n * 2048 + k * 1024); } while (0)
; #define PG8_MMA(ai, bj, At, Bt) do { __builtin_amdgcn_s_setprio(1); _Pragma("unroll") for (int m = 0; m < 4; ++m) _Pragma("unroll") for (int n = 0; n < 2; ++n) _Pragma("unroll") for (int k = 0; k < 2; ++k) \
;         acc[ai][bj][m][n] = __builtin_amdgcn_mfma_f32_16x16x32_bf16(Bt[n][k], At[m][k], acc[ai][bj][m][n], 0, 0, 0); __builtin_amdgcn_s_setprio(0); } while (0)
; #define PG8_WAIT_V(n) asm volatile("s_waitcnt vmcnt(" #n ")" ::: "memory")
; #define PG8_WAIT_L(n) asm volatile("s_waitcnt lgkmcnt(" #n ")" ::: "memory")
; #define PG8_BAR __builtin_amdgcn_s_barrier()
; template <class Epi, class Sched, bool ALIGN_EPI = false, bool SP2 = false>
; __device__ __forceinline__ void gemm_phase(PG8_LAS unsigned char* lds, const Gemm g, const Sched& S, const Epi& E, const bool skip_epi = false) {
;     ...
;             PG8_LDB(B0, 1, 0); PG8_LDB(B1, 1, 1); PG8_SCHED; PG8_LDA(At, 1, 0); PG8_STAGE_A(0, 1, a2, true);
;             PG8_WAIT_V(8); PG8_WAIT_L(0); PG8_BAR; PG8_MMA(0, 0, At, B0); PG8_MMA(0, 1, At, B1); PG8_BAR; PG8_SCHED;
;             PG8_LDA(At, 1, 1); PG8_STAGE(PG8_SB(1, 0), b3, voffB); PG8_STAGE(PG8_SB(1, 1), b3 + hstep, voffB); PG8_STAGE_A(1, 0, a3, true);
;             PG8_WAIT_V(8); PG8_WAIT_L(0); PG8_BAR; PG8_MMA(1, 0, At, B0); PG8_MMA(1, 1, At, B1); PG8_BAR; PG8_SCHED;
;     ...
;         if constexpr (ALIGN_EPI) { if (wr == 0) PG8_BAR; }
	s_setprio 0
	s_add_i32 s58, 0, 0x18000
	s_add_i32 s59, 0, 0x1c000
	v_add_u32_e32 v126, s58, v229
	v_add_u32_e32 v150, s59, v229
	ds_read_b128 v[98:101], v126
	ds_read_b128 v[110:113], v126 offset:1024
	ds_read_b128 v[122:125], v126 offset:2048
	ds_read_b128 v[126:129], v126 offset:3072
	ds_read_b128 v[138:141], v150
	ds_read_b128 v[142:145], v150 offset:1024
	ds_read_b128 v[146:149], v150 offset:2048
	ds_read_b128 v[150:153], v150 offset:3072
	s_add_u32 s20, s26, 0xb0000
	s_addc_u32 s21, s27, 0
	s_mov_b32 m0, s29
	ds_read_b128 v[154:157], v236 offset:32768
	ds_read_b128 v[166:169], v236 offset:33792
	ds_read_b128 v[170:173], v236 offset:34816
	ds_read_b128 v[174:177], v236 offset:35840
	ds_read_b128 v[178:181], v236 offset:36864
	ds_read_b128 v[182:185], v236 offset:37888
	ds_read_b128 v[186:189], v236 offset:38912
	ds_read_b128 v[206:209], v236 offset:39936
	global_load_lds_dwordx4 v190, s[20:21]
	s_mov_b32 m0, s30
	s_nop 0
	global_load_lds_dwordx4 v194, s[20:21]
	s_waitcnt vmcnt(8)
	s_waitcnt lgkmcnt(0)
	s_setprio 3
	s_barrier
	s_waitcnt lgkmcnt(0)
	v_mfma_f32_16x16x32_bf16 v[162:165], v[98:101], v[154:157], v[162:165]
	v_mfma_f32_16x16x32_bf16 v[158:161], v[122:125], v[154:157], v[158:161]
	v_mfma_f32_16x16x32_bf16 v[118:121], v[98:101], v[170:173], v[118:121]
	v_mfma_f32_16x16x32_bf16 v[114:117], v[122:125], v[170:173], v[114:117]
	v_mfma_f32_16x16x32_bf16 v[94:97], v[98:101], v[178:181], v[94:97]
	v_mfma_f32_16x16x32_bf16 v[90:93], v[122:125], v[178:181], v[90:93]
	v_mfma_f32_16x16x32_bf16 v[78:81], v[98:101], v[186:189], v[78:81]
	v_mfma_f32_16x16x32_bf16 v[74:77], v[122:125], v[186:189], v[74:77]
	v_mfma_f32_16x16x32_bf16 v[162:165], v[110:113], v[166:169], v[162:165]
	v_mfma_f32_16x16x32_bf16 v[158:161], v[126:129], v[166:169], v[158:161]
	v_mfma_f32_16x16x32_bf16 v[118:121], v[110:113], v[174:177], v[118:121]
	v_mfma_f32_16x16x32_bf16 v[114:117], v[126:129], v[174:177], v[114:117]
	v_mfma_f32_16x16x32_bf16 v[94:97], v[110:113], v[182:185], v[94:97]
	v_mfma_f32_16x16x32_bf16 v[90:93], v[126:129], v[182:185], v[90:93]
	v_mfma_f32_16x16x32_bf16 v[78:81], v[110:113], v[206:209], v[78:81]
	v_mfma_f32_16x16x32_bf16 v[74:77], v[126:129], v[206:209], v[74:77]
	v_mfma_f32_16x16x32_bf16 v[134:137], v[138:141], v[154:157], v[134:137]
	v_mfma_f32_16x16x32_bf16 v[130:133], v[146:149], v[154:157], v[130:133]
	v_mfma_f32_16x16x32_bf16 v[106:109], v[138:141], v[170:173], v[106:109]
	v_mfma_f32_16x16x32_bf16 v[102:105], v[146:149], v[170:173], v[102:105]
	v_mfma_f32_16x16x32_bf16 v[86:89], v[138:141], v[178:181], v[86:89]
	v_mfma_f32_16x16x32_bf16 v[82:85], v[146:149], v[178:181], v[82:85]
	v_mfma_f32_16x16x32_bf16 v[70:73], v[138:141], v[186:189], v[70:73]
	v_mfma_f32_16x16x32_bf16 v[66:69], v[146:149], v[186:189], v[66:69]
	v_mfma_f32_16x16x32_bf16 v[134:137], v[142:145], v[166:169], v[134:137]
	v_mfma_f32_16x16x32_bf16 v[130:133], v[150:153], v[166:169], v[130:133]
	v_mfma_f32_16x16x32_bf16 v[106:109], v[142:145], v[174:177], v[106:109]
	v_mfma_f32_16x16x32_bf16 v[102:105], v[150:153], v[174:177], v[102:105]
	v_mfma_f32_16x16x32_bf16 v[86:89], v[142:145], v[182:185], v[86:89]
	v_mfma_f32_16x16x32_bf16 v[82:85], v[150:153], v[182:185], v[82:85]
	v_mfma_f32_16x16x32_bf16 v[70:73], v[142:145], v[206:209], v[70:73]
	v_mfma_f32_16x16x32_bf16 v[66:69], v[150:153], v[206:209], v[66:69]
	s_barrier
	s_setprio 0
	s_add_i32 s20, s58, s2
	s_add_i32 m0, s20, 0xffffff80
	ds_read_b128 v[154:157], v236 offset:49152
	ds_read_b128 v[166:169], v236 offset:50176
	ds_read_b128 v[170:173], v236 offset:51200
	ds_read_b128 v[174:177], v236 offset:52224
	ds_read_b128 v[178:181], v236 offset:53248
	ds_read_b128 v[182:185], v236 offset:54272
	ds_read_b128 v[186:189], v236 offset:55296
	ds_read_b128 v[206:209], v236 offset:56320
	global_load_lds_dwordx4 v[210:211], off offset:128
	s_add_i32 m0, s20, 0x1f80
	s_add_u32 s20, s24, 0xb0080
	s_addc_u32 s21, s25, 0
	s_add_i32 s24, s59, s2
	global_load_lds_dwordx4 v[212:213], off offset:128
	s_mov_b32 m0, s24
	s_nop 0
	global_load_lds_dwordx4 v192, s[20:21]
	s_add_i32 m0, s24, 0x2000
	s_nop 0
	global_load_lds_dwordx4 v196, s[20:21]
	s_add_i32 m0, s35, 0xffffff80
	s_nop 0
	global_load_lds_dwordx4 v[214:215], off offset:128
	s_add_i32 m0, s36, 0xffffff80
	s_nop 0
	global_load_lds_dwordx4 v[216:217], off offset:128
	s_waitcnt vmcnt(8)
	s_waitcnt lgkmcnt(0)
	s_setprio 3
	s_barrier
	s_waitcnt lgkmcnt(0)
	v_mfma_f32_16x16x32_bf16 v[62:65], v[98:101], v[154:157], v[62:65]
	v_mfma_f32_16x16x32_bf16 v[58:61], v[122:125], v[154:157], v[58:61]
	v_mfma_f32_16x16x32_bf16 v[46:49], v[98:101], v[170:173], v[46:49]
	v_mfma_f32_16x16x32_bf16 v[42:45], v[122:125], v[170:173], v[42:45]
	v_mfma_f32_16x16x32_bf16 v[30:33], v[98:101], v[178:181], v[30:33]
	v_mfma_f32_16x16x32_bf16 v[26:29], v[122:125], v[178:181], v[26:29]
	v_mfma_f32_16x16x32_bf16 v[14:17], v[98:101], v[186:189], v[14:17]
	v_mfma_f32_16x16x32_bf16 v[10:13], v[122:125], v[186:189], v[10:13]
	v_mfma_f32_16x16x32_bf16 v[62:65], v[110:113], v[166:169], v[62:65]
	v_mfma_f32_16x16x32_bf16 v[58:61], v[126:129], v[166:169], v[58:61]
	v_mfma_f32_16x16x32_bf16 v[46:49], v[110:113], v[174:177], v[46:49]
	v_mfma_f32_16x16x32_bf16 v[42:45], v[126:129], v[174:177], v[42:45]
	v_mfma_f32_16x16x32_bf16 v[30:33], v[110:113], v[182:185], v[30:33]
	v_mfma_f32_16x16x32_bf16 v[26:29], v[126:129], v[182:185], v[26:29]
	v_mfma_f32_16x16x32_bf16 v[14:17], v[110:113], v[206:209], v[14:17]
	v_mfma_f32_16x16x32_bf16 v[10:13], v[126:129], v[206:209], v[10:13]
	v_mfma_f32_16x16x32_bf16 v[54:57], v[138:141], v[154:157], v[54:57]
	v_mfma_f32_16x16x32_bf16 v[50:53], v[146:149], v[154:157], v[50:53]
	v_mfma_f32_16x16x32_bf16 v[38:41], v[138:141], v[170:173], v[38:41]
	v_mfma_f32_16x16x32_bf16 v[34:37], v[146:149], v[170:173], v[34:37]
	v_mfma_f32_16x16x32_bf16 v[22:25], v[138:141], v[178:181], v[22:25]
	v_mfma_f32_16x16x32_bf16 v[18:21], v[146:149], v[178:181], v[18:21]
	v_mfma_f32_16x16x32_bf16 v[6:9], v[138:141], v[186:189], v[6:9]
	v_mfma_f32_16x16x32_bf16 v[2:5], v[146:149], v[186:189], v[2:5]
	v_mfma_f32_16x16x32_bf16 v[54:57], v[142:145], v[166:169], v[54:57]
	v_mfma_f32_16x16x32_bf16 v[50:53], v[150:153], v[166:169], v[50:53]
	v_mfma_f32_16x16x32_bf16 v[38:41], v[142:145], v[174:177], v[38:41]
	v_mfma_f32_16x16x32_bf16 v[34:37], v[150:153], v[174:177], v[34:37]
	v_mfma_f32_16x16x32_bf16 v[22:25], v[142:145], v[182:185], v[22:25]
	v_mfma_f32_16x16x32_bf16 v[18:21], v[150:153], v[182:185], v[18:21]
	v_mfma_f32_16x16x32_bf16 v[6:9], v[142:145], v[206:209], v[6:9]
	v_mfma_f32_16x16x32_bf16 v[2:5], v[150:153], v[206:209], v[2:5]
	s_barrier
	s_setprio 0
	s_add_i32 s57, s57, 2
	s_add_u32 s55, s55, 0x100
	s_addc_u32 s56, s56, 0
	s_cmp_gt_u32 s57, 41
	s_mov_b64 s[20:21], s[22:23]
	s_cbranch_scc0 .LBB0_857
	s_and_b64 vcc, exec, s[16:17]
	s_cbranch_vccz .LBB0_860
	s_barrier

; #define PG8_STAGE_A(b, h, ptr, NX) do { if constexpr (Sched::GATHER) { unsigned gs_[2]; gs_[0] = ((NX) && last_) ? gN[h][0] : gA[h][0]; gs_[1] = ((NX) && last_) ? gN[h][1] : gA[h][1]; PG8_STAGE(PG8_SA(b, h), ptr, gs_); } \
;         else PG8_STAGE(PG8_SA(b, h), (ptr) + ((h) ? hstep : (size_t)0), voffA); } while (0)
; #define PG8_STAGE(bufoff, gbase, voff) do { _Pragma("unroll") for (int _i = 0; _i < 2; ++_i) \
;         __builtin_amdgcn_global_load_lds((const unsigned*)((const char*)(gbase) + (voff)[_i]), (PG8_LAS unsigned*)(lds + (bufoff) + ldsw + _i * 8192), 16, 0, 0); } while (0)
; #define PG8_WAIT_V(n) asm volatile("s_waitcnt vmcnt(" #n ")" ::: "memory")
; #define PG8_WAIT_L(n) asm volatile("s_waitcnt lgkmcnt(" #n ")" ::: "memory")
; template <class Epi, class Sched, bool ALIGN_EPI = false, bool SP2 = false>
; __device__ __forceinline__ void gemm_phase(PG8_LAS unsigned char* lds, const Gemm g, const Sched& S, const Epi& E, const bool skip_epi = false) {
;     ...
;         const char* nA = has_next ? (const char*)g.A + (size_t)nxt.pm * pmstepA + nxt.ko : cA; const char* nB = has_next ? (const char*)g.Bt + (size_t)nxt.pn * tstep + nxt.ko : cB;
;         for (int t = 0; t < nt; t += 2) {
;             const bool last = (t == nt - 2); last_ = last && has_next;
;             const char* a1 = cA + (size_t)(t + 1) * kstep;
;             const char* a2 = last ? nA : cA + (size_t)(t + 2) * kstep; const char* b2 = last ? nB : cB + (size_t)(t + 2) * kstep;
;             const char* a3 = a2 + kstep; const char* b3 = b2 + kstep;
;             if (last && has_next) S.a_ready(nxt);
;             if constexpr (SP2) {
;             PG8_LDB(B0, 0, 0); PG8_LDB(B1, 0, 1); PG8_SCHED; PG8_LDA(At, 0, 0); PG8_STAGE_A(1, 1, a1, false);
;             PG8_WAIT_V(8); PG8_WAIT_L(0); PG8_BAR; PG8_MMA(0, 0, At, B0); PG8_MMA(0, 1, At, B1); PG8_BAR; PG8_SCHED;
;             PG8_LDA(At, 0, 1); PG8_STAGE(PG8_SB(0, 0), b2, voffB); PG8_STAGE(PG8_SB(0, 1), b2 + hstep, voffB); PG8_STAGE_A(0, 0, a2, true);
;             PG8_WAIT_V(8); PG8_WAIT_L(0); PG8_BAR; PG8_MMA(1, 0, At, B0); PG8_MMA(1, 1, At, B1); PG8_BAR; PG8_SCHED;
;     ...
;         for (int a = 0; a < 2; ++a)
; #pragma unroll
;             for (int b = 0; b < 2; ++b)
; #pragma unroll
;                 for (int m = 0; m < 4; ++m)
; #pragma unroll
;                     for (int n = 0; n < 2; ++n) acc[a][b][m][n] = (f32x4){0.f, 0.f, 0.f, 0.f};
.LBB0_943:
	s_ashr_i32 s15, s14, 31
	s_lshl_b64 s[16:17], s[14:15], 19
	s_add_u32 s16, s86, s16
	s_addc_u32 s17, s87, s17
	s_and_b64 s[18:19], s[4:5], exec
	s_cselect_b32 s15, s17, s23
	s_cselect_b32 s54, s16, s22
	s_ashr_i32 s13, s12, 31
	s_lshl_b64 s[18:19], s[12:13], 19
	s_add_u32 s18, s2, s18
	s_addc_u32 s19, s3, s19
	s_and_b64 s[26:27], s[4:5], exec
	s_cselect_b32 s13, s19, s25
	s_cselect_b32 s55, s18, s24
	s_add_u32 s22, s22, 0x40080
	s_addc_u32 s23, s23, 0
	s_add_u32 s56, s24, 0x100
	s_addc_u32 s57, s25, 0
	s_mov_b32 s58, -2
	s_waitcnt vmcnt(0)
	ds_read_b128 v[148:151], v170
	ds_read_b128 v[152:155], v170 offset:1024
	ds_read_b128 v[156:159], v170 offset:2048
	ds_read_b128 v[160:163], v170 offset:3072
	ds_read_b128 v[176:179], v171
	ds_read_b128 v[180:183], v171 offset:1024
	ds_read_b128 v[184:187], v171 offset:2048
	ds_read_b128 v[188:191], v171 offset:3072
	s_add_u32 s24, s22, 0xfffc0080
	s_addc_u32 s25, s23, -1
	s_cmp_eq_u32 s58, 12
	s_cselect_b32 s27, s15, s25
	s_cselect_b32 s26, s54, s24
	s_cselect_b32 s25, s13, s57
	s_cselect_b32 s24, s55, s56
	s_add_i32 m0, s21, 0xc000
	ds_read_b128 v[192:195], v172
	ds_read_b128 v[196:199], v172 offset:1024
	ds_read_b128 v[200:203], v172 offset:2048
	ds_read_b128 v[204:207], v172 offset:3072
	ds_read_b128 v[208:211], v172 offset:4096
	ds_read_b128 v[212:215], v172 offset:5120
	ds_read_b128 v[216:219], v172 offset:6144
	ds_read_b128 v[220:223], v172 offset:7168
	global_load_lds_dwordx4 v140, s[22:23]
	s_add_i32 m0, s21, 0xe000
	s_nop 0
	global_load_lds_dwordx4 v142, s[22:23]
	s_waitcnt vmcnt(8)
	s_waitcnt lgkmcnt(0)
	s_setprio 3
	s_barrier
	s_waitcnt lgkmcnt(0)
	v_mfma_f32_16x16x32_bf16 v[126:129], v[148:151], v[192:195], 0
	v_mfma_f32_16x16x32_bf16 v[122:125], v[156:159], v[192:195], 0
	v_mfma_f32_16x16x32_bf16 v[114:117], v[148:151], v[200:203], 0
	v_mfma_f32_16x16x32_bf16 v[106:109], v[156:159], v[200:203], 0
	v_mfma_f32_16x16x32_bf16 v[98:101], v[148:151], v[208:211], 0
	v_mfma_f32_16x16x32_bf16 v[90:93], v[156:159], v[208:211], 0
	v_mfma_f32_16x16x32_bf16 v[82:85], v[148:151], v[216:219], 0
	v_mfma_f32_16x16x32_bf16 v[74:77], v[156:159], v[216:219], 0
	v_mfma_f32_16x16x32_bf16 v[126:129], v[152:155], v[196:199], v[126:129]
	v_mfma_f32_16x16x32_bf16 v[122:125], v[160:163], v[196:199], v[122:125]
	v_mfma_f32_16x16x32_bf16 v[114:117], v[152:155], v[204:207], v[114:117]
	v_mfma_f32_16x16x32_bf16 v[106:109], v[160:163], v[204:207], v[106:109]
	v_mfma_f32_16x16x32_bf16 v[98:101], v[152:155], v[212:215], v[98:101]
	v_mfma_f32_16x16x32_bf16 v[90:93], v[160:163], v[212:215], v[90:93]
	v_mfma_f32_16x16x32_bf16 v[82:85], v[152:155], v[220:223], v[82:85]
	v_mfma_f32_16x16x32_bf16 v[74:77], v[160:163], v[220:223], v[74:77]
	v_mfma_f32_16x16x32_bf16 v[118:121], v[176:179], v[192:195], 0
	v_mfma_f32_16x16x32_bf16 v[110:113], v[184:187], v[192:195], 0
	v_mfma_f32_16x16x32_bf16 v[102:105], v[176:179], v[200:203], 0
	v_mfma_f32_16x16x32_bf16 v[94:97], v[184:187], v[200:203], 0
	v_mfma_f32_16x16x32_bf16 v[86:89], v[176:179], v[208:211], 0
	v_mfma_f32_16x16x32_bf16 v[78:81], v[184:187], v[208:211], 0
	v_mfma_f32_16x16x32_bf16 v[70:73], v[176:179], v[216:219], 0
	v_mfma_f32_16x16x32_bf16 v[66:69], v[184:187], v[216:219], 0
	v_mfma_f32_16x16x32_bf16 v[118:121], v[180:183], v[196:199], v[118:121]
	v_mfma_f32_16x16x32_bf16 v[110:113], v[188:191], v[196:199], v[110:113]
	v_mfma_f32_16x16x32_bf16 v[102:105], v[180:183], v[204:207], v[102:105]
	v_mfma_f32_16x16x32_bf16 v[94:97], v[188:191], v[204:207], v[94:97]
	v_mfma_f32_16x16x32_bf16 v[86:89], v[180:183], v[212:215], v[86:89]
	v_mfma_f32_16x16x32_bf16 v[78:81], v[188:191], v[212:215], v[78:81]
	v_mfma_f32_16x16x32_bf16 v[70:73], v[180:183], v[220:223], v[70:73]
	v_mfma_f32_16x16x32_bf16 v[66:69], v[188:191], v[220:223], v[66:69]
	s_barrier
	s_setprio 0
	s_add_i32 s59, s48, s28
	v_lshl_add_u64 v[164:165], s[24:25], 0, v[134:135]
	s_mov_b32 m0, s59
	ds_read_b128 v[192:195], v172 offset:16384
	ds_read_b128 v[196:199], v172 offset:17408
	ds_read_b128 v[200:203], v172 offset:18432
	ds_read_b128 v[204:207], v172 offset:19456
	ds_read_b128 v[208:211], v172 offset:20480
	ds_read_b128 v[212:215], v172 offset:21504
	ds_read_b128 v[216:219], v172 offset:22528
	ds_read_b128 v[220:223], v172 offset:23552
	global_load_lds_dwordx4 v[164:165], off
	s_add_i32 m0, s59, 0x2000
	s_add_u32 s60, s24, 0x40000
	v_lshl_add_u64 v[224:225], s[24:25], 0, v[130:131]
	s_addc_u32 s61, s25, 0
	s_add_i32 s59, s49, s28
	global_load_lds_dwordx4 v[224:225], off
	s_mov_b32 m0, s59
	v_lshl_add_u64 v[230:231], s[26:27], 0, v[132:133]
	global_load_lds_dwordx4 v134, s[60:61]
	s_add_i32 m0, s59, 0x2000
	s_nop 0
	global_load_lds_dwordx4 v130, s[60:61]
	v_lshl_add_u64 v[226:227], s[26:27], 0, v[136:137]
	s_mov_b32 m0, s21
	s_nop 0
	global_load_lds_dwordx4 v[226:227], off
	s_mov_b32 m0, s31
	s_nop 0
	global_load_lds_dwordx4 v[230:231], off
	s_waitcnt vmcnt(8)
	s_waitcnt lgkmcnt(0)
	s_setprio 3
	s_barrier
; #define PG8_STAGE_A(b, h, ptr, NX) do { if constexpr (Sched::GATHER) { unsigned gs_[2]; gs_[0] = ((NX) && last_) ? gN[h][0] : gA[h][0]; gs_[1] = ((NX) && last_) ? gN[h][1] : gA[h][1]; PG8_STAGE(PG8_SA(b, h), ptr, gs_); } \
;         else PG8_STAGE(PG8_SA(b, h), (ptr) + ((h) ? hstep : (size_t)0), voffA); } while (0)
; #define PG8_LDA(dst, b, h) do { _Pragma("unroll") for (int m = 0; m < 4; ++m) _Pragma("unroll") for (int k = 0; k < 2; ++k) dst[m][k] = *(const PG8_LAS bf16x8*)(lds + PG8_SA(b, h) + aoff + m * 2048 + k * 1024); } while (0)
; #define PG8_LDB(dst, b, h) do { _Pragma("unroll") for (int n = 0; n < 2; ++n) _Pragma("unroll") for (int k = 0; k < 2; ++k) dst[n][k] = *(const PG8_LAS bf16x8*)(lds + PG8_SB(b, h) + boff + n * 2048 + k * 1024); } while (0)
; #define PG8_MMA(ai, bj, At, Bt) do { __builtin_amdgcn_s_setprio(1); _Pragma("unroll") for (int m = 0; m < 4; ++m) _Pragma("unroll") for (int n = 0; n < 2; ++n) _Pragma("unroll") for (int k = 0; k < 2; ++k) \
;         acc[ai][bj][m][n] = __builtin_amdgcn_mfma_f32_16x16x32_bf16(Bt[n][k], At[m][k], acc[ai][bj][m][n], 0, 0, 0); __builtin_amdgcn_s_setprio(0); } while (0)
; #define PG8_WAIT_V(n) asm volatile("s_waitcnt vmcnt(" #n ")" ::: "memory")
; #define PG8_WAIT_L(n) asm volatile("s_waitcnt lgkmcnt(" #n ")" ::: "memory")
; #define PG8_BAR __builtin_amdgcn_s_barrier()
; #define PG8_SCHED __builtin_amdgcn_sched_barrier(0)
; template <class Epi, class Sched, bool ALIGN_EPI = false, bool SP2 = false>
; __device__ __forceinline__ void gemm_phase(PG8_LAS unsigned char* lds, const Gemm g, const Sched& S, const Epi& E, const bool skip_epi = false) {
;     ...
;             PG8_WAIT_V(8); PG8_WAIT_L(0); PG8_BAR; PG8_MMA(1, 0, At, B0); PG8_MMA(1, 1, At, B1); PG8_BAR; PG8_SCHED;
;             PG8_LDB(B0, 1, 0); PG8_LDB(B1, 1, 1); PG8_SCHED; PG8_LDA(At, 1, 0); PG8_STAGE_A(0, 1, a2, true);
;             PG8_WAIT_V(8); PG8_WAIT_L(0); PG8_BAR; PG8_MMA(0, 0, At, B0); PG8_MMA(0, 1, At, B1); PG8_BAR; PG8_SCHED;
	s_waitcnt lgkmcnt(0)
	v_mfma_f32_16x16x32_bf16 v[62:65], v[148:151], v[192:195], 0
	v_mfma_f32_16x16x32_bf16 v[58:61], v[156:159], v[192:195], 0
	v_mfma_f32_16x16x32_bf16 v[50:53], v[148:151], v[200:203], 0
	v_mfma_f32_16x16x32_bf16 v[42:45], v[156:159], v[200:203], 0
	v_mfma_f32_16x16x32_bf16 v[34:37], v[148:151], v[208:211], 0
	v_mfma_f32_16x16x32_bf16 v[26:29], v[156:159], v[208:211], 0
	v_mfma_f32_16x16x32_bf16 v[18:21], v[148:151], v[216:219], 0
	v_mfma_f32_16x16x32_bf16 v[10:13], v[156:159], v[216:219], 0
	v_mfma_f32_16x16x32_bf16 v[62:65], v[152:155], v[196:199], v[62:65]
	v_mfma_f32_16x16x32_bf16 v[58:61], v[160:163], v[196:199], v[58:61]
	v_mfma_f32_16x16x32_bf16 v[50:53], v[152:155], v[204:207], v[50:53]
	v_mfma_f32_16x16x32_bf16 v[42:45], v[160:163], v[204:207], v[42:45]
	v_mfma_f32_16x16x32_bf16 v[34:37], v[152:155], v[212:215], v[34:37]
	v_mfma_f32_16x16x32_bf16 v[26:29], v[160:163], v[212:215], v[26:29]
	v_mfma_f32_16x16x32_bf16 v[18:21], v[152:155], v[220:223], v[18:21]
	v_mfma_f32_16x16x32_bf16 v[10:13], v[160:163], v[220:223], v[10:13]
	v_mfma_f32_16x16x32_bf16 v[54:57], v[176:179], v[192:195], 0
	v_mfma_f32_16x16x32_bf16 v[46:49], v[184:187], v[192:195], 0
	v_mfma_f32_16x16x32_bf16 v[38:41], v[176:179], v[200:203], 0
	v_mfma_f32_16x16x32_bf16 v[30:33], v[184:187], v[200:203], 0
	v_mfma_f32_16x16x32_bf16 v[22:25], v[176:179], v[208:211], 0
	v_mfma_f32_16x16x32_bf16 v[14:17], v[184:187], v[208:211], 0
	v_mfma_f32_16x16x32_bf16 v[6:9], v[176:179], v[216:219], 0
	v_mfma_f32_16x16x32_bf16 v[2:5], v[184:187], v[216:219], 0
	v_mfma_f32_16x16x32_bf16 v[54:57], v[180:183], v[196:199], v[54:57]
	v_mfma_f32_16x16x32_bf16 v[46:49], v[188:191], v[196:199], v[46:49]
	v_mfma_f32_16x16x32_bf16 v[38:41], v[180:183], v[204:207], v[38:41]
	v_mfma_f32_16x16x32_bf16 v[30:33], v[188:191], v[204:207], v[30:33]
	v_mfma_f32_16x16x32_bf16 v[22:25], v[180:183], v[212:215], v[22:25]
	v_mfma_f32_16x16x32_bf16 v[14:17], v[188:191], v[212:215], v[14:17]
	v_mfma_f32_16x16x32_bf16 v[6:9], v[180:183], v[220:223], v[6:9]
	v_mfma_f32_16x16x32_bf16 v[2:5], v[188:191], v[220:223], v[2:5]
	s_barrier
	s_setprio 0
	s_add_i32 s59, 0, 0x18000
	s_add_i32 s60, 0, 0x1c000
	v_add_u32_e32 v160, s59, v1
	v_add_u32_e32 v188, s60, v1
	ds_read_b128 v[148:151], v160
	ds_read_b128 v[152:155], v160 offset:1024
	ds_read_b128 v[156:159], v160 offset:2048
	ds_read_b128 v[160:163], v160 offset:3072
	ds_read_b128 v[176:179], v188
	ds_read_b128 v[180:183], v188 offset:1024
	ds_read_b128 v[184:187], v188 offset:2048
	ds_read_b128 v[188:191], v188 offset:3072
	s_add_u32 s26, s26, 0x40000
	s_addc_u32 s27, s27, 0
	s_mov_b32 m0, s34
	ds_read_b128 v[192:195], v172 offset:32768
	ds_read_b128 v[196:199], v172 offset:33792
	ds_read_b128 v[200:203], v172 offset:34816
	ds_read_b128 v[204:207], v172 offset:35840
	ds_read_b128 v[208:211], v172 offset:36864
	ds_read_b128 v[212:215], v172 offset:37888
	ds_read_b128 v[216:219], v172 offset:38912
	ds_read_b128 v[220:223], v172 offset:39936
	global_load_lds_dwordx4 v136, s[26:27]
	s_mov_b32 m0, s35
	s_nop 0
	global_load_lds_dwordx4 v132, s[26:27]
	s_waitcnt vmcnt(8)
	s_waitcnt lgkmcnt(0)
	s_setprio 3
	s_barrier
	s_waitcnt lgkmcnt(0)
	v_mfma_f32_16x16x32_bf16 v[126:129], v[148:151], v[192:195], v[126:129]
	v_mfma_f32_16x16x32_bf16 v[122:125], v[156:159], v[192:195], v[122:125]
	v_mfma_f32_16x16x32_bf16 v[114:117], v[148:151], v[200:203], v[114:117]
	v_mfma_f32_16x16x32_bf16 v[106:109], v[156:159], v[200:203], v[106:109]
	v_mfma_f32_16x16x32_bf16 v[98:101], v[148:151], v[208:211], v[98:101]
	v_mfma_f32_16x16x32_bf16 v[90:93], v[156:159], v[208:211], v[90:93]
	v_mfma_f32_16x16x32_bf16 v[82:85], v[148:151], v[216:219], v[82:85]
	v_mfma_f32_16x16x32_bf16 v[74:77], v[156:159], v[216:219], v[74:77]
	v_mfma_f32_16x16x32_bf16 v[126:129], v[152:155], v[196:199], v[126:129]
	v_mfma_f32_16x16x32_bf16 v[122:125], v[160:163], v[196:199], v[122:125]
	v_mfma_f32_16x16x32_bf16 v[114:117], v[152:155], v[204:207], v[114:117]
	v_mfma_f32_16x16x32_bf16 v[106:109], v[160:163], v[204:207], v[106:109]
	v_mfma_f32_16x16x32_bf16 v[98:101], v[152:155], v[212:215], v[98:101]
	v_mfma_f32_16x16x32_bf16 v[90:93], v[160:163], v[212:215], v[90:93]
	v_mfma_f32_16x16x32_bf16 v[82:85], v[152:155], v[220:223], v[82:85]
	v_mfma_f32_16x16x32_bf16 v[74:77], v[160:163], v[220:223], v[74:77]
	v_mfma_f32_16x16x32_bf16 v[118:121], v[176:179], v[192:195], v[118:121]
	v_mfma_f32_16x16x32_bf16 v[110:113], v[184:187], v[192:195], v[110:113]
	v_mfma_f32_16x16x32_bf16 v[102:105], v[176:179], v[200:203], v[102:105]
	v_mfma_f32_16x16x32_bf16 v[94:97], v[184:187], v[200:203], v[94:97]
	v_mfma_f32_16x16x32_bf16 v[86:89], v[176:179], v[208:211], v[86:89]
	v_mfma_f32_16x16x32_bf16 v[78:81], v[184:187], v[208:211], v[78:81]
	v_mfma_f32_16x16x32_bf16 v[70:73], v[176:179], v[216:219], v[70:73]
	v_mfma_f32_16x16x32_bf16 v[66:69], v[184:187], v[216:219], v[66:69]
	v_mfma_f32_16x16x32_bf16 v[118:121], v[180:183], v[196:199], v[118:121]
	v_mfma_f32_16x16x32_bf16 v[110:113], v[188:191], v[196:199], v[110:113]
	v_mfma_f32_16x16x32_bf16 v[102:105], v[180:183], v[204:207], v[102:105]
	v_mfma_f32_16x16x32_bf16 v[94:97], v[188:191], v[204:207], v[94:97]
	v_mfma_f32_16x16x32_bf16 v[86:89], v[180:183], v[212:215], v[86:89]
	v_mfma_f32_16x16x32_bf16 v[78:81], v[188:191], v[212:215], v[78:81]
	v_mfma_f32_16x16x32_bf16 v[70:73], v[180:183], v[220:223], v[70:73]
	v_mfma_f32_16x16x32_bf16 v[66:69], v[188:191], v[220:223], v[66:69]
	s_barrier
; #define PG8_STAGE_A(b, h, ptr, NX) do { if constexpr (Sched::GATHER) { unsigned gs_[2]; gs_[0] = ((NX) && last_) ? gN[h][0] : gA[h][0]; gs_[1] = ((NX) && last_) ? gN[h][1] : gA[h][1]; PG8_STAGE(PG8_SA(b, h), ptr, gs_); } \
;         else PG8_STAGE(PG8_SA(b, h), (ptr) + ((h) ? hstep : (size_t)0), voffA); } while (0)
; #define PG8_STAGE(bufoff, gbase, voff) do { _Pragma("unroll") for (int _i = 0; _i < 2; ++_i) \
;         __builtin_amdgcn_global_load_lds((const unsigned*)((const char*)(gbase) + (voff)[_i]), (PG8_LAS unsigned*)(lds + (bufoff) + ldsw + _i * 8192), 16, 0, 0); } while (0)
; #define PG8_LDA(dst, b, h) do { _Pragma("unroll") for (int m = 0; m < 4; ++m) _Pragma("unroll") for (int k = 0; k < 2; ++k) dst[m][k] = *(const PG8_LAS bf16x8*)(lds + PG8_SA(b, h) + aoff + m * 2048 + k * 1024); } while (0)
; #define PG8_LDB(dst, b, h) do { _Pragma("unroll") for (int n = 0; n < 2; ++n) _Pragma("unroll") for (int k = 0; k < 2; ++k) dst[n][k] = *(const PG8_LAS bf16x8*)(lds + PG8_SB(b, h) + boff + n * 2048 + k * 1024); } while (0)
; #define PG8_WAIT_V(n) asm volatile("s_waitcnt vmcnt(" #n ")" ::: "memory")
; #define PG8_BAR __builtin_amdgcn_s_barrier()
; template <class Epi, class Sched, bool ALIGN_EPI = false, bool SP2 = false>
; __device__ __forceinline__ void gemm_phase(PG8_LAS unsigned char* lds, const Gemm g, const Sched& S, const Epi& E, const bool skip_epi = false) {
;     ...
;             PG8_LDB(B0, 0, 0); PG8_LDB(B1, 0, 1); PG8_SCHED; PG8_LDA(At, 0, 0); PG8_STAGE_A(1, 1, a1, false);
;             PG8_WAIT_V(8); PG8_WAIT_L(0); PG8_BAR; PG8_MMA(0, 0, At, B0); PG8_MMA(0, 1, At, B1); PG8_BAR; PG8_SCHED;
;             PG8_LDA(At, 0, 1); PG8_STAGE(PG8_SB(0, 0), b2, voffB); PG8_STAGE(PG8_SB(0, 1), b2 + hstep, voffB); PG8_STAGE_A(0, 0, a2, true);
;             PG8_WAIT_V(8); PG8_WAIT_L(0); PG8_BAR; PG8_MMA(1, 0, At, B0); PG8_MMA(1, 1, At, B1); PG8_BAR; PG8_SCHED;
;             PG8_LDB(B0, 1, 0); PG8_LDB(B1, 1, 1); PG8_SCHED; PG8_LDA(At, 1, 0); PG8_STAGE_A(0, 1, a2, true);
;             PG8_WAIT_V(8); PG8_WAIT_L(0); PG8_BAR; PG8_MMA(0, 0, At, B0); PG8_MMA(0, 1, At, B1); PG8_BAR; PG8_SCHED;
;             PG8_LDA(At, 1, 1); PG8_STAGE(PG8_SB(1, 0), b3, voffB); PG8_STAGE(PG8_SB(1, 1), b3 + hstep, voffB); PG8_STAGE_A(1, 0, a3, true);
;             PG8_WAIT_V(8); PG8_WAIT_L(0); PG8_BAR; PG8_MMA(1, 0, At, B0); PG8_MMA(1, 1, At, B1); PG8_BAR; PG8_SCHED;
	s_setprio 0
	s_add_i32 s26, s59, s28
	s_add_i32 m0, s26, 0xffffff80
	ds_read_b128 v[192:195], v172 offset:49152
	ds_read_b128 v[196:199], v172 offset:50176
	ds_read_b128 v[200:203], v172 offset:51200
	ds_read_b128 v[204:207], v172 offset:52224
	ds_read_b128 v[208:211], v172 offset:53248
	ds_read_b128 v[212:215], v172 offset:54272
	ds_read_b128 v[216:219], v172 offset:55296
	ds_read_b128 v[220:223], v172 offset:56320
	global_load_lds_dwordx4 v[164:165], off offset:128
	s_add_i32 m0, s26, 0x1f80
	s_add_u32 s24, s24, 0x40080
	s_addc_u32 s25, s25, 0
	s_add_i32 s26, s60, s28
	global_load_lds_dwordx4 v[224:225], off offset:128
	s_mov_b32 m0, s26
	s_nop 0
	global_load_lds_dwordx4 v134, s[24:25]
	s_add_i32 m0, s26, 0x2000
	s_nop 0
	global_load_lds_dwordx4 v130, s[24:25]
	s_add_i32 m0, s37, 0xffffff80
	s_nop 0
	global_load_lds_dwordx4 v[226:227], off offset:128
	s_add_i32 m0, s38, 0xffffff80
	s_nop 0
	global_load_lds_dwordx4 v[230:231], off offset:128
	s_waitcnt vmcnt(8)
	s_waitcnt lgkmcnt(0)
	s_setprio 3
	s_barrier
	s_waitcnt lgkmcnt(0)
	v_mfma_f32_16x16x32_bf16 v[62:65], v[148:151], v[192:195], v[62:65]
	v_mfma_f32_16x16x32_bf16 v[58:61], v[156:159], v[192:195], v[58:61]
	v_mfma_f32_16x16x32_bf16 v[50:53], v[148:151], v[200:203], v[50:53]
	v_mfma_f32_16x16x32_bf16 v[42:45], v[156:159], v[200:203], v[42:45]
	v_mfma_f32_16x16x32_bf16 v[34:37], v[148:151], v[208:211], v[34:37]
	v_mfma_f32_16x16x32_bf16 v[26:29], v[156:159], v[208:211], v[26:29]
	v_mfma_f32_16x16x32_bf16 v[18:21], v[148:151], v[216:219], v[18:21]
	v_mfma_f32_16x16x32_bf16 v[10:13], v[156:159], v[216:219], v[10:13]
	v_mfma_f32_16x16x32_bf16 v[62:65], v[152:155], v[196:199], v[62:65]
	v_mfma_f32_16x16x32_bf16 v[58:61], v[160:163], v[196:199], v[58:61]
	v_mfma_f32_16x16x32_bf16 v[50:53], v[152:155], v[204:207], v[50:53]
	v_mfma_f32_16x16x32_bf16 v[42:45], v[160:163], v[204:207], v[42:45]
	v_mfma_f32_16x16x32_bf16 v[34:37], v[152:155], v[212:215], v[34:37]
	v_mfma_f32_16x16x32_bf16 v[26:29], v[160:163], v[212:215], v[26:29]
	v_mfma_f32_16x16x32_bf16 v[18:21], v[152:155], v[220:223], v[18:21]
	v_mfma_f32_16x16x32_bf16 v[10:13], v[160:163], v[220:223], v[10:13]
	v_mfma_f32_16x16x32_bf16 v[54:57], v[176:179], v[192:195], v[54:57]
	v_mfma_f32_16x16x32_bf16 v[46:49], v[184:187], v[192:195], v[46:49]
	v_mfma_f32_16x16x32_bf16 v[38:41], v[176:179], v[200:203], v[38:41]
	v_mfma_f32_16x16x32_bf16 v[30:33], v[184:187], v[200:203], v[30:33]
	v_mfma_f32_16x16x32_bf16 v[22:25], v[176:179], v[208:211], v[22:25]
	v_mfma_f32_16x16x32_bf16 v[14:17], v[184:187], v[208:211], v[14:17]
	v_mfma_f32_16x16x32_bf16 v[6:9], v[176:179], v[216:219], v[6:9]
	v_mfma_f32_16x16x32_bf16 v[2:5], v[184:187], v[216:219], v[2:5]
	v_mfma_f32_16x16x32_bf16 v[54:57], v[180:183], v[196:199], v[54:57]
	v_mfma_f32_16x16x32_bf16 v[46:49], v[188:191], v[196:199], v[46:49]
	v_mfma_f32_16x16x32_bf16 v[38:41], v[180:183], v[204:207], v[38:41]
	v_mfma_f32_16x16x32_bf16 v[30:33], v[188:191], v[204:207], v[30:33]
	v_mfma_f32_16x16x32_bf16 v[22:25], v[180:183], v[212:215], v[22:25]
	v_mfma_f32_16x16x32_bf16 v[14:17], v[188:191], v[212:215], v[14:17]
	v_mfma_f32_16x16x32_bf16 v[6:9], v[180:183], v[220:223], v[6:9]
	v_mfma_f32_16x16x32_bf16 v[2:5], v[188:191], v[220:223], v[2:5]
	s_barrier
	s_setprio 0
	s_add_i32 s58, s58, 2
	s_add_u32 s22, s22, 0x100
	s_addc_u32 s23, s23, 0
	s_add_u32 s56, s56, 0x100
	s_addc_u32 s57, s57, 0
	s_cmp_gt_u32 s58, 13
.LBB0_944:
	ds_read_b128 v[148:151], v170
	ds_read_b128 v[152:155], v170 offset:1024
	ds_read_b128 v[156:159], v170 offset:2048
	ds_read_b128 v[160:163], v170 offset:3072
	ds_read_b128 v[176:179], v171
	ds_read_b128 v[180:183], v171 offset:1024
	ds_read_b128 v[184:187], v171 offset:2048
	ds_read_b128 v[188:191], v171 offset:3072
	s_add_u32 s24, s22, 0xfffc0080
	s_addc_u32 s25, s23, -1
	s_cmp_eq_u32 s58, 12
	s_cselect_b32 s27, s15, s25
	s_cselect_b32 s26, s54, s24
	s_cselect_b32 s25, s13, s57
	s_cselect_b32 s24, s55, s56
	s_add_i32 m0, s21, 0xc000
	ds_read_b128 v[192:195], v172
	ds_read_b128 v[196:199], v172 offset:1024
	ds_read_b128 v[200:203], v172 offset:2048
	ds_read_b128 v[204:207], v172 offset:3072
	ds_read_b128 v[208:211], v172 offset:4096
	ds_read_b128 v[212:215], v172 offset:5120
	ds_read_b128 v[216:219], v172 offset:6144
	ds_read_b128 v[220:223], v172 offset:7168
	global_load_lds_dwordx4 v140, s[22:23]
	s_add_i32 m0, s21, 0xe000
	s_nop 0
	global_load_lds_dwordx4 v142, s[22:23]
	s_waitcnt vmcnt(8)
	s_waitcnt lgkmcnt(0)
	s_setprio 3
	s_barrier
	s_waitcnt lgkmcnt(0)
	v_mfma_f32_16x16x32_bf16 v[126:129], v[148:151], v[192:195], v[126:129]
	v_mfma_f32_16x16x32_bf16 v[122:125], v[156:159], v[192:195], v[122:125]
	v_mfma_f32_16x16x32_bf16 v[114:117], v[148:151], v[200:203], v[114:117]
	v_mfma_f32_16x16x32_bf16 v[106:109], v[156:159], v[200:203], v[106:109]
	v_mfma_f32_16x16x32_bf16 v[98:101], v[148:151], v[208:211], v[98:101]
	v_mfma_f32_16x16x32_bf16 v[90:93], v[156:159], v[208:211], v[90:93]
	v_mfma_f32_16x16x32_bf16 v[82:85], v[148:151], v[216:219], v[82:85]
	v_mfma_f32_16x16x32_bf16 v[74:77], v[156:159], v[216:219], v[74:77]
	v_mfma_f32_16x16x32_bf16 v[126:129], v[152:155], v[196:199], v[126:129]
	v_mfma_f32_16x16x32_bf16 v[122:125], v[160:163], v[196:199], v[122:125]
	v_mfma_f32_16x16x32_bf16 v[114:117], v[152:155], v[204:207], v[114:117]
	v_mfma_f32_16x16x32_bf16 v[106:109], v[160:163], v[204:207], v[106:109]
	v_mfma_f32_16x16x32_bf16 v[98:101], v[152:155], v[212:215], v[98:101]
	v_mfma_f32_16x16x32_bf16 v[90:93], v[160:163], v[212:215], v[90:93]
	v_mfma_f32_16x16x32_bf16 v[82:85], v[152:155], v[220:223], v[82:85]
	v_mfma_f32_16x16x32_bf16 v[74:77], v[160:163], v[220:223], v[74:77]
	v_mfma_f32_16x16x32_bf16 v[118:121], v[176:179], v[192:195], v[118:121]
	v_mfma_f32_16x16x32_bf16 v[110:113], v[184:187], v[192:195], v[110:113]
	v_mfma_f32_16x16x32_bf16 v[102:105], v[176:179], v[200:203], v[102:105]
	v_mfma_f32_16x16x32_bf16 v[94:97], v[184:187], v[200:203], v[94:97]
	v_mfma_f32_16x16x32_bf16 v[86:89], v[176:179], v[208:211], v[86:89]
	v_mfma_f32_16x16x32_bf16 v[78:81], v[184:187], v[208:211], v[78:81]
	v_mfma_f32_16x16x32_bf16 v[70:73], v[176:179], v[216:219], v[70:73]
	v_mfma_f32_16x16x32_bf16 v[66:69], v[184:187], v[216:219], v[66:69]
	v_mfma_f32_16x16x32_bf16 v[118:121], v[180:183], v[196:199], v[118:121]
	v_mfma_f32_16x16x32_bf16 v[110:113], v[188:191], v[196:199], v[110:113]
	v_mfma_f32_16x16x32_bf16 v[102:105], v[180:183], v[204:207], v[102:105]
	v_mfma_f32_16x16x32_bf16 v[94:97], v[188:191], v[204:207], v[94:97]
	v_mfma_f32_16x16x32_bf16 v[86:89], v[180:183], v[212:215], v[86:89]
	v_mfma_f32_16x16x32_bf16 v[78:81], v[188:191], v[212:215], v[78:81]
	v_mfma_f32_16x16x32_bf16 v[70:73], v[180:183], v[220:223], v[70:73]
	v_mfma_f32_16x16x32_bf16 v[66:69], v[188:191], v[220:223], v[66:69]
	s_barrier
; #define PG8_STAGE_A(b, h, ptr, NX) do { if constexpr (Sched::GATHER) { unsigned gs_[2]; gs_[0] = ((NX) && last_) ? gN[h][0] : gA[h][0]; gs_[1] = ((NX) && last_) ? gN[h][1] : gA[h][1]; PG8_STAGE(PG8_SA(b, h), ptr, gs_); } \
;         else PG8_STAGE(PG8_SA(b, h), (ptr) + ((h) ? hstep : (size_t)0), voffA); } while (0)
; #define PG8_STAGE(bufoff, gbase, voff) do { _Pragma("unroll") for (int _i = 0; _i < 2; ++_i) \
;         __builtin_amdgcn_global_load_lds((const unsigned*)((const char*)(gbase) + (voff)[_i]), (PG8_LAS unsigned*)(lds + (bufoff) + ldsw + _i * 8192), 16, 0, 0); } while (0)
; #define PG8_LDA(dst, b, h) do { _Pragma("unroll") for (int m = 0; m < 4; ++m) _Pragma("unroll") for (int k = 0; k < 2; ++k) dst[m][k] = *(const PG8_LAS bf16x8*)(lds + PG8_SA(b, h) + aoff + m * 2048 + k * 1024); } while (0)
; #define PG8_LDB(dst, b, h) do { _Pragma("unroll") for (int n = 0; n < 2; ++n) _Pragma("unroll") for (int k = 0; k < 2; ++k) dst[n][k] = *(const PG8_LAS bf16x8*)(lds + PG8_SB(b, h) + boff + n * 2048 + k * 1024); } while (0)
; #define PG8_MMA(ai, bj, At, Bt) do { __builtin_amdgcn_s_setprio(1); _Pragma("unroll") for (int m = 0; m < 4; ++m) _Pragma("unroll") for (int n = 0; n < 2; ++n) _Pragma("unroll") for (int k = 0; k < 2; ++k) \
;         acc[ai][bj][m][n] = __builtin_amdgcn_mfma_f32_16x16x32_bf16(Bt[n][k], At[m][k], acc[ai][bj][m][n], 0, 0, 0); __builtin_amdgcn_s_setprio(0); } while (0)
; #define PG8_WAIT_V(n) asm volatile("s_waitcnt vmcnt(" #n ")" ::: "memory")
; #define PG8_WAIT_L(n) asm volatile("s_waitcnt lgkmcnt(" #n ")" ::: "memory")
; #define PG8_BAR __builtin_amdgcn_s_barrier()
; #define PG8_SCHED __builtin_amdgcn_sched_barrier(0)
; template <class Epi, class Sched, bool ALIGN_EPI = false, bool SP2 = false>
; __device__ __forceinline__ void gemm_phase(PG8_LAS unsigned char* lds, const Gemm g, const Sched& S, const Epi& E, const bool skip_epi = false) {
;     ...
;             PG8_WAIT_V(8); PG8_WAIT_L(0); PG8_BAR; PG8_MMA(0, 0, At, B0); PG8_MMA(0, 1, At, B1); PG8_BAR; PG8_SCHED;
;             PG8_LDA(At, 0, 1); PG8_STAGE(PG8_SB(0, 0), b2, voffB); PG8_STAGE(PG8_SB(0, 1), b2 + hstep, voffB); PG8_STAGE_A(0, 0, a2, true);
;             PG8_WAIT_V(8); PG8_WAIT_L(0); PG8_BAR; PG8_MMA(1, 0, At, B0); PG8_MMA(1, 1, At, B1); PG8_BAR; PG8_SCHED;
;             PG8_LDB(B0, 1, 0); PG8_LDB(B1, 1, 1); PG8_SCHED; PG8_LDA(At, 1, 0); PG8_STAGE_A(0, 1, a2, true);
	s_setprio 0
	s_add_i32 s59, s48, s28
	v_lshl_add_u64 v[164:165], s[24:25], 0, v[134:135]
	s_mov_b32 m0, s59
	ds_read_b128 v[192:195], v172 offset:16384
	ds_read_b128 v[196:199], v172 offset:17408
	ds_read_b128 v[200:203], v172 offset:18432
	ds_read_b128 v[204:207], v172 offset:19456
	ds_read_b128 v[208:211], v172 offset:20480
	ds_read_b128 v[212:215], v172 offset:21504
	ds_read_b128 v[216:219], v172 offset:22528
	ds_read_b128 v[220:223], v172 offset:23552
	global_load_lds_dwordx4 v[164:165], off
	s_add_i32 m0, s59, 0x2000
	s_add_u32 s60, s24, 0x40000
	v_lshl_add_u64 v[224:225], s[24:25], 0, v[130:131]
	s_addc_u32 s61, s25, 0
	s_add_i32 s59, s49, s28
	global_load_lds_dwordx4 v[224:225], off
	s_mov_b32 m0, s59
	v_lshl_add_u64 v[230:231], s[26:27], 0, v[132:133]
	global_load_lds_dwordx4 v134, s[60:61]
	s_add_i32 m0, s59, 0x2000
	s_nop 0
	global_load_lds_dwordx4 v130, s[60:61]
	v_lshl_add_u64 v[226:227], s[26:27], 0, v[136:137]
	s_mov_b32 m0, s21
	s_nop 0
	global_load_lds_dwordx4 v[226:227], off
	s_mov_b32 m0, s31
	s_nop 0
	global_load_lds_dwordx4 v[230:231], off
	s_waitcnt vmcnt(8)
	s_waitcnt lgkmcnt(0)
	s_setprio 3
	s_barrier
	s_waitcnt lgkmcnt(0)
	v_mfma_f32_16x16x32_bf16 v[62:65], v[148:151], v[192:195], v[62:65]
	v_mfma_f32_16x16x32_bf16 v[58:61], v[156:159], v[192:195], v[58:61]
	v_mfma_f32_16x16x32_bf16 v[50:53], v[148:151], v[200:203], v[50:53]
	v_mfma_f32_16x16x32_bf16 v[42:45], v[156:159], v[200:203], v[42:45]
	v_mfma_f32_16x16x32_bf16 v[34:37], v[148:151], v[208:211], v[34:37]
	v_mfma_f32_16x16x32_bf16 v[26:29], v[156:159], v[208:211], v[26:29]
	v_mfma_f32_16x16x32_bf16 v[18:21], v[148:151], v[216:219], v[18:21]
	v_mfma_f32_16x16x32_bf16 v[10:13], v[156:159], v[216:219], v[10:13]
	v_mfma_f32_16x16x32_bf16 v[62:65], v[152:155], v[196:199], v[62:65]
	v_mfma_f32_16x16x32_bf16 v[58:61], v[160:163], v[196:199], v[58:61]
	v_mfma_f32_16x16x32_bf16 v[50:53], v[152:155], v[204:207], v[50:53]
	v_mfma_f32_16x16x32_bf16 v[42:45], v[160:163], v[204:207], v[42:45]
	v_mfma_f32_16x16x32_bf16 v[34:37], v[152:155], v[212:215], v[34:37]
	v_mfma_f32_16x16x32_bf16 v[26:29], v[160:163], v[212:215], v[26:29]
	v_mfma_f32_16x16x32_bf16 v[18:21], v[152:155], v[220:223], v[18:21]
	v_mfma_f32_16x16x32_bf16 v[10:13], v[160:163], v[220:223], v[10:13]
	v_mfma_f32_16x16x32_bf16 v[54:57], v[176:179], v[192:195], v[54:57]
	v_mfma_f32_16x16x32_bf16 v[46:49], v[184:187], v[192:195], v[46:49]
	v_mfma_f32_16x16x32_bf16 v[38:41], v[176:179], v[200:203], v[38:41]
	v_mfma_f32_16x16x32_bf16 v[30:33], v[184:187], v[200:203], v[30:33]
	v_mfma_f32_16x16x32_bf16 v[22:25], v[176:179], v[208:211], v[22:25]
	v_mfma_f32_16x16x32_bf16 v[14:17], v[184:187], v[208:211], v[14:17]
	v_mfma_f32_16x16x32_bf16 v[6:9], v[176:179], v[216:219], v[6:9]
	v_mfma_f32_16x16x32_bf16 v[2:5], v[184:187], v[216:219], v[2:5]
	v_mfma_f32_16x16x32_bf16 v[54:57], v[180:183], v[196:199], v[54:57]
	v_mfma_f32_16x16x32_bf16 v[46:49], v[188:191], v[196:199], v[46:49]
	v_mfma_f32_16x16x32_bf16 v[38:41], v[180:183], v[204:207], v[38:41]
	v_mfma_f32_16x16x32_bf16 v[30:33], v[188:191], v[204:207], v[30:33]
	v_mfma_f32_16x16x32_bf16 v[22:25], v[180:183], v[212:215], v[22:25]
	v_mfma_f32_16x16x32_bf16 v[14:17], v[188:191], v[212:215], v[14:17]
	v_mfma_f32_16x16x32_bf16 v[6:9], v[180:183], v[220:223], v[6:9]
	v_mfma_f32_16x16x32_bf16 v[2:5], v[188:191], v[220:223], v[2:5]
	s_barrier
	s_setprio 0
	s_add_i32 s59, 0, 0x18000
	s_add_i32 s60, 0, 0x1c000
	v_add_u32_e32 v160, s59, v1
	v_add_u32_e32 v188, s60, v1
	ds_read_b128 v[148:151], v160
	ds_read_b128 v[152:155], v160 offset:1024
	ds_read_b128 v[156:159], v160 offset:2048
	ds_read_b128 v[160:163], v160 offset:3072
	ds_read_b128 v[176:179], v188
	ds_read_b128 v[180:183], v188 offset:1024
	ds_read_b128 v[184:187], v188 offset:2048
	ds_read_b128 v[188:191], v188 offset:3072
	s_add_u32 s26, s26, 0x40000
	s_addc_u32 s27, s27, 0
	s_mov_b32 m0, s34
	ds_read_b128 v[192:195], v172 offset:32768
	ds_read_b128 v[196:199], v172 offset:33792
	ds_read_b128 v[200:203], v172 offset:34816
	ds_read_b128 v[204:207], v172 offset:35840
	ds_read_b128 v[208:211], v172 offset:36864
	ds_read_b128 v[212:215], v172 offset:37888
	ds_read_b128 v[216:219], v172 offset:38912
	ds_read_b128 v[220:223], v172 offset:39936
	global_load_lds_dwordx4 v136, s[26:27]
	s_mov_b32 m0, s35
	s_nop 0
	global_load_lds_dwordx4 v132, s[26:27]
	s_waitcnt vmcnt(8)
	s_waitcnt lgkmcnt(0)
	s_setprio 3
	s_barrier
; #define PG8_STAGE_A(b, h, ptr, NX) do { if constexpr (Sched::GATHER) { unsigned gs_[2]; gs_[0] = ((NX) && last_) ? gN[h][0] : gA[h][0]; gs_[1] = ((NX) && last_) ? gN[h][1] : gA[h][1]; PG8_STAGE(PG8_SA(b, h), ptr, gs_); } \
;         else PG8_STAGE(PG8_SA(b, h), (ptr) + ((h) ? hstep : (size_t)0), voffA); } while (0)
; #define PG8_STAGE(bufoff, gbase, voff) do { _Pragma("unroll") for (int _i = 0; _i < 2; ++_i) \
;         __builtin_amdgcn_global_load_lds((const unsigned*)((const char*)(gbase) + (voff)[_i]), (PG8_LAS unsigned*)(lds + (bufoff) + ldsw + _i * 8192), 16, 0, 0); } while (0)
; #define PG8_LDA(dst, b, h) do { _Pragma("unroll") for (int m = 0; m < 4; ++m) _Pragma("unroll") for (int k = 0; k < 2; ++k) dst[m][k] = *(const PG8_LAS bf16x8*)(lds + PG8_SA(b, h) + aoff + m * 2048 + k * 1024); } while (0)
; #define PG8_LDB(dst, b, h) do { _Pragma("unroll") for (int n = 0; n < 2; ++n) _Pragma("unroll") for (int k = 0; k < 2; ++k) dst[n][k] = *(const PG8_LAS bf16x8*)(lds + PG8_SB(b, h) + boff + n * 2048 + k * 1024); } while (0)
; #define PG8_WAIT_V(n) asm volatile("s_waitcnt vmcnt(" #n ")" ::: "memory")
; #define PG8_WAIT_L(n) asm volatile("s_waitcnt lgkmcnt(" #n ")" ::: "memory")
; __device__ __forceinline__ void rstd8(const float* SS, int rowb, int lane, float (&rs)[2][4]) {
;     f32x4 p[2][4];
; #pragma unroll
;     for (int ai = 0; ai < 2; ++ai)
; #pragma unroll
;         for (int m = 0; m < 4; ++m) p[ai][m] = *(const f32x4*)(SS + (size_t)(rowb + HALF * ai + 16 * m + (lane >> 2)) * 16 + 4 * (lane & 3));
;     asm volatile("" : "+v"(p[0][0]), "+v"(p[0][1]), "+v"(p[0][2]), "+v"(p[0][3]), "+v"(p[1][0]), "+v"(p[1][1]), "+v"(p[1][2]), "+v"(p[1][3]));
; template <class Epi, class Sched, bool ALIGN_EPI = false, bool SP2 = false>
; __device__ __forceinline__ void gemm_phase(PG8_LAS unsigned char* lds, const Gemm g, const Sched& S, const Epi& E, const bool skip_epi = false) {
;     ...
;             PG8_LDB(B0, 1, 0); PG8_LDB(B1, 1, 1); PG8_SCHED; PG8_LDA(At, 1, 0); PG8_STAGE_A(0, 1, a2, true);
;             PG8_WAIT_V(8); PG8_WAIT_L(0); PG8_BAR; PG8_MMA(0, 0, At, B0); PG8_MMA(0, 1, At, B1); PG8_BAR; PG8_SCHED;
;             PG8_LDA(At, 1, 1); PG8_STAGE(PG8_SB(1, 0), b3, voffB); PG8_STAGE(PG8_SB(1, 1), b3 + hstep, voffB); PG8_STAGE_A(1, 0, a3, true);
;             PG8_WAIT_V(8); PG8_WAIT_L(0); PG8_BAR; PG8_MMA(1, 0, At, B0); PG8_MMA(1, 1, At, B1); PG8_BAR; PG8_SCHED;
	s_waitcnt lgkmcnt(0)
	v_mfma_f32_16x16x32_bf16 v[126:129], v[148:151], v[192:195], v[126:129]
	v_mfma_f32_16x16x32_bf16 v[122:125], v[156:159], v[192:195], v[122:125]
	v_mfma_f32_16x16x32_bf16 v[114:117], v[148:151], v[200:203], v[114:117]
	v_mfma_f32_16x16x32_bf16 v[106:109], v[156:159], v[200:203], v[106:109]
	v_mfma_f32_16x16x32_bf16 v[98:101], v[148:151], v[208:211], v[98:101]
	v_mfma_f32_16x16x32_bf16 v[90:93], v[156:159], v[208:211], v[90:93]
	v_mfma_f32_16x16x32_bf16 v[82:85], v[148:151], v[216:219], v[82:85]
	v_mfma_f32_16x16x32_bf16 v[74:77], v[156:159], v[216:219], v[74:77]
	v_mfma_f32_16x16x32_bf16 v[126:129], v[152:155], v[196:199], v[126:129]
	v_mfma_f32_16x16x32_bf16 v[122:125], v[160:163], v[196:199], v[122:125]
	v_mfma_f32_16x16x32_bf16 v[114:117], v[152:155], v[204:207], v[114:117]
	v_mfma_f32_16x16x32_bf16 v[106:109], v[160:163], v[204:207], v[106:109]
	v_mfma_f32_16x16x32_bf16 v[98:101], v[152:155], v[212:215], v[98:101]
	v_mfma_f32_16x16x32_bf16 v[90:93], v[160:163], v[212:215], v[90:93]
	v_mfma_f32_16x16x32_bf16 v[82:85], v[152:155], v[220:223], v[82:85]
	v_mfma_f32_16x16x32_bf16 v[74:77], v[160:163], v[220:223], v[74:77]
	v_mfma_f32_16x16x32_bf16 v[118:121], v[176:179], v[192:195], v[118:121]
	v_mfma_f32_16x16x32_bf16 v[110:113], v[184:187], v[192:195], v[110:113]
	v_mfma_f32_16x16x32_bf16 v[102:105], v[176:179], v[200:203], v[102:105]
	v_mfma_f32_16x16x32_bf16 v[94:97], v[184:187], v[200:203], v[94:97]
	v_mfma_f32_16x16x32_bf16 v[86:89], v[176:179], v[208:211], v[86:89]
	v_mfma_f32_16x16x32_bf16 v[78:81], v[184:187], v[208:211], v[78:81]
	v_mfma_f32_16x16x32_bf16 v[70:73], v[176:179], v[216:219], v[70:73]
	v_mfma_f32_16x16x32_bf16 v[66:69], v[184:187], v[216:219], v[66:69]
	v_mfma_f32_16x16x32_bf16 v[118:121], v[180:183], v[196:199], v[118:121]
	v_mfma_f32_16x16x32_bf16 v[110:113], v[188:191], v[196:199], v[110:113]
	v_mfma_f32_16x16x32_bf16 v[102:105], v[180:183], v[204:207], v[102:105]
	v_mfma_f32_16x16x32_bf16 v[94:97], v[188:191], v[204:207], v[94:97]
	v_mfma_f32_16x16x32_bf16 v[86:89], v[180:183], v[212:215], v[86:89]
	v_mfma_f32_16x16x32_bf16 v[78:81], v[188:191], v[212:215], v[78:81]
	v_mfma_f32_16x16x32_bf16 v[70:73], v[180:183], v[220:223], v[70:73]
	v_mfma_f32_16x16x32_bf16 v[66:69], v[188:191], v[220:223], v[66:69]
	s_barrier
	s_setprio 0
	s_add_i32 s26, s59, s28
	s_add_i32 m0, s26, 0xffffff80
	ds_read_b128 v[192:195], v172 offset:49152
	ds_read_b128 v[196:199], v172 offset:50176
	ds_read_b128 v[200:203], v172 offset:51200
	ds_read_b128 v[204:207], v172 offset:52224
	ds_read_b128 v[208:211], v172 offset:53248
	ds_read_b128 v[212:215], v172 offset:54272
	ds_read_b128 v[216:219], v172 offset:55296
	ds_read_b128 v[220:223], v172 offset:56320
	global_load_lds_dwordx4 v[164:165], off offset:128
	s_add_i32 m0, s26, 0x1f80
	s_add_u32 s24, s24, 0x40080
	s_addc_u32 s25, s25, 0
	s_add_i32 s26, s60, s28
	global_load_lds_dwordx4 v[224:225], off offset:128
	s_mov_b32 m0, s26
	s_nop 0
	global_load_lds_dwordx4 v134, s[24:25]
	s_add_i32 m0, s26, 0x2000
	s_nop 0
	global_load_lds_dwordx4 v130, s[24:25]
	s_add_i32 m0, s37, 0xffffff80
	s_nop 0
	global_load_lds_dwordx4 v[226:227], off offset:128
	s_add_i32 m0, s38, 0xffffff80
	s_nop 0
	global_load_lds_dwordx4 v[230:231], off offset:128
	s_waitcnt vmcnt(8)
	s_waitcnt lgkmcnt(0)
	s_setprio 3
	s_barrier
	s_waitcnt lgkmcnt(0)
	v_mfma_f32_16x16x32_bf16 v[62:65], v[148:151], v[192:195], v[62:65]
	v_mfma_f32_16x16x32_bf16 v[58:61], v[156:159], v[192:195], v[58:61]
	v_mfma_f32_16x16x32_bf16 v[50:53], v[148:151], v[200:203], v[50:53]
	v_mfma_f32_16x16x32_bf16 v[42:45], v[156:159], v[200:203], v[42:45]
	v_mfma_f32_16x16x32_bf16 v[34:37], v[148:151], v[208:211], v[34:37]
	v_mfma_f32_16x16x32_bf16 v[26:29], v[156:159], v[208:211], v[26:29]
	v_mfma_f32_16x16x32_bf16 v[18:21], v[148:151], v[216:219], v[18:21]
	v_mfma_f32_16x16x32_bf16 v[10:13], v[156:159], v[216:219], v[10:13]
	v_mfma_f32_16x16x32_bf16 v[62:65], v[152:155], v[196:199], v[62:65]
	v_mfma_f32_16x16x32_bf16 v[58:61], v[160:163], v[196:199], v[58:61]
	v_mfma_f32_16x16x32_bf16 v[50:53], v[152:155], v[204:207], v[50:53]
	v_mfma_f32_16x16x32_bf16 v[42:45], v[160:163], v[204:207], v[42:45]
	v_mfma_f32_16x16x32_bf16 v[34:37], v[152:155], v[212:215], v[34:37]
	v_mfma_f32_16x16x32_bf16 v[26:29], v[160:163], v[212:215], v[26:29]
	v_mfma_f32_16x16x32_bf16 v[18:21], v[152:155], v[220:223], v[18:21]
	v_mfma_f32_16x16x32_bf16 v[10:13], v[160:163], v[220:223], v[10:13]
	v_mfma_f32_16x16x32_bf16 v[54:57], v[176:179], v[192:195], v[54:57]
	v_mfma_f32_16x16x32_bf16 v[46:49], v[184:187], v[192:195], v[46:49]
	v_mfma_f32_16x16x32_bf16 v[38:41], v[176:179], v[200:203], v[38:41]
	v_mfma_f32_16x16x32_bf16 v[30:33], v[184:187], v[200:203], v[30:33]
	v_mfma_f32_16x16x32_bf16 v[22:25], v[176:179], v[208:211], v[22:25]
	v_mfma_f32_16x16x32_bf16 v[14:17], v[184:187], v[208:211], v[14:17]
	v_mfma_f32_16x16x32_bf16 v[6:9], v[176:179], v[216:219], v[6:9]
	v_mfma_f32_16x16x32_bf16 v[2:5], v[184:187], v[216:219], v[2:5]
	v_mfma_f32_16x16x32_bf16 v[54:57], v[180:183], v[196:199], v[54:57]
	v_mfma_f32_16x16x32_bf16 v[46:49], v[188:191], v[196:199], v[46:49]
	v_mfma_f32_16x16x32_bf16 v[38:41], v[180:183], v[204:207], v[38:41]
	v_mfma_f32_16x16x32_bf16 v[30:33], v[188:191], v[204:207], v[30:33]
	v_mfma_f32_16x16x32_bf16 v[22:25], v[180:183], v[212:215], v[22:25]
	v_mfma_f32_16x16x32_bf16 v[14:17], v[188:191], v[212:215], v[14:17]
	v_mfma_f32_16x16x32_bf16 v[6:9], v[180:183], v[220:223], v[6:9]
	v_mfma_f32_16x16x32_bf16 v[2:5], v[188:191], v[220:223], v[2:5]
	s_barrier
	s_setprio 0
	s_add_i32 s58, s58, 2
	s_add_u32 s22, s22, 0x100
	s_addc_u32 s23, s23, 0
	s_add_u32 s56, s56, 0x100
	s_addc_u32 s57, s57, 0
	s_cmp_gt_u32 s58, 13
	s_cbranch_scc0 .LBB0_944
	v_lshl_add_u32 v164, s20, 8, v167
	v_ashrrev_i32_e32 v165, 31, v164
	v_lshlrev_b64 v[148:149], 6, v[164:165]
	v_lshl_add_u64 v[148:149], v[138:139], 0, v[148:149]
	v_add_co_u32_e32 v150, vcc, 0x2000, v148
	v_addc_co_u32_e32 v151, vcc, 0, v149, vcc
	global_load_dwordx4 v[176:179], v[148:149], off
	global_load_dwordx4 v[180:183], v[148:149], off offset:1024
	global_load_dwordx4 v[184:187], v[148:149], off offset:2048
	global_load_dwordx4 v[188:191], v[148:149], off offset:3072
	global_load_dwordx4 v[192:195], v[150:151], off
	global_load_dwordx4 v[196:199], v[150:151], off offset:1024
	global_load_dwordx4 v[200:203], v[150:151], off offset:2048
	global_load_dwordx4 v[204:207], v[150:151], off offset:3072
	s_and_b64 vcc, exec, s[10:11]
	s_cbranch_vccz .LBB0_947
	s_barrier

; #define PG8_STAGE_A(b, h, ptr, NX) do { if constexpr (Sched::GATHER) { unsigned gs_[2]; gs_[0] = ((NX) && last_) ? gN[h][0] : gA[h][0]; gs_[1] = ((NX) && last_) ? gN[h][1] : gA[h][1]; PG8_STAGE(PG8_SA(b, h), ptr, gs_); } \
;         else PG8_STAGE(PG8_SA(b, h), (ptr) + ((h) ? hstep : (size_t)0), voffA); } while (0)
; #define PG8_STAGE(bufoff, gbase, voff) do { _Pragma("unroll") for (int _i = 0; _i < 2; ++_i) \
;         __builtin_amdgcn_global_load_lds((const unsigned*)((const char*)(gbase) + (voff)[_i]), (PG8_LAS unsigned*)(lds + (bufoff) + ldsw + _i * 8192), 16, 0, 0); } while (0)
; #define PG8_WAIT_V(n) asm volatile("s_waitcnt vmcnt(" #n ")" ::: "memory")
; #define PG8_WAIT_L(n) asm volatile("s_waitcnt lgkmcnt(" #n ")" ::: "memory")
; template <class Epi, class Sched, bool ALIGN_EPI = false, bool SP2 = false>
; __device__ __forceinline__ void gemm_phase(PG8_LAS unsigned char* lds, const Gemm g, const Sched& S, const Epi& E, const bool skip_epi = false) {
;     ...
;         const char* nA = has_next ? (const char*)g.A + (size_t)nxt.pm * pmstepA + nxt.ko : cA; const char* nB = has_next ? (const char*)g.Bt + (size_t)nxt.pn * tstep + nxt.ko : cB;
;         for (int t = 0; t < nt; t += 2) {
;             const bool last = (t == nt - 2); last_ = last && has_next;
;             const char* a1 = cA + (size_t)(t + 1) * kstep;
;             const char* a2 = last ? nA : cA + (size_t)(t + 2) * kstep; const char* b2 = last ? nB : cB + (size_t)(t + 2) * kstep;
;             const char* a3 = a2 + kstep; const char* b3 = b2 + kstep;
;             if (last && has_next) S.a_ready(nxt);
;             if constexpr (SP2) {
;             PG8_LDB(B0, 0, 0); PG8_LDB(B1, 0, 1); PG8_SCHED; PG8_LDA(At, 0, 0); PG8_STAGE_A(1, 1, a1, false);
;             PG8_WAIT_V(8); PG8_WAIT_L(0); PG8_BAR; PG8_MMA(0, 0, At, B0); PG8_MMA(0, 1, At, B1); PG8_BAR; PG8_SCHED;
;             PG8_LDA(At, 0, 1); PG8_STAGE(PG8_SB(0, 0), b2, voffB); PG8_STAGE(PG8_SB(0, 1), b2 + hstep, voffB); PG8_STAGE_A(0, 0, a2, true);
;             PG8_WAIT_V(8); PG8_WAIT_L(0); PG8_BAR; PG8_MMA(1, 0, At, B0); PG8_MMA(1, 1, At, B1); PG8_BAR; PG8_SCHED;
;     ...
;         for (int a = 0; a < 2; ++a)
; #pragma unroll
;             for (int b = 0; b < 2; ++b)
; #pragma unroll
;                 for (int m = 0; m < 4; ++m)
; #pragma unroll
;                     for (int n = 0; n < 2; ++n) acc[a][b][m][n] = (f32x4){0.f, 0.f, 0.f, 0.f};
.LBB0_1323:
	s_ashr_i32 s25, s24, 31
	s_lshl_b64 s[26:27], s[24:25], 19
	s_add_u32 s26, s46, s26
	s_addc_u32 s27, s47, s27
	s_and_b64 s[28:29], s[6:7], exec
	s_cselect_b32 s25, s27, s35
	s_cselect_b32 s31, s26, s34
	s_ashr_i32 s23, s22, 31
	s_lshl_b64 s[28:29], s[22:23], 19
	s_add_u32 s28, s2, s28
	s_addc_u32 s29, s3, s29
	s_and_b64 s[38:39], s[6:7], exec
	s_cselect_b32 s23, s29, s37
	s_cselect_b32 s60, s28, s36
	s_add_u32 s34, s34, 0x40080
	s_addc_u32 s35, s35, 0
	s_add_u32 s61, s36, 0x100
	s_addc_u32 s62, s37, 0
	s_mov_b32 s63, -2
	s_waitcnt vmcnt(0)
	s_waitcnt lgkmcnt(0)
	ds_read_b128 v[98:101], v225
	ds_read_b128 v[110:113], v225 offset:1024
	ds_read_b128 v[122:125], v225 offset:2048
	ds_read_b128 v[130:133], v225 offset:3072
	ds_read_b128 v[146:149], v226
	ds_read_b128 v[150:153], v226 offset:1024
	ds_read_b128 v[154:157], v226 offset:2048
	ds_read_b128 v[158:161], v226 offset:3072
	s_add_u32 s36, s34, 0xfffc0080
	s_addc_u32 s37, s35, -1
	s_cmp_eq_u32 s63, 12
	s_cselect_b32 s39, s25, s37
	s_cselect_b32 s38, s31, s36
	s_cselect_b32 s37, s23, s62
	s_cselect_b32 s36, s60, s61
	s_add_i32 m0, s41, 0xc000
	ds_read_b128 v[162:165], v227
	ds_read_b128 v[166:169], v227 offset:1024
	ds_read_b128 v[170:173], v227 offset:2048
	ds_read_b128 v[174:177], v227 offset:3072
	ds_read_b128 v[178:181], v227 offset:4096
	ds_read_b128 v[182:185], v227 offset:5120
	ds_read_b128 v[202:205], v227 offset:6144
	ds_read_b128 v[206:209], v227 offset:7168
	global_load_lds_dwordx4 v194, s[34:35]
	s_add_i32 m0, s41, 0xe000
	s_nop 0
	global_load_lds_dwordx4 v196, s[34:35]
	s_waitcnt vmcnt(8)
	s_waitcnt lgkmcnt(0)
	s_setprio 3
	s_barrier
	s_waitcnt lgkmcnt(0)
	v_mfma_f32_16x16x32_bf16 v[142:145], v[98:101], v[162:165], 0
	v_mfma_f32_16x16x32_bf16 v[138:141], v[122:125], v[162:165], 0
	v_mfma_f32_16x16x32_bf16 v[118:121], v[98:101], v[170:173], 0
	v_mfma_f32_16x16x32_bf16 v[114:117], v[122:125], v[170:173], 0
	v_mfma_f32_16x16x32_bf16 v[94:97], v[98:101], v[178:181], 0
	v_mfma_f32_16x16x32_bf16 v[90:93], v[122:125], v[178:181], 0
	v_mfma_f32_16x16x32_bf16 v[78:81], v[98:101], v[202:205], 0
	v_mfma_f32_16x16x32_bf16 v[74:77], v[122:125], v[202:205], 0
	v_mfma_f32_16x16x32_bf16 v[142:145], v[110:113], v[166:169], v[142:145]
	v_mfma_f32_16x16x32_bf16 v[138:141], v[130:133], v[166:169], v[138:141]
	v_mfma_f32_16x16x32_bf16 v[118:121], v[110:113], v[174:177], v[118:121]
	v_mfma_f32_16x16x32_bf16 v[114:117], v[130:133], v[174:177], v[114:117]
	v_mfma_f32_16x16x32_bf16 v[94:97], v[110:113], v[182:185], v[94:97]
	v_mfma_f32_16x16x32_bf16 v[90:93], v[130:133], v[182:185], v[90:93]
	v_mfma_f32_16x16x32_bf16 v[78:81], v[110:113], v[206:209], v[78:81]
	v_mfma_f32_16x16x32_bf16 v[74:77], v[130:133], v[206:209], v[74:77]
	v_mfma_f32_16x16x32_bf16 v[134:137], v[146:149], v[162:165], 0
	v_mfma_f32_16x16x32_bf16 v[126:129], v[154:157], v[162:165], 0
	v_mfma_f32_16x16x32_bf16 v[106:109], v[146:149], v[170:173], 0
	v_mfma_f32_16x16x32_bf16 v[102:105], v[154:157], v[170:173], 0
	v_mfma_f32_16x16x32_bf16 v[86:89], v[146:149], v[178:181], 0
	v_mfma_f32_16x16x32_bf16 v[82:85], v[154:157], v[178:181], 0
	v_mfma_f32_16x16x32_bf16 v[70:73], v[146:149], v[202:205], 0
	v_mfma_f32_16x16x32_bf16 v[66:69], v[154:157], v[202:205], 0
	v_mfma_f32_16x16x32_bf16 v[134:137], v[150:153], v[166:169], v[134:137]
	v_mfma_f32_16x16x32_bf16 v[126:129], v[158:161], v[166:169], v[126:129]
	v_mfma_f32_16x16x32_bf16 v[106:109], v[150:153], v[174:177], v[106:109]
	v_mfma_f32_16x16x32_bf16 v[102:105], v[158:161], v[174:177], v[102:105]
	v_mfma_f32_16x16x32_bf16 v[86:89], v[150:153], v[182:185], v[86:89]
	v_mfma_f32_16x16x32_bf16 v[82:85], v[158:161], v[182:185], v[82:85]
	v_mfma_f32_16x16x32_bf16 v[70:73], v[150:153], v[206:209], v[70:73]
	v_mfma_f32_16x16x32_bf16 v[66:69], v[158:161], v[206:209], v[66:69]
	s_barrier
	s_setprio 0
	s_add_i32 s64, s57, s40
	v_lshl_add_u64 v[210:211], s[36:37], 0, v[188:189]
	s_mov_b32 m0, s64
	ds_read_b128 v[162:165], v227 offset:16384
	ds_read_b128 v[166:169], v227 offset:17408
	ds_read_b128 v[170:173], v227 offset:18432
	ds_read_b128 v[174:177], v227 offset:19456
	ds_read_b128 v[178:181], v227 offset:20480
	ds_read_b128 v[182:185], v227 offset:21504
	ds_read_b128 v[202:205], v227 offset:22528
	ds_read_b128 v[206:209], v227 offset:23552
	global_load_lds_dwordx4 v[210:211], off
	s_add_i32 m0, s64, 0x2000
	s_add_u32 s64, s36, 0x40000
	v_lshl_add_u64 v[212:213], s[36:37], 0, v[192:193]
	s_addc_u32 s65, s37, 0
	s_add_i32 s66, s58, s40
	global_load_lds_dwordx4 v[212:213], off
	s_mov_b32 m0, s66
	v_lshl_add_u64 v[216:217], s[38:39], 0, v[190:191]
	global_load_lds_dwordx4 v188, s[64:65]
	s_add_i32 m0, s66, 0x2000
	s_nop 0
	global_load_lds_dwordx4 v192, s[64:65]
	v_lshl_add_u64 v[214:215], s[38:39], 0, v[186:187]
	s_mov_b32 m0, s41
	s_nop 0
	global_load_lds_dwordx4 v[214:215], off
	s_mov_b32 m0, s44
	s_nop 0
	global_load_lds_dwordx4 v[216:217], off
	s_waitcnt vmcnt(8)
	s_waitcnt lgkmcnt(0)
	s_setprio 3
	s_barrier
; #define PG8_STAGE_A(b, h, ptr, NX) do { if constexpr (Sched::GATHER) { unsigned gs_[2]; gs_[0] = ((NX) && last_) ? gN[h][0] : gA[h][0]; gs_[1] = ((NX) && last_) ? gN[h][1] : gA[h][1]; PG8_STAGE(PG8_SA(b, h), ptr, gs_); } \
;         else PG8_STAGE(PG8_SA(b, h), (ptr) + ((h) ? hstep : (size_t)0), voffA); } while (0)
; #define PG8_LDA(dst, b, h) do { _Pragma("unroll") for (int m = 0; m < 4; ++m) _Pragma("unroll") for (int k = 0; k < 2; ++k) dst[m][k] = *(const PG8_LAS bf16x8*)(lds + PG8_SA(b, h) + aoff + m * 2048 + k * 1024); } while (0)
; #define PG8_LDB(dst, b, h) do { _Pragma("unroll") for (int n = 0; n < 2; ++n) _Pragma("unroll") for (int k = 0; k < 2; ++k) dst[n][k] = *(const PG8_LAS bf16x8*)(lds + PG8_SB(b, h) + boff + n * 2048 + k * 1024); } while (0)
; #define PG8_MMA(ai, bj, At, Bt) do { __builtin_amdgcn_s_setprio(1); _Pragma("unroll") for (int m = 0; m < 4; ++m) _Pragma("unroll") for (int n = 0; n < 2; ++n) _Pragma("unroll") for (int k = 0; k < 2; ++k) \
;         acc[ai][bj][m][n] = __builtin_amdgcn_mfma_f32_16x16x32_bf16(Bt[n][k], At[m][k], acc[ai][bj][m][n], 0, 0, 0); __builtin_amdgcn_s_setprio(0); } while (0)
; #define PG8_WAIT_V(n) asm volatile("s_waitcnt vmcnt(" #n ")" ::: "memory")
; #define PG8_WAIT_L(n) asm volatile("s_waitcnt lgkmcnt(" #n ")" ::: "memory")
; #define PG8_BAR __builtin_amdgcn_s_barrier()
; #define PG8_SCHED __builtin_amdgcn_sched_barrier(0)
; template <class Epi, class Sched, bool ALIGN_EPI = false, bool SP2 = false>
; __device__ __forceinline__ void gemm_phase(PG8_LAS unsigned char* lds, const Gemm g, const Sched& S, const Epi& E, const bool skip_epi = false) {
;     ...
;             PG8_WAIT_V(8); PG8_WAIT_L(0); PG8_BAR; PG8_MMA(1, 0, At, B0); PG8_MMA(1, 1, At, B1); PG8_BAR; PG8_SCHED;
;             PG8_LDB(B0, 1, 0); PG8_LDB(B1, 1, 1); PG8_SCHED; PG8_LDA(At, 1, 0); PG8_STAGE_A(0, 1, a2, true);
;             PG8_WAIT_V(8); PG8_WAIT_L(0); PG8_BAR; PG8_MMA(0, 0, At, B0); PG8_MMA(0, 1, At, B1); PG8_BAR; PG8_SCHED;
	s_waitcnt lgkmcnt(0)
	v_mfma_f32_16x16x32_bf16 v[62:65], v[98:101], v[162:165], 0
	v_mfma_f32_16x16x32_bf16 v[58:61], v[122:125], v[162:165], 0
	v_mfma_f32_16x16x32_bf16 v[46:49], v[98:101], v[170:173], 0
	v_mfma_f32_16x16x32_bf16 v[42:45], v[122:125], v[170:173], 0
	v_mfma_f32_16x16x32_bf16 v[30:33], v[98:101], v[178:181], 0
	v_mfma_f32_16x16x32_bf16 v[26:29], v[122:125], v[178:181], 0
	v_mfma_f32_16x16x32_bf16 v[14:17], v[98:101], v[202:205], 0
	v_mfma_f32_16x16x32_bf16 v[10:13], v[122:125], v[202:205], 0
	v_mfma_f32_16x16x32_bf16 v[62:65], v[110:113], v[166:169], v[62:65]
	v_mfma_f32_16x16x32_bf16 v[58:61], v[130:133], v[166:169], v[58:61]
	v_mfma_f32_16x16x32_bf16 v[46:49], v[110:113], v[174:177], v[46:49]
	v_mfma_f32_16x16x32_bf16 v[42:45], v[130:133], v[174:177], v[42:45]
	v_mfma_f32_16x16x32_bf16 v[30:33], v[110:113], v[182:185], v[30:33]
	v_mfma_f32_16x16x32_bf16 v[26:29], v[130:133], v[182:185], v[26:29]
	v_mfma_f32_16x16x32_bf16 v[14:17], v[110:113], v[206:209], v[14:17]
	v_mfma_f32_16x16x32_bf16 v[10:13], v[130:133], v[206:209], v[10:13]
	v_mfma_f32_16x16x32_bf16 v[54:57], v[146:149], v[162:165], 0
	v_mfma_f32_16x16x32_bf16 v[50:53], v[154:157], v[162:165], 0
	v_mfma_f32_16x16x32_bf16 v[38:41], v[146:149], v[170:173], 0
	v_mfma_f32_16x16x32_bf16 v[34:37], v[154:157], v[170:173], 0
	v_mfma_f32_16x16x32_bf16 v[22:25], v[146:149], v[178:181], 0
	v_mfma_f32_16x16x32_bf16 v[18:21], v[154:157], v[178:181], 0
	v_mfma_f32_16x16x32_bf16 v[6:9], v[146:149], v[202:205], 0
	v_mfma_f32_16x16x32_bf16 v[2:5], v[154:157], v[202:205], 0
	v_mfma_f32_16x16x32_bf16 v[54:57], v[150:153], v[166:169], v[54:57]
	v_mfma_f32_16x16x32_bf16 v[50:53], v[158:161], v[166:169], v[50:53]
	v_mfma_f32_16x16x32_bf16 v[38:41], v[150:153], v[174:177], v[38:41]
	v_mfma_f32_16x16x32_bf16 v[34:37], v[158:161], v[174:177], v[34:37]
	v_mfma_f32_16x16x32_bf16 v[22:25], v[150:153], v[182:185], v[22:25]
	v_mfma_f32_16x16x32_bf16 v[18:21], v[158:161], v[182:185], v[18:21]
	v_mfma_f32_16x16x32_bf16 v[6:9], v[150:153], v[206:209], v[6:9]
	v_mfma_f32_16x16x32_bf16 v[2:5], v[158:161], v[206:209], v[2:5]
	s_barrier
	s_setprio 0
	s_add_i32 s64, 0, 0x18000
	s_add_i32 s65, 0, 0x1c000
	v_add_u32_e32 v130, s64, v220
	v_add_u32_e32 v158, s65, v220
	ds_read_b128 v[98:101], v130
	ds_read_b128 v[110:113], v130 offset:1024
	ds_read_b128 v[122:125], v130 offset:2048
	ds_read_b128 v[130:133], v130 offset:3072
	ds_read_b128 v[146:149], v158
	ds_read_b128 v[150:153], v158 offset:1024
	ds_read_b128 v[154:157], v158 offset:2048
	ds_read_b128 v[158:161], v158 offset:3072
	s_add_u32 s38, s38, 0x40000
	s_addc_u32 s39, s39, 0
	s_mov_b32 m0, s45
	ds_read_b128 v[162:165], v227 offset:32768
	ds_read_b128 v[166:169], v227 offset:33792
	ds_read_b128 v[170:173], v227 offset:34816
	ds_read_b128 v[174:177], v227 offset:35840
	ds_read_b128 v[178:181], v227 offset:36864
	ds_read_b128 v[182:185], v227 offset:37888
	ds_read_b128 v[202:205], v227 offset:38912
	ds_read_b128 v[206:209], v227 offset:39936
	global_load_lds_dwordx4 v186, s[38:39]
	s_mov_b32 m0, s48
	s_nop 0
	global_load_lds_dwordx4 v190, s[38:39]
	s_waitcnt vmcnt(8)
	s_waitcnt lgkmcnt(0)
	s_setprio 3
	s_barrier
	s_waitcnt lgkmcnt(0)
	v_mfma_f32_16x16x32_bf16 v[142:145], v[98:101], v[162:165], v[142:145]
	v_mfma_f32_16x16x32_bf16 v[138:141], v[122:125], v[162:165], v[138:141]
	v_mfma_f32_16x16x32_bf16 v[118:121], v[98:101], v[170:173], v[118:121]
	v_mfma_f32_16x16x32_bf16 v[114:117], v[122:125], v[170:173], v[114:117]
	v_mfma_f32_16x16x32_bf16 v[94:97], v[98:101], v[178:181], v[94:97]
	v_mfma_f32_16x16x32_bf16 v[90:93], v[122:125], v[178:181], v[90:93]
	v_mfma_f32_16x16x32_bf16 v[78:81], v[98:101], v[202:205], v[78:81]
	v_mfma_f32_16x16x32_bf16 v[74:77], v[122:125], v[202:205], v[74:77]
	v_mfma_f32_16x16x32_bf16 v[142:145], v[110:113], v[166:169], v[142:145]
	v_mfma_f32_16x16x32_bf16 v[138:141], v[130:133], v[166:169], v[138:141]
	v_mfma_f32_16x16x32_bf16 v[118:121], v[110:113], v[174:177], v[118:121]
	v_mfma_f32_16x16x32_bf16 v[114:117], v[130:133], v[174:177], v[114:117]
	v_mfma_f32_16x16x32_bf16 v[94:97], v[110:113], v[182:185], v[94:97]
	v_mfma_f32_16x16x32_bf16 v[90:93], v[130:133], v[182:185], v[90:93]
	v_mfma_f32_16x16x32_bf16 v[78:81], v[110:113], v[206:209], v[78:81]
	v_mfma_f32_16x16x32_bf16 v[74:77], v[130:133], v[206:209], v[74:77]
	v_mfma_f32_16x16x32_bf16 v[134:137], v[146:149], v[162:165], v[134:137]
	v_mfma_f32_16x16x32_bf16 v[126:129], v[154:157], v[162:165], v[126:129]
	v_mfma_f32_16x16x32_bf16 v[106:109], v[146:149], v[170:173], v[106:109]
	v_mfma_f32_16x16x32_bf16 v[102:105], v[154:157], v[170:173], v[102:105]
	v_mfma_f32_16x16x32_bf16 v[86:89], v[146:149], v[178:181], v[86:89]
	v_mfma_f32_16x16x32_bf16 v[82:85], v[154:157], v[178:181], v[82:85]
	v_mfma_f32_16x16x32_bf16 v[70:73], v[146:149], v[202:205], v[70:73]
	v_mfma_f32_16x16x32_bf16 v[66:69], v[154:157], v[202:205], v[66:69]
	v_mfma_f32_16x16x32_bf16 v[134:137], v[150:153], v[166:169], v[134:137]
	v_mfma_f32_16x16x32_bf16 v[126:129], v[158:161], v[166:169], v[126:129]
	v_mfma_f32_16x16x32_bf16 v[106:109], v[150:153], v[174:177], v[106:109]
	v_mfma_f32_16x16x32_bf16 v[102:105], v[158:161], v[174:177], v[102:105]
	v_mfma_f32_16x16x32_bf16 v[86:89], v[150:153], v[182:185], v[86:89]
	v_mfma_f32_16x16x32_bf16 v[82:85], v[158:161], v[182:185], v[82:85]
	v_mfma_f32_16x16x32_bf16 v[70:73], v[150:153], v[206:209], v[70:73]
	v_mfma_f32_16x16x32_bf16 v[66:69], v[158:161], v[206:209], v[66:69]
	s_barrier
; #define PG8_STAGE_A(b, h, ptr, NX) do { if constexpr (Sched::GATHER) { unsigned gs_[2]; gs_[0] = ((NX) && last_) ? gN[h][0] : gA[h][0]; gs_[1] = ((NX) && last_) ? gN[h][1] : gA[h][1]; PG8_STAGE(PG8_SA(b, h), ptr, gs_); } \
;         else PG8_STAGE(PG8_SA(b, h), (ptr) + ((h) ? hstep : (size_t)0), voffA); } while (0)
; #define PG8_STAGE(bufoff, gbase, voff) do { _Pragma("unroll") for (int _i = 0; _i < 2; ++_i) \
;         __builtin_amdgcn_global_load_lds((const unsigned*)((const char*)(gbase) + (voff)[_i]), (PG8_LAS unsigned*)(lds + (bufoff) + ldsw + _i * 8192), 16, 0, 0); } while (0)
; #define PG8_LDA(dst, b, h) do { _Pragma("unroll") for (int m = 0; m < 4; ++m) _Pragma("unroll") for (int k = 0; k < 2; ++k) dst[m][k] = *(const PG8_LAS bf16x8*)(lds + PG8_SA(b, h) + aoff + m * 2048 + k * 1024); } while (0)
; #define PG8_LDB(dst, b, h) do { _Pragma("unroll") for (int n = 0; n < 2; ++n) _Pragma("unroll") for (int k = 0; k < 2; ++k) dst[n][k] = *(const PG8_LAS bf16x8*)(lds + PG8_SB(b, h) + boff + n * 2048 + k * 1024); } while (0)
; #define PG8_MMA(ai, bj, At, Bt) do { __builtin_amdgcn_s_setprio(1); _Pragma("unroll") for (int m = 0; m < 4; ++m) _Pragma("unroll") for (int n = 0; n < 2; ++n) _Pragma("unroll") for (int k = 0; k < 2; ++k) \
;         acc[ai][bj][m][n] = __builtin_amdgcn_mfma_f32_16x16x32_bf16(Bt[n][k], At[m][k], acc[ai][bj][m][n], 0, 0, 0); __builtin_amdgcn_s_setprio(0); } while (0)
; #define PG8_WAIT_V(n) asm volatile("s_waitcnt vmcnt(" #n ")" ::: "memory")
; #define PG8_BAR __builtin_amdgcn_s_barrier()
; template <class Epi, class Sched, bool ALIGN_EPI = false, bool SP2 = false>
; __device__ __forceinline__ void gemm_phase(PG8_LAS unsigned char* lds, const Gemm g, const Sched& S, const Epi& E, const bool skip_epi = false) {
;     ...
;             PG8_LDB(B0, 0, 0); PG8_LDB(B1, 0, 1); PG8_SCHED; PG8_LDA(At, 0, 0); PG8_STAGE_A(1, 1, a1, false);
;             PG8_WAIT_V(8); PG8_WAIT_L(0); PG8_BAR; PG8_MMA(0, 0, At, B0); PG8_MMA(0, 1, At, B1); PG8_BAR; PG8_SCHED;
;     ...
;             PG8_WAIT_V(8); PG8_WAIT_L(0); PG8_BAR; PG8_MMA(0, 0, At, B0); PG8_MMA(0, 1, At, B1); PG8_BAR; PG8_SCHED;
;             PG8_LDA(At, 1, 1); PG8_STAGE(PG8_SB(1, 0), b3, voffB); PG8_STAGE(PG8_SB(1, 1), b3 + hstep, voffB); PG8_STAGE_A(1, 0, a3, true);
;             PG8_WAIT_V(8); PG8_WAIT_L(0); PG8_BAR; PG8_MMA(1, 0, At, B0); PG8_MMA(1, 1, At, B1); PG8_BAR; PG8_SCHED;
	s_setprio 0
	s_add_i32 s38, s64, s40
	s_add_i32 m0, s38, 0xffffff80
	ds_read_b128 v[162:165], v227 offset:49152
	ds_read_b128 v[166:169], v227 offset:50176
	ds_read_b128 v[170:173], v227 offset:51200
	ds_read_b128 v[174:177], v227 offset:52224
	ds_read_b128 v[178:181], v227 offset:53248
	ds_read_b128 v[182:185], v227 offset:54272
	ds_read_b128 v[202:205], v227 offset:55296
	ds_read_b128 v[206:209], v227 offset:56320
	global_load_lds_dwordx4 v[210:211], off offset:128
	s_add_i32 m0, s38, 0x1f80
	s_add_u32 s36, s36, 0x40080
	s_addc_u32 s37, s37, 0
	s_add_i32 s38, s65, s40
	global_load_lds_dwordx4 v[212:213], off offset:128
	s_mov_b32 m0, s38
	s_nop 0
	global_load_lds_dwordx4 v188, s[36:37]
	s_add_i32 m0, s38, 0x2000
	s_nop 0
	global_load_lds_dwordx4 v192, s[36:37]
	s_add_i32 m0, s53, 0xffffff80
	s_nop 0
	global_load_lds_dwordx4 v[214:215], off offset:128
	s_add_i32 m0, s54, 0xffffff80
	s_nop 0
	global_load_lds_dwordx4 v[216:217], off offset:128
	s_waitcnt vmcnt(8)
	s_waitcnt lgkmcnt(0)
	s_setprio 3
	s_barrier
	s_waitcnt lgkmcnt(0)
	v_mfma_f32_16x16x32_bf16 v[62:65], v[98:101], v[162:165], v[62:65]
	v_mfma_f32_16x16x32_bf16 v[58:61], v[122:125], v[162:165], v[58:61]
	v_mfma_f32_16x16x32_bf16 v[46:49], v[98:101], v[170:173], v[46:49]
	v_mfma_f32_16x16x32_bf16 v[42:45], v[122:125], v[170:173], v[42:45]
	v_mfma_f32_16x16x32_bf16 v[30:33], v[98:101], v[178:181], v[30:33]
	v_mfma_f32_16x16x32_bf16 v[26:29], v[122:125], v[178:181], v[26:29]
	v_mfma_f32_16x16x32_bf16 v[14:17], v[98:101], v[202:205], v[14:17]
	v_mfma_f32_16x16x32_bf16 v[10:13], v[122:125], v[202:205], v[10:13]
	v_mfma_f32_16x16x32_bf16 v[62:65], v[110:113], v[166:169], v[62:65]
	v_mfma_f32_16x16x32_bf16 v[58:61], v[130:133], v[166:169], v[58:61]
	v_mfma_f32_16x16x32_bf16 v[46:49], v[110:113], v[174:177], v[46:49]
	v_mfma_f32_16x16x32_bf16 v[42:45], v[130:133], v[174:177], v[42:45]
	v_mfma_f32_16x16x32_bf16 v[30:33], v[110:113], v[182:185], v[30:33]
	v_mfma_f32_16x16x32_bf16 v[26:29], v[130:133], v[182:185], v[26:29]
	v_mfma_f32_16x16x32_bf16 v[14:17], v[110:113], v[206:209], v[14:17]
	v_mfma_f32_16x16x32_bf16 v[10:13], v[130:133], v[206:209], v[10:13]
	v_mfma_f32_16x16x32_bf16 v[54:57], v[146:149], v[162:165], v[54:57]
	v_mfma_f32_16x16x32_bf16 v[50:53], v[154:157], v[162:165], v[50:53]
	v_mfma_f32_16x16x32_bf16 v[38:41], v[146:149], v[170:173], v[38:41]
	v_mfma_f32_16x16x32_bf16 v[34:37], v[154:157], v[170:173], v[34:37]
	v_mfma_f32_16x16x32_bf16 v[22:25], v[146:149], v[178:181], v[22:25]
	v_mfma_f32_16x16x32_bf16 v[18:21], v[154:157], v[178:181], v[18:21]
	v_mfma_f32_16x16x32_bf16 v[6:9], v[146:149], v[202:205], v[6:9]
	v_mfma_f32_16x16x32_bf16 v[2:5], v[154:157], v[202:205], v[2:5]
	v_mfma_f32_16x16x32_bf16 v[54:57], v[150:153], v[166:169], v[54:57]
	v_mfma_f32_16x16x32_bf16 v[50:53], v[158:161], v[166:169], v[50:53]
	v_mfma_f32_16x16x32_bf16 v[38:41], v[150:153], v[174:177], v[38:41]
	v_mfma_f32_16x16x32_bf16 v[34:37], v[158:161], v[174:177], v[34:37]
	v_mfma_f32_16x16x32_bf16 v[22:25], v[150:153], v[182:185], v[22:25]
	v_mfma_f32_16x16x32_bf16 v[18:21], v[158:161], v[182:185], v[18:21]
	v_mfma_f32_16x16x32_bf16 v[6:9], v[150:153], v[206:209], v[6:9]
	v_mfma_f32_16x16x32_bf16 v[2:5], v[158:161], v[206:209], v[2:5]
	s_barrier
	s_setprio 0
	s_add_i32 s63, s63, 2
	s_add_u32 s34, s34, 0x100
	s_addc_u32 s35, s35, 0
	s_add_u32 s61, s61, 0x100
	s_addc_u32 s62, s62, 0
	s_cmp_gt_u32 s63, 13
.LBB0_1324:
	ds_read_b128 v[98:101], v225
	ds_read_b128 v[110:113], v225 offset:1024
	ds_read_b128 v[122:125], v225 offset:2048
	ds_read_b128 v[130:133], v225 offset:3072
	ds_read_b128 v[146:149], v226
	ds_read_b128 v[150:153], v226 offset:1024
	ds_read_b128 v[154:157], v226 offset:2048
	ds_read_b128 v[158:161], v226 offset:3072
	s_add_u32 s36, s34, 0xfffc0080
	s_addc_u32 s37, s35, -1
	s_cmp_eq_u32 s63, 12
	s_cselect_b32 s39, s25, s37
	s_cselect_b32 s38, s31, s36
	s_cselect_b32 s37, s23, s62
	s_cselect_b32 s36, s60, s61
	s_add_i32 m0, s41, 0xc000
	ds_read_b128 v[162:165], v227
	ds_read_b128 v[166:169], v227 offset:1024
	ds_read_b128 v[170:173], v227 offset:2048
	ds_read_b128 v[174:177], v227 offset:3072
	ds_read_b128 v[178:181], v227 offset:4096
	ds_read_b128 v[182:185], v227 offset:5120
	ds_read_b128 v[202:205], v227 offset:6144
	ds_read_b128 v[206:209], v227 offset:7168
	global_load_lds_dwordx4 v194, s[34:35]
	s_add_i32 m0, s41, 0xe000
	s_nop 0
	global_load_lds_dwordx4 v196, s[34:35]
	s_waitcnt vmcnt(8)
	s_waitcnt lgkmcnt(0)
	s_setprio 3
	s_barrier
	s_waitcnt lgkmcnt(0)
	v_mfma_f32_16x16x32_bf16 v[142:145], v[98:101], v[162:165], v[142:145]
	v_mfma_f32_16x16x32_bf16 v[138:141], v[122:125], v[162:165], v[138:141]
	v_mfma_f32_16x16x32_bf16 v[118:121], v[98:101], v[170:173], v[118:121]
	v_mfma_f32_16x16x32_bf16 v[114:117], v[122:125], v[170:173], v[114:117]
	v_mfma_f32_16x16x32_bf16 v[94:97], v[98:101], v[178:181], v[94:97]
	v_mfma_f32_16x16x32_bf16 v[90:93], v[122:125], v[178:181], v[90:93]
	v_mfma_f32_16x16x32_bf16 v[78:81], v[98:101], v[202:205], v[78:81]
	v_mfma_f32_16x16x32_bf16 v[74:77], v[122:125], v[202:205], v[74:77]
	v_mfma_f32_16x16x32_bf16 v[142:145], v[110:113], v[166:169], v[142:145]
	v_mfma_f32_16x16x32_bf16 v[138:141], v[130:133], v[166:169], v[138:141]
	v_mfma_f32_16x16x32_bf16 v[118:121], v[110:113], v[174:177], v[118:121]
	v_mfma_f32_16x16x32_bf16 v[114:117], v[130:133], v[174:177], v[114:117]
	v_mfma_f32_16x16x32_bf16 v[94:97], v[110:113], v[182:185], v[94:97]
	v_mfma_f32_16x16x32_bf16 v[90:93], v[130:133], v[182:185], v[90:93]
	v_mfma_f32_16x16x32_bf16 v[78:81], v[110:113], v[206:209], v[78:81]
	v_mfma_f32_16x16x32_bf16 v[74:77], v[130:133], v[206:209], v[74:77]
	v_mfma_f32_16x16x32_bf16 v[134:137], v[146:149], v[162:165], v[134:137]
	v_mfma_f32_16x16x32_bf16 v[126:129], v[154:157], v[162:165], v[126:129]
	v_mfma_f32_16x16x32_bf16 v[106:109], v[146:149], v[170:173], v[106:109]
	v_mfma_f32_16x16x32_bf16 v[102:105], v[154:157], v[170:173], v[102:105]
	v_mfma_f32_16x16x32_bf16 v[86:89], v[146:149], v[178:181], v[86:89]
	v_mfma_f32_16x16x32_bf16 v[82:85], v[154:157], v[178:181], v[82:85]
	v_mfma_f32_16x16x32_bf16 v[70:73], v[146:149], v[202:205], v[70:73]
	v_mfma_f32_16x16x32_bf16 v[66:69], v[154:157], v[202:205], v[66:69]
	v_mfma_f32_16x16x32_bf16 v[134:137], v[150:153], v[166:169], v[134:137]
	v_mfma_f32_16x16x32_bf16 v[126:129], v[158:161], v[166:169], v[126:129]
	v_mfma_f32_16x16x32_bf16 v[106:109], v[150:153], v[174:177], v[106:109]
	v_mfma_f32_16x16x32_bf16 v[102:105], v[158:161], v[174:177], v[102:105]
	v_mfma_f32_16x16x32_bf16 v[86:89], v[150:153], v[182:185], v[86:89]
	v_mfma_f32_16x16x32_bf16 v[82:85], v[158:161], v[182:185], v[82:85]
	v_mfma_f32_16x16x32_bf16 v[70:73], v[150:153], v[206:209], v[70:73]
	v_mfma_f32_16x16x32_bf16 v[66:69], v[158:161], v[206:209], v[66:69]
	s_barrier
; #define PG8_STAGE_A(b, h, ptr, NX) do { if constexpr (Sched::GATHER) { unsigned gs_[2]; gs_[0] = ((NX) && last_) ? gN[h][0] : gA[h][0]; gs_[1] = ((NX) && last_) ? gN[h][1] : gA[h][1]; PG8_STAGE(PG8_SA(b, h), ptr, gs_); } \
;         else PG8_STAGE(PG8_SA(b, h), (ptr) + ((h) ? hstep : (size_t)0), voffA); } while (0)
; #define PG8_STAGE(bufoff, gbase, voff) do { _Pragma("unroll") for (int _i = 0; _i < 2; ++_i) \
;         __builtin_amdgcn_global_load_lds((const unsigned*)((const char*)(gbase) + (voff)[_i]), (PG8_LAS unsigned*)(lds + (bufoff) + ldsw + _i * 8192), 16, 0, 0); } while (0)
; #define PG8_LDA(dst, b, h) do { _Pragma("unroll") for (int m = 0; m < 4; ++m) _Pragma("unroll") for (int k = 0; k < 2; ++k) dst[m][k] = *(const PG8_LAS bf16x8*)(lds + PG8_SA(b, h) + aoff + m * 2048 + k * 1024); } while (0)
; #define PG8_LDB(dst, b, h) do { _Pragma("unroll") for (int n = 0; n < 2; ++n) _Pragma("unroll") for (int k = 0; k < 2; ++k) dst[n][k] = *(const PG8_LAS bf16x8*)(lds + PG8_SB(b, h) + boff + n * 2048 + k * 1024); } while (0)
; #define PG8_MMA(ai, bj, At, Bt) do { __builtin_amdgcn_s_setprio(1); _Pragma("unroll") for (int m = 0; m < 4; ++m) _Pragma("unroll") for (int n = 0; n < 2; ++n) _Pragma("unroll") for (int k = 0; k < 2; ++k) \
;         acc[ai][bj][m][n] = __builtin_amdgcn_mfma_f32_16x16x32_bf16(Bt[n][k], At[m][k], acc[ai][bj][m][n], 0, 0, 0); __builtin_amdgcn_s_setprio(0); } while (0)
; #define PG8_WAIT_V(n) asm volatile("s_waitcnt vmcnt(" #n ")" ::: "memory")
; #define PG8_WAIT_L(n) asm volatile("s_waitcnt lgkmcnt(" #n ")" ::: "memory")
; #define PG8_BAR __builtin_amdgcn_s_barrier()
; #define PG8_SCHED __builtin_amdgcn_sched_barrier(0)
; template <class Epi, class Sched, bool ALIGN_EPI = false, bool SP2 = false>
; __device__ __forceinline__ void gemm_phase(PG8_LAS unsigned char* lds, const Gemm g, const Sched& S, const Epi& E, const bool skip_epi = false) {
;     ...
;             PG8_WAIT_V(8); PG8_WAIT_L(0); PG8_BAR; PG8_MMA(0, 0, At, B0); PG8_MMA(0, 1, At, B1); PG8_BAR; PG8_SCHED;
;             PG8_LDA(At, 0, 1); PG8_STAGE(PG8_SB(0, 0), b2, voffB); PG8_STAGE(PG8_SB(0, 1), b2 + hstep, voffB); PG8_STAGE_A(0, 0, a2, true);
;             PG8_WAIT_V(8); PG8_WAIT_L(0); PG8_BAR; PG8_MMA(1, 0, At, B0); PG8_MMA(1, 1, At, B1); PG8_BAR; PG8_SCHED;
;             PG8_LDB(B0, 1, 0); PG8_LDB(B1, 1, 1); PG8_SCHED; PG8_LDA(At, 1, 0); PG8_STAGE_A(0, 1, a2, true);
	s_setprio 0
	s_add_i32 s64, s57, s40
	v_lshl_add_u64 v[210:211], s[36:37], 0, v[188:189]
	s_mov_b32 m0, s64
	ds_read_b128 v[162:165], v227 offset:16384
	ds_read_b128 v[166:169], v227 offset:17408
	ds_read_b128 v[170:173], v227 offset:18432
	ds_read_b128 v[174:177], v227 offset:19456
	ds_read_b128 v[178:181], v227 offset:20480
	ds_read_b128 v[182:185], v227 offset:21504
	ds_read_b128 v[202:205], v227 offset:22528
	ds_read_b128 v[206:209], v227 offset:23552
	global_load_lds_dwordx4 v[210:211], off
	s_add_i32 m0, s64, 0x2000
	s_add_u32 s64, s36, 0x40000
	v_lshl_add_u64 v[212:213], s[36:37], 0, v[192:193]
	s_addc_u32 s65, s37, 0
	s_add_i32 s66, s58, s40
	global_load_lds_dwordx4 v[212:213], off
	s_mov_b32 m0, s66
	v_lshl_add_u64 v[216:217], s[38:39], 0, v[190:191]
	global_load_lds_dwordx4 v188, s[64:65]
	s_add_i32 m0, s66, 0x2000
	s_nop 0
	global_load_lds_dwordx4 v192, s[64:65]
	v_lshl_add_u64 v[214:215], s[38:39], 0, v[186:187]
	s_mov_b32 m0, s41
	s_nop 0
	global_load_lds_dwordx4 v[214:215], off
	s_mov_b32 m0, s44
	s_nop 0
	global_load_lds_dwordx4 v[216:217], off
	s_waitcnt vmcnt(8)
	s_waitcnt lgkmcnt(0)
	s_setprio 3
	s_barrier
	s_waitcnt lgkmcnt(0)
	v_mfma_f32_16x16x32_bf16 v[62:65], v[98:101], v[162:165], v[62:65]
	v_mfma_f32_16x16x32_bf16 v[58:61], v[122:125], v[162:165], v[58:61]
	v_mfma_f32_16x16x32_bf16 v[46:49], v[98:101], v[170:173], v[46:49]
	v_mfma_f32_16x16x32_bf16 v[42:45], v[122:125], v[170:173], v[42:45]
	v_mfma_f32_16x16x32_bf16 v[30:33], v[98:101], v[178:181], v[30:33]
	v_mfma_f32_16x16x32_bf16 v[26:29], v[122:125], v[178:181], v[26:29]
	v_mfma_f32_16x16x32_bf16 v[14:17], v[98:101], v[202:205], v[14:17]
	v_mfma_f32_16x16x32_bf16 v[10:13], v[122:125], v[202:205], v[10:13]
	v_mfma_f32_16x16x32_bf16 v[62:65], v[110:113], v[166:169], v[62:65]
	v_mfma_f32_16x16x32_bf16 v[58:61], v[130:133], v[166:169], v[58:61]
	v_mfma_f32_16x16x32_bf16 v[46:49], v[110:113], v[174:177], v[46:49]
	v_mfma_f32_16x16x32_bf16 v[42:45], v[130:133], v[174:177], v[42:45]
	v_mfma_f32_16x16x32_bf16 v[30:33], v[110:113], v[182:185], v[30:33]
	v_mfma_f32_16x16x32_bf16 v[26:29], v[130:133], v[182:185], v[26:29]
	v_mfma_f32_16x16x32_bf16 v[14:17], v[110:113], v[206:209], v[14:17]
	v_mfma_f32_16x16x32_bf16 v[10:13], v[130:133], v[206:209], v[10:13]
	v_mfma_f32_16x16x32_bf16 v[54:57], v[146:149], v[162:165], v[54:57]
	v_mfma_f32_16x16x32_bf16 v[50:53], v[154:157], v[162:165], v[50:53]
	v_mfma_f32_16x16x32_bf16 v[38:41], v[146:149], v[170:173], v[38:41]
	v_mfma_f32_16x16x32_bf16 v[34:37], v[154:157], v[170:173], v[34:37]
	v_mfma_f32_16x16x32_bf16 v[22:25], v[146:149], v[178:181], v[22:25]
	v_mfma_f32_16x16x32_bf16 v[18:21], v[154:157], v[178:181], v[18:21]
	v_mfma_f32_16x16x32_bf16 v[6:9], v[146:149], v[202:205], v[6:9]
	v_mfma_f32_16x16x32_bf16 v[2:5], v[154:157], v[202:205], v[2:5]
	v_mfma_f32_16x16x32_bf16 v[54:57], v[150:153], v[166:169], v[54:57]
	v_mfma_f32_16x16x32_bf16 v[50:53], v[158:161], v[166:169], v[50:53]
	v_mfma_f32_16x16x32_bf16 v[38:41], v[150:153], v[174:177], v[38:41]
	v_mfma_f32_16x16x32_bf16 v[34:37], v[158:161], v[174:177], v[34:37]
	v_mfma_f32_16x16x32_bf16 v[22:25], v[150:153], v[182:185], v[22:25]
	v_mfma_f32_16x16x32_bf16 v[18:21], v[158:161], v[182:185], v[18:21]
	v_mfma_f32_16x16x32_bf16 v[6:9], v[150:153], v[206:209], v[6:9]
	v_mfma_f32_16x16x32_bf16 v[2:5], v[158:161], v[206:209], v[2:5]
	s_barrier
	s_setprio 0
	s_add_i32 s64, 0, 0x18000
	s_add_i32 s65, 0, 0x1c000
	v_add_u32_e32 v130, s64, v220
	v_add_u32_e32 v158, s65, v220
	ds_read_b128 v[98:101], v130
	ds_read_b128 v[110:113], v130 offset:1024
	ds_read_b128 v[122:125], v130 offset:2048
	ds_read_b128 v[130:133], v130 offset:3072
	ds_read_b128 v[146:149], v158
	ds_read_b128 v[150:153], v158 offset:1024
	ds_read_b128 v[154:157], v158 offset:2048
	ds_read_b128 v[158:161], v158 offset:3072
	s_add_u32 s38, s38, 0x40000
	s_addc_u32 s39, s39, 0
	s_mov_b32 m0, s45
	ds_read_b128 v[162:165], v227 offset:32768
	ds_read_b128 v[166:169], v227 offset:33792
	ds_read_b128 v[170:173], v227 offset:34816
	ds_read_b128 v[174:177], v227 offset:35840
	ds_read_b128 v[178:181], v227 offset:36864
	ds_read_b128 v[182:185], v227 offset:37888
	ds_read_b128 v[202:205], v227 offset:38912
	ds_read_b128 v[206:209], v227 offset:39936
	global_load_lds_dwordx4 v186, s[38:39]
	s_mov_b32 m0, s48
	s_nop 0
	global_load_lds_dwordx4 v190, s[38:39]
	s_waitcnt vmcnt(8)
	s_waitcnt lgkmcnt(0)
	s_setprio 3
	s_barrier
; #define PG8_STAGE_A(b, h, ptr, NX) do { if constexpr (Sched::GATHER) { unsigned gs_[2]; gs_[0] = ((NX) && last_) ? gN[h][0] : gA[h][0]; gs_[1] = ((NX) && last_) ? gN[h][1] : gA[h][1]; PG8_STAGE(PG8_SA(b, h), ptr, gs_); } \
;         else PG8_STAGE(PG8_SA(b, h), (ptr) + ((h) ? hstep : (size_t)0), voffA); } while (0)
; #define PG8_STAGE(bufoff, gbase, voff) do { _Pragma("unroll") for (int _i = 0; _i < 2; ++_i) \
;         __builtin_amdgcn_global_load_lds((const unsigned*)((const char*)(gbase) + (voff)[_i]), (PG8_LAS unsigned*)(lds + (bufoff) + ldsw + _i * 8192), 16, 0, 0); } while (0)
; #define PG8_LDA(dst, b, h) do { _Pragma("unroll") for (int m = 0; m < 4; ++m) _Pragma("unroll") for (int k = 0; k < 2; ++k) dst[m][k] = *(const PG8_LAS bf16x8*)(lds + PG8_SA(b, h) + aoff + m * 2048 + k * 1024); } while (0)
; #define PG8_LDB(dst, b, h) do { _Pragma("unroll") for (int n = 0; n < 2; ++n) _Pragma("unroll") for (int k = 0; k < 2; ++k) dst[n][k] = *(const PG8_LAS bf16x8*)(lds + PG8_SB(b, h) + boff + n * 2048 + k * 1024); } while (0)
; #define PG8_MMA(ai, bj, At, Bt) do { __builtin_amdgcn_s_setprio(1); _Pragma("unroll") for (int m = 0; m < 4; ++m) _Pragma("unroll") for (int n = 0; n < 2; ++n) _Pragma("unroll") for (int k = 0; k < 2; ++k) \
;         acc[ai][bj][m][n] = __builtin_amdgcn_mfma_f32_16x16x32_bf16(Bt[n][k], At[m][k], acc[ai][bj][m][n], 0, 0, 0); __builtin_amdgcn_s_setprio(0); } while (0)
; #define PG8_WAIT_V(n) asm volatile("s_waitcnt vmcnt(" #n ")" ::: "memory")
; #define PG8_WAIT_L(n) asm volatile("s_waitcnt lgkmcnt(" #n ")" ::: "memory")
; #define PG8_BAR __builtin_amdgcn_s_barrier()
; template <class Epi, class Sched, bool ALIGN_EPI = false, bool SP2 = false>
; __device__ __forceinline__ void gemm_phase(PG8_LAS unsigned char* lds, const Gemm g, const Sched& S, const Epi& E, const bool skip_epi = false) {
;     ...
;             PG8_LDB(B0, 1, 0); PG8_LDB(B1, 1, 1); PG8_SCHED; PG8_LDA(At, 1, 0); PG8_STAGE_A(0, 1, a2, true);
;             PG8_WAIT_V(8); PG8_WAIT_L(0); PG8_BAR; PG8_MMA(0, 0, At, B0); PG8_MMA(0, 1, At, B1); PG8_BAR; PG8_SCHED;
;             PG8_LDA(At, 1, 1); PG8_STAGE(PG8_SB(1, 0), b3, voffB); PG8_STAGE(PG8_SB(1, 1), b3 + hstep, voffB); PG8_STAGE_A(1, 0, a3, true);
;             PG8_WAIT_V(8); PG8_WAIT_L(0); PG8_BAR; PG8_MMA(1, 0, At, B0); PG8_MMA(1, 1, At, B1); PG8_BAR; PG8_SCHED;
;     ...
;         if constexpr (ALIGN_EPI) { if (wr == 0) PG8_BAR; }
	s_waitcnt lgkmcnt(0)
	v_mfma_f32_16x16x32_bf16 v[142:145], v[98:101], v[162:165], v[142:145]
	v_mfma_f32_16x16x32_bf16 v[138:141], v[122:125], v[162:165], v[138:141]
	v_mfma_f32_16x16x32_bf16 v[118:121], v[98:101], v[170:173], v[118:121]
	v_mfma_f32_16x16x32_bf16 v[114:117], v[122:125], v[170:173], v[114:117]
	v_mfma_f32_16x16x32_bf16 v[94:97], v[98:101], v[178:181], v[94:97]
	v_mfma_f32_16x16x32_bf16 v[90:93], v[122:125], v[178:181], v[90:93]
	v_mfma_f32_16x16x32_bf16 v[78:81], v[98:101], v[202:205], v[78:81]
	v_mfma_f32_16x16x32_bf16 v[74:77], v[122:125], v[202:205], v[74:77]
	v_mfma_f32_16x16x32_bf16 v[142:145], v[110:113], v[166:169], v[142:145]
	v_mfma_f32_16x16x32_bf16 v[138:141], v[130:133], v[166:169], v[138:141]
	v_mfma_f32_16x16x32_bf16 v[118:121], v[110:113], v[174:177], v[118:121]
	v_mfma_f32_16x16x32_bf16 v[114:117], v[130:133], v[174:177], v[114:117]
	v_mfma_f32_16x16x32_bf16 v[94:97], v[110:113], v[182:185], v[94:97]
	v_mfma_f32_16x16x32_bf16 v[90:93], v[130:133], v[182:185], v[90:93]
	v_mfma_f32_16x16x32_bf16 v[78:81], v[110:113], v[206:209], v[78:81]
	v_mfma_f32_16x16x32_bf16 v[74:77], v[130:133], v[206:209], v[74:77]
	v_mfma_f32_16x16x32_bf16 v[134:137], v[146:149], v[162:165], v[134:137]
	v_mfma_f32_16x16x32_bf16 v[126:129], v[154:157], v[162:165], v[126:129]
	v_mfma_f32_16x16x32_bf16 v[106:109], v[146:149], v[170:173], v[106:109]
	v_mfma_f32_16x16x32_bf16 v[102:105], v[154:157], v[170:173], v[102:105]
	v_mfma_f32_16x16x32_bf16 v[86:89], v[146:149], v[178:181], v[86:89]
	v_mfma_f32_16x16x32_bf16 v[82:85], v[154:157], v[178:181], v[82:85]
	v_mfma_f32_16x16x32_bf16 v[70:73], v[146:149], v[202:205], v[70:73]
	v_mfma_f32_16x16x32_bf16 v[66:69], v[154:157], v[202:205], v[66:69]
	v_mfma_f32_16x16x32_bf16 v[134:137], v[150:153], v[166:169], v[134:137]
	v_mfma_f32_16x16x32_bf16 v[126:129], v[158:161], v[166:169], v[126:129]
	v_mfma_f32_16x16x32_bf16 v[106:109], v[150:153], v[174:177], v[106:109]
	v_mfma_f32_16x16x32_bf16 v[102:105], v[158:161], v[174:177], v[102:105]
	v_mfma_f32_16x16x32_bf16 v[86:89], v[150:153], v[182:185], v[86:89]
	v_mfma_f32_16x16x32_bf16 v[82:85], v[158:161], v[182:185], v[82:85]
	v_mfma_f32_16x16x32_bf16 v[70:73], v[150:153], v[206:209], v[70:73]
	v_mfma_f32_16x16x32_bf16 v[66:69], v[158:161], v[206:209], v[66:69]
	s_barrier
	s_setprio 0
	s_add_i32 s38, s64, s40
	s_add_i32 m0, s38, 0xffffff80
	ds_read_b128 v[162:165], v227 offset:49152
	ds_read_b128 v[166:169], v227 offset:50176
	ds_read_b128 v[170:173], v227 offset:51200
	ds_read_b128 v[174:177], v227 offset:52224
	ds_read_b128 v[178:181], v227 offset:53248
	ds_read_b128 v[182:185], v227 offset:54272
	ds_read_b128 v[202:205], v227 offset:55296
	ds_read_b128 v[206:209], v227 offset:56320
	global_load_lds_dwordx4 v[210:211], off offset:128
	s_add_i32 m0, s38, 0x1f80
	s_add_u32 s36, s36, 0x40080
	s_addc_u32 s37, s37, 0
	s_add_i32 s38, s65, s40
	global_load_lds_dwordx4 v[212:213], off offset:128
	s_mov_b32 m0, s38
	s_nop 0
	global_load_lds_dwordx4 v188, s[36:37]
	s_add_i32 m0, s38, 0x2000
	s_nop 0
	global_load_lds_dwordx4 v192, s[36:37]
	s_add_i32 m0, s53, 0xffffff80
	s_nop 0
	global_load_lds_dwordx4 v[214:215], off offset:128
	s_add_i32 m0, s54, 0xffffff80
	s_nop 0
	global_load_lds_dwordx4 v[216:217], off offset:128
	s_waitcnt vmcnt(8)
	s_waitcnt lgkmcnt(0)
	s_setprio 3
	s_barrier
	s_waitcnt lgkmcnt(0)
	v_mfma_f32_16x16x32_bf16 v[62:65], v[98:101], v[162:165], v[62:65]
	v_mfma_f32_16x16x32_bf16 v[58:61], v[122:125], v[162:165], v[58:61]
	v_mfma_f32_16x16x32_bf16 v[46:49], v[98:101], v[170:173], v[46:49]
	v_mfma_f32_16x16x32_bf16 v[42:45], v[122:125], v[170:173], v[42:45]
	v_mfma_f32_16x16x32_bf16 v[30:33], v[98:101], v[178:181], v[30:33]
	v_mfma_f32_16x16x32_bf16 v[26:29], v[122:125], v[178:181], v[26:29]
	v_mfma_f32_16x16x32_bf16 v[14:17], v[98:101], v[202:205], v[14:17]
	v_mfma_f32_16x16x32_bf16 v[10:13], v[122:125], v[202:205], v[10:13]
	v_mfma_f32_16x16x32_bf16 v[62:65], v[110:113], v[166:169], v[62:65]
	v_mfma_f32_16x16x32_bf16 v[58:61], v[130:133], v[166:169], v[58:61]
	v_mfma_f32_16x16x32_bf16 v[46:49], v[110:113], v[174:177], v[46:49]
	v_mfma_f32_16x16x32_bf16 v[42:45], v[130:133], v[174:177], v[42:45]
	v_mfma_f32_16x16x32_bf16 v[30:33], v[110:113], v[182:185], v[30:33]
	v_mfma_f32_16x16x32_bf16 v[26:29], v[130:133], v[182:185], v[26:29]
	v_mfma_f32_16x16x32_bf16 v[14:17], v[110:113], v[206:209], v[14:17]
	v_mfma_f32_16x16x32_bf16 v[10:13], v[130:133], v[206:209], v[10:13]
	v_mfma_f32_16x16x32_bf16 v[54:57], v[146:149], v[162:165], v[54:57]
	v_mfma_f32_16x16x32_bf16 v[50:53], v[154:157], v[162:165], v[50:53]
	v_mfma_f32_16x16x32_bf16 v[38:41], v[146:149], v[170:173], v[38:41]
	v_mfma_f32_16x16x32_bf16 v[34:37], v[154:157], v[170:173], v[34:37]
	v_mfma_f32_16x16x32_bf16 v[22:25], v[146:149], v[178:181], v[22:25]
	v_mfma_f32_16x16x32_bf16 v[18:21], v[154:157], v[178:181], v[18:21]
	v_mfma_f32_16x16x32_bf16 v[6:9], v[146:149], v[202:205], v[6:9]
	v_mfma_f32_16x16x32_bf16 v[2:5], v[154:157], v[202:205], v[2:5]
	v_mfma_f32_16x16x32_bf16 v[54:57], v[150:153], v[166:169], v[54:57]
	v_mfma_f32_16x16x32_bf16 v[50:53], v[158:161], v[166:169], v[50:53]
	v_mfma_f32_16x16x32_bf16 v[38:41], v[150:153], v[174:177], v[38:41]
	v_mfma_f32_16x16x32_bf16 v[34:37], v[158:161], v[174:177], v[34:37]
	v_mfma_f32_16x16x32_bf16 v[22:25], v[150:153], v[182:185], v[22:25]
	v_mfma_f32_16x16x32_bf16 v[18:21], v[158:161], v[182:185], v[18:21]
	v_mfma_f32_16x16x32_bf16 v[6:9], v[150:153], v[206:209], v[6:9]
	v_mfma_f32_16x16x32_bf16 v[2:5], v[158:161], v[206:209], v[2:5]
	s_barrier
	s_setprio 0
	s_add_i32 s63, s63, 2
	s_add_u32 s34, s34, 0x100
	s_addc_u32 s35, s35, 0
	s_add_u32 s61, s61, 0x100
	s_addc_u32 s62, s62, 0
	s_cmp_gt_u32 s63, 13
	s_cbranch_scc0 .LBB0_1324
	s_and_b64 vcc, exec, s[14:15]
	s_cbranch_vccz .LBB0_1327
	s_barrier

; #define PG8_STAGE_A(b, h, ptr, NX) do { if constexpr (Sched::GATHER) { unsigned gs_[2]; gs_[0] = ((NX) && last_) ? gN[h][0] : gA[h][0]; gs_[1] = ((NX) && last_) ? gN[h][1] : gA[h][1]; PG8_STAGE(PG8_SA(b, h), ptr, gs_); } \
;         else PG8_STAGE(PG8_SA(b, h), (ptr) + ((h) ? hstep : (size_t)0), voffA); } while (0)
; #define PG8_STAGE(bufoff, gbase, voff) do { _Pragma("unroll") for (int _i = 0; _i < 2; ++_i) \
;         __builtin_amdgcn_global_load_lds((const unsigned*)((const char*)(gbase) + (voff)[_i]), (PG8_LAS unsigned*)(lds + (bufoff) + ldsw + _i * 8192), 16, 0, 0); } while (0)
; #define PG8_LDA(dst, b, h) do { _Pragma("unroll") for (int m = 0; m < 4; ++m) _Pragma("unroll") for (int k = 0; k < 2; ++k) dst[m][k] = *(const PG8_LAS bf16x8*)(lds + PG8_SA(b, h) + aoff + m * 2048 + k * 1024); } while (0)
; #define PG8_LDB(dst, b, h) do { _Pragma("unroll") for (int n = 0; n < 2; ++n) _Pragma("unroll") for (int k = 0; k < 2; ++k) dst[n][k] = *(const PG8_LAS bf16x8*)(lds + PG8_SB(b, h) + boff + n * 2048 + k * 1024); } while (0)
; #define PG8_MMA(ai, bj, At, Bt) do { __builtin_amdgcn_s_setprio(1); _Pragma("unroll") for (int m = 0; m < 4; ++m) _Pragma("unroll") for (int n = 0; n < 2; ++n) _Pragma("unroll") for (int k = 0; k < 2; ++k) \
;         acc[ai][bj][m][n] = __builtin_amdgcn_mfma_f32_16x16x32_bf16(Bt[n][k], At[m][k], acc[ai][bj][m][n], 0, 0, 0); __builtin_amdgcn_s_setprio(0); } while (0)
; #define PG8_WAIT_V(n) asm volatile("s_waitcnt vmcnt(" #n ")" ::: "memory")
; #define PG8_WAIT_L(n) asm volatile("s_waitcnt lgkmcnt(" #n ")" ::: "memory")
; #define PG8_BAR __builtin_amdgcn_s_barrier()
; #define PG8_SCHED __builtin_amdgcn_sched_barrier(0)
; template <class Epi, class Sched, bool ALIGN_EPI = false, bool SP2 = false>
; __device__ __forceinline__ void gemm_phase(PG8_LAS unsigned char* lds, const Gemm g, const Sched& S, const Epi& E, const bool skip_epi = false) {
;     ...
;             PG8_LDB(B0, 0, 0); PG8_LDB(B1, 0, 1); PG8_SCHED; PG8_LDA(At, 0, 0); PG8_STAGE_A(1, 1, a1, false);
;             PG8_WAIT_V(8); PG8_WAIT_L(0); PG8_BAR; PG8_MMA(0, 0, At, B0); PG8_MMA(0, 1, At, B1); PG8_BAR; PG8_SCHED;
;             PG8_LDA(At, 0, 1); PG8_STAGE(PG8_SB(0, 0), b2, voffB); PG8_STAGE(PG8_SB(0, 1), b2 + hstep, voffB); PG8_STAGE_A(0, 0, a2, true);
;             PG8_WAIT_V(8); PG8_WAIT_L(0); PG8_BAR; PG8_MMA(1, 0, At, B0); PG8_MMA(1, 1, At, B1); PG8_BAR; PG8_SCHED;
.Lg5_zero:
.LBB0_1727:
	s_mov_b32 s29, s41
	s_mov_b32 s31, s40
	v_mov_b32_e32 v143, v133
	v_mov_b32_e32 v141, v133
	s_add_u32 s61, s40, 0x100
	v_lshl_add_u64 v[146:147], s[24:25], 0, v[140:141]
	v_lshl_add_u64 v[148:149], s[24:25], 0, v[142:143]
	s_addc_u32 s62, s41, 0
	s_mov_b32 s63, -2
	s_mov_b64 s[40:41], 0
	ds_read_b128 v[166:169], v158
	ds_read_b128 v[170:173], v158 offset:1024
	ds_read_b128 v[174:177], v158 offset:2048
	ds_read_b128 v[178:181], v158 offset:3072
	ds_read_b128 v[182:185], v159
	ds_read_b128 v[186:189], v159 offset:1024
	ds_read_b128 v[190:193], v159 offset:2048
	ds_read_b128 v[194:197], v159 offset:3072
	s_add_u32 s42, s78, s40
	s_addc_u32 s43, s79, s41
	s_add_u32 s44, s42, 0x1aa00100
	s_addc_u32 s45, s43, 0
	s_add_u32 s66, s61, s40
	s_addc_u32 s67, s62, s41
	s_cmpk_eq_i32 s40, 0x700
	s_cselect_b64 s[64:65], -1, 0
	s_and_b64 s[42:43], s[64:65], exec
	s_cselect_b32 s45, s87, s45
	s_cselect_b32 s44, s86, s44
	s_cselect_b32 s42, s31, s66
	s_cselect_b32 s43, s29, s67
	s_and_b64 vcc, s[6:7], s[64:65]
	v_lshl_add_u64 v[226:227], v[148:149], 0, s[40:41]
	s_add_i32 m0, s37, 0xc000
	ds_read_b128 v[198:201], v160
	ds_read_b128 v[202:205], v160 offset:1024
	ds_read_b128 v[206:209], v160 offset:2048
	ds_read_b128 v[210:213], v160 offset:3072
	ds_read_b128 v[214:217], v160 offset:4096
	ds_read_b128 v[218:221], v160 offset:5120
	ds_read_b128 v[222:225], v160 offset:6144
	ds_read_b128 v[230:233], v160 offset:7168
	global_load_lds_dwordx4 v[226:227], off
	v_lshl_add_u64 v[226:227], v[146:147], 0, s[40:41]
	s_add_i32 m0, s37, 0xe000
	s_nop 0
	global_load_lds_dwordx4 v[226:227], off
	s_waitcnt vmcnt(8)
	s_waitcnt lgkmcnt(0)
	s_setprio 3
	s_barrier
	s_waitcnt lgkmcnt(0)
	v_mfma_f32_16x16x32_bf16 v[126:129], v[166:169], v[198:201], 0
	v_mfma_f32_16x16x32_bf16 v[122:125], v[174:177], v[198:201], 0
	v_mfma_f32_16x16x32_bf16 v[110:113], v[166:169], v[206:209], 0
	v_mfma_f32_16x16x32_bf16 v[106:109], v[174:177], v[206:209], 0
	v_mfma_f32_16x16x32_bf16 v[94:97], v[166:169], v[214:217], 0
	v_mfma_f32_16x16x32_bf16 v[90:93], v[174:177], v[214:217], 0
	v_mfma_f32_16x16x32_bf16 v[78:81], v[166:169], v[222:225], 0
	v_mfma_f32_16x16x32_bf16 v[74:77], v[174:177], v[222:225], 0
	v_mfma_f32_16x16x32_bf16 v[126:129], v[170:173], v[202:205], v[126:129]
	v_mfma_f32_16x16x32_bf16 v[122:125], v[178:181], v[202:205], v[122:125]
	v_mfma_f32_16x16x32_bf16 v[110:113], v[170:173], v[210:213], v[110:113]
	v_mfma_f32_16x16x32_bf16 v[106:109], v[178:181], v[210:213], v[106:109]
	v_mfma_f32_16x16x32_bf16 v[94:97], v[170:173], v[218:221], v[94:97]
	v_mfma_f32_16x16x32_bf16 v[90:93], v[178:181], v[218:221], v[90:93]
	v_mfma_f32_16x16x32_bf16 v[78:81], v[170:173], v[230:233], v[78:81]
	v_mfma_f32_16x16x32_bf16 v[74:77], v[178:181], v[230:233], v[74:77]
	v_mfma_f32_16x16x32_bf16 v[118:121], v[182:185], v[198:201], 0
	v_mfma_f32_16x16x32_bf16 v[114:117], v[190:193], v[198:201], 0
	v_mfma_f32_16x16x32_bf16 v[102:105], v[182:185], v[206:209], 0
	v_mfma_f32_16x16x32_bf16 v[98:101], v[190:193], v[206:209], 0
	v_mfma_f32_16x16x32_bf16 v[86:89], v[182:185], v[214:217], 0
	v_mfma_f32_16x16x32_bf16 v[82:85], v[190:193], v[214:217], 0
	v_mfma_f32_16x16x32_bf16 v[70:73], v[182:185], v[222:225], 0
	v_mfma_f32_16x16x32_bf16 v[66:69], v[190:193], v[222:225], 0
	v_mfma_f32_16x16x32_bf16 v[118:121], v[186:189], v[202:205], v[118:121]
	v_mfma_f32_16x16x32_bf16 v[114:117], v[194:197], v[202:205], v[114:117]
	v_mfma_f32_16x16x32_bf16 v[102:105], v[186:189], v[210:213], v[102:105]
	v_mfma_f32_16x16x32_bf16 v[98:101], v[194:197], v[210:213], v[98:101]
	v_mfma_f32_16x16x32_bf16 v[86:89], v[186:189], v[218:221], v[86:89]
	v_mfma_f32_16x16x32_bf16 v[82:85], v[194:197], v[218:221], v[82:85]
	v_mfma_f32_16x16x32_bf16 v[70:73], v[186:189], v[230:233], v[70:73]
	v_mfma_f32_16x16x32_bf16 v[66:69], v[194:197], v[230:233], v[66:69]
	s_barrier
	s_setprio 0
	s_add_i32 s64, s58, s50
	v_lshl_add_u64 v[226:227], s[42:43], 0, v[134:135]
	s_mov_b32 m0, s64
	ds_read_b128 v[198:201], v160 offset:16384
	ds_read_b128 v[202:205], v160 offset:17408
	ds_read_b128 v[206:209], v160 offset:18432
	ds_read_b128 v[210:213], v160 offset:19456
	ds_read_b128 v[214:217], v160 offset:20480
	ds_read_b128 v[218:221], v160 offset:21504
	ds_read_b128 v[222:225], v160 offset:22528
	ds_read_b128 v[230:233], v160 offset:23552
	global_load_lds_dwordx4 v[226:227], off
	s_add_i32 m0, s64, 0x2000
	s_add_u32 s64, s42, 0x40000
	v_lshl_add_u64 v[234:235], s[42:43], 0, v[136:137]
	s_addc_u32 s65, s43, 0
	s_add_i32 s66, s59, s50
	global_load_lds_dwordx4 v[234:235], off
	s_mov_b32 m0, s66
	v_cndmask_b32_e32 v132, v130, v164, vcc
	global_load_lds_dwordx4 v134, s[64:65]
	s_add_i32 m0, s66, 0x2000
	v_lshl_add_u64 v[238:239], s[44:45], 0, v[132:133]
	global_load_lds_dwordx4 v136, s[64:65]
	s_mov_b32 m0, s37
	v_cndmask_b32_e32 v236, v144, v163, vcc
	global_load_lds_dwordx4 v132, s[44:45]
	s_mov_b32 m0, s39
	v_mov_b32_e32 v237, v133
	global_load_lds_dwordx4 v236, s[44:45]
	s_waitcnt vmcnt(8)
	s_waitcnt lgkmcnt(0)
	v_lshl_add_u64 v[236:237], s[44:45], 0, v[236:237]
	s_setprio 3
	s_barrier
; #define PG8_STAGE_A(b, h, ptr, NX) do { if constexpr (Sched::GATHER) { unsigned gs_[2]; gs_[0] = ((NX) && last_) ? gN[h][0] : gA[h][0]; gs_[1] = ((NX) && last_) ? gN[h][1] : gA[h][1]; PG8_STAGE(PG8_SA(b, h), ptr, gs_); } \
;         else PG8_STAGE(PG8_SA(b, h), (ptr) + ((h) ? hstep : (size_t)0), voffA); } while (0)
; #define PG8_LDA(dst, b, h) do { _Pragma("unroll") for (int m = 0; m < 4; ++m) _Pragma("unroll") for (int k = 0; k < 2; ++k) dst[m][k] = *(const PG8_LAS bf16x8*)(lds + PG8_SA(b, h) + aoff + m * 2048 + k * 1024); } while (0)
; #define PG8_LDB(dst, b, h) do { _Pragma("unroll") for (int n = 0; n < 2; ++n) _Pragma("unroll") for (int k = 0; k < 2; ++k) dst[n][k] = *(const PG8_LAS bf16x8*)(lds + PG8_SB(b, h) + boff + n * 2048 + k * 1024); } while (0)
; #define PG8_MMA(ai, bj, At, Bt) do { __builtin_amdgcn_s_setprio(1); _Pragma("unroll") for (int m = 0; m < 4; ++m) _Pragma("unroll") for (int n = 0; n < 2; ++n) _Pragma("unroll") for (int k = 0; k < 2; ++k) \
;         acc[ai][bj][m][n] = __builtin_amdgcn_mfma_f32_16x16x32_bf16(Bt[n][k], At[m][k], acc[ai][bj][m][n], 0, 0, 0); __builtin_amdgcn_s_setprio(0); } while (0)
; #define PG8_WAIT_V(n) asm volatile("s_waitcnt vmcnt(" #n ")" ::: "memory")
; #define PG8_WAIT_L(n) asm volatile("s_waitcnt lgkmcnt(" #n ")" ::: "memory")
; #define PG8_BAR __builtin_amdgcn_s_barrier()
; #define PG8_SCHED __builtin_amdgcn_sched_barrier(0)
; template <class Epi, class Sched, bool ALIGN_EPI = false, bool SP2 = false>
; __device__ __forceinline__ void gemm_phase(PG8_LAS unsigned char* lds, const Gemm g, const Sched& S, const Epi& E, const bool skip_epi = false) {
;     ...
;             PG8_WAIT_V(8); PG8_WAIT_L(0); PG8_BAR; PG8_MMA(1, 0, At, B0); PG8_MMA(1, 1, At, B1); PG8_BAR; PG8_SCHED;
;             PG8_LDB(B0, 1, 0); PG8_LDB(B1, 1, 1); PG8_SCHED; PG8_LDA(At, 1, 0); PG8_STAGE_A(0, 1, a2, true);
;             PG8_WAIT_V(8); PG8_WAIT_L(0); PG8_BAR; PG8_MMA(0, 0, At, B0); PG8_MMA(0, 1, At, B1); PG8_BAR; PG8_SCHED;
	s_waitcnt lgkmcnt(0)
	v_mfma_f32_16x16x32_bf16 v[62:65], v[166:169], v[198:201], 0
	v_mfma_f32_16x16x32_bf16 v[58:61], v[174:177], v[198:201], 0
	v_mfma_f32_16x16x32_bf16 v[38:41], v[166:169], v[206:209], 0
	v_mfma_f32_16x16x32_bf16 v[34:37], v[174:177], v[206:209], 0
	v_mfma_f32_16x16x32_bf16 v[22:25], v[166:169], v[214:217], 0
	v_mfma_f32_16x16x32_bf16 v[18:21], v[174:177], v[214:217], 0
	v_mfma_f32_16x16x32_bf16 v[6:9], v[166:169], v[222:225], 0
	v_mfma_f32_16x16x32_bf16 v[2:5], v[174:177], v[222:225], 0
	v_mfma_f32_16x16x32_bf16 v[62:65], v[170:173], v[202:205], v[62:65]
	v_mfma_f32_16x16x32_bf16 v[58:61], v[178:181], v[202:205], v[58:61]
	v_mfma_f32_16x16x32_bf16 v[38:41], v[170:173], v[210:213], v[38:41]
	v_mfma_f32_16x16x32_bf16 v[34:37], v[178:181], v[210:213], v[34:37]
	v_mfma_f32_16x16x32_bf16 v[22:25], v[170:173], v[218:221], v[22:25]
	v_mfma_f32_16x16x32_bf16 v[18:21], v[178:181], v[218:221], v[18:21]
	v_mfma_f32_16x16x32_bf16 v[6:9], v[170:173], v[230:233], v[6:9]
	v_mfma_f32_16x16x32_bf16 v[2:5], v[178:181], v[230:233], v[2:5]
	v_mfma_f32_16x16x32_bf16 v[50:53], v[182:185], v[198:201], 0
	v_mfma_f32_16x16x32_bf16 v[42:45], v[190:193], v[198:201], 0
	v_mfma_f32_16x16x32_bf16 v[54:57], v[182:185], v[206:209], 0
	v_mfma_f32_16x16x32_bf16 v[46:49], v[190:193], v[206:209], 0
	v_mfma_f32_16x16x32_bf16 v[30:33], v[182:185], v[214:217], 0
	v_mfma_f32_16x16x32_bf16 v[26:29], v[190:193], v[214:217], 0
	v_mfma_f32_16x16x32_bf16 v[14:17], v[182:185], v[222:225], 0
	v_mfma_f32_16x16x32_bf16 v[10:13], v[190:193], v[222:225], 0
	v_mfma_f32_16x16x32_bf16 v[50:53], v[186:189], v[202:205], v[50:53]
	v_mfma_f32_16x16x32_bf16 v[42:45], v[194:197], v[202:205], v[42:45]
	v_mfma_f32_16x16x32_bf16 v[54:57], v[186:189], v[210:213], v[54:57]
	v_mfma_f32_16x16x32_bf16 v[46:49], v[194:197], v[210:213], v[46:49]
	v_mfma_f32_16x16x32_bf16 v[30:33], v[186:189], v[218:221], v[30:33]
	v_mfma_f32_16x16x32_bf16 v[26:29], v[194:197], v[218:221], v[26:29]
	v_mfma_f32_16x16x32_bf16 v[14:17], v[186:189], v[230:233], v[14:17]
	v_mfma_f32_16x16x32_bf16 v[10:13], v[194:197], v[230:233], v[10:13]
	s_barrier
	s_setprio 0
	s_add_i32 s64, 0, 0x18000
	v_add_u32_e32 v132, s64, v154
	s_add_i32 s65, 0, 0x1c000
	ds_read_b128 v[166:169], v132
	ds_read_b128 v[170:173], v132 offset:1024
	ds_read_b128 v[174:177], v132 offset:2048
	ds_read_b128 v[178:181], v132 offset:3072
	v_add_u32_e32 v132, s65, v154
	ds_read_b128 v[182:185], v132
	ds_read_b128 v[186:189], v132 offset:1024
	ds_read_b128 v[190:193], v132 offset:2048
	ds_read_b128 v[194:197], v132 offset:3072
	s_mov_b32 m0, s51
	v_cndmask_b32_e32 v132, v142, v162, vcc
	ds_read_b128 v[198:201], v160 offset:32768
	ds_read_b128 v[202:205], v160 offset:33792
	ds_read_b128 v[206:209], v160 offset:34816
	ds_read_b128 v[210:213], v160 offset:35840
	ds_read_b128 v[214:217], v160 offset:36864
	ds_read_b128 v[218:221], v160 offset:37888
	ds_read_b128 v[222:225], v160 offset:38912
	ds_read_b128 v[230:233], v160 offset:39936
	v_cndmask_b32_e32 v141, v140, v161, vcc
	global_load_lds_dwordx4 v132, s[44:45]
	s_mov_b32 m0, s52
	s_nop 0
	global_load_lds_dwordx4 v141, s[44:45]
	s_waitcnt vmcnt(8)
	s_waitcnt lgkmcnt(0)
	s_setprio 3
	s_barrier
	s_waitcnt lgkmcnt(0)
	v_mfma_f32_16x16x32_bf16 v[126:129], v[166:169], v[198:201], v[126:129]
	v_mfma_f32_16x16x32_bf16 v[122:125], v[174:177], v[198:201], v[122:125]
	v_mfma_f32_16x16x32_bf16 v[110:113], v[166:169], v[206:209], v[110:113]
	v_mfma_f32_16x16x32_bf16 v[106:109], v[174:177], v[206:209], v[106:109]
	v_mfma_f32_16x16x32_bf16 v[94:97], v[166:169], v[214:217], v[94:97]
	v_mfma_f32_16x16x32_bf16 v[90:93], v[174:177], v[214:217], v[90:93]
	v_mfma_f32_16x16x32_bf16 v[78:81], v[166:169], v[222:225], v[78:81]
	v_mfma_f32_16x16x32_bf16 v[74:77], v[174:177], v[222:225], v[74:77]
	v_mfma_f32_16x16x32_bf16 v[126:129], v[170:173], v[202:205], v[126:129]
	v_mfma_f32_16x16x32_bf16 v[122:125], v[178:181], v[202:205], v[122:125]
	v_mfma_f32_16x16x32_bf16 v[110:113], v[170:173], v[210:213], v[110:113]
	v_mfma_f32_16x16x32_bf16 v[106:109], v[178:181], v[210:213], v[106:109]
	v_mfma_f32_16x16x32_bf16 v[94:97], v[170:173], v[218:221], v[94:97]
	v_mfma_f32_16x16x32_bf16 v[90:93], v[178:181], v[218:221], v[90:93]
	v_mfma_f32_16x16x32_bf16 v[78:81], v[170:173], v[230:233], v[78:81]
	v_mfma_f32_16x16x32_bf16 v[74:77], v[178:181], v[230:233], v[74:77]
	v_mfma_f32_16x16x32_bf16 v[118:121], v[182:185], v[198:201], v[118:121]
	v_mfma_f32_16x16x32_bf16 v[114:117], v[190:193], v[198:201], v[114:117]
	v_mfma_f32_16x16x32_bf16 v[102:105], v[182:185], v[206:209], v[102:105]
	v_mfma_f32_16x16x32_bf16 v[98:101], v[190:193], v[206:209], v[98:101]
	v_mfma_f32_16x16x32_bf16 v[86:89], v[182:185], v[214:217], v[86:89]
	v_mfma_f32_16x16x32_bf16 v[82:85], v[190:193], v[214:217], v[82:85]
	v_mfma_f32_16x16x32_bf16 v[70:73], v[182:185], v[222:225], v[70:73]
	v_mfma_f32_16x16x32_bf16 v[66:69], v[190:193], v[222:225], v[66:69]
	v_mfma_f32_16x16x32_bf16 v[118:121], v[186:189], v[202:205], v[118:121]
	v_mfma_f32_16x16x32_bf16 v[114:117], v[194:197], v[202:205], v[114:117]
	v_mfma_f32_16x16x32_bf16 v[102:105], v[186:189], v[210:213], v[102:105]
	v_mfma_f32_16x16x32_bf16 v[98:101], v[194:197], v[210:213], v[98:101]
	v_mfma_f32_16x16x32_bf16 v[86:89], v[186:189], v[218:221], v[86:89]
	v_mfma_f32_16x16x32_bf16 v[82:85], v[194:197], v[218:221], v[82:85]
	v_mfma_f32_16x16x32_bf16 v[70:73], v[186:189], v[230:233], v[70:73]
	v_mfma_f32_16x16x32_bf16 v[66:69], v[194:197], v[230:233], v[66:69]
	s_barrier
; #define PG8_GIDX(G_, PM_) do { if constexpr (Sched::GATHER) { _Pragma("unroll") for (int h_ = 0; h_ < 2; ++h_) _Pragma("unroll") for (int i_ = 0; i_ < 2; ++i_) { int R_, C_; stage_rc(tid * 16 + i_ * 8192, R_, C_); \
;         const int src_ = S.rowsrc[(PM_) * BM + h_ * HALF + R_]; G_[h_][i_] = (unsigned)(src_ * K + C_) * 2u; } } } while (0)
; #define PG8_STAGE_A(b, h, ptr, NX) do { if constexpr (Sched::GATHER) { unsigned gs_[2]; gs_[0] = ((NX) && last_) ? gN[h][0] : gA[h][0]; gs_[1] = ((NX) && last_) ? gN[h][1] : gA[h][1]; PG8_STAGE(PG8_SA(b, h), ptr, gs_); } \
;         else PG8_STAGE(PG8_SA(b, h), (ptr) + ((h) ? hstep : (size_t)0), voffA); } while (0)
; #define PG8_STAGE(bufoff, gbase, voff) do { _Pragma("unroll") for (int _i = 0; _i < 2; ++_i) \
;         __builtin_amdgcn_global_load_lds((const unsigned*)((const char*)(gbase) + (voff)[_i]), (PG8_LAS unsigned*)(lds + (bufoff) + ldsw + _i * 8192), 16, 0, 0); } while (0)
; #define PG8_LDA(dst, b, h) do { _Pragma("unroll") for (int m = 0; m < 4; ++m) _Pragma("unroll") for (int k = 0; k < 2; ++k) dst[m][k] = *(const PG8_LAS bf16x8*)(lds + PG8_SA(b, h) + aoff + m * 2048 + k * 1024); } while (0)
; #define PG8_WAIT_V(n) asm volatile("s_waitcnt vmcnt(" #n ")" ::: "memory")
; #define PG8_WAIT_L(n) asm volatile("s_waitcnt lgkmcnt(" #n ")" ::: "memory")
; #define PG8_BAR __builtin_amdgcn_s_barrier()
; #define PG8_SCHED __builtin_amdgcn_sched_barrier(0)
; template <class Epi, class Sched, bool ALIGN_EPI = false, bool SP2 = false>
; __device__ __forceinline__ void gemm_phase(PG8_LAS unsigned char* lds, const Gemm g, const Sched& S, const Epi& E, const bool skip_epi = false) {
;     ...
;         const bool has_next = S.next(ui + 1, nxt);
;         if (has_next) PG8_GIDX(gN, nxt.pm);
;         const char* nA = has_next ? (const char*)g.A + (size_t)nxt.pm * pmstepA + nxt.ko : cA; const char* nB = has_next ? (const char*)g.Bt + (size_t)nxt.pn * tstep + nxt.ko : cB;
;     ...
;             PG8_WAIT_V(8); PG8_WAIT_L(0); PG8_BAR; PG8_MMA(0, 0, At, B0); PG8_MMA(0, 1, At, B1); PG8_BAR; PG8_SCHED;
;             PG8_LDA(At, 1, 1); PG8_STAGE(PG8_SB(1, 0), b3, voffB); PG8_STAGE(PG8_SB(1, 1), b3 + hstep, voffB); PG8_STAGE_A(1, 0, a3, true);
;             PG8_WAIT_V(8); PG8_WAIT_L(0); PG8_BAR; PG8_MMA(1, 0, At, B0); PG8_MMA(1, 1, At, B1); PG8_BAR; PG8_SCHED;
	s_setprio 0
	s_add_i32 s44, s64, s50
	s_add_i32 m0, s44, 0xffffff80
	ds_read_b128 v[198:201], v160 offset:49152
	ds_read_b128 v[202:205], v160 offset:50176
	ds_read_b128 v[206:209], v160 offset:51200
	ds_read_b128 v[210:213], v160 offset:52224
	ds_read_b128 v[214:217], v160 offset:53248
	ds_read_b128 v[218:221], v160 offset:54272
	ds_read_b128 v[222:225], v160 offset:55296
	ds_read_b128 v[230:233], v160 offset:56320
	global_load_lds_dwordx4 v[226:227], off offset:128
	s_add_i32 m0, s44, 0x1f80
	s_add_u32 s42, s42, 0x40080
	s_addc_u32 s43, s43, 0
	s_add_i32 s44, s65, s50
	global_load_lds_dwordx4 v[234:235], off offset:128
	s_mov_b32 m0, s44
	s_nop 0
	global_load_lds_dwordx4 v134, s[42:43]
	s_add_i32 m0, s44, 0x2000
	s_nop 0
	global_load_lds_dwordx4 v136, s[42:43]
	s_add_i32 m0, s55, 0xffffff80
	s_nop 0
	global_load_lds_dwordx4 v[238:239], off offset:128
	s_add_i32 m0, s56, 0xffffff80
	s_nop 0
	global_load_lds_dwordx4 v[236:237], off offset:128
	s_waitcnt vmcnt(8)
	s_waitcnt lgkmcnt(0)
	s_setprio 3
	s_barrier
	s_waitcnt lgkmcnt(0)
	v_mfma_f32_16x16x32_bf16 v[62:65], v[166:169], v[198:201], v[62:65]
	v_mfma_f32_16x16x32_bf16 v[58:61], v[174:177], v[198:201], v[58:61]
	v_mfma_f32_16x16x32_bf16 v[38:41], v[166:169], v[206:209], v[38:41]
	v_mfma_f32_16x16x32_bf16 v[34:37], v[174:177], v[206:209], v[34:37]
	v_mfma_f32_16x16x32_bf16 v[22:25], v[166:169], v[214:217], v[22:25]
	v_mfma_f32_16x16x32_bf16 v[18:21], v[174:177], v[214:217], v[18:21]
	v_mfma_f32_16x16x32_bf16 v[6:9], v[166:169], v[222:225], v[6:9]
	v_mfma_f32_16x16x32_bf16 v[2:5], v[174:177], v[222:225], v[2:5]
	v_mfma_f32_16x16x32_bf16 v[62:65], v[170:173], v[202:205], v[62:65]
	v_mfma_f32_16x16x32_bf16 v[58:61], v[178:181], v[202:205], v[58:61]
	v_mfma_f32_16x16x32_bf16 v[38:41], v[170:173], v[210:213], v[38:41]
	v_mfma_f32_16x16x32_bf16 v[34:37], v[178:181], v[210:213], v[34:37]
	v_mfma_f32_16x16x32_bf16 v[22:25], v[170:173], v[218:221], v[22:25]
	v_mfma_f32_16x16x32_bf16 v[18:21], v[178:181], v[218:221], v[18:21]
	v_mfma_f32_16x16x32_bf16 v[6:9], v[170:173], v[230:233], v[6:9]
	v_mfma_f32_16x16x32_bf16 v[2:5], v[178:181], v[230:233], v[2:5]
	v_mfma_f32_16x16x32_bf16 v[50:53], v[182:185], v[198:201], v[50:53]
	v_mfma_f32_16x16x32_bf16 v[42:45], v[190:193], v[198:201], v[42:45]
	v_mfma_f32_16x16x32_bf16 v[54:57], v[182:185], v[206:209], v[54:57]
	v_mfma_f32_16x16x32_bf16 v[46:49], v[190:193], v[206:209], v[46:49]
	v_mfma_f32_16x16x32_bf16 v[30:33], v[182:185], v[214:217], v[30:33]
	v_mfma_f32_16x16x32_bf16 v[26:29], v[190:193], v[214:217], v[26:29]
	v_mfma_f32_16x16x32_bf16 v[14:17], v[182:185], v[222:225], v[14:17]
	v_mfma_f32_16x16x32_bf16 v[10:13], v[190:193], v[222:225], v[10:13]
	v_mfma_f32_16x16x32_bf16 v[50:53], v[186:189], v[202:205], v[50:53]
	v_mfma_f32_16x16x32_bf16 v[42:45], v[194:197], v[202:205], v[42:45]
	v_mfma_f32_16x16x32_bf16 v[54:57], v[186:189], v[210:213], v[54:57]
	v_mfma_f32_16x16x32_bf16 v[46:49], v[194:197], v[210:213], v[46:49]
	v_mfma_f32_16x16x32_bf16 v[30:33], v[186:189], v[218:221], v[30:33]
	v_mfma_f32_16x16x32_bf16 v[26:29], v[194:197], v[218:221], v[26:29]
	v_mfma_f32_16x16x32_bf16 v[14:17], v[186:189], v[230:233], v[14:17]
	v_mfma_f32_16x16x32_bf16 v[10:13], v[194:197], v[230:233], v[10:13]
	s_barrier
	s_setprio 0
	s_add_i32 s63, s63, 2
	s_add_u32 s40, s40, 0x100
	s_addc_u32 s41, s41, 0
	s_cmp_gt_u32 s63, 13
	s_andn2_b64 vcc, exec, s[6:7]
	s_cbranch_vccnz .Lg5_nonext
	s_waitcnt vmcnt(8)
	v_readfirstlane_b32 s34, v250
	v_lshl_add_u32 v164, v229, 11, v152
	v_lshl_add_u32 v163, v251, 11, v153
	v_lshl_add_u32 v162, v252, 11, v152
	v_lshl_add_u32 v161, v253, 11, v153
	s_mul_i32 s34, s34, 28
	s_add_i32 s30, s34, s30
	s_ashr_i32 s31, s30, 31
	s_lshl_b64 s[34:35], s[30:31], 19
	v_readlane_b32 s42, v254, 29
	v_readlane_b32 s43, v254, 30
	s_add_u32 s34, s42, s34
	s_addc_u32 s35, s43, s35
	s_mov_b32 s29, s35
	s_mov_b32 s31, s34
.Lg5_nonext:
.LBB0_1728:
	ds_read_b128 v[166:169], v158
	ds_read_b128 v[170:173], v158 offset:1024
	ds_read_b128 v[174:177], v158 offset:2048
	ds_read_b128 v[178:181], v158 offset:3072
	ds_read_b128 v[182:185], v159
	ds_read_b128 v[186:189], v159 offset:1024
	ds_read_b128 v[190:193], v159 offset:2048
	ds_read_b128 v[194:197], v159 offset:3072
	s_add_u32 s42, s78, s40
	s_addc_u32 s43, s79, s41
	s_add_u32 s44, s42, 0x1aa00100
	s_addc_u32 s45, s43, 0
	s_add_u32 s66, s61, s40
	s_addc_u32 s67, s62, s41
	s_cmpk_eq_i32 s40, 0x700
	s_cselect_b64 s[64:65], -1, 0
	s_and_b64 s[42:43], s[64:65], exec
	s_cselect_b32 s45, s87, s45
	s_cselect_b32 s44, s86, s44
	s_cselect_b32 s42, s31, s66
	s_cselect_b32 s43, s29, s67
	s_and_b64 vcc, s[6:7], s[64:65]
	v_lshl_add_u64 v[226:227], v[148:149], 0, s[40:41]
	s_add_i32 m0, s37, 0xc000
	ds_read_b128 v[198:201], v160
	ds_read_b128 v[202:205], v160 offset:1024
	ds_read_b128 v[206:209], v160 offset:2048
	ds_read_b128 v[210:213], v160 offset:3072
	ds_read_b128 v[214:217], v160 offset:4096
	ds_read_b128 v[218:221], v160 offset:5120
	ds_read_b128 v[222:225], v160 offset:6144
	ds_read_b128 v[230:233], v160 offset:7168
	global_load_lds_dwordx4 v[226:227], off
	v_lshl_add_u64 v[226:227], v[146:147], 0, s[40:41]
	s_add_i32 m0, s37, 0xe000
	s_nop 0
	global_load_lds_dwordx4 v[226:227], off
	s_waitcnt vmcnt(8)
	s_waitcnt lgkmcnt(0)
	s_setprio 3
	s_barrier
; #define PG8_STAGE_A(b, h, ptr, NX) do { if constexpr (Sched::GATHER) { unsigned gs_[2]; gs_[0] = ((NX) && last_) ? gN[h][0] : gA[h][0]; gs_[1] = ((NX) && last_) ? gN[h][1] : gA[h][1]; PG8_STAGE(PG8_SA(b, h), ptr, gs_); } \
;         else PG8_STAGE(PG8_SA(b, h), (ptr) + ((h) ? hstep : (size_t)0), voffA); } while (0)
; #define PG8_STAGE(bufoff, gbase, voff) do { _Pragma("unroll") for (int _i = 0; _i < 2; ++_i) \
;         __builtin_amdgcn_global_load_lds((const unsigned*)((const char*)(gbase) + (voff)[_i]), (PG8_LAS unsigned*)(lds + (bufoff) + ldsw + _i * 8192), 16, 0, 0); } while (0)
; #define PG8_LDA(dst, b, h) do { _Pragma("unroll") for (int m = 0; m < 4; ++m) _Pragma("unroll") for (int k = 0; k < 2; ++k) dst[m][k] = *(const PG8_LAS bf16x8*)(lds + PG8_SA(b, h) + aoff + m * 2048 + k * 1024); } while (0)
; #define PG8_LDB(dst, b, h) do { _Pragma("unroll") for (int n = 0; n < 2; ++n) _Pragma("unroll") for (int k = 0; k < 2; ++k) dst[n][k] = *(const PG8_LAS bf16x8*)(lds + PG8_SB(b, h) + boff + n * 2048 + k * 1024); } while (0)
; #define PG8_MMA(ai, bj, At, Bt) do { __builtin_amdgcn_s_setprio(1); _Pragma("unroll") for (int m = 0; m < 4; ++m) _Pragma("unroll") for (int n = 0; n < 2; ++n) _Pragma("unroll") for (int k = 0; k < 2; ++k) \
;         acc[ai][bj][m][n] = __builtin_amdgcn_mfma_f32_16x16x32_bf16(Bt[n][k], At[m][k], acc[ai][bj][m][n], 0, 0, 0); __builtin_amdgcn_s_setprio(0); } while (0)
; #define PG8_WAIT_V(n) asm volatile("s_waitcnt vmcnt(" #n ")" ::: "memory")
; #define PG8_WAIT_L(n) asm volatile("s_waitcnt lgkmcnt(" #n ")" ::: "memory")
; template <class Epi, class Sched, bool ALIGN_EPI = false, bool SP2 = false>
; __device__ __forceinline__ void gemm_phase(PG8_LAS unsigned char* lds, const Gemm g, const Sched& S, const Epi& E, const bool skip_epi = false) {
;     ...
;             PG8_LDB(B0, 0, 0); PG8_LDB(B1, 0, 1); PG8_SCHED; PG8_LDA(At, 0, 0); PG8_STAGE_A(1, 1, a1, false);
;             PG8_WAIT_V(8); PG8_WAIT_L(0); PG8_BAR; PG8_MMA(0, 0, At, B0); PG8_MMA(0, 1, At, B1); PG8_BAR; PG8_SCHED;
;             PG8_LDA(At, 0, 1); PG8_STAGE(PG8_SB(0, 0), b2, voffB); PG8_STAGE(PG8_SB(0, 1), b2 + hstep, voffB); PG8_STAGE_A(0, 0, a2, true);
;             PG8_WAIT_V(8); PG8_WAIT_L(0); PG8_BAR; PG8_MMA(1, 0, At, B0); PG8_MMA(1, 1, At, B1); PG8_BAR; PG8_SCHED;
;             PG8_LDB(B0, 1, 0); PG8_LDB(B1, 1, 1); PG8_SCHED; PG8_LDA(At, 1, 0); PG8_STAGE_A(0, 1, a2, true);
	s_waitcnt lgkmcnt(0)
	v_mfma_f32_16x16x32_bf16 v[126:129], v[166:169], v[198:201], v[126:129]
	v_mfma_f32_16x16x32_bf16 v[122:125], v[174:177], v[198:201], v[122:125]
	v_mfma_f32_16x16x32_bf16 v[110:113], v[166:169], v[206:209], v[110:113]
	v_mfma_f32_16x16x32_bf16 v[106:109], v[174:177], v[206:209], v[106:109]
	v_mfma_f32_16x16x32_bf16 v[94:97], v[166:169], v[214:217], v[94:97]
	v_mfma_f32_16x16x32_bf16 v[90:93], v[174:177], v[214:217], v[90:93]
	v_mfma_f32_16x16x32_bf16 v[78:81], v[166:169], v[222:225], v[78:81]
	v_mfma_f32_16x16x32_bf16 v[74:77], v[174:177], v[222:225], v[74:77]
	v_mfma_f32_16x16x32_bf16 v[126:129], v[170:173], v[202:205], v[126:129]
	v_mfma_f32_16x16x32_bf16 v[122:125], v[178:181], v[202:205], v[122:125]
	v_mfma_f32_16x16x32_bf16 v[110:113], v[170:173], v[210:213], v[110:113]
	v_mfma_f32_16x16x32_bf16 v[106:109], v[178:181], v[210:213], v[106:109]
	v_mfma_f32_16x16x32_bf16 v[94:97], v[170:173], v[218:221], v[94:97]
	v_mfma_f32_16x16x32_bf16 v[90:93], v[178:181], v[218:221], v[90:93]
	v_mfma_f32_16x16x32_bf16 v[78:81], v[170:173], v[230:233], v[78:81]
	v_mfma_f32_16x16x32_bf16 v[74:77], v[178:181], v[230:233], v[74:77]
	v_mfma_f32_16x16x32_bf16 v[118:121], v[182:185], v[198:201], v[118:121]
	v_mfma_f32_16x16x32_bf16 v[114:117], v[190:193], v[198:201], v[114:117]
	v_mfma_f32_16x16x32_bf16 v[102:105], v[182:185], v[206:209], v[102:105]
	v_mfma_f32_16x16x32_bf16 v[98:101], v[190:193], v[206:209], v[98:101]
	v_mfma_f32_16x16x32_bf16 v[86:89], v[182:185], v[214:217], v[86:89]
	v_mfma_f32_16x16x32_bf16 v[82:85], v[190:193], v[214:217], v[82:85]
	v_mfma_f32_16x16x32_bf16 v[70:73], v[182:185], v[222:225], v[70:73]
	v_mfma_f32_16x16x32_bf16 v[66:69], v[190:193], v[222:225], v[66:69]
	v_mfma_f32_16x16x32_bf16 v[118:121], v[186:189], v[202:205], v[118:121]
	v_mfma_f32_16x16x32_bf16 v[114:117], v[194:197], v[202:205], v[114:117]
	v_mfma_f32_16x16x32_bf16 v[102:105], v[186:189], v[210:213], v[102:105]
	v_mfma_f32_16x16x32_bf16 v[98:101], v[194:197], v[210:213], v[98:101]
	v_mfma_f32_16x16x32_bf16 v[86:89], v[186:189], v[218:221], v[86:89]
	v_mfma_f32_16x16x32_bf16 v[82:85], v[194:197], v[218:221], v[82:85]
	v_mfma_f32_16x16x32_bf16 v[70:73], v[186:189], v[230:233], v[70:73]
	v_mfma_f32_16x16x32_bf16 v[66:69], v[194:197], v[230:233], v[66:69]
	s_barrier
	s_setprio 0
	s_add_i32 s64, s58, s50
	v_lshl_add_u64 v[226:227], s[42:43], 0, v[134:135]
	s_mov_b32 m0, s64
	ds_read_b128 v[198:201], v160 offset:16384
	ds_read_b128 v[202:205], v160 offset:17408
	ds_read_b128 v[206:209], v160 offset:18432
	ds_read_b128 v[210:213], v160 offset:19456
	ds_read_b128 v[214:217], v160 offset:20480
	ds_read_b128 v[218:221], v160 offset:21504
	ds_read_b128 v[222:225], v160 offset:22528
	ds_read_b128 v[230:233], v160 offset:23552
	global_load_lds_dwordx4 v[226:227], off
	s_add_i32 m0, s64, 0x2000
	s_add_u32 s64, s42, 0x40000
	v_lshl_add_u64 v[234:235], s[42:43], 0, v[136:137]
	s_addc_u32 s65, s43, 0
	s_add_i32 s66, s59, s50
	global_load_lds_dwordx4 v[234:235], off
	s_mov_b32 m0, s66
	v_cndmask_b32_e32 v132, v130, v164, vcc
	global_load_lds_dwordx4 v134, s[64:65]
	s_add_i32 m0, s66, 0x2000
	v_lshl_add_u64 v[238:239], s[44:45], 0, v[132:133]
	global_load_lds_dwordx4 v136, s[64:65]
	s_mov_b32 m0, s37
	v_cndmask_b32_e32 v236, v144, v163, vcc
	global_load_lds_dwordx4 v132, s[44:45]
	s_mov_b32 m0, s39
	v_mov_b32_e32 v237, v133
	global_load_lds_dwordx4 v236, s[44:45]
	s_waitcnt vmcnt(8)
	s_waitcnt lgkmcnt(0)
	v_lshl_add_u64 v[236:237], s[44:45], 0, v[236:237]
	s_setprio 3
	s_barrier
	s_waitcnt lgkmcnt(0)
	v_mfma_f32_16x16x32_bf16 v[62:65], v[166:169], v[198:201], v[62:65]
	v_mfma_f32_16x16x32_bf16 v[58:61], v[174:177], v[198:201], v[58:61]
	v_mfma_f32_16x16x32_bf16 v[38:41], v[166:169], v[206:209], v[38:41]
	v_mfma_f32_16x16x32_bf16 v[34:37], v[174:177], v[206:209], v[34:37]
	v_mfma_f32_16x16x32_bf16 v[22:25], v[166:169], v[214:217], v[22:25]
	v_mfma_f32_16x16x32_bf16 v[18:21], v[174:177], v[214:217], v[18:21]
	v_mfma_f32_16x16x32_bf16 v[6:9], v[166:169], v[222:225], v[6:9]
	v_mfma_f32_16x16x32_bf16 v[2:5], v[174:177], v[222:225], v[2:5]
	v_mfma_f32_16x16x32_bf16 v[62:65], v[170:173], v[202:205], v[62:65]
	v_mfma_f32_16x16x32_bf16 v[58:61], v[178:181], v[202:205], v[58:61]
	v_mfma_f32_16x16x32_bf16 v[38:41], v[170:173], v[210:213], v[38:41]
	v_mfma_f32_16x16x32_bf16 v[34:37], v[178:181], v[210:213], v[34:37]
	v_mfma_f32_16x16x32_bf16 v[22:25], v[170:173], v[218:221], v[22:25]
	v_mfma_f32_16x16x32_bf16 v[18:21], v[178:181], v[218:221], v[18:21]
	v_mfma_f32_16x16x32_bf16 v[6:9], v[170:173], v[230:233], v[6:9]
	v_mfma_f32_16x16x32_bf16 v[2:5], v[178:181], v[230:233], v[2:5]
	v_mfma_f32_16x16x32_bf16 v[50:53], v[182:185], v[198:201], v[50:53]
	v_mfma_f32_16x16x32_bf16 v[42:45], v[190:193], v[198:201], v[42:45]
	v_mfma_f32_16x16x32_bf16 v[54:57], v[182:185], v[206:209], v[54:57]
	v_mfma_f32_16x16x32_bf16 v[46:49], v[190:193], v[206:209], v[46:49]
	v_mfma_f32_16x16x32_bf16 v[30:33], v[182:185], v[214:217], v[30:33]
	v_mfma_f32_16x16x32_bf16 v[26:29], v[190:193], v[214:217], v[26:29]
	v_mfma_f32_16x16x32_bf16 v[14:17], v[182:185], v[222:225], v[14:17]
	v_mfma_f32_16x16x32_bf16 v[10:13], v[190:193], v[222:225], v[10:13]
	v_mfma_f32_16x16x32_bf16 v[50:53], v[186:189], v[202:205], v[50:53]
	v_mfma_f32_16x16x32_bf16 v[42:45], v[194:197], v[202:205], v[42:45]
	v_mfma_f32_16x16x32_bf16 v[54:57], v[186:189], v[210:213], v[54:57]
	v_mfma_f32_16x16x32_bf16 v[46:49], v[194:197], v[210:213], v[46:49]
	v_mfma_f32_16x16x32_bf16 v[30:33], v[186:189], v[218:221], v[30:33]
	v_mfma_f32_16x16x32_bf16 v[26:29], v[194:197], v[218:221], v[26:29]
	v_mfma_f32_16x16x32_bf16 v[14:17], v[186:189], v[230:233], v[14:17]
	v_mfma_f32_16x16x32_bf16 v[10:13], v[194:197], v[230:233], v[10:13]
	s_barrier
; #define PG8_STAGE_A(b, h, ptr, NX) do { if constexpr (Sched::GATHER) { unsigned gs_[2]; gs_[0] = ((NX) && last_) ? gN[h][0] : gA[h][0]; gs_[1] = ((NX) && last_) ? gN[h][1] : gA[h][1]; PG8_STAGE(PG8_SA(b, h), ptr, gs_); } \
;         else PG8_STAGE(PG8_SA(b, h), (ptr) + ((h) ? hstep : (size_t)0), voffA); } while (0)
; #define PG8_STAGE(bufoff, gbase, voff) do { _Pragma("unroll") for (int _i = 0; _i < 2; ++_i) \
;         __builtin_amdgcn_global_load_lds((const unsigned*)((const char*)(gbase) + (voff)[_i]), (PG8_LAS unsigned*)(lds + (bufoff) + ldsw + _i * 8192), 16, 0, 0); } while (0)
; #define PG8_LDA(dst, b, h) do { _Pragma("unroll") for (int m = 0; m < 4; ++m) _Pragma("unroll") for (int k = 0; k < 2; ++k) dst[m][k] = *(const PG8_LAS bf16x8*)(lds + PG8_SA(b, h) + aoff + m * 2048 + k * 1024); } while (0)
; #define PG8_LDB(dst, b, h) do { _Pragma("unroll") for (int n = 0; n < 2; ++n) _Pragma("unroll") for (int k = 0; k < 2; ++k) dst[n][k] = *(const PG8_LAS bf16x8*)(lds + PG8_SB(b, h) + boff + n * 2048 + k * 1024); } while (0)
; #define PG8_MMA(ai, bj, At, Bt) do { __builtin_amdgcn_s_setprio(1); _Pragma("unroll") for (int m = 0; m < 4; ++m) _Pragma("unroll") for (int n = 0; n < 2; ++n) _Pragma("unroll") for (int k = 0; k < 2; ++k) \
;         acc[ai][bj][m][n] = __builtin_amdgcn_mfma_f32_16x16x32_bf16(Bt[n][k], At[m][k], acc[ai][bj][m][n], 0, 0, 0); __builtin_amdgcn_s_setprio(0); } while (0)
; #define PG8_WAIT_V(n) asm volatile("s_waitcnt vmcnt(" #n ")" ::: "memory")
; #define PG8_WAIT_L(n) asm volatile("s_waitcnt lgkmcnt(" #n ")" ::: "memory")
; #define PG8_BAR __builtin_amdgcn_s_barrier()
; template <class Epi, class Sched, bool ALIGN_EPI = false, bool SP2 = false>
; __device__ __forceinline__ void gemm_phase(PG8_LAS unsigned char* lds, const Gemm g, const Sched& S, const Epi& E, const bool skip_epi = false) {
;     ...
;             PG8_LDB(B0, 1, 0); PG8_LDB(B1, 1, 1); PG8_SCHED; PG8_LDA(At, 1, 0); PG8_STAGE_A(0, 1, a2, true);
;             PG8_WAIT_V(8); PG8_WAIT_L(0); PG8_BAR; PG8_MMA(0, 0, At, B0); PG8_MMA(0, 1, At, B1); PG8_BAR; PG8_SCHED;
;             PG8_LDA(At, 1, 1); PG8_STAGE(PG8_SB(1, 0), b3, voffB); PG8_STAGE(PG8_SB(1, 1), b3 + hstep, voffB); PG8_STAGE_A(1, 0, a3, true);
;             PG8_WAIT_V(8); PG8_WAIT_L(0); PG8_BAR; PG8_MMA(1, 0, At, B0); PG8_MMA(1, 1, At, B1); PG8_BAR; PG8_SCHED;
;     ...
;         if constexpr (ALIGN_EPI) { if (wr == 0) PG8_BAR; }
	s_setprio 0
	s_add_i32 s64, 0, 0x18000
	v_add_u32_e32 v132, s64, v154
	s_add_i32 s65, 0, 0x1c000
	ds_read_b128 v[166:169], v132
	ds_read_b128 v[170:173], v132 offset:1024
	ds_read_b128 v[174:177], v132 offset:2048
	ds_read_b128 v[178:181], v132 offset:3072
	v_add_u32_e32 v132, s65, v154
	ds_read_b128 v[182:185], v132
	ds_read_b128 v[186:189], v132 offset:1024
	ds_read_b128 v[190:193], v132 offset:2048
	ds_read_b128 v[194:197], v132 offset:3072
	s_mov_b32 m0, s51
	v_cndmask_b32_e32 v132, v142, v162, vcc
	ds_read_b128 v[198:201], v160 offset:32768
	ds_read_b128 v[202:205], v160 offset:33792
	ds_read_b128 v[206:209], v160 offset:34816
	ds_read_b128 v[210:213], v160 offset:35840
	ds_read_b128 v[214:217], v160 offset:36864
	ds_read_b128 v[218:221], v160 offset:37888
	ds_read_b128 v[222:225], v160 offset:38912
	ds_read_b128 v[230:233], v160 offset:39936
	v_cndmask_b32_e32 v141, v140, v161, vcc
	global_load_lds_dwordx4 v132, s[44:45]
	s_mov_b32 m0, s52
	s_nop 0
	global_load_lds_dwordx4 v141, s[44:45]
	s_waitcnt vmcnt(8)
	s_waitcnt lgkmcnt(0)
	s_setprio 3
	s_barrier
	s_waitcnt lgkmcnt(0)
	v_mfma_f32_16x16x32_bf16 v[126:129], v[166:169], v[198:201], v[126:129]
	v_mfma_f32_16x16x32_bf16 v[122:125], v[174:177], v[198:201], v[122:125]
	v_mfma_f32_16x16x32_bf16 v[110:113], v[166:169], v[206:209], v[110:113]
	v_mfma_f32_16x16x32_bf16 v[106:109], v[174:177], v[206:209], v[106:109]
	v_mfma_f32_16x16x32_bf16 v[94:97], v[166:169], v[214:217], v[94:97]
	v_mfma_f32_16x16x32_bf16 v[90:93], v[174:177], v[214:217], v[90:93]
	v_mfma_f32_16x16x32_bf16 v[78:81], v[166:169], v[222:225], v[78:81]
	v_mfma_f32_16x16x32_bf16 v[74:77], v[174:177], v[222:225], v[74:77]
	v_mfma_f32_16x16x32_bf16 v[126:129], v[170:173], v[202:205], v[126:129]
	v_mfma_f32_16x16x32_bf16 v[122:125], v[178:181], v[202:205], v[122:125]
	v_mfma_f32_16x16x32_bf16 v[110:113], v[170:173], v[210:213], v[110:113]
	v_mfma_f32_16x16x32_bf16 v[106:109], v[178:181], v[210:213], v[106:109]
	v_mfma_f32_16x16x32_bf16 v[94:97], v[170:173], v[218:221], v[94:97]
	v_mfma_f32_16x16x32_bf16 v[90:93], v[178:181], v[218:221], v[90:93]
	v_mfma_f32_16x16x32_bf16 v[78:81], v[170:173], v[230:233], v[78:81]
	v_mfma_f32_16x16x32_bf16 v[74:77], v[178:181], v[230:233], v[74:77]
	v_mfma_f32_16x16x32_bf16 v[118:121], v[182:185], v[198:201], v[118:121]
	v_mfma_f32_16x16x32_bf16 v[114:117], v[190:193], v[198:201], v[114:117]
	v_mfma_f32_16x16x32_bf16 v[102:105], v[182:185], v[206:209], v[102:105]
	v_mfma_f32_16x16x32_bf16 v[98:101], v[190:193], v[206:209], v[98:101]
	v_mfma_f32_16x16x32_bf16 v[86:89], v[182:185], v[214:217], v[86:89]
	v_mfma_f32_16x16x32_bf16 v[82:85], v[190:193], v[214:217], v[82:85]
	v_mfma_f32_16x16x32_bf16 v[70:73], v[182:185], v[222:225], v[70:73]
	v_mfma_f32_16x16x32_bf16 v[66:69], v[190:193], v[222:225], v[66:69]
	v_mfma_f32_16x16x32_bf16 v[118:121], v[186:189], v[202:205], v[118:121]
	v_mfma_f32_16x16x32_bf16 v[114:117], v[194:197], v[202:205], v[114:117]
	v_mfma_f32_16x16x32_bf16 v[102:105], v[186:189], v[210:213], v[102:105]
	v_mfma_f32_16x16x32_bf16 v[98:101], v[194:197], v[210:213], v[98:101]
	v_mfma_f32_16x16x32_bf16 v[86:89], v[186:189], v[218:221], v[86:89]
	v_mfma_f32_16x16x32_bf16 v[82:85], v[194:197], v[218:221], v[82:85]
	v_mfma_f32_16x16x32_bf16 v[70:73], v[186:189], v[230:233], v[70:73]
	v_mfma_f32_16x16x32_bf16 v[66:69], v[194:197], v[230:233], v[66:69]
	s_barrier
	s_setprio 0
	s_add_i32 s44, s64, s50
	s_add_i32 m0, s44, 0xffffff80
	ds_read_b128 v[198:201], v160 offset:49152
	ds_read_b128 v[202:205], v160 offset:50176
	ds_read_b128 v[206:209], v160 offset:51200
	ds_read_b128 v[210:213], v160 offset:52224
	ds_read_b128 v[214:217], v160 offset:53248
	ds_read_b128 v[218:221], v160 offset:54272
	ds_read_b128 v[222:225], v160 offset:55296
	ds_read_b128 v[230:233], v160 offset:56320
	global_load_lds_dwordx4 v[226:227], off offset:128
	s_add_i32 m0, s44, 0x1f80
	s_add_u32 s42, s42, 0x40080
	s_addc_u32 s43, s43, 0
	s_add_i32 s44, s65, s50
	global_load_lds_dwordx4 v[234:235], off offset:128
	s_mov_b32 m0, s44
	s_nop 0
	global_load_lds_dwordx4 v134, s[42:43]
	s_add_i32 m0, s44, 0x2000
	s_nop 0
	global_load_lds_dwordx4 v136, s[42:43]
	s_add_i32 m0, s55, 0xffffff80
	s_nop 0
	global_load_lds_dwordx4 v[238:239], off offset:128
	s_add_i32 m0, s56, 0xffffff80
	s_nop 0
	global_load_lds_dwordx4 v[236:237], off offset:128
	s_waitcnt vmcnt(8)
	s_waitcnt lgkmcnt(0)
	s_setprio 3
	s_barrier
	s_waitcnt lgkmcnt(0)
	v_mfma_f32_16x16x32_bf16 v[62:65], v[166:169], v[198:201], v[62:65]
	v_mfma_f32_16x16x32_bf16 v[58:61], v[174:177], v[198:201], v[58:61]
	v_mfma_f32_16x16x32_bf16 v[38:41], v[166:169], v[206:209], v[38:41]
	v_mfma_f32_16x16x32_bf16 v[34:37], v[174:177], v[206:209], v[34:37]
	v_mfma_f32_16x16x32_bf16 v[22:25], v[166:169], v[214:217], v[22:25]
	v_mfma_f32_16x16x32_bf16 v[18:21], v[174:177], v[214:217], v[18:21]
	v_mfma_f32_16x16x32_bf16 v[6:9], v[166:169], v[222:225], v[6:9]
	v_mfma_f32_16x16x32_bf16 v[2:5], v[174:177], v[222:225], v[2:5]
	v_mfma_f32_16x16x32_bf16 v[62:65], v[170:173], v[202:205], v[62:65]
	v_mfma_f32_16x16x32_bf16 v[58:61], v[178:181], v[202:205], v[58:61]
	v_mfma_f32_16x16x32_bf16 v[38:41], v[170:173], v[210:213], v[38:41]
	v_mfma_f32_16x16x32_bf16 v[34:37], v[178:181], v[210:213], v[34:37]
	v_mfma_f32_16x16x32_bf16 v[22:25], v[170:173], v[218:221], v[22:25]
	v_mfma_f32_16x16x32_bf16 v[18:21], v[178:181], v[218:221], v[18:21]
	v_mfma_f32_16x16x32_bf16 v[6:9], v[170:173], v[230:233], v[6:9]
	v_mfma_f32_16x16x32_bf16 v[2:5], v[178:181], v[230:233], v[2:5]
	v_mfma_f32_16x16x32_bf16 v[50:53], v[182:185], v[198:201], v[50:53]
	v_mfma_f32_16x16x32_bf16 v[42:45], v[190:193], v[198:201], v[42:45]
	v_mfma_f32_16x16x32_bf16 v[54:57], v[182:185], v[206:209], v[54:57]
	v_mfma_f32_16x16x32_bf16 v[46:49], v[190:193], v[206:209], v[46:49]
	v_mfma_f32_16x16x32_bf16 v[30:33], v[182:185], v[214:217], v[30:33]
	v_mfma_f32_16x16x32_bf16 v[26:29], v[190:193], v[214:217], v[26:29]
	v_mfma_f32_16x16x32_bf16 v[14:17], v[182:185], v[222:225], v[14:17]
	v_mfma_f32_16x16x32_bf16 v[10:13], v[190:193], v[222:225], v[10:13]
	v_mfma_f32_16x16x32_bf16 v[50:53], v[186:189], v[202:205], v[50:53]
	v_mfma_f32_16x16x32_bf16 v[42:45], v[194:197], v[202:205], v[42:45]
	v_mfma_f32_16x16x32_bf16 v[54:57], v[186:189], v[210:213], v[54:57]
	v_mfma_f32_16x16x32_bf16 v[46:49], v[194:197], v[210:213], v[46:49]
	v_mfma_f32_16x16x32_bf16 v[30:33], v[186:189], v[218:221], v[30:33]
	v_mfma_f32_16x16x32_bf16 v[26:29], v[194:197], v[218:221], v[26:29]
	v_mfma_f32_16x16x32_bf16 v[14:17], v[186:189], v[230:233], v[14:17]
	v_mfma_f32_16x16x32_bf16 v[10:13], v[194:197], v[230:233], v[10:13]
	s_barrier
	s_setprio 0
	s_add_i32 s63, s63, 2
	s_add_u32 s40, s40, 0x100
	s_addc_u32 s41, s41, 0
	s_cmp_gt_u32 s63, 13
	s_cbranch_scc0 .LBB0_1728
	s_and_b64 vcc, exec, s[26:27]
	s_cbranch_vccz .LBB0_1731
	s_barrier

; #define PG8_STAGE_A(b, h, ptr, NX) do { if constexpr (Sched::GATHER) { unsigned gs_[2]; gs_[0] = ((NX) && last_) ? gN[h][0] : gA[h][0]; gs_[1] = ((NX) && last_) ? gN[h][1] : gA[h][1]; PG8_STAGE(PG8_SA(b, h), ptr, gs_); } \
;         else PG8_STAGE(PG8_SA(b, h), (ptr) + ((h) ? hstep : (size_t)0), voffA); } while (0)
; #define PG8_STAGE(bufoff, gbase, voff) do { _Pragma("unroll") for (int _i = 0; _i < 2; ++_i) \
;         __builtin_amdgcn_global_load_lds((const unsigned*)((const char*)(gbase) + (voff)[_i]), (PG8_LAS unsigned*)(lds + (bufoff) + ldsw + _i * 8192), 16, 0, 0); } while (0)
; #define PG8_WAIT_V(n) asm volatile("s_waitcnt vmcnt(" #n ")" ::: "memory")
; #define PG8_WAIT_L(n) asm volatile("s_waitcnt lgkmcnt(" #n ")" ::: "memory")
; template <class Epi, class Sched, bool ALIGN_EPI = false, bool SP2 = false>
; __device__ __forceinline__ void gemm_phase(PG8_LAS unsigned char* lds, const Gemm g, const Sched& S, const Epi& E, const bool skip_epi = false) {
;     ...
;         const char* nA = has_next ? (const char*)g.A + (size_t)nxt.pm * pmstepA + nxt.ko : cA; const char* nB = has_next ? (const char*)g.Bt + (size_t)nxt.pn * tstep + nxt.ko : cB;
;         for (int t = 0; t < nt; t += 2) {
;             const bool last = (t == nt - 2); last_ = last && has_next;
;             const char* a1 = cA + (size_t)(t + 1) * kstep;
;             const char* a2 = last ? nA : cA + (size_t)(t + 2) * kstep; const char* b2 = last ? nB : cB + (size_t)(t + 2) * kstep;
;             const char* a3 = a2 + kstep; const char* b3 = b2 + kstep;
;             if (last && has_next) S.a_ready(nxt);
;             if constexpr (SP2) {
;             PG8_LDB(B0, 0, 0); PG8_LDB(B1, 0, 1); PG8_SCHED; PG8_LDA(At, 0, 0); PG8_STAGE_A(1, 1, a1, false);
;             PG8_WAIT_V(8); PG8_WAIT_L(0); PG8_BAR; PG8_MMA(0, 0, At, B0); PG8_MMA(0, 1, At, B1); PG8_BAR; PG8_SCHED;
;             PG8_LDA(At, 0, 1); PG8_STAGE(PG8_SB(0, 0), b2, voffB); PG8_STAGE(PG8_SB(0, 1), b2 + hstep, voffB); PG8_STAGE_A(0, 0, a2, true);
;             PG8_WAIT_V(8); PG8_WAIT_L(0); PG8_BAR; PG8_MMA(1, 0, At, B0); PG8_MMA(1, 1, At, B1); PG8_BAR; PG8_SCHED;
;     ...
;         for (int a = 0; a < 2; ++a)
; #pragma unroll
;             for (int b = 0; b < 2; ++b)
; #pragma unroll
;                 for (int m = 0; m < 4; ++m)
; #pragma unroll
;                     for (int n = 0; n < 2; ++n) acc[a][b][m][n] = (f32x4){0.f, 0.f, 0.f, 0.f};
.LBB0_1822:
	s_add_u32 s67, s40, 0x100
	s_addc_u32 s68, s41, 0
	s_mov_b32 s69, -2
	ds_read_b128 v[160:163], v157
	ds_read_b128 v[164:167], v157 offset:1024
	ds_read_b128 v[168:171], v157 offset:2048
	ds_read_b128 v[172:175], v157 offset:3072
	ds_read_b128 v[176:179], v158
	ds_read_b128 v[180:183], v158 offset:1024
	ds_read_b128 v[184:187], v158 offset:2048
	ds_read_b128 v[188:191], v158 offset:3072
	s_add_u32 s40, s38, 0x100
	s_addc_u32 s41, s39, 0
	s_cmp_eq_u32 s69, 52
	s_cselect_b32 s45, s7, s41
	s_cselect_b32 s44, s6, s40
	s_cselect_b32 s43, s35, s68
	s_cselect_b32 s42, s34, s67
	v_lshl_add_u64 v[152:153], s[38:39], 0, v[140:141]
	s_add_i32 m0, s37, 0xc000
	ds_read_b128 v[192:195], v159
	ds_read_b128 v[196:199], v159 offset:1024
	ds_read_b128 v[200:203], v159 offset:2048
	ds_read_b128 v[204:207], v159 offset:3072
	ds_read_b128 v[208:211], v159 offset:4096
	ds_read_b128 v[212:215], v159 offset:5120
	ds_read_b128 v[216:219], v159 offset:6144
	ds_read_b128 v[220:223], v159 offset:7168
	global_load_lds_dwordx4 v[152:153], off
	v_lshl_add_u64 v[152:153], s[38:39], 0, v[142:143]
	s_add_i32 m0, s37, 0xe000
	s_nop 0
	global_load_lds_dwordx4 v[152:153], off
	s_waitcnt vmcnt(8)
	s_waitcnt lgkmcnt(0)
	s_setprio 3
	s_barrier
	s_waitcnt lgkmcnt(0)
	v_mfma_f32_16x16x32_bf16 v[126:129], v[160:163], v[192:195], 0
	v_mfma_f32_16x16x32_bf16 v[122:125], v[168:171], v[192:195], 0
	v_mfma_f32_16x16x32_bf16 v[118:121], v[160:163], v[200:203], 0
	v_mfma_f32_16x16x32_bf16 v[114:117], v[168:171], v[200:203], 0
	v_mfma_f32_16x16x32_bf16 v[106:109], v[160:163], v[208:211], 0
	v_mfma_f32_16x16x32_bf16 v[98:101], v[168:171], v[208:211], 0
	v_mfma_f32_16x16x32_bf16 v[78:81], v[160:163], v[216:219], 0
	v_mfma_f32_16x16x32_bf16 v[74:77], v[168:171], v[216:219], 0
	v_mfma_f32_16x16x32_bf16 v[126:129], v[164:167], v[196:199], v[126:129]
	v_mfma_f32_16x16x32_bf16 v[122:125], v[172:175], v[196:199], v[122:125]
	v_mfma_f32_16x16x32_bf16 v[118:121], v[164:167], v[204:207], v[118:121]
	v_mfma_f32_16x16x32_bf16 v[114:117], v[172:175], v[204:207], v[114:117]
	v_mfma_f32_16x16x32_bf16 v[106:109], v[164:167], v[212:215], v[106:109]
	v_mfma_f32_16x16x32_bf16 v[98:101], v[172:175], v[212:215], v[98:101]
	v_mfma_f32_16x16x32_bf16 v[78:81], v[164:167], v[220:223], v[78:81]
	v_mfma_f32_16x16x32_bf16 v[74:77], v[172:175], v[220:223], v[74:77]
	v_mfma_f32_16x16x32_bf16 v[110:113], v[176:179], v[192:195], 0
	v_mfma_f32_16x16x32_bf16 v[102:105], v[184:187], v[192:195], 0
	v_mfma_f32_16x16x32_bf16 v[94:97], v[176:179], v[200:203], 0
	v_mfma_f32_16x16x32_bf16 v[90:93], v[184:187], v[200:203], 0
	v_mfma_f32_16x16x32_bf16 v[86:89], v[176:179], v[208:211], 0
	v_mfma_f32_16x16x32_bf16 v[82:85], v[184:187], v[208:211], 0
	v_mfma_f32_16x16x32_bf16 v[70:73], v[176:179], v[216:219], 0
	v_mfma_f32_16x16x32_bf16 v[66:69], v[184:187], v[216:219], 0
	v_mfma_f32_16x16x32_bf16 v[110:113], v[180:183], v[196:199], v[110:113]
	v_mfma_f32_16x16x32_bf16 v[102:105], v[188:191], v[196:199], v[102:105]
	v_mfma_f32_16x16x32_bf16 v[94:97], v[180:183], v[204:207], v[94:97]
	v_mfma_f32_16x16x32_bf16 v[90:93], v[188:191], v[204:207], v[90:93]
	v_mfma_f32_16x16x32_bf16 v[86:89], v[180:183], v[212:215], v[86:89]
	v_mfma_f32_16x16x32_bf16 v[82:85], v[188:191], v[212:215], v[82:85]
	v_mfma_f32_16x16x32_bf16 v[70:73], v[180:183], v[220:223], v[70:73]
	v_mfma_f32_16x16x32_bf16 v[66:69], v[188:191], v[220:223], v[66:69]
	s_barrier
	s_setprio 0
	s_add_i32 s38, s60, s51
	v_lshl_add_u64 v[152:153], s[42:43], 0, v[134:135]
	s_mov_b32 m0, s38
	ds_read_b128 v[192:195], v159 offset:16384
	ds_read_b128 v[196:199], v159 offset:17408
	ds_read_b128 v[200:203], v159 offset:18432
	ds_read_b128 v[204:207], v159 offset:19456
	ds_read_b128 v[208:211], v159 offset:20480
	ds_read_b128 v[212:215], v159 offset:21504
	ds_read_b128 v[216:219], v159 offset:22528
	ds_read_b128 v[220:223], v159 offset:23552
	global_load_lds_dwordx4 v[152:153], off
	s_add_i32 m0, s38, 0x2000
	s_add_u32 s38, s42, 0xe0000
	v_lshl_add_u64 v[224:225], s[42:43], 0, v[138:139]
	s_addc_u32 s39, s43, 0
	s_add_i32 s70, s61, s51
	global_load_lds_dwordx4 v[224:225], off
	s_mov_b32 m0, s70
	v_lshl_add_u64 v[230:231], s[44:45], 0, v[136:137]
	global_load_lds_dwordx4 v134, s[38:39]
	s_add_i32 m0, s70, 0x2000
	s_nop 0
	global_load_lds_dwordx4 v138, s[38:39]
	v_lshl_add_u64 v[226:227], s[44:45], 0, v[132:133]
	s_mov_b32 m0, s37
	s_nop 0
	global_load_lds_dwordx4 v[226:227], off
	s_mov_b32 m0, s52
	s_nop 0
	global_load_lds_dwordx4 v[230:231], off
	s_waitcnt vmcnt(8)
	s_waitcnt lgkmcnt(0)
	s_setprio 3
	s_barrier
	s_waitcnt lgkmcnt(0)
	v_mfma_f32_16x16x32_bf16 v[62:65], v[160:163], v[192:195], 0
	v_mfma_f32_16x16x32_bf16 v[58:61], v[168:171], v[192:195], 0
	v_mfma_f32_16x16x32_bf16 v[50:53], v[160:163], v[200:203], 0
	v_mfma_f32_16x16x32_bf16 v[42:45], v[168:171], v[200:203], 0
	v_mfma_f32_16x16x32_bf16 v[34:37], v[160:163], v[208:211], 0
	v_mfma_f32_16x16x32_bf16 v[26:29], v[168:171], v[208:211], 0
	v_mfma_f32_16x16x32_bf16 v[18:21], v[160:163], v[216:219], 0
	v_mfma_f32_16x16x32_bf16 v[10:13], v[168:171], v[216:219], 0
	v_mfma_f32_16x16x32_bf16 v[62:65], v[164:167], v[196:199], v[62:65]
	v_mfma_f32_16x16x32_bf16 v[58:61], v[172:175], v[196:199], v[58:61]
	v_mfma_f32_16x16x32_bf16 v[50:53], v[164:167], v[204:207], v[50:53]
	v_mfma_f32_16x16x32_bf16 v[42:45], v[172:175], v[204:207], v[42:45]
	v_mfma_f32_16x16x32_bf16 v[34:37], v[164:167], v[212:215], v[34:37]
	v_mfma_f32_16x16x32_bf16 v[26:29], v[172:175], v[212:215], v[26:29]
	v_mfma_f32_16x16x32_bf16 v[18:21], v[164:167], v[220:223], v[18:21]
	v_mfma_f32_16x16x32_bf16 v[10:13], v[172:175], v[220:223], v[10:13]
	v_mfma_f32_16x16x32_bf16 v[54:57], v[176:179], v[192:195], 0
	v_mfma_f32_16x16x32_bf16 v[46:49], v[184:187], v[192:195], 0
	v_mfma_f32_16x16x32_bf16 v[38:41], v[176:179], v[200:203], 0
	v_mfma_f32_16x16x32_bf16 v[30:33], v[184:187], v[200:203], 0
	v_mfma_f32_16x16x32_bf16 v[22:25], v[176:179], v[208:211], 0
	v_mfma_f32_16x16x32_bf16 v[14:17], v[184:187], v[208:211], 0
	v_mfma_f32_16x16x32_bf16 v[6:9], v[176:179], v[216:219], 0
	v_mfma_f32_16x16x32_bf16 v[2:5], v[184:187], v[216:219], 0
	v_mfma_f32_16x16x32_bf16 v[54:57], v[180:183], v[196:199], v[54:57]
	v_mfma_f32_16x16x32_bf16 v[46:49], v[188:191], v[196:199], v[46:49]
	v_mfma_f32_16x16x32_bf16 v[38:41], v[180:183], v[204:207], v[38:41]
	v_mfma_f32_16x16x32_bf16 v[30:33], v[188:191], v[204:207], v[30:33]
	v_mfma_f32_16x16x32_bf16 v[22:25], v[180:183], v[212:215], v[22:25]
	v_mfma_f32_16x16x32_bf16 v[14:17], v[188:191], v[212:215], v[14:17]
	v_mfma_f32_16x16x32_bf16 v[6:9], v[180:183], v[220:223], v[6:9]
	v_mfma_f32_16x16x32_bf16 v[2:5], v[188:191], v[220:223], v[2:5]
	s_barrier
; #define PG8_STAGE_A(b, h, ptr, NX) do { if constexpr (Sched::GATHER) { unsigned gs_[2]; gs_[0] = ((NX) && last_) ? gN[h][0] : gA[h][0]; gs_[1] = ((NX) && last_) ? gN[h][1] : gA[h][1]; PG8_STAGE(PG8_SA(b, h), ptr, gs_); } \
;         else PG8_STAGE(PG8_SA(b, h), (ptr) + ((h) ? hstep : (size_t)0), voffA); } while (0)
; #define PG8_STAGE(bufoff, gbase, voff) do { _Pragma("unroll") for (int _i = 0; _i < 2; ++_i) \
;         __builtin_amdgcn_global_load_lds((const unsigned*)((const char*)(gbase) + (voff)[_i]), (PG8_LAS unsigned*)(lds + (bufoff) + ldsw + _i * 8192), 16, 0, 0); } while (0)
; #define PG8_LDA(dst, b, h) do { _Pragma("unroll") for (int m = 0; m < 4; ++m) _Pragma("unroll") for (int k = 0; k < 2; ++k) dst[m][k] = *(const PG8_LAS bf16x8*)(lds + PG8_SA(b, h) + aoff + m * 2048 + k * 1024); } while (0)
; #define PG8_LDB(dst, b, h) do { _Pragma("unroll") for (int n = 0; n < 2; ++n) _Pragma("unroll") for (int k = 0; k < 2; ++k) dst[n][k] = *(const PG8_LAS bf16x8*)(lds + PG8_SB(b, h) + boff + n * 2048 + k * 1024); } while (0)
; #define PG8_MMA(ai, bj, At, Bt) do { __builtin_amdgcn_s_setprio(1); _Pragma("unroll") for (int m = 0; m < 4; ++m) _Pragma("unroll") for (int n = 0; n < 2; ++n) _Pragma("unroll") for (int k = 0; k < 2; ++k) \
;         acc[ai][bj][m][n] = __builtin_amdgcn_mfma_f32_16x16x32_bf16(Bt[n][k], At[m][k], acc[ai][bj][m][n], 0, 0, 0); __builtin_amdgcn_s_setprio(0); } while (0)
; #define PG8_WAIT_V(n) asm volatile("s_waitcnt vmcnt(" #n ")" ::: "memory")
; #define PG8_WAIT_L(n) asm volatile("s_waitcnt lgkmcnt(" #n ")" ::: "memory")
; #define PG8_BAR __builtin_amdgcn_s_barrier()
; #define PG8_SCHED __builtin_amdgcn_sched_barrier(0)
; template <class Epi, class Sched, bool ALIGN_EPI = false, bool SP2 = false>
; __device__ __forceinline__ void gemm_phase(PG8_LAS unsigned char* lds, const Gemm g, const Sched& S, const Epi& E, const bool skip_epi = false) {
;     ...
;             PG8_LDB(B0, 1, 0); PG8_LDB(B1, 1, 1); PG8_SCHED; PG8_LDA(At, 1, 0); PG8_STAGE_A(0, 1, a2, true);
;             PG8_WAIT_V(8); PG8_WAIT_L(0); PG8_BAR; PG8_MMA(0, 0, At, B0); PG8_MMA(0, 1, At, B1); PG8_BAR; PG8_SCHED;
;             PG8_LDA(At, 1, 1); PG8_STAGE(PG8_SB(1, 0), b3, voffB); PG8_STAGE(PG8_SB(1, 1), b3 + hstep, voffB); PG8_STAGE_A(1, 0, a3, true);
;             PG8_WAIT_V(8); PG8_WAIT_L(0); PG8_BAR; PG8_MMA(1, 0, At, B0); PG8_MMA(1, 1, At, B1); PG8_BAR; PG8_SCHED;
	s_setprio 0
	s_add_i32 s70, 0, 0x18000
	v_add_u32_e32 v130, s70, v147
	s_add_i32 s71, 0, 0x1c000
	ds_read_b128 v[160:163], v130
	ds_read_b128 v[164:167], v130 offset:1024
	ds_read_b128 v[168:171], v130 offset:2048
	ds_read_b128 v[172:175], v130 offset:3072
	v_add_u32_e32 v130, s71, v147
	ds_read_b128 v[176:179], v130
	ds_read_b128 v[180:183], v130 offset:1024
	ds_read_b128 v[184:187], v130 offset:2048
	ds_read_b128 v[188:191], v130 offset:3072
	s_add_u32 s38, s44, 0xe0000
	s_addc_u32 s39, s45, 0
	s_mov_b32 m0, s53
	ds_read_b128 v[192:195], v159 offset:32768
	ds_read_b128 v[196:199], v159 offset:33792
	ds_read_b128 v[200:203], v159 offset:34816
	ds_read_b128 v[204:207], v159 offset:35840
	ds_read_b128 v[208:211], v159 offset:36864
	ds_read_b128 v[212:215], v159 offset:37888
	ds_read_b128 v[216:219], v159 offset:38912
	ds_read_b128 v[220:223], v159 offset:39936
	global_load_lds_dwordx4 v132, s[38:39]
	s_mov_b32 m0, s54
	s_nop 0
	global_load_lds_dwordx4 v136, s[38:39]
	s_waitcnt vmcnt(8)
	s_waitcnt lgkmcnt(0)
	s_setprio 3
	s_barrier
	s_waitcnt lgkmcnt(0)
	v_mfma_f32_16x16x32_bf16 v[126:129], v[160:163], v[192:195], v[126:129]
	v_mfma_f32_16x16x32_bf16 v[122:125], v[168:171], v[192:195], v[122:125]
	v_mfma_f32_16x16x32_bf16 v[118:121], v[160:163], v[200:203], v[118:121]
	v_mfma_f32_16x16x32_bf16 v[114:117], v[168:171], v[200:203], v[114:117]
	v_mfma_f32_16x16x32_bf16 v[106:109], v[160:163], v[208:211], v[106:109]
	v_mfma_f32_16x16x32_bf16 v[98:101], v[168:171], v[208:211], v[98:101]
	v_mfma_f32_16x16x32_bf16 v[78:81], v[160:163], v[216:219], v[78:81]
	v_mfma_f32_16x16x32_bf16 v[74:77], v[168:171], v[216:219], v[74:77]
	v_mfma_f32_16x16x32_bf16 v[126:129], v[164:167], v[196:199], v[126:129]
	v_mfma_f32_16x16x32_bf16 v[122:125], v[172:175], v[196:199], v[122:125]
	v_mfma_f32_16x16x32_bf16 v[118:121], v[164:167], v[204:207], v[118:121]
	v_mfma_f32_16x16x32_bf16 v[114:117], v[172:175], v[204:207], v[114:117]
	v_mfma_f32_16x16x32_bf16 v[106:109], v[164:167], v[212:215], v[106:109]
	v_mfma_f32_16x16x32_bf16 v[98:101], v[172:175], v[212:215], v[98:101]
	v_mfma_f32_16x16x32_bf16 v[78:81], v[164:167], v[220:223], v[78:81]
	v_mfma_f32_16x16x32_bf16 v[74:77], v[172:175], v[220:223], v[74:77]
	v_mfma_f32_16x16x32_bf16 v[110:113], v[176:179], v[192:195], v[110:113]
	v_mfma_f32_16x16x32_bf16 v[102:105], v[184:187], v[192:195], v[102:105]
	v_mfma_f32_16x16x32_bf16 v[94:97], v[176:179], v[200:203], v[94:97]
	v_mfma_f32_16x16x32_bf16 v[90:93], v[184:187], v[200:203], v[90:93]
	v_mfma_f32_16x16x32_bf16 v[86:89], v[176:179], v[208:211], v[86:89]
	v_mfma_f32_16x16x32_bf16 v[82:85], v[184:187], v[208:211], v[82:85]
	v_mfma_f32_16x16x32_bf16 v[70:73], v[176:179], v[216:219], v[70:73]
	v_mfma_f32_16x16x32_bf16 v[66:69], v[184:187], v[216:219], v[66:69]
	v_mfma_f32_16x16x32_bf16 v[110:113], v[180:183], v[196:199], v[110:113]
	v_mfma_f32_16x16x32_bf16 v[102:105], v[188:191], v[196:199], v[102:105]
	v_mfma_f32_16x16x32_bf16 v[94:97], v[180:183], v[204:207], v[94:97]
	v_mfma_f32_16x16x32_bf16 v[90:93], v[188:191], v[204:207], v[90:93]
	v_mfma_f32_16x16x32_bf16 v[86:89], v[180:183], v[212:215], v[86:89]
	v_mfma_f32_16x16x32_bf16 v[82:85], v[188:191], v[212:215], v[82:85]
	v_mfma_f32_16x16x32_bf16 v[70:73], v[180:183], v[220:223], v[70:73]
	v_mfma_f32_16x16x32_bf16 v[66:69], v[188:191], v[220:223], v[66:69]
	s_barrier
	s_setprio 0
	s_add_i32 s38, s70, s51
	s_add_i32 m0, s38, 0xffffff80
	ds_read_b128 v[192:195], v159 offset:49152
	ds_read_b128 v[196:199], v159 offset:50176
	ds_read_b128 v[200:203], v159 offset:51200
	ds_read_b128 v[204:207], v159 offset:52224
	ds_read_b128 v[208:211], v159 offset:53248
	ds_read_b128 v[212:215], v159 offset:54272
	ds_read_b128 v[216:219], v159 offset:55296
	ds_read_b128 v[220:223], v159 offset:56320
	global_load_lds_dwordx4 v[152:153], off offset:128
	s_add_i32 m0, s38, 0x1f80
	s_add_u32 s38, s42, 0xe0080
	s_addc_u32 s39, s43, 0
	s_add_i32 s42, s71, s51
	global_load_lds_dwordx4 v[224:225], off offset:128
	s_mov_b32 m0, s42
	s_nop 0
	global_load_lds_dwordx4 v134, s[38:39]
	s_add_i32 m0, s42, 0x2000
	s_nop 0
	global_load_lds_dwordx4 v138, s[38:39]
	s_add_i32 m0, s57, 0xffffff80
	s_nop 0
	global_load_lds_dwordx4 v[226:227], off offset:128
	s_add_i32 m0, s58, 0xffffff80
	s_nop 0
	global_load_lds_dwordx4 v[230:231], off offset:128
	s_waitcnt vmcnt(8)
	s_waitcnt lgkmcnt(0)
	s_setprio 3
	s_barrier
	s_waitcnt lgkmcnt(0)
	v_mfma_f32_16x16x32_bf16 v[62:65], v[160:163], v[192:195], v[62:65]
	v_mfma_f32_16x16x32_bf16 v[58:61], v[168:171], v[192:195], v[58:61]
	v_mfma_f32_16x16x32_bf16 v[50:53], v[160:163], v[200:203], v[50:53]
	v_mfma_f32_16x16x32_bf16 v[42:45], v[168:171], v[200:203], v[42:45]
	v_mfma_f32_16x16x32_bf16 v[34:37], v[160:163], v[208:211], v[34:37]
	v_mfma_f32_16x16x32_bf16 v[26:29], v[168:171], v[208:211], v[26:29]
	v_mfma_f32_16x16x32_bf16 v[18:21], v[160:163], v[216:219], v[18:21]
	v_mfma_f32_16x16x32_bf16 v[10:13], v[168:171], v[216:219], v[10:13]
	v_mfma_f32_16x16x32_bf16 v[62:65], v[164:167], v[196:199], v[62:65]
	v_mfma_f32_16x16x32_bf16 v[58:61], v[172:175], v[196:199], v[58:61]
	v_mfma_f32_16x16x32_bf16 v[50:53], v[164:167], v[204:207], v[50:53]
	v_mfma_f32_16x16x32_bf16 v[42:45], v[172:175], v[204:207], v[42:45]
	v_mfma_f32_16x16x32_bf16 v[34:37], v[164:167], v[212:215], v[34:37]
	v_mfma_f32_16x16x32_bf16 v[26:29], v[172:175], v[212:215], v[26:29]
	v_mfma_f32_16x16x32_bf16 v[18:21], v[164:167], v[220:223], v[18:21]
	v_mfma_f32_16x16x32_bf16 v[10:13], v[172:175], v[220:223], v[10:13]
	v_mfma_f32_16x16x32_bf16 v[54:57], v[176:179], v[192:195], v[54:57]
	v_mfma_f32_16x16x32_bf16 v[46:49], v[184:187], v[192:195], v[46:49]
	v_mfma_f32_16x16x32_bf16 v[38:41], v[176:179], v[200:203], v[38:41]
	v_mfma_f32_16x16x32_bf16 v[30:33], v[184:187], v[200:203], v[30:33]
	v_mfma_f32_16x16x32_bf16 v[22:25], v[176:179], v[208:211], v[22:25]
	v_mfma_f32_16x16x32_bf16 v[14:17], v[184:187], v[208:211], v[14:17]
	v_mfma_f32_16x16x32_bf16 v[6:9], v[176:179], v[216:219], v[6:9]
	v_mfma_f32_16x16x32_bf16 v[2:5], v[184:187], v[216:219], v[2:5]
	v_mfma_f32_16x16x32_bf16 v[54:57], v[180:183], v[196:199], v[54:57]
	v_mfma_f32_16x16x32_bf16 v[46:49], v[188:191], v[196:199], v[46:49]
	v_mfma_f32_16x16x32_bf16 v[38:41], v[180:183], v[204:207], v[38:41]
	v_mfma_f32_16x16x32_bf16 v[30:33], v[188:191], v[204:207], v[30:33]
	v_mfma_f32_16x16x32_bf16 v[22:25], v[180:183], v[212:215], v[22:25]
	v_mfma_f32_16x16x32_bf16 v[14:17], v[188:191], v[212:215], v[14:17]
	v_mfma_f32_16x16x32_bf16 v[6:9], v[180:183], v[220:223], v[6:9]
	v_mfma_f32_16x16x32_bf16 v[2:5], v[188:191], v[220:223], v[2:5]
	s_barrier
	s_setprio 0
	s_add_i32 s69, s69, 2
	s_add_u32 s67, s67, 0x100
	s_addc_u32 s68, s68, 0
	s_cmp_gt_u32 s69, 53
	s_mov_b64 s[38:39], s[40:41]
; #define PG8_STAGE_A(b, h, ptr, NX) do { if constexpr (Sched::GATHER) { unsigned gs_[2]; gs_[0] = ((NX) && last_) ? gN[h][0] : gA[h][0]; gs_[1] = ((NX) && last_) ? gN[h][1] : gA[h][1]; PG8_STAGE(PG8_SA(b, h), ptr, gs_); } \
;         else PG8_STAGE(PG8_SA(b, h), (ptr) + ((h) ? hstep : (size_t)0), voffA); } while (0)
; #define PG8_STAGE(bufoff, gbase, voff) do { _Pragma("unroll") for (int _i = 0; _i < 2; ++_i) \
;         __builtin_amdgcn_global_load_lds((const unsigned*)((const char*)(gbase) + (voff)[_i]), (PG8_LAS unsigned*)(lds + (bufoff) + ldsw + _i * 8192), 16, 0, 0); } while (0)
; #define PG8_LDA(dst, b, h) do { _Pragma("unroll") for (int m = 0; m < 4; ++m) _Pragma("unroll") for (int k = 0; k < 2; ++k) dst[m][k] = *(const PG8_LAS bf16x8*)(lds + PG8_SA(b, h) + aoff + m * 2048 + k * 1024); } while (0)
; #define PG8_LDB(dst, b, h) do { _Pragma("unroll") for (int n = 0; n < 2; ++n) _Pragma("unroll") for (int k = 0; k < 2; ++k) dst[n][k] = *(const PG8_LAS bf16x8*)(lds + PG8_SB(b, h) + boff + n * 2048 + k * 1024); } while (0)
; #define PG8_MMA(ai, bj, At, Bt) do { __builtin_amdgcn_s_setprio(1); _Pragma("unroll") for (int m = 0; m < 4; ++m) _Pragma("unroll") for (int n = 0; n < 2; ++n) _Pragma("unroll") for (int k = 0; k < 2; ++k) \
;         acc[ai][bj][m][n] = __builtin_amdgcn_mfma_f32_16x16x32_bf16(Bt[n][k], At[m][k], acc[ai][bj][m][n], 0, 0, 0); __builtin_amdgcn_s_setprio(0); } while (0)
; #define PG8_WAIT_V(n) asm volatile("s_waitcnt vmcnt(" #n ")" ::: "memory")
; #define PG8_WAIT_L(n) asm volatile("s_waitcnt lgkmcnt(" #n ")" ::: "memory")
; template <class Epi, class Sched, bool ALIGN_EPI = false, bool SP2 = false>
; __device__ __forceinline__ void gemm_phase(PG8_LAS unsigned char* lds, const Gemm g, const Sched& S, const Epi& E, const bool skip_epi = false) {
;     ...
;             PG8_LDB(B0, 0, 0); PG8_LDB(B1, 0, 1); PG8_SCHED; PG8_LDA(At, 0, 0); PG8_STAGE_A(1, 1, a1, false);
;             PG8_WAIT_V(8); PG8_WAIT_L(0); PG8_BAR; PG8_MMA(0, 0, At, B0); PG8_MMA(0, 1, At, B1); PG8_BAR; PG8_SCHED;
;             PG8_LDA(At, 0, 1); PG8_STAGE(PG8_SB(0, 0), b2, voffB); PG8_STAGE(PG8_SB(0, 1), b2 + hstep, voffB); PG8_STAGE_A(0, 0, a2, true);
;             PG8_WAIT_V(8); PG8_WAIT_L(0); PG8_BAR; PG8_MMA(1, 0, At, B0); PG8_MMA(1, 1, At, B1); PG8_BAR; PG8_SCHED;
;             PG8_LDB(B0, 1, 0); PG8_LDB(B1, 1, 1); PG8_SCHED; PG8_LDA(At, 1, 0); PG8_STAGE_A(0, 1, a2, true);
.LBB0_1823:
	ds_read_b128 v[160:163], v157
	ds_read_b128 v[164:167], v157 offset:1024
	ds_read_b128 v[168:171], v157 offset:2048
	ds_read_b128 v[172:175], v157 offset:3072
	ds_read_b128 v[176:179], v158
	ds_read_b128 v[180:183], v158 offset:1024
	ds_read_b128 v[184:187], v158 offset:2048
	ds_read_b128 v[188:191], v158 offset:3072
	s_add_u32 s40, s38, 0x100
	s_addc_u32 s41, s39, 0
	s_cmp_eq_u32 s69, 52
	s_cselect_b32 s45, s7, s41
	s_cselect_b32 s44, s6, s40
	s_cselect_b32 s43, s35, s68
	s_cselect_b32 s42, s34, s67
	v_lshl_add_u64 v[152:153], s[38:39], 0, v[140:141]
	s_add_i32 m0, s37, 0xc000
	ds_read_b128 v[192:195], v159
	ds_read_b128 v[196:199], v159 offset:1024
	ds_read_b128 v[200:203], v159 offset:2048
	ds_read_b128 v[204:207], v159 offset:3072
	ds_read_b128 v[208:211], v159 offset:4096
	ds_read_b128 v[212:215], v159 offset:5120
	ds_read_b128 v[216:219], v159 offset:6144
	ds_read_b128 v[220:223], v159 offset:7168
	global_load_lds_dwordx4 v[152:153], off
	v_lshl_add_u64 v[152:153], s[38:39], 0, v[142:143]
	s_add_i32 m0, s37, 0xe000
	s_nop 0
	global_load_lds_dwordx4 v[152:153], off
	s_waitcnt vmcnt(8)
	s_waitcnt lgkmcnt(0)
	s_setprio 3
	s_barrier
	s_waitcnt lgkmcnt(0)
	v_mfma_f32_16x16x32_bf16 v[126:129], v[160:163], v[192:195], v[126:129]
	v_mfma_f32_16x16x32_bf16 v[122:125], v[168:171], v[192:195], v[122:125]
	v_mfma_f32_16x16x32_bf16 v[118:121], v[160:163], v[200:203], v[118:121]
	v_mfma_f32_16x16x32_bf16 v[114:117], v[168:171], v[200:203], v[114:117]
	v_mfma_f32_16x16x32_bf16 v[106:109], v[160:163], v[208:211], v[106:109]
	v_mfma_f32_16x16x32_bf16 v[98:101], v[168:171], v[208:211], v[98:101]
	v_mfma_f32_16x16x32_bf16 v[78:81], v[160:163], v[216:219], v[78:81]
	v_mfma_f32_16x16x32_bf16 v[74:77], v[168:171], v[216:219], v[74:77]
	v_mfma_f32_16x16x32_bf16 v[126:129], v[164:167], v[196:199], v[126:129]
	v_mfma_f32_16x16x32_bf16 v[122:125], v[172:175], v[196:199], v[122:125]
	v_mfma_f32_16x16x32_bf16 v[118:121], v[164:167], v[204:207], v[118:121]
	v_mfma_f32_16x16x32_bf16 v[114:117], v[172:175], v[204:207], v[114:117]
	v_mfma_f32_16x16x32_bf16 v[106:109], v[164:167], v[212:215], v[106:109]
	v_mfma_f32_16x16x32_bf16 v[98:101], v[172:175], v[212:215], v[98:101]
	v_mfma_f32_16x16x32_bf16 v[78:81], v[164:167], v[220:223], v[78:81]
	v_mfma_f32_16x16x32_bf16 v[74:77], v[172:175], v[220:223], v[74:77]
	v_mfma_f32_16x16x32_bf16 v[110:113], v[176:179], v[192:195], v[110:113]
	v_mfma_f32_16x16x32_bf16 v[102:105], v[184:187], v[192:195], v[102:105]
	v_mfma_f32_16x16x32_bf16 v[94:97], v[176:179], v[200:203], v[94:97]
	v_mfma_f32_16x16x32_bf16 v[90:93], v[184:187], v[200:203], v[90:93]
	v_mfma_f32_16x16x32_bf16 v[86:89], v[176:179], v[208:211], v[86:89]
	v_mfma_f32_16x16x32_bf16 v[82:85], v[184:187], v[208:211], v[82:85]
	v_mfma_f32_16x16x32_bf16 v[70:73], v[176:179], v[216:219], v[70:73]
	v_mfma_f32_16x16x32_bf16 v[66:69], v[184:187], v[216:219], v[66:69]
	v_mfma_f32_16x16x32_bf16 v[110:113], v[180:183], v[196:199], v[110:113]
	v_mfma_f32_16x16x32_bf16 v[102:105], v[188:191], v[196:199], v[102:105]
	v_mfma_f32_16x16x32_bf16 v[94:97], v[180:183], v[204:207], v[94:97]
	v_mfma_f32_16x16x32_bf16 v[90:93], v[188:191], v[204:207], v[90:93]
	v_mfma_f32_16x16x32_bf16 v[86:89], v[180:183], v[212:215], v[86:89]
	v_mfma_f32_16x16x32_bf16 v[82:85], v[188:191], v[212:215], v[82:85]
	v_mfma_f32_16x16x32_bf16 v[70:73], v[180:183], v[220:223], v[70:73]
	v_mfma_f32_16x16x32_bf16 v[66:69], v[188:191], v[220:223], v[66:69]
	s_barrier
	s_setprio 0
	s_add_i32 s38, s60, s51
	v_lshl_add_u64 v[152:153], s[42:43], 0, v[134:135]
	s_mov_b32 m0, s38
	ds_read_b128 v[192:195], v159 offset:16384
	ds_read_b128 v[196:199], v159 offset:17408
	ds_read_b128 v[200:203], v159 offset:18432
	ds_read_b128 v[204:207], v159 offset:19456
	ds_read_b128 v[208:211], v159 offset:20480
	ds_read_b128 v[212:215], v159 offset:21504
	ds_read_b128 v[216:219], v159 offset:22528
	ds_read_b128 v[220:223], v159 offset:23552
	global_load_lds_dwordx4 v[152:153], off
	s_add_i32 m0, s38, 0x2000
	s_add_u32 s38, s42, 0xe0000
	v_lshl_add_u64 v[224:225], s[42:43], 0, v[138:139]
	s_addc_u32 s39, s43, 0
	s_add_i32 s70, s61, s51
	global_load_lds_dwordx4 v[224:225], off
	s_mov_b32 m0, s70
	v_lshl_add_u64 v[230:231], s[44:45], 0, v[136:137]
	global_load_lds_dwordx4 v134, s[38:39]
	s_add_i32 m0, s70, 0x2000
	s_nop 0
	global_load_lds_dwordx4 v138, s[38:39]
	v_lshl_add_u64 v[226:227], s[44:45], 0, v[132:133]
	s_mov_b32 m0, s37
	s_nop 0
	global_load_lds_dwordx4 v[226:227], off
	s_mov_b32 m0, s52
	s_nop 0
	global_load_lds_dwordx4 v[230:231], off
	s_waitcnt vmcnt(8)
	s_waitcnt lgkmcnt(0)
	s_setprio 3
	s_barrier
; #define PG8_STAGE_A(b, h, ptr, NX) do { if constexpr (Sched::GATHER) { unsigned gs_[2]; gs_[0] = ((NX) && last_) ? gN[h][0] : gA[h][0]; gs_[1] = ((NX) && last_) ? gN[h][1] : gA[h][1]; PG8_STAGE(PG8_SA(b, h), ptr, gs_); } \
;         else PG8_STAGE(PG8_SA(b, h), (ptr) + ((h) ? hstep : (size_t)0), voffA); } while (0)
; #define PG8_LDA(dst, b, h) do { _Pragma("unroll") for (int m = 0; m < 4; ++m) _Pragma("unroll") for (int k = 0; k < 2; ++k) dst[m][k] = *(const PG8_LAS bf16x8*)(lds + PG8_SA(b, h) + aoff + m * 2048 + k * 1024); } while (0)
; #define PG8_LDB(dst, b, h) do { _Pragma("unroll") for (int n = 0; n < 2; ++n) _Pragma("unroll") for (int k = 0; k < 2; ++k) dst[n][k] = *(const PG8_LAS bf16x8*)(lds + PG8_SB(b, h) + boff + n * 2048 + k * 1024); } while (0)
; #define PG8_MMA(ai, bj, At, Bt) do { __builtin_amdgcn_s_setprio(1); _Pragma("unroll") for (int m = 0; m < 4; ++m) _Pragma("unroll") for (int n = 0; n < 2; ++n) _Pragma("unroll") for (int k = 0; k < 2; ++k) \
;         acc[ai][bj][m][n] = __builtin_amdgcn_mfma_f32_16x16x32_bf16(Bt[n][k], At[m][k], acc[ai][bj][m][n], 0, 0, 0); __builtin_amdgcn_s_setprio(0); } while (0)
; #define PG8_WAIT_V(n) asm volatile("s_waitcnt vmcnt(" #n ")" ::: "memory")
; #define PG8_WAIT_L(n) asm volatile("s_waitcnt lgkmcnt(" #n ")" ::: "memory")
; #define PG8_BAR __builtin_amdgcn_s_barrier()
; #define PG8_SCHED __builtin_amdgcn_sched_barrier(0)
; template <class Epi, class Sched, bool ALIGN_EPI = false, bool SP2 = false>
; __device__ __forceinline__ void gemm_phase(PG8_LAS unsigned char* lds, const Gemm g, const Sched& S, const Epi& E, const bool skip_epi = false) {
;     ...
;             PG8_WAIT_V(8); PG8_WAIT_L(0); PG8_BAR; PG8_MMA(1, 0, At, B0); PG8_MMA(1, 1, At, B1); PG8_BAR; PG8_SCHED;
;             PG8_LDB(B0, 1, 0); PG8_LDB(B1, 1, 1); PG8_SCHED; PG8_LDA(At, 1, 0); PG8_STAGE_A(0, 1, a2, true);
;             PG8_WAIT_V(8); PG8_WAIT_L(0); PG8_BAR; PG8_MMA(0, 0, At, B0); PG8_MMA(0, 1, At, B1); PG8_BAR; PG8_SCHED;
	s_waitcnt lgkmcnt(0)
	v_mfma_f32_16x16x32_bf16 v[62:65], v[160:163], v[192:195], v[62:65]
	v_mfma_f32_16x16x32_bf16 v[58:61], v[168:171], v[192:195], v[58:61]
	v_mfma_f32_16x16x32_bf16 v[50:53], v[160:163], v[200:203], v[50:53]
	v_mfma_f32_16x16x32_bf16 v[42:45], v[168:171], v[200:203], v[42:45]
	v_mfma_f32_16x16x32_bf16 v[34:37], v[160:163], v[208:211], v[34:37]
	v_mfma_f32_16x16x32_bf16 v[26:29], v[168:171], v[208:211], v[26:29]
	v_mfma_f32_16x16x32_bf16 v[18:21], v[160:163], v[216:219], v[18:21]
	v_mfma_f32_16x16x32_bf16 v[10:13], v[168:171], v[216:219], v[10:13]
	v_mfma_f32_16x16x32_bf16 v[62:65], v[164:167], v[196:199], v[62:65]
	v_mfma_f32_16x16x32_bf16 v[58:61], v[172:175], v[196:199], v[58:61]
	v_mfma_f32_16x16x32_bf16 v[50:53], v[164:167], v[204:207], v[50:53]
	v_mfma_f32_16x16x32_bf16 v[42:45], v[172:175], v[204:207], v[42:45]
	v_mfma_f32_16x16x32_bf16 v[34:37], v[164:167], v[212:215], v[34:37]
	v_mfma_f32_16x16x32_bf16 v[26:29], v[172:175], v[212:215], v[26:29]
	v_mfma_f32_16x16x32_bf16 v[18:21], v[164:167], v[220:223], v[18:21]
	v_mfma_f32_16x16x32_bf16 v[10:13], v[172:175], v[220:223], v[10:13]
	v_mfma_f32_16x16x32_bf16 v[54:57], v[176:179], v[192:195], v[54:57]
	v_mfma_f32_16x16x32_bf16 v[46:49], v[184:187], v[192:195], v[46:49]
	v_mfma_f32_16x16x32_bf16 v[38:41], v[176:179], v[200:203], v[38:41]
	v_mfma_f32_16x16x32_bf16 v[30:33], v[184:187], v[200:203], v[30:33]
	v_mfma_f32_16x16x32_bf16 v[22:25], v[176:179], v[208:211], v[22:25]
	v_mfma_f32_16x16x32_bf16 v[14:17], v[184:187], v[208:211], v[14:17]
	v_mfma_f32_16x16x32_bf16 v[6:9], v[176:179], v[216:219], v[6:9]
	v_mfma_f32_16x16x32_bf16 v[2:5], v[184:187], v[216:219], v[2:5]
	v_mfma_f32_16x16x32_bf16 v[54:57], v[180:183], v[196:199], v[54:57]
	v_mfma_f32_16x16x32_bf16 v[46:49], v[188:191], v[196:199], v[46:49]
	v_mfma_f32_16x16x32_bf16 v[38:41], v[180:183], v[204:207], v[38:41]
	v_mfma_f32_16x16x32_bf16 v[30:33], v[188:191], v[204:207], v[30:33]
	v_mfma_f32_16x16x32_bf16 v[22:25], v[180:183], v[212:215], v[22:25]
	v_mfma_f32_16x16x32_bf16 v[14:17], v[188:191], v[212:215], v[14:17]
	v_mfma_f32_16x16x32_bf16 v[6:9], v[180:183], v[220:223], v[6:9]
	v_mfma_f32_16x16x32_bf16 v[2:5], v[188:191], v[220:223], v[2:5]
	s_barrier
	s_setprio 0
	s_add_i32 s70, 0, 0x18000
	v_add_u32_e32 v130, s70, v147
	s_add_i32 s71, 0, 0x1c000
	ds_read_b128 v[160:163], v130
	ds_read_b128 v[164:167], v130 offset:1024
	ds_read_b128 v[168:171], v130 offset:2048
	ds_read_b128 v[172:175], v130 offset:3072
	v_add_u32_e32 v130, s71, v147
	ds_read_b128 v[176:179], v130
	ds_read_b128 v[180:183], v130 offset:1024
	ds_read_b128 v[184:187], v130 offset:2048
	ds_read_b128 v[188:191], v130 offset:3072
	s_add_u32 s38, s44, 0xe0000
	s_addc_u32 s39, s45, 0
	s_mov_b32 m0, s53
	ds_read_b128 v[192:195], v159 offset:32768
	ds_read_b128 v[196:199], v159 offset:33792
	ds_read_b128 v[200:203], v159 offset:34816
	ds_read_b128 v[204:207], v159 offset:35840
	ds_read_b128 v[208:211], v159 offset:36864
	ds_read_b128 v[212:215], v159 offset:37888
	ds_read_b128 v[216:219], v159 offset:38912
	ds_read_b128 v[220:223], v159 offset:39936
	global_load_lds_dwordx4 v132, s[38:39]
	s_mov_b32 m0, s54
	s_nop 0
	global_load_lds_dwordx4 v136, s[38:39]
	s_waitcnt vmcnt(8)
	s_waitcnt lgkmcnt(0)
	s_setprio 3
	s_barrier
	s_waitcnt lgkmcnt(0)
	v_mfma_f32_16x16x32_bf16 v[126:129], v[160:163], v[192:195], v[126:129]
	v_mfma_f32_16x16x32_bf16 v[122:125], v[168:171], v[192:195], v[122:125]
	v_mfma_f32_16x16x32_bf16 v[118:121], v[160:163], v[200:203], v[118:121]
	v_mfma_f32_16x16x32_bf16 v[114:117], v[168:171], v[200:203], v[114:117]
	v_mfma_f32_16x16x32_bf16 v[106:109], v[160:163], v[208:211], v[106:109]
	v_mfma_f32_16x16x32_bf16 v[98:101], v[168:171], v[208:211], v[98:101]
	v_mfma_f32_16x16x32_bf16 v[78:81], v[160:163], v[216:219], v[78:81]
	v_mfma_f32_16x16x32_bf16 v[74:77], v[168:171], v[216:219], v[74:77]
	v_mfma_f32_16x16x32_bf16 v[126:129], v[164:167], v[196:199], v[126:129]
	v_mfma_f32_16x16x32_bf16 v[122:125], v[172:175], v[196:199], v[122:125]
	v_mfma_f32_16x16x32_bf16 v[118:121], v[164:167], v[204:207], v[118:121]
	v_mfma_f32_16x16x32_bf16 v[114:117], v[172:175], v[204:207], v[114:117]
	v_mfma_f32_16x16x32_bf16 v[106:109], v[164:167], v[212:215], v[106:109]
	v_mfma_f32_16x16x32_bf16 v[98:101], v[172:175], v[212:215], v[98:101]
	v_mfma_f32_16x16x32_bf16 v[78:81], v[164:167], v[220:223], v[78:81]
	v_mfma_f32_16x16x32_bf16 v[74:77], v[172:175], v[220:223], v[74:77]
	v_mfma_f32_16x16x32_bf16 v[110:113], v[176:179], v[192:195], v[110:113]
	v_mfma_f32_16x16x32_bf16 v[102:105], v[184:187], v[192:195], v[102:105]
	v_mfma_f32_16x16x32_bf16 v[94:97], v[176:179], v[200:203], v[94:97]
	v_mfma_f32_16x16x32_bf16 v[90:93], v[184:187], v[200:203], v[90:93]
	v_mfma_f32_16x16x32_bf16 v[86:89], v[176:179], v[208:211], v[86:89]
	v_mfma_f32_16x16x32_bf16 v[82:85], v[184:187], v[208:211], v[82:85]
	v_mfma_f32_16x16x32_bf16 v[70:73], v[176:179], v[216:219], v[70:73]
	v_mfma_f32_16x16x32_bf16 v[66:69], v[184:187], v[216:219], v[66:69]
	v_mfma_f32_16x16x32_bf16 v[110:113], v[180:183], v[196:199], v[110:113]
	v_mfma_f32_16x16x32_bf16 v[102:105], v[188:191], v[196:199], v[102:105]
	v_mfma_f32_16x16x32_bf16 v[94:97], v[180:183], v[204:207], v[94:97]
	v_mfma_f32_16x16x32_bf16 v[90:93], v[188:191], v[204:207], v[90:93]
	v_mfma_f32_16x16x32_bf16 v[86:89], v[180:183], v[212:215], v[86:89]
	v_mfma_f32_16x16x32_bf16 v[82:85], v[188:191], v[212:215], v[82:85]
	v_mfma_f32_16x16x32_bf16 v[70:73], v[180:183], v[220:223], v[70:73]
	v_mfma_f32_16x16x32_bf16 v[66:69], v[188:191], v[220:223], v[66:69]
	s_barrier
; #define PG8_STAGE_A(b, h, ptr, NX) do { if constexpr (Sched::GATHER) { unsigned gs_[2]; gs_[0] = ((NX) && last_) ? gN[h][0] : gA[h][0]; gs_[1] = ((NX) && last_) ? gN[h][1] : gA[h][1]; PG8_STAGE(PG8_SA(b, h), ptr, gs_); } \
;         else PG8_STAGE(PG8_SA(b, h), (ptr) + ((h) ? hstep : (size_t)0), voffA); } while (0)
; #define PG8_STAGE(bufoff, gbase, voff) do { _Pragma("unroll") for (int _i = 0; _i < 2; ++_i) \
;         __builtin_amdgcn_global_load_lds((const unsigned*)((const char*)(gbase) + (voff)[_i]), (PG8_LAS unsigned*)(lds + (bufoff) + ldsw + _i * 8192), 16, 0, 0); } while (0)
; #define PG8_LDA(dst, b, h) do { _Pragma("unroll") for (int m = 0; m < 4; ++m) _Pragma("unroll") for (int k = 0; k < 2; ++k) dst[m][k] = *(const PG8_LAS bf16x8*)(lds + PG8_SA(b, h) + aoff + m * 2048 + k * 1024); } while (0)
; #define PG8_MMA(ai, bj, At, Bt) do { __builtin_amdgcn_s_setprio(1); _Pragma("unroll") for (int m = 0; m < 4; ++m) _Pragma("unroll") for (int n = 0; n < 2; ++n) _Pragma("unroll") for (int k = 0; k < 2; ++k) \
;         acc[ai][bj][m][n] = __builtin_amdgcn_mfma_f32_16x16x32_bf16(Bt[n][k], At[m][k], acc[ai][bj][m][n], 0, 0, 0); __builtin_amdgcn_s_setprio(0); } while (0)
; #define PG8_WAIT_V(n) asm volatile("s_waitcnt vmcnt(" #n ")" ::: "memory")
; #define PG8_WAIT_L(n) asm volatile("s_waitcnt lgkmcnt(" #n ")" ::: "memory")
; #define PG8_BAR __builtin_amdgcn_s_barrier()
; #define PG8_SCHED __builtin_amdgcn_sched_barrier(0)
; template <class Epi, class Sched, bool ALIGN_EPI = false, bool SP2 = false>
; __device__ __forceinline__ void gemm_phase(PG8_LAS unsigned char* lds, const Gemm g, const Sched& S, const Epi& E, const bool skip_epi = false) {
;     ...
;             PG8_WAIT_V(8); PG8_WAIT_L(0); PG8_BAR; PG8_MMA(0, 0, At, B0); PG8_MMA(0, 1, At, B1); PG8_BAR; PG8_SCHED;
;             PG8_LDA(At, 1, 1); PG8_STAGE(PG8_SB(1, 0), b3, voffB); PG8_STAGE(PG8_SB(1, 1), b3 + hstep, voffB); PG8_STAGE_A(1, 0, a3, true);
;             PG8_WAIT_V(8); PG8_WAIT_L(0); PG8_BAR; PG8_MMA(1, 0, At, B0); PG8_MMA(1, 1, At, B1); PG8_BAR; PG8_SCHED;
;     ...
;         if constexpr (ALIGN_EPI) { if (wr == 0) PG8_BAR; }
	s_setprio 0
	s_add_i32 s38, s70, s51
	s_add_i32 m0, s38, 0xffffff80
	ds_read_b128 v[192:195], v159 offset:49152
	ds_read_b128 v[196:199], v159 offset:50176
	ds_read_b128 v[200:203], v159 offset:51200
	ds_read_b128 v[204:207], v159 offset:52224
	ds_read_b128 v[208:211], v159 offset:53248
	ds_read_b128 v[212:215], v159 offset:54272
	ds_read_b128 v[216:219], v159 offset:55296
	ds_read_b128 v[220:223], v159 offset:56320
	global_load_lds_dwordx4 v[152:153], off offset:128
	s_add_i32 m0, s38, 0x1f80
	s_add_u32 s38, s42, 0xe0080
	s_addc_u32 s39, s43, 0
	s_add_i32 s42, s71, s51
	global_load_lds_dwordx4 v[224:225], off offset:128
	s_mov_b32 m0, s42
	s_nop 0
	global_load_lds_dwordx4 v134, s[38:39]
	s_add_i32 m0, s42, 0x2000
	s_nop 0
	global_load_lds_dwordx4 v138, s[38:39]
	s_add_i32 m0, s57, 0xffffff80
	s_nop 0
	global_load_lds_dwordx4 v[226:227], off offset:128
	s_add_i32 m0, s58, 0xffffff80
	s_nop 0
	global_load_lds_dwordx4 v[230:231], off offset:128
	s_waitcnt vmcnt(8)
	s_waitcnt lgkmcnt(0)
	s_setprio 3
	s_barrier
	s_waitcnt lgkmcnt(0)
	v_mfma_f32_16x16x32_bf16 v[62:65], v[160:163], v[192:195], v[62:65]
	v_mfma_f32_16x16x32_bf16 v[58:61], v[168:171], v[192:195], v[58:61]
	v_mfma_f32_16x16x32_bf16 v[50:53], v[160:163], v[200:203], v[50:53]
	v_mfma_f32_16x16x32_bf16 v[42:45], v[168:171], v[200:203], v[42:45]
	v_mfma_f32_16x16x32_bf16 v[34:37], v[160:163], v[208:211], v[34:37]
	v_mfma_f32_16x16x32_bf16 v[26:29], v[168:171], v[208:211], v[26:29]
	v_mfma_f32_16x16x32_bf16 v[18:21], v[160:163], v[216:219], v[18:21]
	v_mfma_f32_16x16x32_bf16 v[10:13], v[168:171], v[216:219], v[10:13]
	v_mfma_f32_16x16x32_bf16 v[62:65], v[164:167], v[196:199], v[62:65]
	v_mfma_f32_16x16x32_bf16 v[58:61], v[172:175], v[196:199], v[58:61]
	v_mfma_f32_16x16x32_bf16 v[50:53], v[164:167], v[204:207], v[50:53]
	v_mfma_f32_16x16x32_bf16 v[42:45], v[172:175], v[204:207], v[42:45]
	v_mfma_f32_16x16x32_bf16 v[34:37], v[164:167], v[212:215], v[34:37]
	v_mfma_f32_16x16x32_bf16 v[26:29], v[172:175], v[212:215], v[26:29]
	v_mfma_f32_16x16x32_bf16 v[18:21], v[164:167], v[220:223], v[18:21]
	v_mfma_f32_16x16x32_bf16 v[10:13], v[172:175], v[220:223], v[10:13]
	v_mfma_f32_16x16x32_bf16 v[54:57], v[176:179], v[192:195], v[54:57]
	v_mfma_f32_16x16x32_bf16 v[46:49], v[184:187], v[192:195], v[46:49]
	v_mfma_f32_16x16x32_bf16 v[38:41], v[176:179], v[200:203], v[38:41]
	v_mfma_f32_16x16x32_bf16 v[30:33], v[184:187], v[200:203], v[30:33]
	v_mfma_f32_16x16x32_bf16 v[22:25], v[176:179], v[208:211], v[22:25]
	v_mfma_f32_16x16x32_bf16 v[14:17], v[184:187], v[208:211], v[14:17]
	v_mfma_f32_16x16x32_bf16 v[6:9], v[176:179], v[216:219], v[6:9]
	v_mfma_f32_16x16x32_bf16 v[2:5], v[184:187], v[216:219], v[2:5]
	v_mfma_f32_16x16x32_bf16 v[54:57], v[180:183], v[196:199], v[54:57]
	v_mfma_f32_16x16x32_bf16 v[46:49], v[188:191], v[196:199], v[46:49]
	v_mfma_f32_16x16x32_bf16 v[38:41], v[180:183], v[204:207], v[38:41]
	v_mfma_f32_16x16x32_bf16 v[30:33], v[188:191], v[204:207], v[30:33]
	v_mfma_f32_16x16x32_bf16 v[22:25], v[180:183], v[212:215], v[22:25]
	v_mfma_f32_16x16x32_bf16 v[14:17], v[188:191], v[212:215], v[14:17]
	v_mfma_f32_16x16x32_bf16 v[6:9], v[180:183], v[220:223], v[6:9]
	v_mfma_f32_16x16x32_bf16 v[2:5], v[188:191], v[220:223], v[2:5]
	s_barrier
	s_setprio 0
	s_add_i32 s69, s69, 2
	s_add_u32 s67, s67, 0x100
	s_addc_u32 s68, s68, 0
	s_cmp_gt_u32 s69, 53
	s_mov_b64 s[38:39], s[40:41]
	s_cbranch_scc0 .LBB0_1823
	s_and_b64 vcc, exec, s[20:21]
	s_cbranch_vccz .LBB0_1826
	s_barrier

; #define PG8_STAGE_A(b, h, ptr, NX) do { if constexpr (Sched::GATHER) { unsigned gs_[2]; gs_[0] = ((NX) && last_) ? gN[h][0] : gA[h][0]; gs_[1] = ((NX) && last_) ? gN[h][1] : gA[h][1]; PG8_STAGE(PG8_SA(b, h), ptr, gs_); } \
;         else PG8_STAGE(PG8_SA(b, h), (ptr) + ((h) ? hstep : (size_t)0), voffA); } while (0)
; #define PG8_STAGE(bufoff, gbase, voff) do { _Pragma("unroll") for (int _i = 0; _i < 2; ++_i) \
;         __builtin_amdgcn_global_load_lds((const unsigned*)((const char*)(gbase) + (voff)[_i]), (PG8_LAS unsigned*)(lds + (bufoff) + ldsw + _i * 8192), 16, 0, 0); } while (0)
; #define PG8_LDA(dst, b, h) do { _Pragma("unroll") for (int m = 0; m < 4; ++m) _Pragma("unroll") for (int k = 0; k < 2; ++k) dst[m][k] = *(const PG8_LAS bf16x8*)(lds + PG8_SA(b, h) + aoff + m * 2048 + k * 1024); } while (0)
; #define PG8_LDB(dst, b, h) do { _Pragma("unroll") for (int n = 0; n < 2; ++n) _Pragma("unroll") for (int k = 0; k < 2; ++k) dst[n][k] = *(const PG8_LAS bf16x8*)(lds + PG8_SB(b, h) + boff + n * 2048 + k * 1024); } while (0)
; #define PG8_WAIT_V(n) asm volatile("s_waitcnt vmcnt(" #n ")" ::: "memory")
; #define PG8_WAIT_L(n) asm volatile("s_waitcnt lgkmcnt(" #n ")" ::: "memory")
; template <class Epi, class Sched, bool ALIGN_EPI = false, bool SP2 = false>
; __device__ __forceinline__ void gemm_phase(PG8_LAS unsigned char* lds, const Gemm g, const Sched& S, const Epi& E, const bool skip_epi = false) {
;     ...
;         for (int t = 0; t < nt; t += 2) {
;             const bool last = (t == nt - 2); last_ = last && has_next;
;             const char* a1 = cA + (size_t)(t + 1) * kstep;
;             const char* a2 = last ? nA : cA + (size_t)(t + 2) * kstep; const char* b2 = last ? nB : cB + (size_t)(t + 2) * kstep;
;             const char* a3 = a2 + kstep; const char* b3 = b2 + kstep;
;             if (last && has_next) S.a_ready(nxt);
;             if constexpr (SP2) {
;             PG8_LDB(B0, 0, 0); PG8_LDB(B1, 0, 1); PG8_SCHED; PG8_LDA(At, 0, 0); PG8_STAGE_A(1, 1, a1, false);
;             PG8_WAIT_V(8); PG8_WAIT_L(0); PG8_BAR; PG8_MMA(0, 0, At, B0); PG8_MMA(0, 1, At, B1); PG8_BAR; PG8_SCHED;
;             PG8_LDA(At, 0, 1); PG8_STAGE(PG8_SB(0, 0), b2, voffB); PG8_STAGE(PG8_SB(0, 1), b2 + hstep, voffB); PG8_STAGE_A(0, 0, a2, true);
;             PG8_WAIT_V(8); PG8_WAIT_L(0); PG8_BAR; PG8_MMA(1, 0, At, B0); PG8_MMA(1, 1, At, B1); PG8_BAR; PG8_SCHED;
.LBB0_1843:
	s_add_u32 s54, s30, 0x100
	s_addc_u32 s55, s31, 0
	s_mov_b32 s56, -2
	ds_read_b128 v[142:145], v150
	ds_read_b128 v[154:157], v150 offset:1024
	ds_read_b128 v[158:161], v150 offset:2048
	ds_read_b128 v[162:165], v150 offset:3072
	ds_read_b128 v[166:169], v151
	ds_read_b128 v[170:173], v151 offset:1024
	ds_read_b128 v[174:177], v151 offset:2048
	ds_read_b128 v[178:181], v151 offset:3072
	s_add_u32 s30, s28, 0x100
	s_addc_u32 s31, s29, 0
	s_cmp_eq_u32 s56, 10
	s_cselect_b32 s37, s7, s31
	s_cselect_b32 s36, s6, s30
	s_cselect_b32 s35, s25, s55
	s_cselect_b32 s34, s24, s54
	v_lshl_add_u64 v[214:215], s[28:29], 0, v[136:137]
	s_add_i32 m0, s38, 0xc000
	ds_read_b128 v[182:185], v152
	ds_read_b128 v[186:189], v152 offset:1024
	ds_read_b128 v[190:193], v152 offset:2048
	ds_read_b128 v[194:197], v152 offset:3072
	ds_read_b128 v[198:201], v152 offset:4096
	ds_read_b128 v[202:205], v152 offset:5120
	ds_read_b128 v[206:209], v152 offset:6144
	ds_read_b128 v[210:213], v152 offset:7168
	global_load_lds_dwordx4 v[214:215], off
	v_lshl_add_u64 v[214:215], s[28:29], 0, v[138:139]
	s_add_i32 m0, s38, 0xe000
	s_nop 0
	global_load_lds_dwordx4 v[214:215], off
	s_waitcnt vmcnt(8)
	s_waitcnt lgkmcnt(0)
	s_setprio 3
	s_barrier
	s_waitcnt lgkmcnt(0)
	v_mfma_f32_16x16x32_bf16 v[126:129], v[142:145], v[182:185], 0
	v_mfma_f32_16x16x32_bf16 v[122:125], v[158:161], v[182:185], 0
	v_mfma_f32_16x16x32_bf16 v[110:113], v[142:145], v[190:193], 0
	v_mfma_f32_16x16x32_bf16 v[106:109], v[158:161], v[190:193], 0
	v_mfma_f32_16x16x32_bf16 v[94:97], v[142:145], v[198:201], 0
	v_mfma_f32_16x16x32_bf16 v[90:93], v[158:161], v[198:201], 0
	v_mfma_f32_16x16x32_bf16 v[78:81], v[142:145], v[206:209], 0
	v_mfma_f32_16x16x32_bf16 v[74:77], v[158:161], v[206:209], 0
	v_mfma_f32_16x16x32_bf16 v[126:129], v[154:157], v[186:189], v[126:129]
	v_mfma_f32_16x16x32_bf16 v[122:125], v[162:165], v[186:189], v[122:125]
	v_mfma_f32_16x16x32_bf16 v[110:113], v[154:157], v[194:197], v[110:113]
	v_mfma_f32_16x16x32_bf16 v[106:109], v[162:165], v[194:197], v[106:109]
	v_mfma_f32_16x16x32_bf16 v[94:97], v[154:157], v[202:205], v[94:97]
	v_mfma_f32_16x16x32_bf16 v[90:93], v[162:165], v[202:205], v[90:93]
	v_mfma_f32_16x16x32_bf16 v[78:81], v[154:157], v[210:213], v[78:81]
	v_mfma_f32_16x16x32_bf16 v[74:77], v[162:165], v[210:213], v[74:77]
	v_mfma_f32_16x16x32_bf16 v[118:121], v[166:169], v[182:185], 0
	v_mfma_f32_16x16x32_bf16 v[114:117], v[174:177], v[182:185], 0
	v_mfma_f32_16x16x32_bf16 v[102:105], v[166:169], v[190:193], 0
	v_mfma_f32_16x16x32_bf16 v[98:101], v[174:177], v[190:193], 0
	v_mfma_f32_16x16x32_bf16 v[86:89], v[166:169], v[198:201], 0
	v_mfma_f32_16x16x32_bf16 v[82:85], v[174:177], v[198:201], 0
	v_mfma_f32_16x16x32_bf16 v[70:73], v[166:169], v[206:209], 0
	v_mfma_f32_16x16x32_bf16 v[66:69], v[174:177], v[206:209], 0
	v_mfma_f32_16x16x32_bf16 v[118:121], v[170:173], v[186:189], v[118:121]
	v_mfma_f32_16x16x32_bf16 v[114:117], v[178:181], v[186:189], v[114:117]
	v_mfma_f32_16x16x32_bf16 v[102:105], v[170:173], v[194:197], v[102:105]
	v_mfma_f32_16x16x32_bf16 v[98:101], v[178:181], v[194:197], v[98:101]
	v_mfma_f32_16x16x32_bf16 v[86:89], v[170:173], v[202:205], v[86:89]
	v_mfma_f32_16x16x32_bf16 v[82:85], v[178:181], v[202:205], v[82:85]
	v_mfma_f32_16x16x32_bf16 v[70:73], v[170:173], v[210:213], v[70:73]
	v_mfma_f32_16x16x32_bf16 v[66:69], v[178:181], v[210:213], v[66:69]
	s_barrier
	s_setprio 0
	s_add_i32 s28, s50, s3
	v_lshl_add_u64 v[214:215], s[34:35], 0, v[132:133]
	s_mov_b32 m0, s28
	ds_read_b128 v[182:185], v152 offset:16384
	ds_read_b128 v[186:189], v152 offset:17408
	ds_read_b128 v[190:193], v152 offset:18432
	ds_read_b128 v[194:197], v152 offset:19456
	ds_read_b128 v[198:201], v152 offset:20480
	ds_read_b128 v[202:205], v152 offset:21504
	ds_read_b128 v[206:209], v152 offset:22528
	ds_read_b128 v[210:213], v152 offset:23552
	global_load_lds_dwordx4 v[214:215], off
	s_add_i32 m0, s28, 0x2000
	s_add_u32 s28, s34, 0xe0000
	v_lshl_add_u64 v[216:217], s[34:35], 0, v[134:135]
	s_addc_u32 s29, s35, 0
	s_add_i32 s57, s51, s3
	global_load_lds_dwordx4 v[216:217], off
	s_mov_b32 m0, s57
	v_lshl_add_u64 v[220:221], s[36:37], 0, v[134:135]
	global_load_lds_dwordx4 v132, s[28:29]
	s_add_i32 m0, s57, 0x2000
	s_nop 0
	global_load_lds_dwordx4 v134, s[28:29]
	v_lshl_add_u64 v[218:219], s[36:37], 0, v[132:133]
	s_mov_b32 m0, s38
	s_nop 0
	global_load_lds_dwordx4 v[218:219], off
	s_mov_b32 m0, s39
	s_nop 0
	global_load_lds_dwordx4 v[220:221], off
	s_waitcnt vmcnt(8)
	s_waitcnt lgkmcnt(0)
	s_setprio 3
	s_barrier
	s_waitcnt lgkmcnt(0)
	v_mfma_f32_16x16x32_bf16 v[62:65], v[142:145], v[182:185], 0
	v_mfma_f32_16x16x32_bf16 v[58:61], v[158:161], v[182:185], 0
	v_mfma_f32_16x16x32_bf16 v[46:49], v[142:145], v[190:193], 0
	v_mfma_f32_16x16x32_bf16 v[42:45], v[158:161], v[190:193], 0
	v_mfma_f32_16x16x32_bf16 v[30:33], v[142:145], v[198:201], 0
	v_mfma_f32_16x16x32_bf16 v[26:29], v[158:161], v[198:201], 0
	v_mfma_f32_16x16x32_bf16 v[14:17], v[142:145], v[206:209], 0
	v_mfma_f32_16x16x32_bf16 v[10:13], v[158:161], v[206:209], 0
	v_mfma_f32_16x16x32_bf16 v[62:65], v[154:157], v[186:189], v[62:65]
	v_mfma_f32_16x16x32_bf16 v[58:61], v[162:165], v[186:189], v[58:61]
	v_mfma_f32_16x16x32_bf16 v[46:49], v[154:157], v[194:197], v[46:49]
	v_mfma_f32_16x16x32_bf16 v[42:45], v[162:165], v[194:197], v[42:45]
	v_mfma_f32_16x16x32_bf16 v[30:33], v[154:157], v[202:205], v[30:33]
	v_mfma_f32_16x16x32_bf16 v[26:29], v[162:165], v[202:205], v[26:29]
	v_mfma_f32_16x16x32_bf16 v[14:17], v[154:157], v[210:213], v[14:17]
	v_mfma_f32_16x16x32_bf16 v[10:13], v[162:165], v[210:213], v[10:13]
	v_mfma_f32_16x16x32_bf16 v[54:57], v[166:169], v[182:185], 0
	v_mfma_f32_16x16x32_bf16 v[50:53], v[174:177], v[182:185], 0
	v_mfma_f32_16x16x32_bf16 v[38:41], v[166:169], v[190:193], 0
	v_mfma_f32_16x16x32_bf16 v[34:37], v[174:177], v[190:193], 0
	v_mfma_f32_16x16x32_bf16 v[22:25], v[166:169], v[198:201], 0
	v_mfma_f32_16x16x32_bf16 v[18:21], v[174:177], v[198:201], 0
	v_mfma_f32_16x16x32_bf16 v[6:9], v[166:169], v[206:209], 0
	v_mfma_f32_16x16x32_bf16 v[2:5], v[174:177], v[206:209], 0
	v_mfma_f32_16x16x32_bf16 v[54:57], v[170:173], v[186:189], v[54:57]
	v_mfma_f32_16x16x32_bf16 v[50:53], v[178:181], v[186:189], v[50:53]
	v_mfma_f32_16x16x32_bf16 v[38:41], v[170:173], v[194:197], v[38:41]
	v_mfma_f32_16x16x32_bf16 v[34:37], v[178:181], v[194:197], v[34:37]
	v_mfma_f32_16x16x32_bf16 v[22:25], v[170:173], v[202:205], v[22:25]
	v_mfma_f32_16x16x32_bf16 v[18:21], v[178:181], v[202:205], v[18:21]
	v_mfma_f32_16x16x32_bf16 v[6:9], v[170:173], v[210:213], v[6:9]
	v_mfma_f32_16x16x32_bf16 v[2:5], v[178:181], v[210:213], v[2:5]
	s_barrier
; #define PG8_STAGE_A(b, h, ptr, NX) do { if constexpr (Sched::GATHER) { unsigned gs_[2]; gs_[0] = ((NX) && last_) ? gN[h][0] : gA[h][0]; gs_[1] = ((NX) && last_) ? gN[h][1] : gA[h][1]; PG8_STAGE(PG8_SA(b, h), ptr, gs_); } \
;         else PG8_STAGE(PG8_SA(b, h), (ptr) + ((h) ? hstep : (size_t)0), voffA); } while (0)
; #define PG8_STAGE(bufoff, gbase, voff) do { _Pragma("unroll") for (int _i = 0; _i < 2; ++_i) \
;         __builtin_amdgcn_global_load_lds((const unsigned*)((const char*)(gbase) + (voff)[_i]), (PG8_LAS unsigned*)(lds + (bufoff) + ldsw + _i * 8192), 16, 0, 0); } while (0)
; #define PG8_LDA(dst, b, h) do { _Pragma("unroll") for (int m = 0; m < 4; ++m) _Pragma("unroll") for (int k = 0; k < 2; ++k) dst[m][k] = *(const PG8_LAS bf16x8*)(lds + PG8_SA(b, h) + aoff + m * 2048 + k * 1024); } while (0)
; #define PG8_LDB(dst, b, h) do { _Pragma("unroll") for (int n = 0; n < 2; ++n) _Pragma("unroll") for (int k = 0; k < 2; ++k) dst[n][k] = *(const PG8_LAS bf16x8*)(lds + PG8_SB(b, h) + boff + n * 2048 + k * 1024); } while (0)
; #define PG8_MMA(ai, bj, At, Bt) do { __builtin_amdgcn_s_setprio(1); _Pragma("unroll") for (int m = 0; m < 4; ++m) _Pragma("unroll") for (int n = 0; n < 2; ++n) _Pragma("unroll") for (int k = 0; k < 2; ++k) \
;         acc[ai][bj][m][n] = __builtin_amdgcn_mfma_f32_16x16x32_bf16(Bt[n][k], At[m][k], acc[ai][bj][m][n], 0, 0, 0); __builtin_amdgcn_s_setprio(0); } while (0)
; #define PG8_WAIT_V(n) asm volatile("s_waitcnt vmcnt(" #n ")" ::: "memory")
; #define PG8_WAIT_L(n) asm volatile("s_waitcnt lgkmcnt(" #n ")" ::: "memory")
; #define PG8_BAR __builtin_amdgcn_s_barrier()
; #define PG8_SCHED __builtin_amdgcn_sched_barrier(0)
; template <class Epi, class Sched, bool ALIGN_EPI = false, bool SP2 = false>
; __device__ __forceinline__ void gemm_phase(PG8_LAS unsigned char* lds, const Gemm g, const Sched& S, const Epi& E, const bool skip_epi = false) {
;     ...
;             PG8_LDB(B0, 1, 0); PG8_LDB(B1, 1, 1); PG8_SCHED; PG8_LDA(At, 1, 0); PG8_STAGE_A(0, 1, a2, true);
;             PG8_WAIT_V(8); PG8_WAIT_L(0); PG8_BAR; PG8_MMA(0, 0, At, B0); PG8_MMA(0, 1, At, B1); PG8_BAR; PG8_SCHED;
;             PG8_LDA(At, 1, 1); PG8_STAGE(PG8_SB(1, 0), b3, voffB); PG8_STAGE(PG8_SB(1, 1), b3 + hstep, voffB); PG8_STAGE_A(1, 0, a3, true);
;             PG8_WAIT_V(8); PG8_WAIT_L(0); PG8_BAR; PG8_MMA(1, 0, At, B0); PG8_MMA(1, 1, At, B1); PG8_BAR; PG8_SCHED;
	s_setprio 0
	s_add_i32 s57, 0, 0x18000
	v_add_u32_e32 v130, s57, v146
	s_add_i32 s58, 0, 0x1c000
	ds_read_b128 v[142:145], v130
	ds_read_b128 v[154:157], v130 offset:1024
	ds_read_b128 v[158:161], v130 offset:2048
	ds_read_b128 v[162:165], v130 offset:3072
	v_add_u32_e32 v130, s58, v146
	ds_read_b128 v[166:169], v130
	ds_read_b128 v[170:173], v130 offset:1024
	ds_read_b128 v[174:177], v130 offset:2048
	ds_read_b128 v[178:181], v130 offset:3072
	s_add_u32 s28, s36, 0xe0000
	s_addc_u32 s29, s37, 0
	s_mov_b32 m0, s40
	ds_read_b128 v[182:185], v152 offset:32768
	ds_read_b128 v[186:189], v152 offset:33792
	ds_read_b128 v[190:193], v152 offset:34816
	ds_read_b128 v[194:197], v152 offset:35840
	ds_read_b128 v[198:201], v152 offset:36864
	ds_read_b128 v[202:205], v152 offset:37888
	ds_read_b128 v[206:209], v152 offset:38912
	ds_read_b128 v[210:213], v152 offset:39936
	global_load_lds_dwordx4 v132, s[28:29]
	s_mov_b32 m0, s41
	s_nop 0
	global_load_lds_dwordx4 v134, s[28:29]
	s_waitcnt vmcnt(8)
	s_waitcnt lgkmcnt(0)
	s_setprio 3
	s_barrier
	s_waitcnt lgkmcnt(0)
	v_mfma_f32_16x16x32_bf16 v[126:129], v[142:145], v[182:185], v[126:129]
	v_mfma_f32_16x16x32_bf16 v[122:125], v[158:161], v[182:185], v[122:125]
	v_mfma_f32_16x16x32_bf16 v[110:113], v[142:145], v[190:193], v[110:113]
	v_mfma_f32_16x16x32_bf16 v[106:109], v[158:161], v[190:193], v[106:109]
	v_mfma_f32_16x16x32_bf16 v[94:97], v[142:145], v[198:201], v[94:97]
	v_mfma_f32_16x16x32_bf16 v[90:93], v[158:161], v[198:201], v[90:93]
	v_mfma_f32_16x16x32_bf16 v[78:81], v[142:145], v[206:209], v[78:81]
	v_mfma_f32_16x16x32_bf16 v[74:77], v[158:161], v[206:209], v[74:77]
	v_mfma_f32_16x16x32_bf16 v[126:129], v[154:157], v[186:189], v[126:129]
	v_mfma_f32_16x16x32_bf16 v[122:125], v[162:165], v[186:189], v[122:125]
	v_mfma_f32_16x16x32_bf16 v[110:113], v[154:157], v[194:197], v[110:113]
	v_mfma_f32_16x16x32_bf16 v[106:109], v[162:165], v[194:197], v[106:109]
	v_mfma_f32_16x16x32_bf16 v[94:97], v[154:157], v[202:205], v[94:97]
	v_mfma_f32_16x16x32_bf16 v[90:93], v[162:165], v[202:205], v[90:93]
	v_mfma_f32_16x16x32_bf16 v[78:81], v[154:157], v[210:213], v[78:81]
	v_mfma_f32_16x16x32_bf16 v[74:77], v[162:165], v[210:213], v[74:77]
	v_mfma_f32_16x16x32_bf16 v[118:121], v[166:169], v[182:185], v[118:121]
	v_mfma_f32_16x16x32_bf16 v[114:117], v[174:177], v[182:185], v[114:117]
	v_mfma_f32_16x16x32_bf16 v[102:105], v[166:169], v[190:193], v[102:105]
	v_mfma_f32_16x16x32_bf16 v[98:101], v[174:177], v[190:193], v[98:101]
	v_mfma_f32_16x16x32_bf16 v[86:89], v[166:169], v[198:201], v[86:89]
	v_mfma_f32_16x16x32_bf16 v[82:85], v[174:177], v[198:201], v[82:85]
	v_mfma_f32_16x16x32_bf16 v[70:73], v[166:169], v[206:209], v[70:73]
	v_mfma_f32_16x16x32_bf16 v[66:69], v[174:177], v[206:209], v[66:69]
	v_mfma_f32_16x16x32_bf16 v[118:121], v[170:173], v[186:189], v[118:121]
	v_mfma_f32_16x16x32_bf16 v[114:117], v[178:181], v[186:189], v[114:117]
	v_mfma_f32_16x16x32_bf16 v[102:105], v[170:173], v[194:197], v[102:105]
	v_mfma_f32_16x16x32_bf16 v[98:101], v[178:181], v[194:197], v[98:101]
	v_mfma_f32_16x16x32_bf16 v[86:89], v[170:173], v[202:205], v[86:89]
	v_mfma_f32_16x16x32_bf16 v[82:85], v[178:181], v[202:205], v[82:85]
	v_mfma_f32_16x16x32_bf16 v[70:73], v[170:173], v[210:213], v[70:73]
	v_mfma_f32_16x16x32_bf16 v[66:69], v[178:181], v[210:213], v[66:69]
	s_barrier
	s_setprio 0
	s_add_i32 s28, s57, s3
	s_add_i32 m0, s28, 0xffffff80
	ds_read_b128 v[182:185], v152 offset:49152
	ds_read_b128 v[186:189], v152 offset:50176
	ds_read_b128 v[190:193], v152 offset:51200
	ds_read_b128 v[194:197], v152 offset:52224
	ds_read_b128 v[198:201], v152 offset:53248
	ds_read_b128 v[202:205], v152 offset:54272
	ds_read_b128 v[206:209], v152 offset:55296
	ds_read_b128 v[210:213], v152 offset:56320
	global_load_lds_dwordx4 v[214:215], off offset:128
	s_add_i32 m0, s28, 0x1f80
	s_add_u32 s28, s34, 0xe0080
	s_addc_u32 s29, s35, 0
	s_add_i32 s34, s58, s3
	global_load_lds_dwordx4 v[216:217], off offset:128
	s_mov_b32 m0, s34
	s_nop 0
	global_load_lds_dwordx4 v132, s[28:29]
	s_add_i32 m0, s34, 0x2000
	s_nop 0
	global_load_lds_dwordx4 v134, s[28:29]
	s_add_i32 m0, s46, 0xffffff80
	s_nop 0
	global_load_lds_dwordx4 v[218:219], off offset:128
	s_add_i32 m0, s47, 0xffffff80
	s_nop 0
	global_load_lds_dwordx4 v[220:221], off offset:128
	s_waitcnt vmcnt(8)
	s_waitcnt lgkmcnt(0)
	s_setprio 3
	s_barrier
	s_waitcnt lgkmcnt(0)
	v_mfma_f32_16x16x32_bf16 v[62:65], v[142:145], v[182:185], v[62:65]
	v_mfma_f32_16x16x32_bf16 v[58:61], v[158:161], v[182:185], v[58:61]
	v_mfma_f32_16x16x32_bf16 v[46:49], v[142:145], v[190:193], v[46:49]
	v_mfma_f32_16x16x32_bf16 v[42:45], v[158:161], v[190:193], v[42:45]
	v_mfma_f32_16x16x32_bf16 v[30:33], v[142:145], v[198:201], v[30:33]
	v_mfma_f32_16x16x32_bf16 v[26:29], v[158:161], v[198:201], v[26:29]
	v_mfma_f32_16x16x32_bf16 v[14:17], v[142:145], v[206:209], v[14:17]
	v_mfma_f32_16x16x32_bf16 v[10:13], v[158:161], v[206:209], v[10:13]
	v_mfma_f32_16x16x32_bf16 v[62:65], v[154:157], v[186:189], v[62:65]
	v_mfma_f32_16x16x32_bf16 v[58:61], v[162:165], v[186:189], v[58:61]
	v_mfma_f32_16x16x32_bf16 v[46:49], v[154:157], v[194:197], v[46:49]
	v_mfma_f32_16x16x32_bf16 v[42:45], v[162:165], v[194:197], v[42:45]
	v_mfma_f32_16x16x32_bf16 v[30:33], v[154:157], v[202:205], v[30:33]
	v_mfma_f32_16x16x32_bf16 v[26:29], v[162:165], v[202:205], v[26:29]
	v_mfma_f32_16x16x32_bf16 v[14:17], v[154:157], v[210:213], v[14:17]
	v_mfma_f32_16x16x32_bf16 v[10:13], v[162:165], v[210:213], v[10:13]
	v_mfma_f32_16x16x32_bf16 v[54:57], v[166:169], v[182:185], v[54:57]
	v_mfma_f32_16x16x32_bf16 v[50:53], v[174:177], v[182:185], v[50:53]
	v_mfma_f32_16x16x32_bf16 v[38:41], v[166:169], v[190:193], v[38:41]
	v_mfma_f32_16x16x32_bf16 v[34:37], v[174:177], v[190:193], v[34:37]
	v_mfma_f32_16x16x32_bf16 v[22:25], v[166:169], v[198:201], v[22:25]
	v_mfma_f32_16x16x32_bf16 v[18:21], v[174:177], v[198:201], v[18:21]
	v_mfma_f32_16x16x32_bf16 v[6:9], v[166:169], v[206:209], v[6:9]
	v_mfma_f32_16x16x32_bf16 v[2:5], v[174:177], v[206:209], v[2:5]
	v_mfma_f32_16x16x32_bf16 v[54:57], v[170:173], v[186:189], v[54:57]
	v_mfma_f32_16x16x32_bf16 v[50:53], v[178:181], v[186:189], v[50:53]
	v_mfma_f32_16x16x32_bf16 v[38:41], v[170:173], v[194:197], v[38:41]
	v_mfma_f32_16x16x32_bf16 v[34:37], v[178:181], v[194:197], v[34:37]
	v_mfma_f32_16x16x32_bf16 v[22:25], v[170:173], v[202:205], v[22:25]
	v_mfma_f32_16x16x32_bf16 v[18:21], v[178:181], v[202:205], v[18:21]
	v_mfma_f32_16x16x32_bf16 v[6:9], v[170:173], v[210:213], v[6:9]
	v_mfma_f32_16x16x32_bf16 v[2:5], v[178:181], v[210:213], v[2:5]
	s_barrier
	s_setprio 0
	s_add_i32 s56, s56, 2
	s_add_u32 s54, s54, 0x100
	s_addc_u32 s55, s55, 0
	s_cmp_gt_u32 s56, 11
	s_mov_b64 s[28:29], s[30:31]
; #define PG8_STAGE_A(b, h, ptr, NX) do { if constexpr (Sched::GATHER) { unsigned gs_[2]; gs_[0] = ((NX) && last_) ? gN[h][0] : gA[h][0]; gs_[1] = ((NX) && last_) ? gN[h][1] : gA[h][1]; PG8_STAGE(PG8_SA(b, h), ptr, gs_); } \
;         else PG8_STAGE(PG8_SA(b, h), (ptr) + ((h) ? hstep : (size_t)0), voffA); } while (0)
; #define PG8_STAGE(bufoff, gbase, voff) do { _Pragma("unroll") for (int _i = 0; _i < 2; ++_i) \
;         __builtin_amdgcn_global_load_lds((const unsigned*)((const char*)(gbase) + (voff)[_i]), (PG8_LAS unsigned*)(lds + (bufoff) + ldsw + _i * 8192), 16, 0, 0); } while (0)
; #define PG8_LDA(dst, b, h) do { _Pragma("unroll") for (int m = 0; m < 4; ++m) _Pragma("unroll") for (int k = 0; k < 2; ++k) dst[m][k] = *(const PG8_LAS bf16x8*)(lds + PG8_SA(b, h) + aoff + m * 2048 + k * 1024); } while (0)
; #define PG8_LDB(dst, b, h) do { _Pragma("unroll") for (int n = 0; n < 2; ++n) _Pragma("unroll") for (int k = 0; k < 2; ++k) dst[n][k] = *(const PG8_LAS bf16x8*)(lds + PG8_SB(b, h) + boff + n * 2048 + k * 1024); } while (0)
; #define PG8_WAIT_V(n) asm volatile("s_waitcnt vmcnt(" #n ")" ::: "memory")
; #define PG8_WAIT_L(n) asm volatile("s_waitcnt lgkmcnt(" #n ")" ::: "memory")
; template <class Epi, class Sched, bool ALIGN_EPI = false, bool SP2 = false>
; __device__ __forceinline__ void gemm_phase(PG8_LAS unsigned char* lds, const Gemm g, const Sched& S, const Epi& E, const bool skip_epi = false) {
;     ...
;         for (int t = 0; t < nt; t += 2) {
;             const bool last = (t == nt - 2); last_ = last && has_next;
;             const char* a1 = cA + (size_t)(t + 1) * kstep;
;             const char* a2 = last ? nA : cA + (size_t)(t + 2) * kstep; const char* b2 = last ? nB : cB + (size_t)(t + 2) * kstep;
;             const char* a3 = a2 + kstep; const char* b3 = b2 + kstep;
;             if (last && has_next) S.a_ready(nxt);
;             if constexpr (SP2) {
;             PG8_LDB(B0, 0, 0); PG8_LDB(B1, 0, 1); PG8_SCHED; PG8_LDA(At, 0, 0); PG8_STAGE_A(1, 1, a1, false);
;             PG8_WAIT_V(8); PG8_WAIT_L(0); PG8_BAR; PG8_MMA(0, 0, At, B0); PG8_MMA(0, 1, At, B1); PG8_BAR; PG8_SCHED;
;             PG8_LDA(At, 0, 1); PG8_STAGE(PG8_SB(0, 0), b2, voffB); PG8_STAGE(PG8_SB(0, 1), b2 + hstep, voffB); PG8_STAGE_A(0, 0, a2, true);
;             PG8_WAIT_V(8); PG8_WAIT_L(0); PG8_BAR; PG8_MMA(1, 0, At, B0); PG8_MMA(1, 1, At, B1); PG8_BAR; PG8_SCHED;
.LBB0_1844:
	ds_read_b128 v[142:145], v150
	ds_read_b128 v[154:157], v150 offset:1024
	ds_read_b128 v[158:161], v150 offset:2048
	ds_read_b128 v[162:165], v150 offset:3072
	ds_read_b128 v[166:169], v151
	ds_read_b128 v[170:173], v151 offset:1024
	ds_read_b128 v[174:177], v151 offset:2048
	ds_read_b128 v[178:181], v151 offset:3072
	s_add_u32 s30, s28, 0x100
	s_addc_u32 s31, s29, 0
	s_cmp_eq_u32 s56, 10
	s_cselect_b32 s37, s7, s31
	s_cselect_b32 s36, s6, s30
	s_cselect_b32 s35, s25, s55
	s_cselect_b32 s34, s24, s54
	v_lshl_add_u64 v[214:215], s[28:29], 0, v[136:137]
	s_add_i32 m0, s38, 0xc000
	ds_read_b128 v[182:185], v152
	ds_read_b128 v[186:189], v152 offset:1024
	ds_read_b128 v[190:193], v152 offset:2048
	ds_read_b128 v[194:197], v152 offset:3072
	ds_read_b128 v[198:201], v152 offset:4096
	ds_read_b128 v[202:205], v152 offset:5120
	ds_read_b128 v[206:209], v152 offset:6144
	ds_read_b128 v[210:213], v152 offset:7168
	global_load_lds_dwordx4 v[214:215], off
	v_lshl_add_u64 v[214:215], s[28:29], 0, v[138:139]
	s_add_i32 m0, s38, 0xe000
	s_nop 0
	global_load_lds_dwordx4 v[214:215], off
	s_waitcnt vmcnt(8)
	s_waitcnt lgkmcnt(0)
	s_setprio 3
	s_barrier
	s_waitcnt lgkmcnt(0)
	v_mfma_f32_16x16x32_bf16 v[126:129], v[142:145], v[182:185], v[126:129]
	v_mfma_f32_16x16x32_bf16 v[122:125], v[158:161], v[182:185], v[122:125]
	v_mfma_f32_16x16x32_bf16 v[110:113], v[142:145], v[190:193], v[110:113]
	v_mfma_f32_16x16x32_bf16 v[106:109], v[158:161], v[190:193], v[106:109]
	v_mfma_f32_16x16x32_bf16 v[94:97], v[142:145], v[198:201], v[94:97]
	v_mfma_f32_16x16x32_bf16 v[90:93], v[158:161], v[198:201], v[90:93]
	v_mfma_f32_16x16x32_bf16 v[78:81], v[142:145], v[206:209], v[78:81]
	v_mfma_f32_16x16x32_bf16 v[74:77], v[158:161], v[206:209], v[74:77]
	v_mfma_f32_16x16x32_bf16 v[126:129], v[154:157], v[186:189], v[126:129]
	v_mfma_f32_16x16x32_bf16 v[122:125], v[162:165], v[186:189], v[122:125]
	v_mfma_f32_16x16x32_bf16 v[110:113], v[154:157], v[194:197], v[110:113]
	v_mfma_f32_16x16x32_bf16 v[106:109], v[162:165], v[194:197], v[106:109]
	v_mfma_f32_16x16x32_bf16 v[94:97], v[154:157], v[202:205], v[94:97]
	v_mfma_f32_16x16x32_bf16 v[90:93], v[162:165], v[202:205], v[90:93]
	v_mfma_f32_16x16x32_bf16 v[78:81], v[154:157], v[210:213], v[78:81]
	v_mfma_f32_16x16x32_bf16 v[74:77], v[162:165], v[210:213], v[74:77]
	v_mfma_f32_16x16x32_bf16 v[118:121], v[166:169], v[182:185], v[118:121]
	v_mfma_f32_16x16x32_bf16 v[114:117], v[174:177], v[182:185], v[114:117]
	v_mfma_f32_16x16x32_bf16 v[102:105], v[166:169], v[190:193], v[102:105]
	v_mfma_f32_16x16x32_bf16 v[98:101], v[174:177], v[190:193], v[98:101]
	v_mfma_f32_16x16x32_bf16 v[86:89], v[166:169], v[198:201], v[86:89]
	v_mfma_f32_16x16x32_bf16 v[82:85], v[174:177], v[198:201], v[82:85]
	v_mfma_f32_16x16x32_bf16 v[70:73], v[166:169], v[206:209], v[70:73]
	v_mfma_f32_16x16x32_bf16 v[66:69], v[174:177], v[206:209], v[66:69]
	v_mfma_f32_16x16x32_bf16 v[118:121], v[170:173], v[186:189], v[118:121]
	v_mfma_f32_16x16x32_bf16 v[114:117], v[178:181], v[186:189], v[114:117]
	v_mfma_f32_16x16x32_bf16 v[102:105], v[170:173], v[194:197], v[102:105]
	v_mfma_f32_16x16x32_bf16 v[98:101], v[178:181], v[194:197], v[98:101]
	v_mfma_f32_16x16x32_bf16 v[86:89], v[170:173], v[202:205], v[86:89]
	v_mfma_f32_16x16x32_bf16 v[82:85], v[178:181], v[202:205], v[82:85]
	v_mfma_f32_16x16x32_bf16 v[70:73], v[170:173], v[210:213], v[70:73]
	v_mfma_f32_16x16x32_bf16 v[66:69], v[178:181], v[210:213], v[66:69]
	s_barrier
	s_setprio 0
	s_add_i32 s28, s50, s3
	v_lshl_add_u64 v[214:215], s[34:35], 0, v[132:133]
	s_mov_b32 m0, s28
	ds_read_b128 v[182:185], v152 offset:16384
	ds_read_b128 v[186:189], v152 offset:17408
	ds_read_b128 v[190:193], v152 offset:18432
	ds_read_b128 v[194:197], v152 offset:19456
	ds_read_b128 v[198:201], v152 offset:20480
	ds_read_b128 v[202:205], v152 offset:21504
	ds_read_b128 v[206:209], v152 offset:22528
	ds_read_b128 v[210:213], v152 offset:23552
	global_load_lds_dwordx4 v[214:215], off
	s_add_i32 m0, s28, 0x2000
	s_add_u32 s28, s34, 0xe0000
	v_lshl_add_u64 v[216:217], s[34:35], 0, v[134:135]
	s_addc_u32 s29, s35, 0
	s_add_i32 s57, s51, s3
	global_load_lds_dwordx4 v[216:217], off
	s_mov_b32 m0, s57
	v_lshl_add_u64 v[220:221], s[36:37], 0, v[134:135]
	global_load_lds_dwordx4 v132, s[28:29]
	s_add_i32 m0, s57, 0x2000
	s_nop 0
	global_load_lds_dwordx4 v134, s[28:29]
	v_lshl_add_u64 v[218:219], s[36:37], 0, v[132:133]
	s_mov_b32 m0, s38
	s_nop 0
	global_load_lds_dwordx4 v[218:219], off
	s_mov_b32 m0, s39
	s_nop 0
	global_load_lds_dwordx4 v[220:221], off
	s_waitcnt vmcnt(8)
	s_waitcnt lgkmcnt(0)
	s_setprio 3
	s_barrier
; #define PG8_STAGE_A(b, h, ptr, NX) do { if constexpr (Sched::GATHER) { unsigned gs_[2]; gs_[0] = ((NX) && last_) ? gN[h][0] : gA[h][0]; gs_[1] = ((NX) && last_) ? gN[h][1] : gA[h][1]; PG8_STAGE(PG8_SA(b, h), ptr, gs_); } \
;         else PG8_STAGE(PG8_SA(b, h), (ptr) + ((h) ? hstep : (size_t)0), voffA); } while (0)
; #define PG8_STAGE(bufoff, gbase, voff) do { _Pragma("unroll") for (int _i = 0; _i < 2; ++_i) \
;         __builtin_amdgcn_global_load_lds((const unsigned*)((const char*)(gbase) + (voff)[_i]), (PG8_LAS unsigned*)(lds + (bufoff) + ldsw + _i * 8192), 16, 0, 0); } while (0)
; #define PG8_LDA(dst, b, h) do { _Pragma("unroll") for (int m = 0; m < 4; ++m) _Pragma("unroll") for (int k = 0; k < 2; ++k) dst[m][k] = *(const PG8_LAS bf16x8*)(lds + PG8_SA(b, h) + aoff + m * 2048 + k * 1024); } while (0)
; #define PG8_LDB(dst, b, h) do { _Pragma("unroll") for (int n = 0; n < 2; ++n) _Pragma("unroll") for (int k = 0; k < 2; ++k) dst[n][k] = *(const PG8_LAS bf16x8*)(lds + PG8_SB(b, h) + boff + n * 2048 + k * 1024); } while (0)
; #define PG8_MMA(ai, bj, At, Bt) do { __builtin_amdgcn_s_setprio(1); _Pragma("unroll") for (int m = 0; m < 4; ++m) _Pragma("unroll") for (int n = 0; n < 2; ++n) _Pragma("unroll") for (int k = 0; k < 2; ++k) \
;         acc[ai][bj][m][n] = __builtin_amdgcn_mfma_f32_16x16x32_bf16(Bt[n][k], At[m][k], acc[ai][bj][m][n], 0, 0, 0); __builtin_amdgcn_s_setprio(0); } while (0)
; #define PG8_WAIT_V(n) asm volatile("s_waitcnt vmcnt(" #n ")" ::: "memory")
; #define PG8_WAIT_L(n) asm volatile("s_waitcnt lgkmcnt(" #n ")" ::: "memory")
; #define PG8_BAR __builtin_amdgcn_s_barrier()
; #define PG8_SCHED __builtin_amdgcn_sched_barrier(0)
; template <class Epi, class Sched, bool ALIGN_EPI = false, bool SP2 = false>
; __device__ __forceinline__ void gemm_phase(PG8_LAS unsigned char* lds, const Gemm g, const Sched& S, const Epi& E, const bool skip_epi = false) {
;     ...
;             PG8_WAIT_V(8); PG8_WAIT_L(0); PG8_BAR; PG8_MMA(1, 0, At, B0); PG8_MMA(1, 1, At, B1); PG8_BAR; PG8_SCHED;
;             PG8_LDB(B0, 1, 0); PG8_LDB(B1, 1, 1); PG8_SCHED; PG8_LDA(At, 1, 0); PG8_STAGE_A(0, 1, a2, true);
;             PG8_WAIT_V(8); PG8_WAIT_L(0); PG8_BAR; PG8_MMA(0, 0, At, B0); PG8_MMA(0, 1, At, B1); PG8_BAR; PG8_SCHED;
;             PG8_LDA(At, 1, 1); PG8_STAGE(PG8_SB(1, 0), b3, voffB); PG8_STAGE(PG8_SB(1, 1), b3 + hstep, voffB); PG8_STAGE_A(1, 0, a3, true);
	s_waitcnt lgkmcnt(0)
	v_mfma_f32_16x16x32_bf16 v[62:65], v[142:145], v[182:185], v[62:65]
	v_mfma_f32_16x16x32_bf16 v[58:61], v[158:161], v[182:185], v[58:61]
	v_mfma_f32_16x16x32_bf16 v[46:49], v[142:145], v[190:193], v[46:49]
	v_mfma_f32_16x16x32_bf16 v[42:45], v[158:161], v[190:193], v[42:45]
	v_mfma_f32_16x16x32_bf16 v[30:33], v[142:145], v[198:201], v[30:33]
	v_mfma_f32_16x16x32_bf16 v[26:29], v[158:161], v[198:201], v[26:29]
	v_mfma_f32_16x16x32_bf16 v[14:17], v[142:145], v[206:209], v[14:17]
	v_mfma_f32_16x16x32_bf16 v[10:13], v[158:161], v[206:209], v[10:13]
	v_mfma_f32_16x16x32_bf16 v[62:65], v[154:157], v[186:189], v[62:65]
	v_mfma_f32_16x16x32_bf16 v[58:61], v[162:165], v[186:189], v[58:61]
	v_mfma_f32_16x16x32_bf16 v[46:49], v[154:157], v[194:197], v[46:49]
	v_mfma_f32_16x16x32_bf16 v[42:45], v[162:165], v[194:197], v[42:45]
	v_mfma_f32_16x16x32_bf16 v[30:33], v[154:157], v[202:205], v[30:33]
	v_mfma_f32_16x16x32_bf16 v[26:29], v[162:165], v[202:205], v[26:29]
	v_mfma_f32_16x16x32_bf16 v[14:17], v[154:157], v[210:213], v[14:17]
	v_mfma_f32_16x16x32_bf16 v[10:13], v[162:165], v[210:213], v[10:13]
	v_mfma_f32_16x16x32_bf16 v[54:57], v[166:169], v[182:185], v[54:57]
	v_mfma_f32_16x16x32_bf16 v[50:53], v[174:177], v[182:185], v[50:53]
	v_mfma_f32_16x16x32_bf16 v[38:41], v[166:169], v[190:193], v[38:41]
	v_mfma_f32_16x16x32_bf16 v[34:37], v[174:177], v[190:193], v[34:37]
	v_mfma_f32_16x16x32_bf16 v[22:25], v[166:169], v[198:201], v[22:25]
	v_mfma_f32_16x16x32_bf16 v[18:21], v[174:177], v[198:201], v[18:21]
	v_mfma_f32_16x16x32_bf16 v[6:9], v[166:169], v[206:209], v[6:9]
	v_mfma_f32_16x16x32_bf16 v[2:5], v[174:177], v[206:209], v[2:5]
	v_mfma_f32_16x16x32_bf16 v[54:57], v[170:173], v[186:189], v[54:57]
	v_mfma_f32_16x16x32_bf16 v[50:53], v[178:181], v[186:189], v[50:53]
	v_mfma_f32_16x16x32_bf16 v[38:41], v[170:173], v[194:197], v[38:41]
	v_mfma_f32_16x16x32_bf16 v[34:37], v[178:181], v[194:197], v[34:37]
	v_mfma_f32_16x16x32_bf16 v[22:25], v[170:173], v[202:205], v[22:25]
	v_mfma_f32_16x16x32_bf16 v[18:21], v[178:181], v[202:205], v[18:21]
	v_mfma_f32_16x16x32_bf16 v[6:9], v[170:173], v[210:213], v[6:9]
	v_mfma_f32_16x16x32_bf16 v[2:5], v[178:181], v[210:213], v[2:5]
	s_barrier
	s_setprio 0
	s_add_i32 s57, 0, 0x18000
	v_add_u32_e32 v130, s57, v146
	s_add_i32 s58, 0, 0x1c000
	ds_read_b128 v[142:145], v130
	ds_read_b128 v[154:157], v130 offset:1024
	ds_read_b128 v[158:161], v130 offset:2048
	ds_read_b128 v[162:165], v130 offset:3072
	v_add_u32_e32 v130, s58, v146
	ds_read_b128 v[166:169], v130
	ds_read_b128 v[170:173], v130 offset:1024
	ds_read_b128 v[174:177], v130 offset:2048
	ds_read_b128 v[178:181], v130 offset:3072
	s_add_u32 s28, s36, 0xe0000
	s_addc_u32 s29, s37, 0
	s_mov_b32 m0, s40
	ds_read_b128 v[182:185], v152 offset:32768
	ds_read_b128 v[186:189], v152 offset:33792
	ds_read_b128 v[190:193], v152 offset:34816
	ds_read_b128 v[194:197], v152 offset:35840
	ds_read_b128 v[198:201], v152 offset:36864
	ds_read_b128 v[202:205], v152 offset:37888
	ds_read_b128 v[206:209], v152 offset:38912
	ds_read_b128 v[210:213], v152 offset:39936
	global_load_lds_dwordx4 v132, s[28:29]
	s_mov_b32 m0, s41
	s_nop 0
	global_load_lds_dwordx4 v134, s[28:29]
	s_waitcnt vmcnt(8)
	s_waitcnt lgkmcnt(0)
	s_setprio 3
	s_barrier
	s_waitcnt lgkmcnt(0)
	v_mfma_f32_16x16x32_bf16 v[126:129], v[142:145], v[182:185], v[126:129]
	v_mfma_f32_16x16x32_bf16 v[122:125], v[158:161], v[182:185], v[122:125]
	v_mfma_f32_16x16x32_bf16 v[110:113], v[142:145], v[190:193], v[110:113]
	v_mfma_f32_16x16x32_bf16 v[106:109], v[158:161], v[190:193], v[106:109]
	v_mfma_f32_16x16x32_bf16 v[94:97], v[142:145], v[198:201], v[94:97]
	v_mfma_f32_16x16x32_bf16 v[90:93], v[158:161], v[198:201], v[90:93]
	v_mfma_f32_16x16x32_bf16 v[78:81], v[142:145], v[206:209], v[78:81]
	v_mfma_f32_16x16x32_bf16 v[74:77], v[158:161], v[206:209], v[74:77]
	v_mfma_f32_16x16x32_bf16 v[126:129], v[154:157], v[186:189], v[126:129]
	v_mfma_f32_16x16x32_bf16 v[122:125], v[162:165], v[186:189], v[122:125]
	v_mfma_f32_16x16x32_bf16 v[110:113], v[154:157], v[194:197], v[110:113]
	v_mfma_f32_16x16x32_bf16 v[106:109], v[162:165], v[194:197], v[106:109]
	v_mfma_f32_16x16x32_bf16 v[94:97], v[154:157], v[202:205], v[94:97]
	v_mfma_f32_16x16x32_bf16 v[90:93], v[162:165], v[202:205], v[90:93]
	v_mfma_f32_16x16x32_bf16 v[78:81], v[154:157], v[210:213], v[78:81]
	v_mfma_f32_16x16x32_bf16 v[74:77], v[162:165], v[210:213], v[74:77]
	v_mfma_f32_16x16x32_bf16 v[118:121], v[166:169], v[182:185], v[118:121]
	v_mfma_f32_16x16x32_bf16 v[114:117], v[174:177], v[182:185], v[114:117]
	v_mfma_f32_16x16x32_bf16 v[102:105], v[166:169], v[190:193], v[102:105]
	v_mfma_f32_16x16x32_bf16 v[98:101], v[174:177], v[190:193], v[98:101]
	v_mfma_f32_16x16x32_bf16 v[86:89], v[166:169], v[198:201], v[86:89]
	v_mfma_f32_16x16x32_bf16 v[82:85], v[174:177], v[198:201], v[82:85]
	v_mfma_f32_16x16x32_bf16 v[70:73], v[166:169], v[206:209], v[70:73]
	v_mfma_f32_16x16x32_bf16 v[66:69], v[174:177], v[206:209], v[66:69]
	v_mfma_f32_16x16x32_bf16 v[118:121], v[170:173], v[186:189], v[118:121]
	v_mfma_f32_16x16x32_bf16 v[114:117], v[178:181], v[186:189], v[114:117]
	v_mfma_f32_16x16x32_bf16 v[102:105], v[170:173], v[194:197], v[102:105]
	v_mfma_f32_16x16x32_bf16 v[98:101], v[178:181], v[194:197], v[98:101]
	v_mfma_f32_16x16x32_bf16 v[86:89], v[170:173], v[202:205], v[86:89]
	v_mfma_f32_16x16x32_bf16 v[82:85], v[178:181], v[202:205], v[82:85]
	v_mfma_f32_16x16x32_bf16 v[70:73], v[170:173], v[210:213], v[70:73]
	v_mfma_f32_16x16x32_bf16 v[66:69], v[178:181], v[210:213], v[66:69]
	s_barrier
; #define PG8_STAGE_A(b, h, ptr, NX) do { if constexpr (Sched::GATHER) { unsigned gs_[2]; gs_[0] = ((NX) && last_) ? gN[h][0] : gA[h][0]; gs_[1] = ((NX) && last_) ? gN[h][1] : gA[h][1]; PG8_STAGE(PG8_SA(b, h), ptr, gs_); } \
;         else PG8_STAGE(PG8_SA(b, h), (ptr) + ((h) ? hstep : (size_t)0), voffA); } while (0)
; #define PG8_STAGE(bufoff, gbase, voff) do { _Pragma("unroll") for (int _i = 0; _i < 2; ++_i) \
;         __builtin_amdgcn_global_load_lds((const unsigned*)((const char*)(gbase) + (voff)[_i]), (PG8_LAS unsigned*)(lds + (bufoff) + ldsw + _i * 8192), 16, 0, 0); } while (0)
; #define PG8_LDA(dst, b, h) do { _Pragma("unroll") for (int m = 0; m < 4; ++m) _Pragma("unroll") for (int k = 0; k < 2; ++k) dst[m][k] = *(const PG8_LAS bf16x8*)(lds + PG8_SA(b, h) + aoff + m * 2048 + k * 1024); } while (0)
; #define PG8_MMA(ai, bj, At, Bt) do { __builtin_amdgcn_s_setprio(1); _Pragma("unroll") for (int m = 0; m < 4; ++m) _Pragma("unroll") for (int n = 0; n < 2; ++n) _Pragma("unroll") for (int k = 0; k < 2; ++k) \
;         acc[ai][bj][m][n] = __builtin_amdgcn_mfma_f32_16x16x32_bf16(Bt[n][k], At[m][k], acc[ai][bj][m][n], 0, 0, 0); __builtin_amdgcn_s_setprio(0); } while (0)
; #define PG8_WAIT_V(n) asm volatile("s_waitcnt vmcnt(" #n ")" ::: "memory")
; #define PG8_WAIT_L(n) asm volatile("s_waitcnt lgkmcnt(" #n ")" ::: "memory")
; #define PG8_BAR __builtin_amdgcn_s_barrier()
; #define PG8_SCHED __builtin_amdgcn_sched_barrier(0)
; template <class Epi, class Sched, bool ALIGN_EPI = false, bool SP2 = false>
; __device__ __forceinline__ void gemm_phase(PG8_LAS unsigned char* lds, const Gemm g, const Sched& S, const Epi& E, const bool skip_epi = false) {
;     ...
;         for (int t = 0; t < nt; t += 2) {
;             const bool last = (t == nt - 2); last_ = last && has_next;
;     ...
;             PG8_LDA(At, 1, 1); PG8_STAGE(PG8_SB(1, 0), b3, voffB); PG8_STAGE(PG8_SB(1, 1), b3 + hstep, voffB); PG8_STAGE_A(1, 0, a3, true);
;             PG8_WAIT_V(8); PG8_WAIT_L(0); PG8_BAR; PG8_MMA(1, 0, At, B0); PG8_MMA(1, 1, At, B1); PG8_BAR; PG8_SCHED;
	s_setprio 0
	s_add_i32 s28, s57, s3
	s_add_i32 m0, s28, 0xffffff80
	ds_read_b128 v[182:185], v152 offset:49152
	ds_read_b128 v[186:189], v152 offset:50176
	ds_read_b128 v[190:193], v152 offset:51200
	ds_read_b128 v[194:197], v152 offset:52224
	ds_read_b128 v[198:201], v152 offset:53248
	ds_read_b128 v[202:205], v152 offset:54272
	ds_read_b128 v[206:209], v152 offset:55296
	ds_read_b128 v[210:213], v152 offset:56320
	global_load_lds_dwordx4 v[214:215], off offset:128
	s_add_i32 m0, s28, 0x1f80
	s_add_u32 s28, s34, 0xe0080
	s_addc_u32 s29, s35, 0
	s_add_i32 s34, s58, s3
	global_load_lds_dwordx4 v[216:217], off offset:128
	s_mov_b32 m0, s34
	s_nop 0
	global_load_lds_dwordx4 v132, s[28:29]
	s_add_i32 m0, s34, 0x2000
	s_nop 0
	global_load_lds_dwordx4 v134, s[28:29]
	s_add_i32 m0, s46, 0xffffff80
	s_nop 0
	global_load_lds_dwordx4 v[218:219], off offset:128
	s_add_i32 m0, s47, 0xffffff80
	s_nop 0
	global_load_lds_dwordx4 v[220:221], off offset:128
	s_waitcnt vmcnt(8)
	s_waitcnt lgkmcnt(0)
	s_setprio 3
	s_barrier
	s_waitcnt lgkmcnt(0)
	v_mfma_f32_16x16x32_bf16 v[62:65], v[142:145], v[182:185], v[62:65]
	v_mfma_f32_16x16x32_bf16 v[58:61], v[158:161], v[182:185], v[58:61]
	v_mfma_f32_16x16x32_bf16 v[46:49], v[142:145], v[190:193], v[46:49]
	v_mfma_f32_16x16x32_bf16 v[42:45], v[158:161], v[190:193], v[42:45]
	v_mfma_f32_16x16x32_bf16 v[30:33], v[142:145], v[198:201], v[30:33]
	v_mfma_f32_16x16x32_bf16 v[26:29], v[158:161], v[198:201], v[26:29]
	v_mfma_f32_16x16x32_bf16 v[14:17], v[142:145], v[206:209], v[14:17]
	v_mfma_f32_16x16x32_bf16 v[10:13], v[158:161], v[206:209], v[10:13]
	v_mfma_f32_16x16x32_bf16 v[62:65], v[154:157], v[186:189], v[62:65]
	v_mfma_f32_16x16x32_bf16 v[58:61], v[162:165], v[186:189], v[58:61]
	v_mfma_f32_16x16x32_bf16 v[46:49], v[154:157], v[194:197], v[46:49]
	v_mfma_f32_16x16x32_bf16 v[42:45], v[162:165], v[194:197], v[42:45]
	v_mfma_f32_16x16x32_bf16 v[30:33], v[154:157], v[202:205], v[30:33]
	v_mfma_f32_16x16x32_bf16 v[26:29], v[162:165], v[202:205], v[26:29]
	v_mfma_f32_16x16x32_bf16 v[14:17], v[154:157], v[210:213], v[14:17]
	v_mfma_f32_16x16x32_bf16 v[10:13], v[162:165], v[210:213], v[10:13]
	v_mfma_f32_16x16x32_bf16 v[54:57], v[166:169], v[182:185], v[54:57]
	v_mfma_f32_16x16x32_bf16 v[50:53], v[174:177], v[182:185], v[50:53]
	v_mfma_f32_16x16x32_bf16 v[38:41], v[166:169], v[190:193], v[38:41]
	v_mfma_f32_16x16x32_bf16 v[34:37], v[174:177], v[190:193], v[34:37]
	v_mfma_f32_16x16x32_bf16 v[22:25], v[166:169], v[198:201], v[22:25]
	v_mfma_f32_16x16x32_bf16 v[18:21], v[174:177], v[198:201], v[18:21]
	v_mfma_f32_16x16x32_bf16 v[6:9], v[166:169], v[206:209], v[6:9]
	v_mfma_f32_16x16x32_bf16 v[2:5], v[174:177], v[206:209], v[2:5]
	v_mfma_f32_16x16x32_bf16 v[54:57], v[170:173], v[186:189], v[54:57]
	v_mfma_f32_16x16x32_bf16 v[50:53], v[178:181], v[186:189], v[50:53]
	v_mfma_f32_16x16x32_bf16 v[38:41], v[170:173], v[194:197], v[38:41]
	v_mfma_f32_16x16x32_bf16 v[34:37], v[178:181], v[194:197], v[34:37]
	v_mfma_f32_16x16x32_bf16 v[22:25], v[170:173], v[202:205], v[22:25]
	v_mfma_f32_16x16x32_bf16 v[18:21], v[178:181], v[202:205], v[18:21]
	v_mfma_f32_16x16x32_bf16 v[6:9], v[170:173], v[210:213], v[6:9]
	v_mfma_f32_16x16x32_bf16 v[2:5], v[178:181], v[210:213], v[2:5]
	s_barrier
	s_setprio 0
	s_add_i32 s56, s56, 2
	s_add_u32 s54, s54, 0x100
	s_addc_u32 s55, s55, 0
	s_cmp_gt_u32 s56, 11
	s_mov_b64 s[28:29], s[30:31]
	s_cbranch_scc0 .LBB0_1844
	s_and_b64 vcc, exec, s[20:21]
	s_cbranch_vccz .LBB0_1847
	s_barrier
